# PEER gather: expert row loads carry the non-temporal hint
# baseline (speedup 1.0000x reference)
.LBB0_1138:
	v_and_b32_e32 v4, 15, v148
	v_cmp_eq_u32_e32 vcc, 0, v4
	v_lshlrev_b32_e32 v5, 5, v40
	v_add_u32_e32 v10, 0x80, v148
	v_cndmask_b32_e32 v10, v10, v5, vcc
	v_cmp_gt_u32_e64 s[6:7], 8, v4
	v_lshl_add_u32 v32, v10, 2, v111
	v_and_b32_e32 v36, 12, v148
	v_cndmask_b32_e64 v10, 0, v252, s[6:7]
	v_cmp_lt_u32_e64 s[6:7], 3, v4
	v_lshl_or_b32 v4, v41, 3, v5
	v_add_u32_e32 v34, 0x400, v4
	v_lshlrev_b32_e32 v4, 4, v41
	v_lshl_or_b32 v35, v40, 6, v4
	ds_bpermute_b32 v4, v36, v130
	v_cmp_eq_u32_e32 vcc, 3, v41
	v_cmp_eq_u32_e64 s[2:3], 2, v41
	v_cmp_eq_u32_e64 s[4:5], 1, v41
	v_lshlrev_b32_e32 v129, 4, v148
	s_waitcnt lgkmcnt(0)
	v_mul_lo_u32 v4, v4, s43
	v_add_u32_e32 v5, v4, v35
	v_add_u32_e32 v4, v4, v34
	buffer_load_dwordx4 v[38:41], v5, s[44:47], 0 offen nt
	buffer_load_dwordx2 v[42:43], v4, s[44:47], 0 offen nt
	buffer_load_dwordx4 v[44:47], v5, s[44:47], s21 offen nt
	buffer_load_dwordx2 v[48:49], v4, s[44:47], s33 offen nt
	buffer_load_dwordx4 v[50:53], v5, s[44:47], s20 offen nt
	buffer_load_dwordx2 v[54:55], v4, s[44:47], s21 offen nt
	buffer_load_dwordx4 v[56:59], v5, s[44:47], s23 offen nt
	buffer_load_dwordx2 v[60:61], v4, s[44:47], s94 offen nt
	s_mov_b32 s0, 0
	v_cndmask_b32_e64 v33, 1.0, v10, s[6:7]
	ds_bpermute_b32 v4, v36, v130 offset:16
	s_waitcnt lgkmcnt(0)
	v_mul_lo_u32 v4, v4, s43
	v_add_u32_e32 v5, v4, v35
	v_add_u32_e32 v4, v4, v34
	buffer_load_dwordx4 v[62:65], v5, s[44:47], 0 offen nt
	buffer_load_dwordx4 v[68:71], v5, s[44:47], s20 offen nt
	buffer_load_dwordx4 v[74:77], v5, s[44:47], s21 offen nt
	buffer_load_dwordx4 v[86:89], v5, s[44:47], s23 offen nt
	buffer_load_dwordx2 v[66:67], v4, s[44:47], 0 offen nt
	buffer_load_dwordx2 v[78:79], v4, s[44:47], s33 offen nt
	buffer_load_dwordx2 v[72:73], v4, s[44:47], s21 offen nt
	buffer_load_dwordx2 v[90:91], v4, s[44:47], s94 offen nt
	ds_bpermute_b32 v4, v36, v130 offset:32
	s_waitcnt lgkmcnt(0)
	v_mul_lo_u32 v4, v4, s43
	v_add_u32_e32 v5, v4, v35
	v_add_u32_e32 v4, v4, v34
	buffer_load_dwordx4 v[92:95], v5, s[44:47], 0 offen nt
	buffer_load_dwordx4 v[98:101], v5, s[44:47], s20 offen nt
	buffer_load_dwordx4 v[150:153], v5, s[44:47], s21 offen nt
	buffer_load_dwordx4 v[156:159], v5, s[44:47], s23 offen nt
	buffer_load_dwordx2 v[96:97], v4, s[44:47], 0 offen nt
	buffer_load_dwordx2 v[154:155], v4, s[44:47], s33 offen nt
	buffer_load_dwordx2 v[102:103], v4, s[44:47], s21 offen nt
	buffer_load_dwordx2 v[160:161], v4, s[44:47], s94 offen nt
	ds_bpermute_b32 v4, v36, v130 offset:48
	s_waitcnt lgkmcnt(0)
	v_mul_lo_u32 v4, v4, s43
	v_add_u32_e32 v5, v4, v35
	v_add_u32_e32 v4, v4, v34
	buffer_load_dwordx4 v[162:165], v5, s[44:47], 0 offen nt
	buffer_load_dwordx4 v[168:171], v5, s[44:47], s20 offen nt
	buffer_load_dwordx4 v[174:177], v5, s[44:47], s21 offen nt
	buffer_load_dwordx4 v[216:219], v5, s[44:47], s23 offen nt
	buffer_load_dwordx2 v[166:167], v4, s[44:47], 0 offen nt
	buffer_load_dwordx2 v[178:179], v4, s[44:47], s33 offen nt
	buffer_load_dwordx2 v[172:173], v4, s[44:47], s21 offen nt
	buffer_load_dwordx2 v[220:221], v4, s[44:47], s94 offen nt
	v_mov_b32_e32 v22, v28
	v_mov_b32_e32 v23, v29
	v_mov_b32_e32 v16, v30
	v_mov_b32_e32 v17, v31
	s_waitcnt vmcnt(30)
	v_mfma_f32_16x16x128_f8f6f4 v[38:41], v[38:43], v[18:23], 0 cbsz:2 blgp:2
	v_mov_b32_e32 v10, v24
	v_mov_b32_e32 v11, v25
	v_mov_b32_e32 v4, v26
	s_waitcnt vmcnt(28)
	v_mfma_f32_16x16x128_f8f6f4 v[28:31], v[44:49], v[12:17], v[38:41] cbsz:2 blgp:2
	v_mov_b32_e32 v5, v27
	s_waitcnt vmcnt(26)
	v_mfma_f32_16x16x128_f8f6f4 v[28:31], v[50:55], v[6:11], v[28:31] cbsz:2 blgp:2
	s_waitcnt vmcnt(24)
	v_mfma_f32_16x16x128_f8f6f4 v[24:27], v[56:61], v[0:5], v[28:31] cbsz:2 blgp:2
	s_nop 7
	v_cndmask_b32_e64 v24, v24, v25, s[4:5]
	v_cndmask_b32_e64 v24, v24, v26, s[2:3]
	v_cndmask_b32_e32 v24, v24, v27, vcc
	v_mul_f32_e32 v25, v33, v24
	s_nop 1
	v_mov_b32_dpp v25, v25 quad_perm:[1,0,3,2] row_mask:0xf bank_mask:0xf bound_ctrl:1
	v_fmac_f32_e32 v25, v33, v24
	s_nop 1
	v_add_f32_dpp v24, v25, v25 quad_perm:[2,3,0,1] row_mask:0xf bank_mask:0xf bound_ctrl:1
	s_nop 1
	v_add_f32_dpp v24, v24, v24 row_half_mirror row_mask:0xf bank_mask:0xf bound_ctrl:1
	ds_write_b32 v32, v24 offset:49152
	ds_bpermute_b32 v24, v36, v130 offset:64
	s_waitcnt lgkmcnt(0)
	v_mul_lo_u32 v24, v24, s43
	v_add_u32_e32 v28, v24, v35
	v_add_u32_e32 v30, v24, v34
	buffer_load_dwordx4 v[24:27], v28, s[44:47], 0 offen nt
	buffer_load_dwordx4 v[38:41], v28, s[44:47], s20 offen nt
	buffer_load_dwordx4 v[44:47], v28, s[44:47], s21 offen nt
	buffer_load_dwordx4 v[50:53], v28, s[44:47], s23 offen nt
	s_nop 0
	buffer_load_dwordx2 v[28:29], v30, s[44:47], 0 offen nt
	buffer_load_dwordx2 v[48:49], v30, s[44:47], s33 offen nt
	buffer_load_dwordx2 v[42:43], v30, s[44:47], s21 offen nt
	buffer_load_dwordx2 v[54:55], v30, s[44:47], s94 offen nt
	s_waitcnt vmcnt(27)
	v_mfma_f32_16x16x128_f8f6f4 v[56:59], v[62:67], v[18:23], 0 cbsz:2 blgp:2
	s_waitcnt vmcnt(26)
	v_mfma_f32_16x16x128_f8f6f4 v[56:59], v[74:79], v[12:17], v[56:59] cbsz:2 blgp:2
	s_waitcnt vmcnt(25)
	v_mfma_f32_16x16x128_f8f6f4 v[56:59], v[68:73], v[6:11], v[56:59] cbsz:2 blgp:2
	s_waitcnt vmcnt(24)
	v_mfma_f32_16x16x128_f8f6f4 v[56:59], v[86:91], v[0:5], v[56:59] cbsz:2 blgp:2
	s_nop 7
	v_cndmask_b32_e64 v30, v56, v57, s[4:5]
	v_cndmask_b32_e64 v30, v30, v58, s[2:3]
	v_cndmask_b32_e32 v30, v30, v59, vcc
	v_mul_f32_e32 v31, v33, v30
	s_nop 1
	v_mov_b32_dpp v31, v31 quad_perm:[1,0,3,2] row_mask:0xf bank_mask:0xf bound_ctrl:1
	v_fmac_f32_e32 v31, v33, v30
	s_nop 1
	v_add_f32_dpp v30, v31, v31 quad_perm:[2,3,0,1] row_mask:0xf bank_mask:0xf bound_ctrl:1
	s_nop 1
	v_add_f32_dpp v30, v30, v30 row_half_mirror row_mask:0xf bank_mask:0xf bound_ctrl:1
	ds_write_b32 v32, v30 offset:49156
	ds_bpermute_b32 v30, v36, v130 offset:80
	s_waitcnt lgkmcnt(0)
	v_mul_lo_u32 v30, v30, s43
	v_add_u32_e32 v31, v30, v35
	v_add_u32_e32 v30, v30, v34
	buffer_load_dwordx4 v[56:59], v31, s[44:47], 0 offen nt
	buffer_load_dwordx4 v[62:65], v31, s[44:47], s20 offen nt
	buffer_load_dwordx4 v[68:71], v31, s[44:47], s21 offen nt
	buffer_load_dwordx4 v[74:77], v31, s[44:47], s23 offen nt
	buffer_load_dwordx2 v[60:61], v30, s[44:47], 0 offen nt
	buffer_load_dwordx2 v[72:73], v30, s[44:47], s33 offen nt
	buffer_load_dwordx2 v[66:67], v30, s[44:47], s21 offen nt
	buffer_load_dwordx2 v[78:79], v30, s[44:47], s94 offen nt
	s_waitcnt vmcnt(27)
	v_mfma_f32_16x16x128_f8f6f4 v[86:89], v[92:97], v[18:23], 0 cbsz:2 blgp:2
	s_waitcnt vmcnt(26)
	v_mfma_f32_16x16x128_f8f6f4 v[86:89], v[150:155], v[12:17], v[86:89] cbsz:2 blgp:2
	s_waitcnt vmcnt(25)
	v_mfma_f32_16x16x128_f8f6f4 v[86:89], v[98:103], v[6:11], v[86:89] cbsz:2 blgp:2
	s_waitcnt vmcnt(24)
	v_mfma_f32_16x16x128_f8f6f4 v[86:89], v[156:161], v[0:5], v[86:89] cbsz:2 blgp:2
	s_nop 7
	v_cndmask_b32_e64 v30, v86, v87, s[4:5]
	v_cndmask_b32_e64 v30, v30, v88, s[2:3]
	v_cndmask_b32_e32 v30, v30, v89, vcc
	v_mul_f32_e32 v31, v33, v30
	s_nop 1
	v_mov_b32_dpp v31, v31 quad_perm:[1,0,3,2] row_mask:0xf bank_mask:0xf bound_ctrl:1
	v_fmac_f32_e32 v31, v33, v30
	s_nop 1
	v_add_f32_dpp v30, v31, v31 quad_perm:[2,3,0,1] row_mask:0xf bank_mask:0xf bound_ctrl:1
	s_nop 1
	v_add_f32_dpp v30, v30, v30 row_half_mirror row_mask:0xf bank_mask:0xf bound_ctrl:1
	ds_write_b32 v32, v30 offset:49160
	ds_bpermute_b32 v30, v36, v130 offset:96
	s_waitcnt lgkmcnt(0)
	v_mul_lo_u32 v30, v30, s43
	v_add_u32_e32 v31, v30, v35
	v_add_u32_e32 v30, v30, v34
	buffer_load_dwordx4 v[86:89], v31, s[44:47], 0 offen nt
	buffer_load_dwordx4 v[92:95], v31, s[44:47], s20 offen nt
	buffer_load_dwordx4 v[98:101], v31, s[44:47], s21 offen nt
	buffer_load_dwordx4 v[150:153], v31, s[44:47], s23 offen nt
	buffer_load_dwordx2 v[90:91], v30, s[44:47], 0 offen nt
	buffer_load_dwordx2 v[102:103], v30, s[44:47], s33 offen nt
	buffer_load_dwordx2 v[96:97], v30, s[44:47], s21 offen nt
	buffer_load_dwordx2 v[154:155], v30, s[44:47], s94 offen nt
	s_waitcnt vmcnt(27)
	v_mfma_f32_16x16x128_f8f6f4 v[156:159], v[162:167], v[18:23], 0 cbsz:2 blgp:2
	s_waitcnt vmcnt(26)
	v_mfma_f32_16x16x128_f8f6f4 v[156:159], v[174:179], v[12:17], v[156:159] cbsz:2 blgp:2
	s_waitcnt vmcnt(25)
	v_mfma_f32_16x16x128_f8f6f4 v[156:159], v[168:173], v[6:11], v[156:159] cbsz:2 blgp:2
	s_waitcnt vmcnt(24)
	v_mfma_f32_16x16x128_f8f6f4 v[156:159], v[216:221], v[0:5], v[156:159] cbsz:2 blgp:2
	s_nop 7
	v_cndmask_b32_e64 v30, v156, v157, s[4:5]
	v_cndmask_b32_e64 v30, v30, v158, s[2:3]
	v_cndmask_b32_e32 v30, v30, v159, vcc
	v_mul_f32_e32 v31, v33, v30
	s_nop 1
	v_mov_b32_dpp v31, v31 quad_perm:[1,0,3,2] row_mask:0xf bank_mask:0xf bound_ctrl:1
	v_fmac_f32_e32 v31, v33, v30
	s_nop 1
	v_add_f32_dpp v30, v31, v31 quad_perm:[2,3,0,1] row_mask:0xf bank_mask:0xf bound_ctrl:1
	s_nop 1
	v_add_f32_dpp v30, v30, v30 row_half_mirror row_mask:0xf bank_mask:0xf bound_ctrl:1
	ds_write_b32 v32, v30 offset:49164
	ds_bpermute_b32 v30, v36, v130 offset:112
	s_waitcnt lgkmcnt(0)
	v_mul_lo_u32 v30, v30, s43
	v_add_u32_e32 v31, v30, v35
	v_add_u32_e32 v30, v30, v34
	buffer_load_dwordx4 v[156:159], v31, s[44:47], 0 offen nt
	buffer_load_dwordx4 v[162:165], v31, s[44:47], s20 offen nt
	buffer_load_dwordx4 v[168:171], v31, s[44:47], s21 offen nt
	buffer_load_dwordx4 v[174:177], v31, s[44:47], s23 offen nt
	buffer_load_dwordx2 v[160:161], v30, s[44:47], 0 offen nt
	buffer_load_dwordx2 v[172:173], v30, s[44:47], s33 offen nt
	buffer_load_dwordx2 v[166:167], v30, s[44:47], s21 offen nt
	buffer_load_dwordx2 v[178:179], v30, s[44:47], s94 offen nt
	s_waitcnt vmcnt(27)
	v_mfma_f32_16x16x128_f8f6f4 v[24:27], v[24:29], v[18:23], 0 cbsz:2 blgp:2
	s_waitcnt vmcnt(26)
	v_mfma_f32_16x16x128_f8f6f4 v[24:27], v[44:49], v[12:17], v[24:27] cbsz:2 blgp:2
	s_waitcnt vmcnt(25)
	v_mfma_f32_16x16x128_f8f6f4 v[24:27], v[38:43], v[6:11], v[24:27] cbsz:2 blgp:2
	s_waitcnt vmcnt(24)
	v_mfma_f32_16x16x128_f8f6f4 v[24:27], v[50:55], v[0:5], v[24:27] cbsz:2 blgp:2
	s_nop 7
	v_cndmask_b32_e64 v24, v24, v25, s[4:5]
	v_cndmask_b32_e64 v24, v24, v26, s[2:3]
	v_cndmask_b32_e32 v24, v24, v27, vcc
	v_mul_f32_e32 v25, v33, v24
	s_nop 1
	v_mov_b32_dpp v25, v25 quad_perm:[1,0,3,2] row_mask:0xf bank_mask:0xf bound_ctrl:1
	v_fmac_f32_e32 v25, v33, v24
	s_nop 1
	v_add_f32_dpp v24, v25, v25 quad_perm:[2,3,0,1] row_mask:0xf bank_mask:0xf bound_ctrl:1
	s_nop 1
	v_add_f32_dpp v24, v24, v24 row_half_mirror row_mask:0xf bank_mask:0xf bound_ctrl:1
	ds_write_b32 v32, v24 offset:49168
	ds_bpermute_b32 v24, v36, v130 offset:128
	s_waitcnt lgkmcnt(0)
	v_mul_lo_u32 v24, v24, s43
	v_add_u32_e32 v28, v24, v35
	v_add_u32_e32 v30, v24, v34
	buffer_load_dwordx4 v[24:27], v28, s[44:47], 0 offen nt
	buffer_load_dwordx4 v[38:41], v28, s[44:47], s20 offen nt
	buffer_load_dwordx4 v[44:47], v28, s[44:47], s21 offen nt
	buffer_load_dwordx4 v[50:53], v28, s[44:47], s23 offen nt
	s_nop 0
	buffer_load_dwordx2 v[28:29], v30, s[44:47], 0 offen nt
	buffer_load_dwordx2 v[48:49], v30, s[44:47], s33 offen nt
	buffer_load_dwordx2 v[42:43], v30, s[44:47], s21 offen nt
	buffer_load_dwordx2 v[54:55], v30, s[44:47], s94 offen nt
	s_waitcnt vmcnt(27)
	v_mfma_f32_16x16x128_f8f6f4 v[56:59], v[56:61], v[18:23], 0 cbsz:2 blgp:2
	s_waitcnt vmcnt(26)
	v_mfma_f32_16x16x128_f8f6f4 v[56:59], v[68:73], v[12:17], v[56:59] cbsz:2 blgp:2
	s_waitcnt vmcnt(25)
	v_mfma_f32_16x16x128_f8f6f4 v[56:59], v[62:67], v[6:11], v[56:59] cbsz:2 blgp:2
	s_waitcnt vmcnt(24)
	v_mfma_f32_16x16x128_f8f6f4 v[56:59], v[74:79], v[0:5], v[56:59] cbsz:2 blgp:2
	s_nop 7
	v_cndmask_b32_e64 v30, v56, v57, s[4:5]
	v_cndmask_b32_e64 v30, v30, v58, s[2:3]
	v_cndmask_b32_e32 v30, v30, v59, vcc
	v_mul_f32_e32 v31, v33, v30
	s_nop 1
	v_mov_b32_dpp v31, v31 quad_perm:[1,0,3,2] row_mask:0xf bank_mask:0xf bound_ctrl:1
	v_fmac_f32_e32 v31, v33, v30
	s_nop 1
	v_add_f32_dpp v30, v31, v31 quad_perm:[2,3,0,1] row_mask:0xf bank_mask:0xf bound_ctrl:1
	s_nop 1
	v_add_f32_dpp v30, v30, v30 row_half_mirror row_mask:0xf bank_mask:0xf bound_ctrl:1
	ds_write_b32 v32, v30 offset:49172
	ds_bpermute_b32 v30, v36, v130 offset:144
	s_waitcnt lgkmcnt(0)
	v_mul_lo_u32 v30, v30, s43
	v_add_u32_e32 v31, v30, v35
	v_add_u32_e32 v30, v30, v34
	buffer_load_dwordx4 v[56:59], v31, s[44:47], 0 offen nt
	buffer_load_dwordx4 v[62:65], v31, s[44:47], s20 offen nt
	buffer_load_dwordx4 v[68:71], v31, s[44:47], s21 offen nt
	buffer_load_dwordx4 v[74:77], v31, s[44:47], s23 offen nt
	buffer_load_dwordx2 v[60:61], v30, s[44:47], 0 offen nt
	buffer_load_dwordx2 v[72:73], v30, s[44:47], s33 offen nt
	buffer_load_dwordx2 v[66:67], v30, s[44:47], s21 offen nt
	buffer_load_dwordx2 v[78:79], v30, s[44:47], s94 offen nt
	s_waitcnt vmcnt(27)
	v_mfma_f32_16x16x128_f8f6f4 v[86:89], v[86:91], v[18:23], 0 cbsz:2 blgp:2
	s_waitcnt vmcnt(26)
	v_mfma_f32_16x16x128_f8f6f4 v[86:89], v[98:103], v[12:17], v[86:89] cbsz:2 blgp:2
	s_waitcnt vmcnt(25)
	v_mfma_f32_16x16x128_f8f6f4 v[86:89], v[92:97], v[6:11], v[86:89] cbsz:2 blgp:2
	s_waitcnt vmcnt(24)
	v_mfma_f32_16x16x128_f8f6f4 v[86:89], v[150:155], v[0:5], v[86:89] cbsz:2 blgp:2
	s_nop 7
	v_cndmask_b32_e64 v30, v86, v87, s[4:5]
	v_cndmask_b32_e64 v30, v30, v88, s[2:3]
	v_cndmask_b32_e32 v30, v30, v89, vcc
	v_mul_f32_e32 v31, v33, v30
	s_nop 1
	v_mov_b32_dpp v31, v31 quad_perm:[1,0,3,2] row_mask:0xf bank_mask:0xf bound_ctrl:1
	v_fmac_f32_e32 v31, v33, v30
	s_nop 1
	v_add_f32_dpp v30, v31, v31 quad_perm:[2,3,0,1] row_mask:0xf bank_mask:0xf bound_ctrl:1
	s_nop 1
	v_add_f32_dpp v30, v30, v30 row_half_mirror row_mask:0xf bank_mask:0xf bound_ctrl:1
	ds_write_b32 v32, v30 offset:49176
	ds_bpermute_b32 v30, v36, v130 offset:160
	s_waitcnt lgkmcnt(0)
	v_mul_lo_u32 v30, v30, s43
	v_add_u32_e32 v31, v30, v35
	v_add_u32_e32 v30, v30, v34
	buffer_load_dwordx4 v[86:89], v31, s[44:47], 0 offen nt
	buffer_load_dwordx4 v[92:95], v31, s[44:47], s20 offen nt
	buffer_load_dwordx4 v[98:101], v31, s[44:47], s21 offen nt
	buffer_load_dwordx4 v[150:153], v31, s[44:47], s23 offen nt
	buffer_load_dwordx2 v[90:91], v30, s[44:47], 0 offen nt
	buffer_load_dwordx2 v[102:103], v30, s[44:47], s33 offen nt
	buffer_load_dwordx2 v[96:97], v30, s[44:47], s21 offen nt
	buffer_load_dwordx2 v[154:155], v30, s[44:47], s94 offen nt
	s_waitcnt vmcnt(27)
	v_mfma_f32_16x16x128_f8f6f4 v[156:159], v[156:161], v[18:23], 0 cbsz:2 blgp:2
	s_waitcnt vmcnt(26)
	v_mfma_f32_16x16x128_f8f6f4 v[156:159], v[168:173], v[12:17], v[156:159] cbsz:2 blgp:2
	s_waitcnt vmcnt(25)
	v_mfma_f32_16x16x128_f8f6f4 v[156:159], v[162:167], v[6:11], v[156:159] cbsz:2 blgp:2
	s_waitcnt vmcnt(24)
	v_mfma_f32_16x16x128_f8f6f4 v[156:159], v[174:179], v[0:5], v[156:159] cbsz:2 blgp:2
	s_nop 7
	v_cndmask_b32_e64 v30, v156, v157, s[4:5]
	v_cndmask_b32_e64 v30, v30, v158, s[2:3]
	v_cndmask_b32_e32 v30, v30, v159, vcc
	v_mul_f32_e32 v31, v33, v30
	s_nop 1
	v_mov_b32_dpp v31, v31 quad_perm:[1,0,3,2] row_mask:0xf bank_mask:0xf bound_ctrl:1
	v_fmac_f32_e32 v31, v33, v30
	s_nop 1
	v_add_f32_dpp v30, v31, v31 quad_perm:[2,3,0,1] row_mask:0xf bank_mask:0xf bound_ctrl:1
	s_nop 1
	v_add_f32_dpp v30, v30, v30 row_half_mirror row_mask:0xf bank_mask:0xf bound_ctrl:1
	ds_write_b32 v32, v30 offset:49180
	ds_bpermute_b32 v30, v36, v130 offset:176
	s_waitcnt lgkmcnt(0)
	v_mul_lo_u32 v30, v30, s43
	v_add_u32_e32 v31, v30, v35
	v_add_u32_e32 v30, v30, v34
	buffer_load_dwordx4 v[156:159], v31, s[44:47], 0 offen nt
	buffer_load_dwordx4 v[162:165], v31, s[44:47], s20 offen nt
	buffer_load_dwordx4 v[168:171], v31, s[44:47], s21 offen nt
	buffer_load_dwordx4 v[174:177], v31, s[44:47], s23 offen nt
	buffer_load_dwordx2 v[160:161], v30, s[44:47], 0 offen nt
	buffer_load_dwordx2 v[172:173], v30, s[44:47], s33 offen nt
	buffer_load_dwordx2 v[166:167], v30, s[44:47], s21 offen nt
	buffer_load_dwordx2 v[178:179], v30, s[44:47], s94 offen nt
	s_waitcnt vmcnt(27)
	v_mfma_f32_16x16x128_f8f6f4 v[24:27], v[24:29], v[18:23], 0 cbsz:2 blgp:2
	s_waitcnt vmcnt(26)
	v_mfma_f32_16x16x128_f8f6f4 v[24:27], v[44:49], v[12:17], v[24:27] cbsz:2 blgp:2
	s_waitcnt vmcnt(25)
	v_mfma_f32_16x16x128_f8f6f4 v[24:27], v[38:43], v[6:11], v[24:27] cbsz:2 blgp:2
	s_waitcnt vmcnt(24)
	v_mfma_f32_16x16x128_f8f6f4 v[24:27], v[50:55], v[0:5], v[24:27] cbsz:2 blgp:2
	s_nop 7
	v_cndmask_b32_e64 v24, v24, v25, s[4:5]
	v_cndmask_b32_e64 v24, v24, v26, s[2:3]
	v_cndmask_b32_e32 v24, v24, v27, vcc
	v_mul_f32_e32 v25, v33, v24
	s_nop 1
	v_mov_b32_dpp v25, v25 quad_perm:[1,0,3,2] row_mask:0xf bank_mask:0xf bound_ctrl:1
	v_fmac_f32_e32 v25, v33, v24
	s_nop 1
	v_add_f32_dpp v24, v25, v25 quad_perm:[2,3,0,1] row_mask:0xf bank_mask:0xf bound_ctrl:1
	s_nop 1
	v_add_f32_dpp v24, v24, v24 row_half_mirror row_mask:0xf bank_mask:0xf bound_ctrl:1
	ds_write_b32 v32, v24 offset:49184
	ds_bpermute_b32 v24, v36, v130 offset:192
	s_waitcnt lgkmcnt(0)
	v_mul_lo_u32 v24, v24, s43
	v_add_u32_e32 v28, v24, v35
	v_add_u32_e32 v30, v24, v34
	buffer_load_dwordx4 v[24:27], v28, s[44:47], 0 offen nt
	buffer_load_dwordx4 v[38:41], v28, s[44:47], s20 offen nt
	buffer_load_dwordx4 v[44:47], v28, s[44:47], s21 offen nt
	buffer_load_dwordx4 v[50:53], v28, s[44:47], s23 offen nt
	s_nop 0
	buffer_load_dwordx2 v[28:29], v30, s[44:47], 0 offen nt
	buffer_load_dwordx2 v[48:49], v30, s[44:47], s33 offen nt
	buffer_load_dwordx2 v[42:43], v30, s[44:47], s21 offen nt
	buffer_load_dwordx2 v[54:55], v30, s[44:47], s94 offen nt
	s_waitcnt vmcnt(27)
	v_mfma_f32_16x16x128_f8f6f4 v[56:59], v[56:61], v[18:23], 0 cbsz:2 blgp:2
	s_waitcnt vmcnt(26)
	v_mfma_f32_16x16x128_f8f6f4 v[56:59], v[68:73], v[12:17], v[56:59] cbsz:2 blgp:2
	s_waitcnt vmcnt(25)
	v_mfma_f32_16x16x128_f8f6f4 v[56:59], v[62:67], v[6:11], v[56:59] cbsz:2 blgp:2
	s_waitcnt vmcnt(24)
	v_mfma_f32_16x16x128_f8f6f4 v[56:59], v[74:79], v[0:5], v[56:59] cbsz:2 blgp:2
	s_nop 7
	v_cndmask_b32_e64 v30, v56, v57, s[4:5]
	v_cndmask_b32_e64 v30, v30, v58, s[2:3]
	v_cndmask_b32_e32 v30, v30, v59, vcc
	v_mul_f32_e32 v31, v33, v30
	s_nop 1
	v_mov_b32_dpp v31, v31 quad_perm:[1,0,3,2] row_mask:0xf bank_mask:0xf bound_ctrl:1
	v_fmac_f32_e32 v31, v33, v30
	s_nop 1
	v_add_f32_dpp v30, v31, v31 quad_perm:[2,3,0,1] row_mask:0xf bank_mask:0xf bound_ctrl:1
	s_nop 1
	v_add_f32_dpp v30, v30, v30 row_half_mirror row_mask:0xf bank_mask:0xf bound_ctrl:1
	ds_write_b32 v32, v30 offset:49188
	ds_bpermute_b32 v30, v36, v130 offset:208
	s_waitcnt lgkmcnt(0)
	v_mul_lo_u32 v30, v30, s43
	v_add_u32_e32 v31, v30, v35
	v_add_u32_e32 v30, v30, v34
	buffer_load_dwordx4 v[56:59], v31, s[44:47], 0 offen nt
	buffer_load_dwordx4 v[62:65], v31, s[44:47], s20 offen nt
	buffer_load_dwordx4 v[68:71], v31, s[44:47], s21 offen nt
	buffer_load_dwordx4 v[74:77], v31, s[44:47], s23 offen nt
	buffer_load_dwordx2 v[60:61], v30, s[44:47], 0 offen nt
	buffer_load_dwordx2 v[72:73], v30, s[44:47], s33 offen nt
	buffer_load_dwordx2 v[66:67], v30, s[44:47], s21 offen nt
	buffer_load_dwordx2 v[78:79], v30, s[44:47], s94 offen nt
	s_waitcnt vmcnt(27)
	v_mfma_f32_16x16x128_f8f6f4 v[86:89], v[86:91], v[18:23], 0 cbsz:2 blgp:2
	s_waitcnt vmcnt(26)
	v_mfma_f32_16x16x128_f8f6f4 v[86:89], v[98:103], v[12:17], v[86:89] cbsz:2 blgp:2
	s_waitcnt vmcnt(25)
	v_mfma_f32_16x16x128_f8f6f4 v[86:89], v[92:97], v[6:11], v[86:89] cbsz:2 blgp:2
	s_waitcnt vmcnt(24)
	v_mfma_f32_16x16x128_f8f6f4 v[86:89], v[150:155], v[0:5], v[86:89] cbsz:2 blgp:2
	s_nop 7
	v_cndmask_b32_e64 v30, v86, v87, s[4:5]
	v_cndmask_b32_e64 v30, v30, v88, s[2:3]
	v_cndmask_b32_e32 v30, v30, v89, vcc
	v_mul_f32_e32 v31, v33, v30
	s_nop 1
	v_mov_b32_dpp v31, v31 quad_perm:[1,0,3,2] row_mask:0xf bank_mask:0xf bound_ctrl:1
	v_fmac_f32_e32 v31, v33, v30
	s_nop 1
	v_add_f32_dpp v30, v31, v31 quad_perm:[2,3,0,1] row_mask:0xf bank_mask:0xf bound_ctrl:1
	s_nop 1
	v_add_f32_dpp v30, v30, v30 row_half_mirror row_mask:0xf bank_mask:0xf bound_ctrl:1
	ds_write_b32 v32, v30 offset:49192
	ds_bpermute_b32 v30, v36, v130 offset:224
	s_waitcnt lgkmcnt(0)
	v_mul_lo_u32 v30, v30, s43
	v_add_u32_e32 v31, v30, v35
	v_add_u32_e32 v30, v30, v34
	buffer_load_dwordx4 v[86:89], v31, s[44:47], 0 offen nt
	buffer_load_dwordx4 v[92:95], v31, s[44:47], s20 offen nt
	buffer_load_dwordx4 v[98:101], v31, s[44:47], s21 offen nt
	buffer_load_dwordx4 v[150:153], v31, s[44:47], s23 offen nt
	buffer_load_dwordx2 v[90:91], v30, s[44:47], 0 offen nt
	buffer_load_dwordx2 v[102:103], v30, s[44:47], s33 offen nt
	buffer_load_dwordx2 v[96:97], v30, s[44:47], s21 offen nt
	buffer_load_dwordx2 v[154:155], v30, s[44:47], s94 offen nt
	s_waitcnt vmcnt(27)
	v_mfma_f32_16x16x128_f8f6f4 v[156:159], v[156:161], v[18:23], 0 cbsz:2 blgp:2
	s_waitcnt vmcnt(26)
	v_mfma_f32_16x16x128_f8f6f4 v[156:159], v[168:173], v[12:17], v[156:159] cbsz:2 blgp:2
	s_waitcnt vmcnt(25)
	v_mfma_f32_16x16x128_f8f6f4 v[156:159], v[162:167], v[6:11], v[156:159] cbsz:2 blgp:2
	s_waitcnt vmcnt(24)
	v_mfma_f32_16x16x128_f8f6f4 v[156:159], v[174:179], v[0:5], v[156:159] cbsz:2 blgp:2
	s_nop 7
	v_cndmask_b32_e64 v30, v156, v157, s[4:5]
	v_cndmask_b32_e64 v30, v30, v158, s[2:3]
	v_cndmask_b32_e32 v30, v30, v159, vcc
	v_mul_f32_e32 v31, v33, v30
	s_nop 1
	v_mov_b32_dpp v31, v31 quad_perm:[1,0,3,2] row_mask:0xf bank_mask:0xf bound_ctrl:1
	v_fmac_f32_e32 v31, v33, v30
	s_nop 1
	v_add_f32_dpp v30, v31, v31 quad_perm:[2,3,0,1] row_mask:0xf bank_mask:0xf bound_ctrl:1
	s_nop 1
	v_add_f32_dpp v30, v30, v30 row_half_mirror row_mask:0xf bank_mask:0xf bound_ctrl:1
	ds_write_b32 v32, v30 offset:49196
	ds_bpermute_b32 v30, v36, v130 offset:240
	s_waitcnt lgkmcnt(0)
	v_mul_lo_u32 v30, v30, s43
	v_add_u32_e32 v31, v30, v35
	v_add_u32_e32 v30, v30, v34
	buffer_load_dwordx4 v[156:159], v31, s[44:47], 0 offen nt
	buffer_load_dwordx4 v[162:165], v31, s[44:47], s20 offen nt
	buffer_load_dwordx4 v[168:171], v31, s[44:47], s21 offen nt
	buffer_load_dwordx4 v[174:177], v31, s[44:47], s23 offen nt
	buffer_load_dwordx2 v[160:161], v30, s[44:47], 0 offen nt
	buffer_load_dwordx2 v[172:173], v30, s[44:47], s33 offen nt
	buffer_load_dwordx2 v[166:167], v30, s[44:47], s21 offen nt
	buffer_load_dwordx2 v[178:179], v30, s[44:47], s94 offen nt
	s_waitcnt vmcnt(27)
	v_mfma_f32_16x16x128_f8f6f4 v[24:27], v[24:29], v[18:23], 0 cbsz:2 blgp:2
	s_waitcnt vmcnt(26)
	v_mfma_f32_16x16x128_f8f6f4 v[24:27], v[44:49], v[12:17], v[24:27] cbsz:2 blgp:2
	s_waitcnt vmcnt(25)
	v_mfma_f32_16x16x128_f8f6f4 v[24:27], v[38:43], v[6:11], v[24:27] cbsz:2 blgp:2
	s_waitcnt vmcnt(24)
	v_mfma_f32_16x16x128_f8f6f4 v[24:27], v[50:55], v[0:5], v[24:27] cbsz:2 blgp:2
	s_nop 7
	v_cndmask_b32_e64 v24, v24, v25, s[4:5]
	v_cndmask_b32_e64 v24, v24, v26, s[2:3]
	v_cndmask_b32_e32 v24, v24, v27, vcc
	v_mul_f32_e32 v25, v33, v24
	s_nop 1
	v_mov_b32_dpp v25, v25 quad_perm:[1,0,3,2] row_mask:0xf bank_mask:0xf bound_ctrl:1
	v_fmac_f32_e32 v25, v33, v24
	s_nop 1
	v_add_f32_dpp v24, v25, v25 quad_perm:[2,3,0,1] row_mask:0xf bank_mask:0xf bound_ctrl:1
	s_nop 1
	v_add_f32_dpp v24, v24, v24 row_half_mirror row_mask:0xf bank_mask:0xf bound_ctrl:1
	ds_write_b32 v32, v24 offset:49200
	ds_bpermute_b32 v24, v36, v128
	s_waitcnt lgkmcnt(0)
	v_mul_lo_u32 v24, v24, s43
	v_add_u32_e32 v28, v24, v35
	v_add_u32_e32 v30, v24, v34
	buffer_load_dwordx4 v[24:27], v28, s[44:47], 0 offen nt
	buffer_load_dwordx4 v[38:41], v28, s[44:47], s20 offen nt
	buffer_load_dwordx4 v[44:47], v28, s[44:47], s21 offen nt
	buffer_load_dwordx4 v[50:53], v28, s[44:47], s23 offen nt
	s_nop 0
	buffer_load_dwordx2 v[28:29], v30, s[44:47], 0 offen nt
	buffer_load_dwordx2 v[48:49], v30, s[44:47], s33 offen nt
	buffer_load_dwordx2 v[42:43], v30, s[44:47], s21 offen nt
	buffer_load_dwordx2 v[54:55], v30, s[44:47], s94 offen nt
	s_waitcnt vmcnt(27)
	v_mfma_f32_16x16x128_f8f6f4 v[56:59], v[56:61], v[18:23], 0 cbsz:2 blgp:2
	s_waitcnt vmcnt(26)
	v_mfma_f32_16x16x128_f8f6f4 v[56:59], v[68:73], v[12:17], v[56:59] cbsz:2 blgp:2
	s_waitcnt vmcnt(25)
	v_mfma_f32_16x16x128_f8f6f4 v[56:59], v[62:67], v[6:11], v[56:59] cbsz:2 blgp:2
	s_waitcnt vmcnt(24)
	v_mfma_f32_16x16x128_f8f6f4 v[56:59], v[74:79], v[0:5], v[56:59] cbsz:2 blgp:2
	s_nop 7
	v_cndmask_b32_e64 v30, v56, v57, s[4:5]
	v_cndmask_b32_e64 v30, v30, v58, s[2:3]
	v_cndmask_b32_e32 v30, v30, v59, vcc
	v_mul_f32_e32 v31, v33, v30
	s_nop 1
	v_mov_b32_dpp v31, v31 quad_perm:[1,0,3,2] row_mask:0xf bank_mask:0xf bound_ctrl:1
	v_fmac_f32_e32 v31, v33, v30
	s_nop 1
	v_add_f32_dpp v30, v31, v31 quad_perm:[2,3,0,1] row_mask:0xf bank_mask:0xf bound_ctrl:1
	s_nop 1
	v_add_f32_dpp v30, v30, v30 row_half_mirror row_mask:0xf bank_mask:0xf bound_ctrl:1
	ds_write_b32 v32, v30 offset:49204
	ds_bpermute_b32 v30, v36, v128 offset:16
	s_waitcnt lgkmcnt(0)
	v_mul_lo_u32 v30, v30, s43
	v_add_u32_e32 v31, v30, v35
	v_add_u32_e32 v30, v30, v34
	buffer_load_dwordx4 v[56:59], v31, s[44:47], 0 offen nt
	buffer_load_dwordx4 v[62:65], v31, s[44:47], s20 offen nt
	buffer_load_dwordx4 v[68:71], v31, s[44:47], s21 offen nt
	buffer_load_dwordx4 v[74:77], v31, s[44:47], s23 offen nt
	buffer_load_dwordx2 v[60:61], v30, s[44:47], 0 offen nt
	buffer_load_dwordx2 v[72:73], v30, s[44:47], s33 offen nt
	buffer_load_dwordx2 v[66:67], v30, s[44:47], s21 offen nt
	buffer_load_dwordx2 v[78:79], v30, s[44:47], s94 offen nt
	s_waitcnt vmcnt(27)
	v_mfma_f32_16x16x128_f8f6f4 v[86:89], v[86:91], v[18:23], 0 cbsz:2 blgp:2
	s_waitcnt vmcnt(26)
	v_mfma_f32_16x16x128_f8f6f4 v[86:89], v[98:103], v[12:17], v[86:89] cbsz:2 blgp:2
	s_waitcnt vmcnt(25)
	v_mfma_f32_16x16x128_f8f6f4 v[86:89], v[92:97], v[6:11], v[86:89] cbsz:2 blgp:2
	s_waitcnt vmcnt(24)
	v_mfma_f32_16x16x128_f8f6f4 v[86:89], v[150:155], v[0:5], v[86:89] cbsz:2 blgp:2
	s_nop 7
	v_cndmask_b32_e64 v30, v86, v87, s[4:5]
	v_cndmask_b32_e64 v30, v30, v88, s[2:3]
	v_cndmask_b32_e32 v30, v30, v89, vcc
	v_mul_f32_e32 v31, v33, v30
	s_nop 1
	v_mov_b32_dpp v31, v31 quad_perm:[1,0,3,2] row_mask:0xf bank_mask:0xf bound_ctrl:1
	v_fmac_f32_e32 v31, v33, v30
	s_nop 1
	v_add_f32_dpp v30, v31, v31 quad_perm:[2,3,0,1] row_mask:0xf bank_mask:0xf bound_ctrl:1
	s_nop 1
	v_add_f32_dpp v30, v30, v30 row_half_mirror row_mask:0xf bank_mask:0xf bound_ctrl:1
	ds_write_b32 v32, v30 offset:49208
	ds_bpermute_b32 v30, v36, v128 offset:32
	s_waitcnt lgkmcnt(0)
	v_mul_lo_u32 v30, v30, s43
	v_add_u32_e32 v31, v30, v35
	v_add_u32_e32 v30, v30, v34
	buffer_load_dwordx4 v[86:89], v31, s[44:47], 0 offen nt
	buffer_load_dwordx4 v[92:95], v31, s[44:47], s20 offen nt
	buffer_load_dwordx4 v[98:101], v31, s[44:47], s21 offen nt
	buffer_load_dwordx4 v[150:153], v31, s[44:47], s23 offen nt
	buffer_load_dwordx2 v[90:91], v30, s[44:47], 0 offen nt
	buffer_load_dwordx2 v[102:103], v30, s[44:47], s33 offen nt
	buffer_load_dwordx2 v[96:97], v30, s[44:47], s21 offen nt
	buffer_load_dwordx2 v[154:155], v30, s[44:47], s94 offen nt
	s_waitcnt vmcnt(27)
	v_mfma_f32_16x16x128_f8f6f4 v[156:159], v[156:161], v[18:23], 0 cbsz:2 blgp:2
	s_waitcnt vmcnt(26)
	v_mfma_f32_16x16x128_f8f6f4 v[156:159], v[168:173], v[12:17], v[156:159] cbsz:2 blgp:2
	s_waitcnt vmcnt(25)
	v_mfma_f32_16x16x128_f8f6f4 v[156:159], v[162:167], v[6:11], v[156:159] cbsz:2 blgp:2
	s_waitcnt vmcnt(24)
	v_mfma_f32_16x16x128_f8f6f4 v[156:159], v[174:179], v[0:5], v[156:159] cbsz:2 blgp:2
	s_nop 7
	v_cndmask_b32_e64 v30, v156, v157, s[4:5]
	v_cndmask_b32_e64 v30, v30, v158, s[2:3]
	v_cndmask_b32_e32 v30, v30, v159, vcc
	v_mul_f32_e32 v31, v33, v30
	s_nop 1
	v_mov_b32_dpp v31, v31 quad_perm:[1,0,3,2] row_mask:0xf bank_mask:0xf bound_ctrl:1
	v_fmac_f32_e32 v31, v33, v30
	s_nop 1
	v_add_f32_dpp v30, v31, v31 quad_perm:[2,3,0,1] row_mask:0xf bank_mask:0xf bound_ctrl:1
	s_nop 1
	v_add_f32_dpp v30, v30, v30 row_half_mirror row_mask:0xf bank_mask:0xf bound_ctrl:1
	ds_write_b32 v32, v30 offset:49212
	ds_bpermute_b32 v30, v36, v128 offset:48
	s_waitcnt lgkmcnt(0)
	v_mul_lo_u32 v30, v30, s43
	v_add_u32_e32 v31, v30, v35
	v_add_u32_e32 v30, v30, v34
	buffer_load_dwordx4 v[156:159], v31, s[44:47], 0 offen nt
	buffer_load_dwordx4 v[162:165], v31, s[44:47], s20 offen nt
	buffer_load_dwordx4 v[168:171], v31, s[44:47], s21 offen nt
	buffer_load_dwordx4 v[174:177], v31, s[44:47], s23 offen nt
	buffer_load_dwordx2 v[160:161], v30, s[44:47], 0 offen nt
	buffer_load_dwordx2 v[172:173], v30, s[44:47], s33 offen nt
	buffer_load_dwordx2 v[166:167], v30, s[44:47], s21 offen nt
	buffer_load_dwordx2 v[178:179], v30, s[44:47], s94 offen nt
	s_waitcnt vmcnt(27)
	v_mfma_f32_16x16x128_f8f6f4 v[24:27], v[24:29], v[18:23], 0 cbsz:2 blgp:2
	s_waitcnt vmcnt(26)
	v_mfma_f32_16x16x128_f8f6f4 v[24:27], v[44:49], v[12:17], v[24:27] cbsz:2 blgp:2
	s_waitcnt vmcnt(25)
	v_mfma_f32_16x16x128_f8f6f4 v[24:27], v[38:43], v[6:11], v[24:27] cbsz:2 blgp:2
	s_waitcnt vmcnt(24)
	v_mfma_f32_16x16x128_f8f6f4 v[24:27], v[50:55], v[0:5], v[24:27] cbsz:2 blgp:2
	s_nop 7
	v_cndmask_b32_e64 v24, v24, v25, s[4:5]
	v_cndmask_b32_e64 v24, v24, v26, s[2:3]
	v_cndmask_b32_e32 v24, v24, v27, vcc
	v_mul_f32_e32 v25, v33, v24
	s_nop 1
	v_mov_b32_dpp v25, v25 quad_perm:[1,0,3,2] row_mask:0xf bank_mask:0xf bound_ctrl:1
	v_fmac_f32_e32 v25, v33, v24
	s_nop 1
	v_add_f32_dpp v24, v25, v25 quad_perm:[2,3,0,1] row_mask:0xf bank_mask:0xf bound_ctrl:1
	s_nop 1
	v_add_f32_dpp v24, v24, v24 row_half_mirror row_mask:0xf bank_mask:0xf bound_ctrl:1
	ds_write_b32 v32, v24 offset:49216
	ds_bpermute_b32 v24, v36, v128 offset:64
	s_waitcnt lgkmcnt(0)
	v_mul_lo_u32 v24, v24, s43
	v_add_u32_e32 v28, v24, v35
	v_add_u32_e32 v30, v24, v34
	buffer_load_dwordx4 v[24:27], v28, s[44:47], 0 offen nt
	buffer_load_dwordx4 v[38:41], v28, s[44:47], s20 offen nt
	buffer_load_dwordx4 v[44:47], v28, s[44:47], s21 offen nt
	buffer_load_dwordx4 v[50:53], v28, s[44:47], s23 offen nt
	s_nop 0
	buffer_load_dwordx2 v[28:29], v30, s[44:47], 0 offen nt
	buffer_load_dwordx2 v[48:49], v30, s[44:47], s33 offen nt
	buffer_load_dwordx2 v[42:43], v30, s[44:47], s21 offen nt
	buffer_load_dwordx2 v[54:55], v30, s[44:47], s94 offen nt
	s_waitcnt vmcnt(27)
	v_mfma_f32_16x16x128_f8f6f4 v[56:59], v[56:61], v[18:23], 0 cbsz:2 blgp:2
	s_waitcnt vmcnt(26)
	v_mfma_f32_16x16x128_f8f6f4 v[56:59], v[68:73], v[12:17], v[56:59] cbsz:2 blgp:2
	s_waitcnt vmcnt(25)
	v_mfma_f32_16x16x128_f8f6f4 v[56:59], v[62:67], v[6:11], v[56:59] cbsz:2 blgp:2
	s_waitcnt vmcnt(24)
	v_mfma_f32_16x16x128_f8f6f4 v[56:59], v[74:79], v[0:5], v[56:59] cbsz:2 blgp:2
	s_nop 7
	v_cndmask_b32_e64 v30, v56, v57, s[4:5]
	v_cndmask_b32_e64 v30, v30, v58, s[2:3]
	v_cndmask_b32_e32 v30, v30, v59, vcc
	v_mul_f32_e32 v31, v33, v30
	s_nop 1
	v_mov_b32_dpp v31, v31 quad_perm:[1,0,3,2] row_mask:0xf bank_mask:0xf bound_ctrl:1
	v_fmac_f32_e32 v31, v33, v30
	s_nop 1
	v_add_f32_dpp v30, v31, v31 quad_perm:[2,3,0,1] row_mask:0xf bank_mask:0xf bound_ctrl:1
	s_nop 1
	v_add_f32_dpp v30, v30, v30 row_half_mirror row_mask:0xf bank_mask:0xf bound_ctrl:1
	ds_write_b32 v32, v30 offset:49220
	ds_bpermute_b32 v30, v36, v128 offset:80
	s_waitcnt lgkmcnt(0)
	v_mul_lo_u32 v30, v30, s43
	v_add_u32_e32 v31, v30, v35
	v_add_u32_e32 v30, v30, v34
	buffer_load_dwordx4 v[56:59], v31, s[44:47], 0 offen nt
	buffer_load_dwordx4 v[62:65], v31, s[44:47], s20 offen nt
	buffer_load_dwordx4 v[68:71], v31, s[44:47], s21 offen nt
	buffer_load_dwordx4 v[74:77], v31, s[44:47], s23 offen nt
	buffer_load_dwordx2 v[60:61], v30, s[44:47], 0 offen nt
	buffer_load_dwordx2 v[72:73], v30, s[44:47], s33 offen nt
	buffer_load_dwordx2 v[66:67], v30, s[44:47], s21 offen nt
	buffer_load_dwordx2 v[78:79], v30, s[44:47], s94 offen nt
	s_waitcnt vmcnt(27)
	v_mfma_f32_16x16x128_f8f6f4 v[86:89], v[86:91], v[18:23], 0 cbsz:2 blgp:2
	s_waitcnt vmcnt(26)
	v_mfma_f32_16x16x128_f8f6f4 v[86:89], v[98:103], v[12:17], v[86:89] cbsz:2 blgp:2
	s_waitcnt vmcnt(25)
	v_mfma_f32_16x16x128_f8f6f4 v[86:89], v[92:97], v[6:11], v[86:89] cbsz:2 blgp:2
	s_waitcnt vmcnt(24)
	v_mfma_f32_16x16x128_f8f6f4 v[86:89], v[150:155], v[0:5], v[86:89] cbsz:2 blgp:2
	s_nop 7
	v_cndmask_b32_e64 v30, v86, v87, s[4:5]
	v_cndmask_b32_e64 v30, v30, v88, s[2:3]
	v_cndmask_b32_e32 v30, v30, v89, vcc
	v_mul_f32_e32 v31, v33, v30
	s_nop 1
	v_mov_b32_dpp v31, v31 quad_perm:[1,0,3,2] row_mask:0xf bank_mask:0xf bound_ctrl:1
	v_fmac_f32_e32 v31, v33, v30
	s_nop 1
	v_add_f32_dpp v30, v31, v31 quad_perm:[2,3,0,1] row_mask:0xf bank_mask:0xf bound_ctrl:1
	s_nop 1
	v_add_f32_dpp v30, v30, v30 row_half_mirror row_mask:0xf bank_mask:0xf bound_ctrl:1
	ds_write_b32 v32, v30 offset:49224
	ds_bpermute_b32 v30, v36, v128 offset:96
	s_waitcnt lgkmcnt(0)
	v_mul_lo_u32 v30, v30, s43
	v_add_u32_e32 v31, v30, v35
	v_add_u32_e32 v30, v30, v34
	buffer_load_dwordx4 v[86:89], v31, s[44:47], 0 offen nt
	buffer_load_dwordx4 v[92:95], v31, s[44:47], s20 offen nt
	buffer_load_dwordx4 v[98:101], v31, s[44:47], s21 offen nt
	buffer_load_dwordx4 v[150:153], v31, s[44:47], s23 offen nt
	buffer_load_dwordx2 v[90:91], v30, s[44:47], 0 offen nt
	buffer_load_dwordx2 v[102:103], v30, s[44:47], s33 offen nt
	buffer_load_dwordx2 v[96:97], v30, s[44:47], s21 offen nt
	buffer_load_dwordx2 v[154:155], v30, s[44:47], s94 offen nt
	s_waitcnt vmcnt(27)
	v_mfma_f32_16x16x128_f8f6f4 v[156:159], v[156:161], v[18:23], 0 cbsz:2 blgp:2
	s_waitcnt vmcnt(26)
	v_mfma_f32_16x16x128_f8f6f4 v[156:159], v[168:173], v[12:17], v[156:159] cbsz:2 blgp:2
	s_waitcnt vmcnt(25)
	v_mfma_f32_16x16x128_f8f6f4 v[156:159], v[162:167], v[6:11], v[156:159] cbsz:2 blgp:2
	s_waitcnt vmcnt(24)
	v_mfma_f32_16x16x128_f8f6f4 v[156:159], v[174:179], v[0:5], v[156:159] cbsz:2 blgp:2
	s_nop 7
	v_cndmask_b32_e64 v30, v156, v157, s[4:5]
	v_cndmask_b32_e64 v30, v30, v158, s[2:3]
	v_cndmask_b32_e32 v30, v30, v159, vcc
	v_mul_f32_e32 v31, v33, v30
	s_nop 1
	v_mov_b32_dpp v31, v31 quad_perm:[1,0,3,2] row_mask:0xf bank_mask:0xf bound_ctrl:1
	v_fmac_f32_e32 v31, v33, v30
	s_nop 1
	v_add_f32_dpp v30, v31, v31 quad_perm:[2,3,0,1] row_mask:0xf bank_mask:0xf bound_ctrl:1
	s_nop 1
	v_add_f32_dpp v30, v30, v30 row_half_mirror row_mask:0xf bank_mask:0xf bound_ctrl:1
	ds_write_b32 v32, v30 offset:49228
	ds_bpermute_b32 v30, v36, v128 offset:112
	s_waitcnt lgkmcnt(0)
	v_mul_lo_u32 v30, v30, s43
	v_add_u32_e32 v31, v30, v35
	v_add_u32_e32 v30, v30, v34
	buffer_load_dwordx4 v[156:159], v31, s[44:47], 0 offen nt
	buffer_load_dwordx4 v[162:165], v31, s[44:47], s20 offen nt
	buffer_load_dwordx4 v[168:171], v31, s[44:47], s21 offen nt
	buffer_load_dwordx4 v[174:177], v31, s[44:47], s23 offen nt
	buffer_load_dwordx2 v[160:161], v30, s[44:47], 0 offen nt
	buffer_load_dwordx2 v[172:173], v30, s[44:47], s33 offen nt
	buffer_load_dwordx2 v[166:167], v30, s[44:47], s21 offen nt
	buffer_load_dwordx2 v[178:179], v30, s[44:47], s94 offen nt
	s_waitcnt vmcnt(27)
	v_mfma_f32_16x16x128_f8f6f4 v[24:27], v[24:29], v[18:23], 0 cbsz:2 blgp:2
	s_waitcnt vmcnt(26)
	v_mfma_f32_16x16x128_f8f6f4 v[24:27], v[44:49], v[12:17], v[24:27] cbsz:2 blgp:2
	s_waitcnt vmcnt(25)
	v_mfma_f32_16x16x128_f8f6f4 v[24:27], v[38:43], v[6:11], v[24:27] cbsz:2 blgp:2
	s_waitcnt vmcnt(24)
	v_mfma_f32_16x16x128_f8f6f4 v[24:27], v[50:55], v[0:5], v[24:27] cbsz:2 blgp:2
	s_nop 7
	v_cndmask_b32_e64 v24, v24, v25, s[4:5]
	v_cndmask_b32_e64 v24, v24, v26, s[2:3]
	v_cndmask_b32_e32 v24, v24, v27, vcc
	v_mul_f32_e32 v25, v33, v24
	s_nop 1
	v_mov_b32_dpp v25, v25 quad_perm:[1,0,3,2] row_mask:0xf bank_mask:0xf bound_ctrl:1
	v_fmac_f32_e32 v25, v33, v24
	s_nop 1
	v_add_f32_dpp v24, v25, v25 quad_perm:[2,3,0,1] row_mask:0xf bank_mask:0xf bound_ctrl:1
	s_nop 1
	v_add_f32_dpp v24, v24, v24 row_half_mirror row_mask:0xf bank_mask:0xf bound_ctrl:1
	ds_write_b32 v32, v24 offset:49232
	ds_bpermute_b32 v24, v36, v128 offset:128
	s_waitcnt lgkmcnt(0)
	v_mul_lo_u32 v24, v24, s43
	v_add_u32_e32 v28, v24, v35
	v_add_u32_e32 v30, v24, v34
	buffer_load_dwordx4 v[24:27], v28, s[44:47], 0 offen nt
	buffer_load_dwordx4 v[38:41], v28, s[44:47], s20 offen nt
	buffer_load_dwordx4 v[44:47], v28, s[44:47], s21 offen nt
	buffer_load_dwordx4 v[50:53], v28, s[44:47], s23 offen nt
	s_nop 0
	buffer_load_dwordx2 v[28:29], v30, s[44:47], 0 offen nt
	buffer_load_dwordx2 v[48:49], v30, s[44:47], s33 offen nt
	buffer_load_dwordx2 v[42:43], v30, s[44:47], s21 offen nt
	buffer_load_dwordx2 v[54:55], v30, s[44:47], s94 offen nt
	s_waitcnt vmcnt(27)
	v_mfma_f32_16x16x128_f8f6f4 v[56:59], v[56:61], v[18:23], 0 cbsz:2 blgp:2
	s_waitcnt vmcnt(26)
	v_mfma_f32_16x16x128_f8f6f4 v[56:59], v[68:73], v[12:17], v[56:59] cbsz:2 blgp:2
	s_waitcnt vmcnt(25)
	v_mfma_f32_16x16x128_f8f6f4 v[56:59], v[62:67], v[6:11], v[56:59] cbsz:2 blgp:2
	s_waitcnt vmcnt(24)
	v_mfma_f32_16x16x128_f8f6f4 v[56:59], v[74:79], v[0:5], v[56:59] cbsz:2 blgp:2
	s_nop 7
	v_cndmask_b32_e64 v30, v56, v57, s[4:5]
	v_cndmask_b32_e64 v30, v30, v58, s[2:3]
	v_cndmask_b32_e32 v30, v30, v59, vcc
	v_mul_f32_e32 v31, v33, v30
	s_nop 1
	v_mov_b32_dpp v31, v31 quad_perm:[1,0,3,2] row_mask:0xf bank_mask:0xf bound_ctrl:1
	v_fmac_f32_e32 v31, v33, v30
	s_nop 1
	v_add_f32_dpp v30, v31, v31 quad_perm:[2,3,0,1] row_mask:0xf bank_mask:0xf bound_ctrl:1
	s_nop 1
	v_add_f32_dpp v30, v30, v30 row_half_mirror row_mask:0xf bank_mask:0xf bound_ctrl:1
	ds_write_b32 v32, v30 offset:49236
	ds_bpermute_b32 v30, v36, v128 offset:144
	s_waitcnt lgkmcnt(0)
	v_mul_lo_u32 v30, v30, s43
	v_add_u32_e32 v31, v30, v35
	v_add_u32_e32 v30, v30, v34
	buffer_load_dwordx4 v[56:59], v31, s[44:47], 0 offen nt
	buffer_load_dwordx4 v[62:65], v31, s[44:47], s20 offen nt
	buffer_load_dwordx4 v[68:71], v31, s[44:47], s21 offen nt
	buffer_load_dwordx4 v[74:77], v31, s[44:47], s23 offen nt
	buffer_load_dwordx2 v[60:61], v30, s[44:47], 0 offen nt
	buffer_load_dwordx2 v[72:73], v30, s[44:47], s33 offen nt
	buffer_load_dwordx2 v[66:67], v30, s[44:47], s21 offen nt
	buffer_load_dwordx2 v[78:79], v30, s[44:47], s94 offen nt
	s_waitcnt vmcnt(27)
	v_mfma_f32_16x16x128_f8f6f4 v[86:89], v[86:91], v[18:23], 0 cbsz:2 blgp:2
	s_waitcnt vmcnt(26)
	v_mfma_f32_16x16x128_f8f6f4 v[86:89], v[98:103], v[12:17], v[86:89] cbsz:2 blgp:2
	s_waitcnt vmcnt(25)
	v_mfma_f32_16x16x128_f8f6f4 v[86:89], v[92:97], v[6:11], v[86:89] cbsz:2 blgp:2
	s_waitcnt vmcnt(24)
	v_mfma_f32_16x16x128_f8f6f4 v[86:89], v[150:155], v[0:5], v[86:89] cbsz:2 blgp:2
	s_nop 7
	v_cndmask_b32_e64 v30, v86, v87, s[4:5]
	v_cndmask_b32_e64 v30, v30, v88, s[2:3]
	v_cndmask_b32_e32 v30, v30, v89, vcc
	v_mul_f32_e32 v31, v33, v30
	s_nop 1
	v_mov_b32_dpp v31, v31 quad_perm:[1,0,3,2] row_mask:0xf bank_mask:0xf bound_ctrl:1
	v_fmac_f32_e32 v31, v33, v30
	s_nop 1
	v_add_f32_dpp v30, v31, v31 quad_perm:[2,3,0,1] row_mask:0xf bank_mask:0xf bound_ctrl:1
	s_nop 1
	v_add_f32_dpp v30, v30, v30 row_half_mirror row_mask:0xf bank_mask:0xf bound_ctrl:1
	ds_write_b32 v32, v30 offset:49240
	ds_bpermute_b32 v30, v36, v128 offset:160
	s_waitcnt lgkmcnt(0)
	v_mul_lo_u32 v30, v30, s43
	v_add_u32_e32 v31, v30, v35
	v_add_u32_e32 v30, v30, v34
	buffer_load_dwordx4 v[86:89], v31, s[44:47], 0 offen nt
	buffer_load_dwordx4 v[92:95], v31, s[44:47], s20 offen nt
	buffer_load_dwordx4 v[98:101], v31, s[44:47], s21 offen nt
	buffer_load_dwordx4 v[150:153], v31, s[44:47], s23 offen nt
	buffer_load_dwordx2 v[90:91], v30, s[44:47], 0 offen nt
	buffer_load_dwordx2 v[102:103], v30, s[44:47], s33 offen nt
	buffer_load_dwordx2 v[96:97], v30, s[44:47], s21 offen nt
	buffer_load_dwordx2 v[154:155], v30, s[44:47], s94 offen nt
	s_waitcnt vmcnt(27)
	v_mfma_f32_16x16x128_f8f6f4 v[156:159], v[156:161], v[18:23], 0 cbsz:2 blgp:2
	s_waitcnt vmcnt(26)
	v_mfma_f32_16x16x128_f8f6f4 v[156:159], v[168:173], v[12:17], v[156:159] cbsz:2 blgp:2
	s_waitcnt vmcnt(25)
	v_mfma_f32_16x16x128_f8f6f4 v[156:159], v[162:167], v[6:11], v[156:159] cbsz:2 blgp:2
	s_waitcnt vmcnt(24)
	v_mfma_f32_16x16x128_f8f6f4 v[156:159], v[174:179], v[0:5], v[156:159] cbsz:2 blgp:2
	s_nop 7
	v_cndmask_b32_e64 v30, v156, v157, s[4:5]
	v_cndmask_b32_e64 v30, v30, v158, s[2:3]
	v_cndmask_b32_e32 v30, v30, v159, vcc
	v_mul_f32_e32 v31, v33, v30
	s_nop 1
	v_mov_b32_dpp v31, v31 quad_perm:[1,0,3,2] row_mask:0xf bank_mask:0xf bound_ctrl:1
	v_fmac_f32_e32 v31, v33, v30
	s_nop 1
	v_add_f32_dpp v30, v31, v31 quad_perm:[2,3,0,1] row_mask:0xf bank_mask:0xf bound_ctrl:1
	s_nop 1
	v_add_f32_dpp v30, v30, v30 row_half_mirror row_mask:0xf bank_mask:0xf bound_ctrl:1
	ds_write_b32 v32, v30 offset:49244
	ds_bpermute_b32 v30, v36, v128 offset:176
	s_waitcnt lgkmcnt(0)
	v_mul_lo_u32 v30, v30, s43
	v_add_u32_e32 v31, v30, v35
	v_add_u32_e32 v30, v30, v34
	buffer_load_dwordx4 v[156:159], v31, s[44:47], 0 offen nt
	buffer_load_dwordx4 v[162:165], v31, s[44:47], s20 offen nt
	buffer_load_dwordx4 v[168:171], v31, s[44:47], s21 offen nt
	buffer_load_dwordx4 v[174:177], v31, s[44:47], s23 offen nt
	buffer_load_dwordx2 v[160:161], v30, s[44:47], 0 offen nt
	buffer_load_dwordx2 v[172:173], v30, s[44:47], s33 offen nt
	buffer_load_dwordx2 v[166:167], v30, s[44:47], s21 offen nt
	buffer_load_dwordx2 v[178:179], v30, s[44:47], s94 offen nt
	s_waitcnt vmcnt(27)
	v_mfma_f32_16x16x128_f8f6f4 v[24:27], v[24:29], v[18:23], 0 cbsz:2 blgp:2
	s_waitcnt vmcnt(26)
	v_mfma_f32_16x16x128_f8f6f4 v[24:27], v[44:49], v[12:17], v[24:27] cbsz:2 blgp:2
	s_waitcnt vmcnt(25)
	v_mfma_f32_16x16x128_f8f6f4 v[24:27], v[38:43], v[6:11], v[24:27] cbsz:2 blgp:2
	s_waitcnt vmcnt(24)
	v_mfma_f32_16x16x128_f8f6f4 v[24:27], v[50:55], v[0:5], v[24:27] cbsz:2 blgp:2
	s_nop 7
	v_cndmask_b32_e64 v24, v24, v25, s[4:5]
	v_cndmask_b32_e64 v24, v24, v26, s[2:3]
	v_cndmask_b32_e32 v24, v24, v27, vcc
	v_mul_f32_e32 v25, v33, v24
	s_nop 1
	v_mov_b32_dpp v25, v25 quad_perm:[1,0,3,2] row_mask:0xf bank_mask:0xf bound_ctrl:1
	v_fmac_f32_e32 v25, v33, v24
	s_nop 1
	v_add_f32_dpp v24, v25, v25 quad_perm:[2,3,0,1] row_mask:0xf bank_mask:0xf bound_ctrl:1
	s_nop 1
	v_add_f32_dpp v24, v24, v24 row_half_mirror row_mask:0xf bank_mask:0xf bound_ctrl:1
	ds_write_b32 v32, v24 offset:49248
	ds_bpermute_b32 v24, v36, v128 offset:192
	s_waitcnt lgkmcnt(0)
	v_mul_lo_u32 v24, v24, s43
	v_add_u32_e32 v28, v24, v35
	v_add_u32_e32 v30, v24, v34
	buffer_load_dwordx4 v[24:27], v28, s[44:47], 0 offen nt
	buffer_load_dwordx4 v[38:41], v28, s[44:47], s20 offen nt
	buffer_load_dwordx4 v[44:47], v28, s[44:47], s21 offen nt
	buffer_load_dwordx4 v[50:53], v28, s[44:47], s23 offen nt
	s_nop 0
	buffer_load_dwordx2 v[28:29], v30, s[44:47], 0 offen nt
	buffer_load_dwordx2 v[48:49], v30, s[44:47], s33 offen nt
	buffer_load_dwordx2 v[42:43], v30, s[44:47], s21 offen nt
	buffer_load_dwordx2 v[54:55], v30, s[44:47], s94 offen nt
	s_waitcnt vmcnt(27)
	v_mfma_f32_16x16x128_f8f6f4 v[56:59], v[56:61], v[18:23], 0 cbsz:2 blgp:2
	s_waitcnt vmcnt(26)
	v_mfma_f32_16x16x128_f8f6f4 v[56:59], v[68:73], v[12:17], v[56:59] cbsz:2 blgp:2
	s_waitcnt vmcnt(25)
	v_mfma_f32_16x16x128_f8f6f4 v[56:59], v[62:67], v[6:11], v[56:59] cbsz:2 blgp:2
	s_waitcnt vmcnt(24)
	v_mfma_f32_16x16x128_f8f6f4 v[56:59], v[74:79], v[0:5], v[56:59] cbsz:2 blgp:2
	s_nop 7
	v_cndmask_b32_e64 v30, v56, v57, s[4:5]
	v_cndmask_b32_e64 v30, v30, v58, s[2:3]
	v_cndmask_b32_e32 v30, v30, v59, vcc
	v_mul_f32_e32 v31, v33, v30
	s_nop 1
	v_mov_b32_dpp v31, v31 quad_perm:[1,0,3,2] row_mask:0xf bank_mask:0xf bound_ctrl:1
	v_fmac_f32_e32 v31, v33, v30
	s_nop 1
	v_add_f32_dpp v30, v31, v31 quad_perm:[2,3,0,1] row_mask:0xf bank_mask:0xf bound_ctrl:1
	s_nop 1
	v_add_f32_dpp v30, v30, v30 row_half_mirror row_mask:0xf bank_mask:0xf bound_ctrl:1
	ds_write_b32 v32, v30 offset:49252
	ds_bpermute_b32 v30, v36, v128 offset:208
	s_waitcnt lgkmcnt(0)
	v_mul_lo_u32 v30, v30, s43
	v_add_u32_e32 v31, v30, v35
	v_add_u32_e32 v30, v30, v34
	buffer_load_dwordx4 v[56:59], v31, s[44:47], 0 offen nt
	buffer_load_dwordx4 v[62:65], v31, s[44:47], s20 offen nt
	buffer_load_dwordx4 v[68:71], v31, s[44:47], s21 offen nt
	buffer_load_dwordx4 v[74:77], v31, s[44:47], s23 offen nt
	buffer_load_dwordx2 v[60:61], v30, s[44:47], 0 offen nt
	buffer_load_dwordx2 v[72:73], v30, s[44:47], s33 offen nt
	buffer_load_dwordx2 v[66:67], v30, s[44:47], s21 offen nt
	buffer_load_dwordx2 v[78:79], v30, s[44:47], s94 offen nt
	s_waitcnt vmcnt(27)
	v_mfma_f32_16x16x128_f8f6f4 v[86:89], v[86:91], v[18:23], 0 cbsz:2 blgp:2
	s_waitcnt vmcnt(26)
	v_mfma_f32_16x16x128_f8f6f4 v[86:89], v[98:103], v[12:17], v[86:89] cbsz:2 blgp:2
	s_waitcnt vmcnt(25)
	v_mfma_f32_16x16x128_f8f6f4 v[86:89], v[92:97], v[6:11], v[86:89] cbsz:2 blgp:2
	s_waitcnt vmcnt(24)
	v_mfma_f32_16x16x128_f8f6f4 v[86:89], v[150:155], v[0:5], v[86:89] cbsz:2 blgp:2
	s_nop 7
	v_cndmask_b32_e64 v30, v86, v87, s[4:5]
	v_cndmask_b32_e64 v30, v30, v88, s[2:3]
	v_cndmask_b32_e32 v30, v30, v89, vcc
	v_mul_f32_e32 v31, v33, v30
	s_nop 1
	v_mov_b32_dpp v31, v31 quad_perm:[1,0,3,2] row_mask:0xf bank_mask:0xf bound_ctrl:1
	v_fmac_f32_e32 v31, v33, v30
	s_nop 1
	v_add_f32_dpp v30, v31, v31 quad_perm:[2,3,0,1] row_mask:0xf bank_mask:0xf bound_ctrl:1
	s_nop 1
	v_add_f32_dpp v30, v30, v30 row_half_mirror row_mask:0xf bank_mask:0xf bound_ctrl:1
	ds_write_b32 v32, v30 offset:49256
	ds_bpermute_b32 v30, v36, v128 offset:224
	s_waitcnt lgkmcnt(0)
	v_mul_lo_u32 v30, v30, s43
	v_add_u32_e32 v31, v30, v35
	v_add_u32_e32 v30, v30, v34
	buffer_load_dwordx4 v[86:89], v31, s[44:47], 0 offen nt
	buffer_load_dwordx4 v[92:95], v31, s[44:47], s20 offen nt
	buffer_load_dwordx4 v[98:101], v31, s[44:47], s21 offen nt
	buffer_load_dwordx4 v[150:153], v31, s[44:47], s23 offen nt
	buffer_load_dwordx2 v[90:91], v30, s[44:47], 0 offen nt
	buffer_load_dwordx2 v[102:103], v30, s[44:47], s33 offen nt
	buffer_load_dwordx2 v[96:97], v30, s[44:47], s21 offen nt
	buffer_load_dwordx2 v[154:155], v30, s[44:47], s94 offen nt
	s_waitcnt vmcnt(27)
	v_mfma_f32_16x16x128_f8f6f4 v[156:159], v[156:161], v[18:23], 0 cbsz:2 blgp:2
	s_waitcnt vmcnt(26)
	v_mfma_f32_16x16x128_f8f6f4 v[156:159], v[168:173], v[12:17], v[156:159] cbsz:2 blgp:2
	s_waitcnt vmcnt(25)
	v_mfma_f32_16x16x128_f8f6f4 v[156:159], v[162:167], v[6:11], v[156:159] cbsz:2 blgp:2
	s_waitcnt vmcnt(24)
	v_mfma_f32_16x16x128_f8f6f4 v[156:159], v[174:179], v[0:5], v[156:159] cbsz:2 blgp:2
	s_nop 7
	v_cndmask_b32_e64 v30, v156, v157, s[4:5]
	v_cndmask_b32_e64 v30, v30, v158, s[2:3]
	v_cndmask_b32_e32 v30, v30, v159, vcc
	v_mul_f32_e32 v31, v33, v30
	s_nop 1
	v_mov_b32_dpp v31, v31 quad_perm:[1,0,3,2] row_mask:0xf bank_mask:0xf bound_ctrl:1
	v_fmac_f32_e32 v31, v33, v30
	s_nop 1
	v_add_f32_dpp v30, v31, v31 quad_perm:[2,3,0,1] row_mask:0xf bank_mask:0xf bound_ctrl:1
	s_nop 1
	v_add_f32_dpp v30, v30, v30 row_half_mirror row_mask:0xf bank_mask:0xf bound_ctrl:1
	ds_write_b32 v32, v30 offset:49260
	ds_bpermute_b32 v30, v36, v128 offset:240
	s_waitcnt lgkmcnt(0)
	v_mul_lo_u32 v30, v30, s43
	v_add_u32_e32 v31, v30, v35
	v_add_u32_e32 v30, v30, v34
	buffer_load_dwordx4 v[156:159], v31, s[44:47], 0 offen nt
	buffer_load_dwordx4 v[162:165], v31, s[44:47], s20 offen nt
	buffer_load_dwordx4 v[168:171], v31, s[44:47], s21 offen nt
	buffer_load_dwordx4 v[174:177], v31, s[44:47], s23 offen nt
	buffer_load_dwordx2 v[160:161], v30, s[44:47], 0 offen nt
	buffer_load_dwordx2 v[172:173], v30, s[44:47], s33 offen nt
	buffer_load_dwordx2 v[166:167], v30, s[44:47], s21 offen nt
	buffer_load_dwordx2 v[178:179], v30, s[44:47], s94 offen nt
	s_waitcnt vmcnt(27)
	v_mfma_f32_16x16x128_f8f6f4 v[24:27], v[24:29], v[18:23], 0 cbsz:2 blgp:2
	s_waitcnt vmcnt(26)
	v_mfma_f32_16x16x128_f8f6f4 v[24:27], v[44:49], v[12:17], v[24:27] cbsz:2 blgp:2
	s_waitcnt vmcnt(25)
	v_mfma_f32_16x16x128_f8f6f4 v[24:27], v[38:43], v[6:11], v[24:27] cbsz:2 blgp:2
	s_waitcnt vmcnt(24)
	v_mfma_f32_16x16x128_f8f6f4 v[24:27], v[50:55], v[0:5], v[24:27] cbsz:2 blgp:2
	s_nop 7
	v_cndmask_b32_e64 v24, v24, v25, s[4:5]
	v_cndmask_b32_e64 v24, v24, v26, s[2:3]
	v_cndmask_b32_e32 v24, v24, v27, vcc
	v_mul_f32_e32 v25, v33, v24
	s_nop 1
	v_mov_b32_dpp v25, v25 quad_perm:[1,0,3,2] row_mask:0xf bank_mask:0xf bound_ctrl:1
	v_fmac_f32_e32 v25, v33, v24
	s_nop 1
	v_add_f32_dpp v24, v25, v25 quad_perm:[2,3,0,1] row_mask:0xf bank_mask:0xf bound_ctrl:1
	s_nop 1
	v_add_f32_dpp v24, v24, v24 row_half_mirror row_mask:0xf bank_mask:0xf bound_ctrl:1
	ds_write_b32 v32, v24 offset:49264
	s_waitcnt vmcnt(19)
	v_mfma_f32_16x16x128_f8f6f4 v[24:27], v[56:61], v[18:23], 0 cbsz:2 blgp:2
	s_waitcnt vmcnt(18)
	v_mfma_f32_16x16x128_f8f6f4 v[24:27], v[68:73], v[12:17], v[24:27] cbsz:2 blgp:2
	s_waitcnt vmcnt(17)
	v_mfma_f32_16x16x128_f8f6f4 v[24:27], v[62:67], v[6:11], v[24:27] cbsz:2 blgp:2
	s_waitcnt vmcnt(16)
	v_mfma_f32_16x16x128_f8f6f4 v[24:27], v[74:79], v[0:5], v[24:27] cbsz:2 blgp:2
	s_nop 7
	v_cndmask_b32_e64 v24, v24, v25, s[4:5]
	v_cndmask_b32_e64 v24, v24, v26, s[2:3]
	v_cndmask_b32_e32 v24, v24, v27, vcc
	v_mul_f32_e32 v25, v33, v24
	s_nop 1
	v_mov_b32_dpp v25, v25 quad_perm:[1,0,3,2] row_mask:0xf bank_mask:0xf bound_ctrl:1
	v_fmac_f32_e32 v25, v33, v24
	s_nop 1
	v_add_f32_dpp v24, v25, v25 quad_perm:[2,3,0,1] row_mask:0xf bank_mask:0xf bound_ctrl:1
	s_nop 1
	v_add_f32_dpp v24, v24, v24 row_half_mirror row_mask:0xf bank_mask:0xf bound_ctrl:1
	ds_write_b32 v32, v24 offset:49268
	s_waitcnt vmcnt(11)
	v_mfma_f32_16x16x128_f8f6f4 v[24:27], v[86:91], v[18:23], 0 cbsz:2 blgp:2
	s_waitcnt vmcnt(10)
	v_mfma_f32_16x16x128_f8f6f4 v[24:27], v[98:103], v[12:17], v[24:27] cbsz:2 blgp:2
	s_waitcnt vmcnt(9)
	v_mfma_f32_16x16x128_f8f6f4 v[24:27], v[92:97], v[6:11], v[24:27] cbsz:2 blgp:2
	s_waitcnt vmcnt(8)
	v_mfma_f32_16x16x128_f8f6f4 v[24:27], v[150:155], v[0:5], v[24:27] cbsz:2 blgp:2
	s_nop 7
	v_cndmask_b32_e64 v24, v24, v25, s[4:5]
	v_cndmask_b32_e64 v24, v24, v26, s[2:3]
	v_cndmask_b32_e32 v24, v24, v27, vcc
	v_mul_f32_e32 v25, v33, v24
	s_nop 1
	v_mov_b32_dpp v25, v25 quad_perm:[1,0,3,2] row_mask:0xf bank_mask:0xf bound_ctrl:1
	v_fmac_f32_e32 v25, v33, v24
	s_nop 1
	v_add_f32_dpp v24, v25, v25 quad_perm:[2,3,0,1] row_mask:0xf bank_mask:0xf bound_ctrl:1
	s_nop 1
	v_add_f32_dpp v24, v24, v24 row_half_mirror row_mask:0xf bank_mask:0xf bound_ctrl:1
	ds_write_b32 v32, v24 offset:49272
	s_waitcnt vmcnt(3)
	v_mfma_f32_16x16x128_f8f6f4 v[18:21], v[156:161], v[18:23], 0 cbsz:2 blgp:2
	s_waitcnt vmcnt(2)
	v_mfma_f32_16x16x128_f8f6f4 v[12:15], v[168:173], v[12:17], v[18:21] cbsz:2 blgp:2
	s_waitcnt vmcnt(1)
	v_mfma_f32_16x16x128_f8f6f4 v[6:9], v[162:167], v[6:11], v[12:15] cbsz:2 blgp:2
	s_waitcnt vmcnt(0)
	v_mfma_f32_16x16x128_f8f6f4 v[0:3], v[174:179], v[0:5], v[6:9] cbsz:2 blgp:2
	s_nop 7
	v_cndmask_b32_e64 v0, v0, v1, s[4:5]
	v_cndmask_b32_e64 v0, v0, v2, s[2:3]
	v_cndmask_b32_e32 v0, v0, v3, vcc
	v_mul_f32_e32 v1, v33, v0
	s_nop 1
	v_mov_b32_dpp v1, v1 quad_perm:[1,0,3,2] row_mask:0xf bank_mask:0xf bound_ctrl:1
	v_fmac_f32_e32 v1, v33, v0
	s_nop 1
	v_add_f32_dpp v0, v1, v1 quad_perm:[2,3,0,1] row_mask:0xf bank_mask:0xf bound_ctrl:1
	s_nop 1
	v_add_f32_dpp v0, v0, v0 row_half_mirror row_mask:0xf bank_mask:0xf bound_ctrl:1
	ds_write_b32 v32, v0 offset:49276
	v_mul_u32_u24_e32 v240, 0x600, v130
	v_mul_u32_u24_e32 v241, 0x600, v128
	v_add_u32_e32 v240, 0x8000000, v240
	v_add_u32_e32 v241, 0x8000000, v241
	v_lshrrev_b32_e32 v0, 1, v129
	v_readlane_b32 s100, v240, 0
	v_readlane_b32 s101, v240, 1
	v_readlane_b32 s2, v240, 2
	v_readlane_b32 s3, v240, 3
	s_nop 1
	buffer_load_dwordx4 v[74:77], v129, s[44:47], s100 offen nt
	buffer_load_dwordx2 v[78:79], v0, s[44:47], s100 offen offset:1024 nt
	buffer_load_dwordx4 v[68:71], v129, s[44:47], s101 offen nt
	buffer_load_dwordx2 v[72:73], v0, s[44:47], s101 offen offset:1024 nt
	buffer_load_dwordx4 v[56:59], v129, s[44:47], s2 offen nt
	buffer_load_dwordx2 v[60:61], v0, s[44:47], s2 offen offset:1024 nt
	buffer_load_dwordx4 v[44:47], v129, s[44:47], s3 offen nt
	buffer_load_dwordx2 v[48:49], v0, s[44:47], s3 offen offset:1024 nt
	v_add_u32_e32 v210, 0x400, v0
	v_readlane_b32 s100, v240, 4
	v_readlane_b32 s101, v240, 5
	v_readlane_b32 s2, v240, 6
	v_readlane_b32 s3, v240, 7
	s_nop 1
	buffer_load_dwordx4 v[62:65], v129, s[44:47], s100 offen nt
	buffer_load_dwordx2 v[66:67], v0, s[44:47], s100 offen offset:1024 nt
	buffer_load_dwordx4 v[50:53], v129, s[44:47], s101 offen nt
	buffer_load_dwordx2 v[54:55], v0, s[44:47], s101 offen offset:1024 nt
	buffer_load_dwordx4 v[38:41], v129, s[44:47], s2 offen nt
	buffer_load_dwordx2 v[42:43], v0, s[44:47], s2 offen offset:1024 nt
	buffer_load_dwordx4 v[32:35], v129, s[44:47], s3 offen nt
	buffer_load_dwordx2 v[36:37], v0, s[44:47], s3 offen offset:1024 nt
	v_div_scale_f32 v2, s[2:3], v80, v80, 1.0
	v_rcp_f32_e32 v3, v2
	v_div_scale_f32 v4, vcc, 1.0, v80, 1.0
	v_and_b32_e32 v1, -4, v148
	v_fma_f32 v0, -v2, v3, 1.0
	v_fmac_f32_e32 v3, v0, v3
	v_mul_f32_e32 v5, v4, v3
	v_fma_f32 v0, -v2, v5, v4
	v_fmac_f32_e32 v5, v0, v3
	v_lshlrev_b32_e32 v0, 7, v148
	v_and_b32_e32 v0, 0x180, v0
	v_add3_u32 v0, v111, v0, v1
	v_add_u32_e32 v0, 0xc000, v0
	ds_read2_b32 v[0:1], v0 offset1:16
	v_fma_f32 v2, -v2, v5, v4
	v_div_fmas_f32 v2, v2, v3, v5
	v_div_fixup_f32 v2, v2, v80, 1.0
	s_mov_b32 s1, 0x3e6d3388
	s_waitcnt lgkmcnt(0)
	v_mul_f32_e32 v0, v2, v0
	v_mul_f32_e32 v0, v83, v0
	v_fma_f32 v3, |v0|, s1, 1.0
	v_rcp_f32_e32 v3, v3
	v_mul_f32_e32 v5, v0, v0
	v_mul_f32_e32 v5, 0xbf38aa3b, v5
	v_exp_f32_e32 v5, v5
	v_fmamk_f32 v4, v3, 0x3f07dc22, v184
	v_fmaak_f32 v4, v3, v4, 0x3f35f0e3
	v_fmaak_f32 v4, v3, v4, 0xbe11a98e
	v_mul_f32_e32 v1, v2, v1
	v_fmaak_f32 v4, v3, v4, 0x3e027906
	v_mul_f32_e32 v3, v3, v4
	v_mul_f32_e32 v1, v82, v1
	v_mul_f32_e32 v3, v5, v3
	v_fma_f32 v5, |v1|, s1, 1.0
	v_rcp_f32_e32 v5, v5
	v_mul_f32_e32 v4, v0, v3
	v_fma_f32 v3, -v0, v3, v0
	v_cmp_gt_f32_e32 vcc, 0, v0
	v_mul_f32_e32 v2, v206, v84
	v_mov_b32_e32 v180, 0
	v_cndmask_b32_e32 v0, v3, v4, vcc
	v_mul_f32_e32 v211, v2, v0
	v_mul_f32_e32 v2, v1, v1
	v_fmamk_f32 v0, v5, 0x3f07dc22, v184
	v_mul_f32_e32 v2, 0xbf38aa3b, v2
	v_fmaak_f32 v0, v5, v0, 0x3f35f0e3
	v_exp_f32_e32 v2, v2
	v_fmaak_f32 v0, v5, v0, 0xbe11a98e
	v_fmaak_f32 v0, v5, v0, 0x3e027906
	v_mul_f32_e32 v0, v5, v0
	v_mul_f32_e32 v0, v2, v0
	v_mul_f32_e32 v2, v1, v0
	v_fma_f32 v0, -v1, v0, v1
	v_cmp_gt_f32_e32 vcc, 0, v1
	v_mul_f32_e32 v1, v205, v81
	v_mov_b32_e32 v181, v180
	v_cndmask_b32_e32 v0, v0, v2, vcc
	v_mul_f32_e32 v131, v1, v0
	v_mov_b32_e32 v178, v180
	v_mov_b32_e32 v179, v180
	v_mov_b32_e32 v176, v180
	v_mov_b32_e32 v177, v180
	v_mov_b32_e32 v174, v180
	v_mov_b32_e32 v175, v180
	v_mov_b32_e32 v172, v180
	v_mov_b32_e32 v173, v180
	v_mov_b32_e32 v170, v180
	v_mov_b32_e32 v171, v180
	v_mov_b32_e32 v168, v180
	v_mov_b32_e32 v169, v180
	v_mov_b32_e32 v166, v180
	v_mov_b32_e32 v167, v180
	v_mov_b32_e32 v164, v180
	v_mov_b32_e32 v165, v180
	v_mov_b32_e32 v162, v180
	v_mov_b32_e32 v163, v180
	v_mov_b32_e32 v160, v180
	v_mov_b32_e32 v161, v180
	v_mov_b32_e32 v158, v180
	v_mov_b32_e32 v159, v180
	v_mov_b32_e32 v156, v180
	v_mov_b32_e32 v157, v180
	v_mov_b32_e32 v154, v180
	v_mov_b32_e32 v155, v180
	v_mov_b32_e32 v152, v180
	v_mov_b32_e32 v153, v180
	v_mov_b32_e32 v150, v180
	v_mov_b32_e32 v151, v180
	v_readlane_b32 s2, v240, 8
	v_readlane_b32 s3, v240, 9
	v_readlane_b32 s100, v240, 10
	v_readlane_b32 s101, v240, 11
	s_nop 1
	buffer_load_dwordx4 v[98:101], v129, s[44:47], s2 offen nt
	buffer_load_dwordx2 v[102:103], v210, s[44:47], s2 offen nt
	buffer_load_dwordx4 v[92:95], v129, s[44:47], s3 offen nt
	buffer_load_dwordx2 v[96:97], v210, s[44:47], s3 offen nt
	buffer_load_dwordx4 v[86:89], v129, s[44:47], s100 offen nt
	buffer_load_dwordx2 v[90:91], v210, s[44:47], s100 offen nt
	buffer_load_dwordx4 v[80:83], v129, s[44:47], s101 offen nt
	buffer_load_dwordx2 v[84:85], v210, s[44:47], s101 offen nt
	v_readlane_b32 s2, v211, 0
	s_waitcnt vmcnt(22)
	v_cvt_scalef32_pk32_f32_fp6 v[0:31], v[74:79], 1.0
	v_pk_fma_f32 v[74:75], v[0:1], s[2:3], v[180:181] op_sel_hi:[1,0,1]
	v_pk_fma_f32 v[76:77], v[2:3], s[2:3], v[178:179] op_sel_hi:[1,0,1]
	v_pk_fma_f32 v[78:79], v[4:5], s[2:3], v[176:177] op_sel_hi:[1,0,1]
	v_pk_fma_f32 v[174:175], v[6:7], s[2:3], v[174:175] op_sel_hi:[1,0,1]
	v_pk_fma_f32 v[172:173], v[8:9], s[2:3], v[172:173] op_sel_hi:[1,0,1]
	v_pk_fma_f32 v[170:171], v[10:11], s[2:3], v[170:171] op_sel_hi:[1,0,1]
	v_pk_fma_f32 v[168:169], v[12:13], s[2:3], v[168:169] op_sel_hi:[1,0,1]
	v_pk_fma_f32 v[166:167], v[14:15], s[2:3], v[166:167] op_sel_hi:[1,0,1]
	v_pk_fma_f32 v[164:165], v[16:17], s[2:3], v[164:165] op_sel_hi:[1,0,1]
	v_pk_fma_f32 v[162:163], v[18:19], s[2:3], v[162:163] op_sel_hi:[1,0,1]
	v_pk_fma_f32 v[160:161], v[20:21], s[2:3], v[160:161] op_sel_hi:[1,0,1]
	v_pk_fma_f32 v[158:159], v[22:23], s[2:3], v[158:159] op_sel_hi:[1,0,1]
	v_pk_fma_f32 v[156:157], v[24:25], s[2:3], v[156:157] op_sel_hi:[1,0,1]
	v_pk_fma_f32 v[154:155], v[26:27], s[2:3], v[154:155] op_sel_hi:[1,0,1]
	v_pk_fma_f32 v[152:153], v[28:29], s[2:3], v[152:153] op_sel_hi:[1,0,1]
	v_pk_fma_f32 v[150:151], v[30:31], s[2:3], v[150:151] op_sel_hi:[1,0,1]
	v_readlane_b32 s2, v211, 1
	s_waitcnt vmcnt(20)
	v_cvt_scalef32_pk32_f32_fp6 v[0:31], v[68:73], 1.0
	v_pk_fma_f32 v[68:69], v[0:1], s[2:3], v[74:75] op_sel_hi:[1,0,1]
	v_pk_fma_f32 v[70:71], v[2:3], s[2:3], v[76:77] op_sel_hi:[1,0,1]
	v_pk_fma_f32 v[72:73], v[4:5], s[2:3], v[78:79] op_sel_hi:[1,0,1]
	v_pk_fma_f32 v[74:75], v[6:7], s[2:3], v[174:175] op_sel_hi:[1,0,1]
	v_pk_fma_f32 v[76:77], v[8:9], s[2:3], v[172:173] op_sel_hi:[1,0,1]
	v_pk_fma_f32 v[78:79], v[10:11], s[2:3], v[170:171] op_sel_hi:[1,0,1]
	v_pk_fma_f32 v[168:169], v[12:13], s[2:3], v[168:169] op_sel_hi:[1,0,1]
	v_pk_fma_f32 v[166:167], v[14:15], s[2:3], v[166:167] op_sel_hi:[1,0,1]
	v_pk_fma_f32 v[164:165], v[16:17], s[2:3], v[164:165] op_sel_hi:[1,0,1]
	v_pk_fma_f32 v[162:163], v[18:19], s[2:3], v[162:163] op_sel_hi:[1,0,1]
	v_pk_fma_f32 v[160:161], v[20:21], s[2:3], v[160:161] op_sel_hi:[1,0,1]
	v_pk_fma_f32 v[158:159], v[22:23], s[2:3], v[158:159] op_sel_hi:[1,0,1]
	v_pk_fma_f32 v[156:157], v[24:25], s[2:3], v[156:157] op_sel_hi:[1,0,1]
	v_pk_fma_f32 v[154:155], v[26:27], s[2:3], v[154:155] op_sel_hi:[1,0,1]
	v_pk_fma_f32 v[152:153], v[28:29], s[2:3], v[152:153] op_sel_hi:[1,0,1]
	v_pk_fma_f32 v[150:151], v[30:31], s[2:3], v[150:151] op_sel_hi:[1,0,1]
	v_readlane_b32 s2, v211, 2
	s_waitcnt vmcnt(18)
	v_cvt_scalef32_pk32_f32_fp6 v[0:31], v[56:61], 1.0
	v_pk_fma_f32 v[56:57], v[0:1], s[2:3], v[68:69] op_sel_hi:[1,0,1]
	v_pk_fma_f32 v[58:59], v[2:3], s[2:3], v[70:71] op_sel_hi:[1,0,1]
	v_pk_fma_f32 v[60:61], v[4:5], s[2:3], v[72:73] op_sel_hi:[1,0,1]
	v_pk_fma_f32 v[68:69], v[6:7], s[2:3], v[74:75] op_sel_hi:[1,0,1]
	v_pk_fma_f32 v[70:71], v[8:9], s[2:3], v[76:77] op_sel_hi:[1,0,1]
	v_pk_fma_f32 v[72:73], v[10:11], s[2:3], v[78:79] op_sel_hi:[1,0,1]
	v_pk_fma_f32 v[74:75], v[12:13], s[2:3], v[168:169] op_sel_hi:[1,0,1]
	v_pk_fma_f32 v[76:77], v[14:15], s[2:3], v[166:167] op_sel_hi:[1,0,1]
	v_pk_fma_f32 v[78:79], v[16:17], s[2:3], v[164:165] op_sel_hi:[1,0,1]
	v_pk_fma_f32 v[162:163], v[18:19], s[2:3], v[162:163] op_sel_hi:[1,0,1]
	v_pk_fma_f32 v[160:161], v[20:21], s[2:3], v[160:161] op_sel_hi:[1,0,1]
	v_pk_fma_f32 v[158:159], v[22:23], s[2:3], v[158:159] op_sel_hi:[1,0,1]
	v_pk_fma_f32 v[156:157], v[24:25], s[2:3], v[156:157] op_sel_hi:[1,0,1]
	v_pk_fma_f32 v[154:155], v[26:27], s[2:3], v[154:155] op_sel_hi:[1,0,1]
	v_pk_fma_f32 v[152:153], v[28:29], s[2:3], v[152:153] op_sel_hi:[1,0,1]
	v_pk_fma_f32 v[150:151], v[30:31], s[2:3], v[150:151] op_sel_hi:[1,0,1]
	v_readlane_b32 s2, v211, 3
	s_waitcnt vmcnt(16)
	v_cvt_scalef32_pk32_f32_fp6 v[0:31], v[44:49], 1.0
	v_pk_fma_f32 v[164:165], v[0:1], s[2:3], v[56:57] op_sel_hi:[1,0,1]
	v_pk_fma_f32 v[166:167], v[2:3], s[2:3], v[58:59] op_sel_hi:[1,0,1]
	v_pk_fma_f32 v[168:169], v[4:5], s[2:3], v[60:61] op_sel_hi:[1,0,1]
	v_pk_fma_f32 v[170:171], v[6:7], s[2:3], v[68:69] op_sel_hi:[1,0,1]
	v_pk_fma_f32 v[172:173], v[8:9], s[2:3], v[70:71] op_sel_hi:[1,0,1]
	v_pk_fma_f32 v[174:175], v[10:11], s[2:3], v[72:73] op_sel_hi:[1,0,1]
	v_pk_fma_f32 v[176:177], v[12:13], s[2:3], v[74:75] op_sel_hi:[1,0,1]
	v_pk_fma_f32 v[178:179], v[14:15], s[2:3], v[76:77] op_sel_hi:[1,0,1]
	v_pk_fma_f32 v[180:181], v[16:17], s[2:3], v[78:79] op_sel_hi:[1,0,1]
	v_pk_fma_f32 v[162:163], v[18:19], s[2:3], v[162:163] op_sel_hi:[1,0,1]
	v_pk_fma_f32 v[160:161], v[20:21], s[2:3], v[160:161] op_sel_hi:[1,0,1]
	v_pk_fma_f32 v[158:159], v[22:23], s[2:3], v[158:159] op_sel_hi:[1,0,1]
	v_pk_fma_f32 v[156:157], v[24:25], s[2:3], v[156:157] op_sel_hi:[1,0,1]
	v_pk_fma_f32 v[154:155], v[26:27], s[2:3], v[154:155] op_sel_hi:[1,0,1]
	v_pk_fma_f32 v[152:153], v[28:29], s[2:3], v[152:153] op_sel_hi:[1,0,1]
	v_pk_fma_f32 v[150:151], v[30:31], s[2:3], v[150:151] op_sel_hi:[1,0,1]
	v_readlane_b32 s2, v240, 12
	v_readlane_b32 s3, v240, 13
	v_readlane_b32 s100, v240, 14
	v_readlane_b32 s101, v240, 15
	s_nop 1
	buffer_load_dwordx4 v[74:77], v129, s[44:47], s2 offen nt
	buffer_load_dwordx2 v[78:79], v210, s[44:47], s2 offen nt
	buffer_load_dwordx4 v[68:71], v129, s[44:47], s3 offen nt
	buffer_load_dwordx2 v[72:73], v210, s[44:47], s3 offen nt
	buffer_load_dwordx4 v[56:59], v129, s[44:47], s100 offen nt
	buffer_load_dwordx2 v[60:61], v210, s[44:47], s100 offen nt
	buffer_load_dwordx4 v[44:47], v129, s[44:47], s101 offen nt
	buffer_load_dwordx2 v[48:49], v210, s[44:47], s101 offen nt
	v_readlane_b32 s2, v211, 4
	s_waitcnt vmcnt(22)
	v_cvt_scalef32_pk32_f32_fp6 v[0:31], v[62:67], 1.0
	v_pk_fma_f32 v[62:63], v[0:1], s[2:3], v[164:165] op_sel_hi:[1,0,1]
	v_pk_fma_f32 v[64:65], v[2:3], s[2:3], v[166:167] op_sel_hi:[1,0,1]
	v_pk_fma_f32 v[66:67], v[4:5], s[2:3], v[168:169] op_sel_hi:[1,0,1]
	v_pk_fma_f32 v[164:165], v[6:7], s[2:3], v[170:171] op_sel_hi:[1,0,1]
	v_pk_fma_f32 v[166:167], v[8:9], s[2:3], v[172:173] op_sel_hi:[1,0,1]
	v_pk_fma_f32 v[168:169], v[10:11], s[2:3], v[174:175] op_sel_hi:[1,0,1]
	v_pk_fma_f32 v[170:171], v[12:13], s[2:3], v[176:177] op_sel_hi:[1,0,1]
	v_pk_fma_f32 v[172:173], v[14:15], s[2:3], v[178:179] op_sel_hi:[1,0,1]
	v_pk_fma_f32 v[174:175], v[16:17], s[2:3], v[180:181] op_sel_hi:[1,0,1]
	v_pk_fma_f32 v[162:163], v[18:19], s[2:3], v[162:163] op_sel_hi:[1,0,1]
	v_pk_fma_f32 v[160:161], v[20:21], s[2:3], v[160:161] op_sel_hi:[1,0,1]
	v_pk_fma_f32 v[158:159], v[22:23], s[2:3], v[158:159] op_sel_hi:[1,0,1]
	v_pk_fma_f32 v[156:157], v[24:25], s[2:3], v[156:157] op_sel_hi:[1,0,1]
	v_pk_fma_f32 v[154:155], v[26:27], s[2:3], v[154:155] op_sel_hi:[1,0,1]
	v_pk_fma_f32 v[152:153], v[28:29], s[2:3], v[152:153] op_sel_hi:[1,0,1]
	v_pk_fma_f32 v[150:151], v[30:31], s[2:3], v[150:151] op_sel_hi:[1,0,1]
	v_readlane_b32 s2, v211, 5
	s_waitcnt vmcnt(20)
	v_cvt_scalef32_pk32_f32_fp6 v[0:31], v[50:55], 1.0
	v_pk_fma_f32 v[50:51], v[0:1], s[2:3], v[62:63] op_sel_hi:[1,0,1]
	v_pk_fma_f32 v[52:53], v[2:3], s[2:3], v[64:65] op_sel_hi:[1,0,1]
	v_pk_fma_f32 v[54:55], v[4:5], s[2:3], v[66:67] op_sel_hi:[1,0,1]
	v_pk_fma_f32 v[62:63], v[6:7], s[2:3], v[164:165] op_sel_hi:[1,0,1]
	v_pk_fma_f32 v[64:65], v[8:9], s[2:3], v[166:167] op_sel_hi:[1,0,1]
	v_pk_fma_f32 v[66:67], v[10:11], s[2:3], v[168:169] op_sel_hi:[1,0,1]
	v_pk_fma_f32 v[164:165], v[12:13], s[2:3], v[170:171] op_sel_hi:[1,0,1]
	v_pk_fma_f32 v[166:167], v[14:15], s[2:3], v[172:173] op_sel_hi:[1,0,1]
	v_pk_fma_f32 v[168:169], v[16:17], s[2:3], v[174:175] op_sel_hi:[1,0,1]
	v_pk_fma_f32 v[162:163], v[18:19], s[2:3], v[162:163] op_sel_hi:[1,0,1]
	v_pk_fma_f32 v[160:161], v[20:21], s[2:3], v[160:161] op_sel_hi:[1,0,1]
	v_pk_fma_f32 v[158:159], v[22:23], s[2:3], v[158:159] op_sel_hi:[1,0,1]
	v_pk_fma_f32 v[156:157], v[24:25], s[2:3], v[156:157] op_sel_hi:[1,0,1]
	v_pk_fma_f32 v[154:155], v[26:27], s[2:3], v[154:155] op_sel_hi:[1,0,1]
	v_pk_fma_f32 v[152:153], v[28:29], s[2:3], v[152:153] op_sel_hi:[1,0,1]
	v_pk_fma_f32 v[150:151], v[30:31], s[2:3], v[150:151] op_sel_hi:[1,0,1]
	v_readlane_b32 s2, v211, 6
	s_waitcnt vmcnt(18)
	v_cvt_scalef32_pk32_f32_fp6 v[0:31], v[38:43], 1.0
	v_pk_fma_f32 v[38:39], v[0:1], s[2:3], v[50:51] op_sel_hi:[1,0,1]
	v_pk_fma_f32 v[40:41], v[2:3], s[2:3], v[52:53] op_sel_hi:[1,0,1]
	v_pk_fma_f32 v[42:43], v[4:5], s[2:3], v[54:55] op_sel_hi:[1,0,1]
	v_pk_fma_f32 v[50:51], v[6:7], s[2:3], v[62:63] op_sel_hi:[1,0,1]
	v_pk_fma_f32 v[52:53], v[8:9], s[2:3], v[64:65] op_sel_hi:[1,0,1]
	v_pk_fma_f32 v[54:55], v[10:11], s[2:3], v[66:67] op_sel_hi:[1,0,1]
	v_pk_fma_f32 v[62:63], v[12:13], s[2:3], v[164:165] op_sel_hi:[1,0,1]
	v_pk_fma_f32 v[64:65], v[14:15], s[2:3], v[166:167] op_sel_hi:[1,0,1]
	v_pk_fma_f32 v[66:67], v[16:17], s[2:3], v[168:169] op_sel_hi:[1,0,1]
	v_pk_fma_f32 v[162:163], v[18:19], s[2:3], v[162:163] op_sel_hi:[1,0,1]
	v_pk_fma_f32 v[160:161], v[20:21], s[2:3], v[160:161] op_sel_hi:[1,0,1]
	v_pk_fma_f32 v[158:159], v[22:23], s[2:3], v[158:159] op_sel_hi:[1,0,1]
	v_pk_fma_f32 v[156:157], v[24:25], s[2:3], v[156:157] op_sel_hi:[1,0,1]
	v_pk_fma_f32 v[154:155], v[26:27], s[2:3], v[154:155] op_sel_hi:[1,0,1]
	v_pk_fma_f32 v[152:153], v[28:29], s[2:3], v[152:153] op_sel_hi:[1,0,1]
	v_pk_fma_f32 v[150:151], v[30:31], s[2:3], v[150:151] op_sel_hi:[1,0,1]
	v_readlane_b32 s2, v211, 7
	s_waitcnt vmcnt(16)
	v_cvt_scalef32_pk32_f32_fp6 v[0:31], v[32:37], 1.0
	v_pk_fma_f32 v[164:165], v[0:1], s[2:3], v[38:39] op_sel_hi:[1,0,1]
	v_pk_fma_f32 v[166:167], v[2:3], s[2:3], v[40:41] op_sel_hi:[1,0,1]
	v_pk_fma_f32 v[168:169], v[4:5], s[2:3], v[42:43] op_sel_hi:[1,0,1]
	v_pk_fma_f32 v[170:171], v[6:7], s[2:3], v[50:51] op_sel_hi:[1,0,1]
	v_pk_fma_f32 v[172:173], v[8:9], s[2:3], v[52:53] op_sel_hi:[1,0,1]
	v_pk_fma_f32 v[174:175], v[10:11], s[2:3], v[54:55] op_sel_hi:[1,0,1]
	v_pk_fma_f32 v[176:177], v[12:13], s[2:3], v[62:63] op_sel_hi:[1,0,1]
	v_pk_fma_f32 v[178:179], v[14:15], s[2:3], v[64:65] op_sel_hi:[1,0,1]
	v_pk_fma_f32 v[180:181], v[16:17], s[2:3], v[66:67] op_sel_hi:[1,0,1]
	v_pk_fma_f32 v[162:163], v[18:19], s[2:3], v[162:163] op_sel_hi:[1,0,1]
	v_pk_fma_f32 v[160:161], v[20:21], s[2:3], v[160:161] op_sel_hi:[1,0,1]
	v_pk_fma_f32 v[158:159], v[22:23], s[2:3], v[158:159] op_sel_hi:[1,0,1]
	v_pk_fma_f32 v[156:157], v[24:25], s[2:3], v[156:157] op_sel_hi:[1,0,1]
	v_pk_fma_f32 v[154:155], v[26:27], s[2:3], v[154:155] op_sel_hi:[1,0,1]
	v_pk_fma_f32 v[152:153], v[28:29], s[2:3], v[152:153] op_sel_hi:[1,0,1]
	v_pk_fma_f32 v[150:151], v[30:31], s[2:3], v[150:151] op_sel_hi:[1,0,1]
	v_readlane_b32 s2, v240, 16
	v_readlane_b32 s3, v240, 17
	v_readlane_b32 s100, v240, 18
	v_readlane_b32 s101, v240, 19
	s_nop 1
	buffer_load_dwordx4 v[62:65], v129, s[44:47], s2 offen nt
	buffer_load_dwordx2 v[66:67], v210, s[44:47], s2 offen nt
	buffer_load_dwordx4 v[50:53], v129, s[44:47], s3 offen nt
	buffer_load_dwordx2 v[54:55], v210, s[44:47], s3 offen nt
	buffer_load_dwordx4 v[38:41], v129, s[44:47], s100 offen nt
	buffer_load_dwordx2 v[42:43], v210, s[44:47], s100 offen nt
	buffer_load_dwordx4 v[32:35], v129, s[44:47], s101 offen nt
	buffer_load_dwordx2 v[36:37], v210, s[44:47], s101 offen nt
	v_readlane_b32 s2, v211, 8
	s_waitcnt vmcnt(22)
	v_cvt_scalef32_pk32_f32_fp6 v[0:31], v[98:103], 1.0
	v_pk_fma_f32 v[98:99], v[0:1], s[2:3], v[164:165] op_sel_hi:[1,0,1]
	v_pk_fma_f32 v[100:101], v[2:3], s[2:3], v[166:167] op_sel_hi:[1,0,1]
	v_pk_fma_f32 v[102:103], v[4:5], s[2:3], v[168:169] op_sel_hi:[1,0,1]
	v_pk_fma_f32 v[164:165], v[6:7], s[2:3], v[170:171] op_sel_hi:[1,0,1]
	v_pk_fma_f32 v[166:167], v[8:9], s[2:3], v[172:173] op_sel_hi:[1,0,1]
	v_pk_fma_f32 v[168:169], v[10:11], s[2:3], v[174:175] op_sel_hi:[1,0,1]
	v_pk_fma_f32 v[170:171], v[12:13], s[2:3], v[176:177] op_sel_hi:[1,0,1]
	v_pk_fma_f32 v[172:173], v[14:15], s[2:3], v[178:179] op_sel_hi:[1,0,1]
	v_pk_fma_f32 v[174:175], v[16:17], s[2:3], v[180:181] op_sel_hi:[1,0,1]
	v_pk_fma_f32 v[162:163], v[18:19], s[2:3], v[162:163] op_sel_hi:[1,0,1]
	v_pk_fma_f32 v[160:161], v[20:21], s[2:3], v[160:161] op_sel_hi:[1,0,1]
	v_pk_fma_f32 v[158:159], v[22:23], s[2:3], v[158:159] op_sel_hi:[1,0,1]
	v_pk_fma_f32 v[156:157], v[24:25], s[2:3], v[156:157] op_sel_hi:[1,0,1]
	v_pk_fma_f32 v[154:155], v[26:27], s[2:3], v[154:155] op_sel_hi:[1,0,1]
	v_pk_fma_f32 v[152:153], v[28:29], s[2:3], v[152:153] op_sel_hi:[1,0,1]
	v_pk_fma_f32 v[150:151], v[30:31], s[2:3], v[150:151] op_sel_hi:[1,0,1]
	v_readlane_b32 s2, v211, 9
	s_waitcnt vmcnt(20)
	v_cvt_scalef32_pk32_f32_fp6 v[0:31], v[92:97], 1.0
	v_pk_fma_f32 v[92:93], v[0:1], s[2:3], v[98:99] op_sel_hi:[1,0,1]
	v_pk_fma_f32 v[94:95], v[2:3], s[2:3], v[100:101] op_sel_hi:[1,0,1]
	v_pk_fma_f32 v[96:97], v[4:5], s[2:3], v[102:103] op_sel_hi:[1,0,1]
	v_pk_fma_f32 v[98:99], v[6:7], s[2:3], v[164:165] op_sel_hi:[1,0,1]
	v_pk_fma_f32 v[100:101], v[8:9], s[2:3], v[166:167] op_sel_hi:[1,0,1]
	v_pk_fma_f32 v[102:103], v[10:11], s[2:3], v[168:169] op_sel_hi:[1,0,1]
	v_pk_fma_f32 v[164:165], v[12:13], s[2:3], v[170:171] op_sel_hi:[1,0,1]
	v_pk_fma_f32 v[166:167], v[14:15], s[2:3], v[172:173] op_sel_hi:[1,0,1]
	v_pk_fma_f32 v[168:169], v[16:17], s[2:3], v[174:175] op_sel_hi:[1,0,1]
	v_pk_fma_f32 v[162:163], v[18:19], s[2:3], v[162:163] op_sel_hi:[1,0,1]
	v_pk_fma_f32 v[160:161], v[20:21], s[2:3], v[160:161] op_sel_hi:[1,0,1]
	v_pk_fma_f32 v[158:159], v[22:23], s[2:3], v[158:159] op_sel_hi:[1,0,1]
	v_pk_fma_f32 v[156:157], v[24:25], s[2:3], v[156:157] op_sel_hi:[1,0,1]
	v_pk_fma_f32 v[154:155], v[26:27], s[2:3], v[154:155] op_sel_hi:[1,0,1]
	v_pk_fma_f32 v[152:153], v[28:29], s[2:3], v[152:153] op_sel_hi:[1,0,1]
	v_pk_fma_f32 v[150:151], v[30:31], s[2:3], v[150:151] op_sel_hi:[1,0,1]
	v_readlane_b32 s2, v211, 10
	s_waitcnt vmcnt(18)
	v_cvt_scalef32_pk32_f32_fp6 v[0:31], v[86:91], 1.0
	v_pk_fma_f32 v[86:87], v[0:1], s[2:3], v[92:93] op_sel_hi:[1,0,1]
	v_pk_fma_f32 v[88:89], v[2:3], s[2:3], v[94:95] op_sel_hi:[1,0,1]
	v_pk_fma_f32 v[90:91], v[4:5], s[2:3], v[96:97] op_sel_hi:[1,0,1]
	v_pk_fma_f32 v[92:93], v[6:7], s[2:3], v[98:99] op_sel_hi:[1,0,1]
	v_pk_fma_f32 v[94:95], v[8:9], s[2:3], v[100:101] op_sel_hi:[1,0,1]
	v_pk_fma_f32 v[96:97], v[10:11], s[2:3], v[102:103] op_sel_hi:[1,0,1]
	v_pk_fma_f32 v[98:99], v[12:13], s[2:3], v[164:165] op_sel_hi:[1,0,1]
	v_pk_fma_f32 v[100:101], v[14:15], s[2:3], v[166:167] op_sel_hi:[1,0,1]
	v_pk_fma_f32 v[102:103], v[16:17], s[2:3], v[168:169] op_sel_hi:[1,0,1]
	v_pk_fma_f32 v[162:163], v[18:19], s[2:3], v[162:163] op_sel_hi:[1,0,1]
	v_pk_fma_f32 v[160:161], v[20:21], s[2:3], v[160:161] op_sel_hi:[1,0,1]
	v_pk_fma_f32 v[158:159], v[22:23], s[2:3], v[158:159] op_sel_hi:[1,0,1]
	v_pk_fma_f32 v[156:157], v[24:25], s[2:3], v[156:157] op_sel_hi:[1,0,1]
	v_pk_fma_f32 v[154:155], v[26:27], s[2:3], v[154:155] op_sel_hi:[1,0,1]
	v_pk_fma_f32 v[152:153], v[28:29], s[2:3], v[152:153] op_sel_hi:[1,0,1]
	v_pk_fma_f32 v[150:151], v[30:31], s[2:3], v[150:151] op_sel_hi:[1,0,1]
	v_readlane_b32 s2, v211, 11
	s_waitcnt vmcnt(16)
	v_cvt_scalef32_pk32_f32_fp6 v[0:31], v[80:85], 1.0
	v_pk_fma_f32 v[180:181], v[0:1], s[2:3], v[86:87] op_sel_hi:[1,0,1]
	v_pk_fma_f32 v[178:179], v[2:3], s[2:3], v[88:89] op_sel_hi:[1,0,1]
	v_pk_fma_f32 v[176:177], v[4:5], s[2:3], v[90:91] op_sel_hi:[1,0,1]
	v_pk_fma_f32 v[174:175], v[6:7], s[2:3], v[92:93] op_sel_hi:[1,0,1]
	v_pk_fma_f32 v[172:173], v[8:9], s[2:3], v[94:95] op_sel_hi:[1,0,1]
	v_pk_fma_f32 v[170:171], v[10:11], s[2:3], v[96:97] op_sel_hi:[1,0,1]
	v_pk_fma_f32 v[168:169], v[12:13], s[2:3], v[98:99] op_sel_hi:[1,0,1]
	v_pk_fma_f32 v[166:167], v[14:15], s[2:3], v[100:101] op_sel_hi:[1,0,1]
	v_pk_fma_f32 v[164:165], v[16:17], s[2:3], v[102:103] op_sel_hi:[1,0,1]
	v_pk_fma_f32 v[162:163], v[18:19], s[2:3], v[162:163] op_sel_hi:[1,0,1]
	v_pk_fma_f32 v[160:161], v[20:21], s[2:3], v[160:161] op_sel_hi:[1,0,1]
	v_pk_fma_f32 v[158:159], v[22:23], s[2:3], v[158:159] op_sel_hi:[1,0,1]
	v_pk_fma_f32 v[156:157], v[24:25], s[2:3], v[156:157] op_sel_hi:[1,0,1]
	v_pk_fma_f32 v[154:155], v[26:27], s[2:3], v[154:155] op_sel_hi:[1,0,1]
	v_pk_fma_f32 v[152:153], v[28:29], s[2:3], v[152:153] op_sel_hi:[1,0,1]
	v_pk_fma_f32 v[150:151], v[30:31], s[2:3], v[150:151] op_sel_hi:[1,0,1]
	v_readlane_b32 s2, v240, 20
	v_readlane_b32 s3, v240, 21
	v_readlane_b32 s100, v240, 22
	v_readlane_b32 s101, v240, 23
	s_nop 1
	buffer_load_dwordx4 v[98:101], v129, s[44:47], s2 offen nt
	buffer_load_dwordx2 v[102:103], v210, s[44:47], s2 offen nt
	buffer_load_dwordx4 v[92:95], v129, s[44:47], s3 offen nt
	buffer_load_dwordx2 v[96:97], v210, s[44:47], s3 offen nt
	buffer_load_dwordx4 v[86:89], v129, s[44:47], s100 offen nt
	buffer_load_dwordx2 v[90:91], v210, s[44:47], s100 offen nt
	buffer_load_dwordx4 v[80:83], v129, s[44:47], s101 offen nt
	buffer_load_dwordx2 v[84:85], v210, s[44:47], s101 offen nt
	v_readlane_b32 s2, v211, 12
	s_waitcnt vmcnt(22)
	v_cvt_scalef32_pk32_f32_fp6 v[0:31], v[74:79], 1.0
	v_pk_fma_f32 v[74:75], v[0:1], s[2:3], v[180:181] op_sel_hi:[1,0,1]
	v_pk_fma_f32 v[76:77], v[2:3], s[2:3], v[178:179] op_sel_hi:[1,0,1]
	v_pk_fma_f32 v[78:79], v[4:5], s[2:3], v[176:177] op_sel_hi:[1,0,1]
	v_pk_fma_f32 v[174:175], v[6:7], s[2:3], v[174:175] op_sel_hi:[1,0,1]
	v_pk_fma_f32 v[172:173], v[8:9], s[2:3], v[172:173] op_sel_hi:[1,0,1]
	v_pk_fma_f32 v[170:171], v[10:11], s[2:3], v[170:171] op_sel_hi:[1,0,1]
	v_pk_fma_f32 v[168:169], v[12:13], s[2:3], v[168:169] op_sel_hi:[1,0,1]
	v_pk_fma_f32 v[166:167], v[14:15], s[2:3], v[166:167] op_sel_hi:[1,0,1]
	v_pk_fma_f32 v[164:165], v[16:17], s[2:3], v[164:165] op_sel_hi:[1,0,1]
	v_pk_fma_f32 v[162:163], v[18:19], s[2:3], v[162:163] op_sel_hi:[1,0,1]
	v_pk_fma_f32 v[160:161], v[20:21], s[2:3], v[160:161] op_sel_hi:[1,0,1]
	v_pk_fma_f32 v[158:159], v[22:23], s[2:3], v[158:159] op_sel_hi:[1,0,1]
	v_pk_fma_f32 v[156:157], v[24:25], s[2:3], v[156:157] op_sel_hi:[1,0,1]
	v_pk_fma_f32 v[154:155], v[26:27], s[2:3], v[154:155] op_sel_hi:[1,0,1]
	v_pk_fma_f32 v[152:153], v[28:29], s[2:3], v[152:153] op_sel_hi:[1,0,1]
	v_pk_fma_f32 v[150:151], v[30:31], s[2:3], v[150:151] op_sel_hi:[1,0,1]
	v_readlane_b32 s2, v211, 13
	s_waitcnt vmcnt(20)
	v_cvt_scalef32_pk32_f32_fp6 v[0:31], v[68:73], 1.0
	v_pk_fma_f32 v[68:69], v[0:1], s[2:3], v[74:75] op_sel_hi:[1,0,1]
	v_pk_fma_f32 v[70:71], v[2:3], s[2:3], v[76:77] op_sel_hi:[1,0,1]
	v_pk_fma_f32 v[72:73], v[4:5], s[2:3], v[78:79] op_sel_hi:[1,0,1]
	v_pk_fma_f32 v[74:75], v[6:7], s[2:3], v[174:175] op_sel_hi:[1,0,1]
	v_pk_fma_f32 v[76:77], v[8:9], s[2:3], v[172:173] op_sel_hi:[1,0,1]
	v_pk_fma_f32 v[78:79], v[10:11], s[2:3], v[170:171] op_sel_hi:[1,0,1]
	v_pk_fma_f32 v[168:169], v[12:13], s[2:3], v[168:169] op_sel_hi:[1,0,1]
	v_pk_fma_f32 v[166:167], v[14:15], s[2:3], v[166:167] op_sel_hi:[1,0,1]
	v_pk_fma_f32 v[164:165], v[16:17], s[2:3], v[164:165] op_sel_hi:[1,0,1]
	v_pk_fma_f32 v[162:163], v[18:19], s[2:3], v[162:163] op_sel_hi:[1,0,1]
	v_pk_fma_f32 v[160:161], v[20:21], s[2:3], v[160:161] op_sel_hi:[1,0,1]
	v_pk_fma_f32 v[158:159], v[22:23], s[2:3], v[158:159] op_sel_hi:[1,0,1]
	v_pk_fma_f32 v[156:157], v[24:25], s[2:3], v[156:157] op_sel_hi:[1,0,1]
	v_pk_fma_f32 v[154:155], v[26:27], s[2:3], v[154:155] op_sel_hi:[1,0,1]
	v_pk_fma_f32 v[152:153], v[28:29], s[2:3], v[152:153] op_sel_hi:[1,0,1]
	v_pk_fma_f32 v[150:151], v[30:31], s[2:3], v[150:151] op_sel_hi:[1,0,1]
	v_readlane_b32 s2, v211, 14
	s_waitcnt vmcnt(18)
	v_cvt_scalef32_pk32_f32_fp6 v[0:31], v[56:61], 1.0
	v_pk_fma_f32 v[56:57], v[0:1], s[2:3], v[68:69] op_sel_hi:[1,0,1]
	v_pk_fma_f32 v[58:59], v[2:3], s[2:3], v[70:71] op_sel_hi:[1,0,1]
	v_pk_fma_f32 v[60:61], v[4:5], s[2:3], v[72:73] op_sel_hi:[1,0,1]
	v_pk_fma_f32 v[68:69], v[6:7], s[2:3], v[74:75] op_sel_hi:[1,0,1]
	v_pk_fma_f32 v[70:71], v[8:9], s[2:3], v[76:77] op_sel_hi:[1,0,1]
	v_pk_fma_f32 v[72:73], v[10:11], s[2:3], v[78:79] op_sel_hi:[1,0,1]
	v_pk_fma_f32 v[74:75], v[12:13], s[2:3], v[168:169] op_sel_hi:[1,0,1]
	v_pk_fma_f32 v[76:77], v[14:15], s[2:3], v[166:167] op_sel_hi:[1,0,1]
	v_pk_fma_f32 v[78:79], v[16:17], s[2:3], v[164:165] op_sel_hi:[1,0,1]
	v_pk_fma_f32 v[162:163], v[18:19], s[2:3], v[162:163] op_sel_hi:[1,0,1]
	v_pk_fma_f32 v[160:161], v[20:21], s[2:3], v[160:161] op_sel_hi:[1,0,1]
	v_pk_fma_f32 v[158:159], v[22:23], s[2:3], v[158:159] op_sel_hi:[1,0,1]
	v_pk_fma_f32 v[156:157], v[24:25], s[2:3], v[156:157] op_sel_hi:[1,0,1]
	v_pk_fma_f32 v[154:155], v[26:27], s[2:3], v[154:155] op_sel_hi:[1,0,1]
	v_pk_fma_f32 v[152:153], v[28:29], s[2:3], v[152:153] op_sel_hi:[1,0,1]
	v_pk_fma_f32 v[150:151], v[30:31], s[2:3], v[150:151] op_sel_hi:[1,0,1]
	v_readlane_b32 s2, v211, 15
	s_waitcnt vmcnt(16)
	v_cvt_scalef32_pk32_f32_fp6 v[0:31], v[44:49], 1.0
	v_pk_fma_f32 v[164:165], v[0:1], s[2:3], v[56:57] op_sel_hi:[1,0,1]
	v_pk_fma_f32 v[166:167], v[2:3], s[2:3], v[58:59] op_sel_hi:[1,0,1]
	v_pk_fma_f32 v[168:169], v[4:5], s[2:3], v[60:61] op_sel_hi:[1,0,1]
	v_pk_fma_f32 v[170:171], v[6:7], s[2:3], v[68:69] op_sel_hi:[1,0,1]
	v_pk_fma_f32 v[172:173], v[8:9], s[2:3], v[70:71] op_sel_hi:[1,0,1]
	v_pk_fma_f32 v[174:175], v[10:11], s[2:3], v[72:73] op_sel_hi:[1,0,1]
	v_pk_fma_f32 v[176:177], v[12:13], s[2:3], v[74:75] op_sel_hi:[1,0,1]
	v_pk_fma_f32 v[178:179], v[14:15], s[2:3], v[76:77] op_sel_hi:[1,0,1]
	v_pk_fma_f32 v[180:181], v[16:17], s[2:3], v[78:79] op_sel_hi:[1,0,1]
	v_pk_fma_f32 v[162:163], v[18:19], s[2:3], v[162:163] op_sel_hi:[1,0,1]
	v_pk_fma_f32 v[160:161], v[20:21], s[2:3], v[160:161] op_sel_hi:[1,0,1]
	v_pk_fma_f32 v[158:159], v[22:23], s[2:3], v[158:159] op_sel_hi:[1,0,1]
	v_pk_fma_f32 v[156:157], v[24:25], s[2:3], v[156:157] op_sel_hi:[1,0,1]
	v_pk_fma_f32 v[154:155], v[26:27], s[2:3], v[154:155] op_sel_hi:[1,0,1]
	v_pk_fma_f32 v[152:153], v[28:29], s[2:3], v[152:153] op_sel_hi:[1,0,1]
	v_pk_fma_f32 v[150:151], v[30:31], s[2:3], v[150:151] op_sel_hi:[1,0,1]
	v_readlane_b32 s2, v240, 24
	v_readlane_b32 s3, v240, 25
	v_readlane_b32 s100, v240, 26
	v_readlane_b32 s101, v240, 27
	s_nop 1
	buffer_load_dwordx4 v[74:77], v129, s[44:47], s2 offen nt
	buffer_load_dwordx2 v[78:79], v210, s[44:47], s2 offen nt
	buffer_load_dwordx4 v[68:71], v129, s[44:47], s3 offen nt
	buffer_load_dwordx2 v[72:73], v210, s[44:47], s3 offen nt
	buffer_load_dwordx4 v[56:59], v129, s[44:47], s100 offen nt
	buffer_load_dwordx2 v[60:61], v210, s[44:47], s100 offen nt
	buffer_load_dwordx4 v[44:47], v129, s[44:47], s101 offen nt
	buffer_load_dwordx2 v[48:49], v210, s[44:47], s101 offen nt
	v_readlane_b32 s2, v211, 16
	s_waitcnt vmcnt(22)
	v_cvt_scalef32_pk32_f32_fp6 v[0:31], v[62:67], 1.0
	v_pk_fma_f32 v[62:63], v[0:1], s[2:3], v[164:165] op_sel_hi:[1,0,1]
	v_pk_fma_f32 v[64:65], v[2:3], s[2:3], v[166:167] op_sel_hi:[1,0,1]
	v_pk_fma_f32 v[66:67], v[4:5], s[2:3], v[168:169] op_sel_hi:[1,0,1]
	v_pk_fma_f32 v[164:165], v[6:7], s[2:3], v[170:171] op_sel_hi:[1,0,1]
	v_pk_fma_f32 v[166:167], v[8:9], s[2:3], v[172:173] op_sel_hi:[1,0,1]
	v_pk_fma_f32 v[168:169], v[10:11], s[2:3], v[174:175] op_sel_hi:[1,0,1]
	v_pk_fma_f32 v[170:171], v[12:13], s[2:3], v[176:177] op_sel_hi:[1,0,1]
	v_pk_fma_f32 v[172:173], v[14:15], s[2:3], v[178:179] op_sel_hi:[1,0,1]
	v_pk_fma_f32 v[174:175], v[16:17], s[2:3], v[180:181] op_sel_hi:[1,0,1]
	v_pk_fma_f32 v[162:163], v[18:19], s[2:3], v[162:163] op_sel_hi:[1,0,1]
	v_pk_fma_f32 v[160:161], v[20:21], s[2:3], v[160:161] op_sel_hi:[1,0,1]
	v_pk_fma_f32 v[158:159], v[22:23], s[2:3], v[158:159] op_sel_hi:[1,0,1]
	v_pk_fma_f32 v[156:157], v[24:25], s[2:3], v[156:157] op_sel_hi:[1,0,1]
	v_pk_fma_f32 v[154:155], v[26:27], s[2:3], v[154:155] op_sel_hi:[1,0,1]
	v_pk_fma_f32 v[152:153], v[28:29], s[2:3], v[152:153] op_sel_hi:[1,0,1]
	v_pk_fma_f32 v[150:151], v[30:31], s[2:3], v[150:151] op_sel_hi:[1,0,1]
	v_readlane_b32 s2, v211, 17
	s_waitcnt vmcnt(20)
	v_cvt_scalef32_pk32_f32_fp6 v[0:31], v[50:55], 1.0
	v_pk_fma_f32 v[50:51], v[0:1], s[2:3], v[62:63] op_sel_hi:[1,0,1]
	v_pk_fma_f32 v[52:53], v[2:3], s[2:3], v[64:65] op_sel_hi:[1,0,1]
	v_pk_fma_f32 v[54:55], v[4:5], s[2:3], v[66:67] op_sel_hi:[1,0,1]
	v_pk_fma_f32 v[62:63], v[6:7], s[2:3], v[164:165] op_sel_hi:[1,0,1]
	v_pk_fma_f32 v[64:65], v[8:9], s[2:3], v[166:167] op_sel_hi:[1,0,1]
	v_pk_fma_f32 v[66:67], v[10:11], s[2:3], v[168:169] op_sel_hi:[1,0,1]
	v_pk_fma_f32 v[164:165], v[12:13], s[2:3], v[170:171] op_sel_hi:[1,0,1]
	v_pk_fma_f32 v[166:167], v[14:15], s[2:3], v[172:173] op_sel_hi:[1,0,1]
	v_pk_fma_f32 v[168:169], v[16:17], s[2:3], v[174:175] op_sel_hi:[1,0,1]
	v_pk_fma_f32 v[162:163], v[18:19], s[2:3], v[162:163] op_sel_hi:[1,0,1]
	v_pk_fma_f32 v[160:161], v[20:21], s[2:3], v[160:161] op_sel_hi:[1,0,1]
	v_pk_fma_f32 v[158:159], v[22:23], s[2:3], v[158:159] op_sel_hi:[1,0,1]
	v_pk_fma_f32 v[156:157], v[24:25], s[2:3], v[156:157] op_sel_hi:[1,0,1]
	v_pk_fma_f32 v[154:155], v[26:27], s[2:3], v[154:155] op_sel_hi:[1,0,1]
	v_pk_fma_f32 v[152:153], v[28:29], s[2:3], v[152:153] op_sel_hi:[1,0,1]
	v_pk_fma_f32 v[150:151], v[30:31], s[2:3], v[150:151] op_sel_hi:[1,0,1]
	v_readlane_b32 s2, v211, 18
	s_waitcnt vmcnt(18)
	v_cvt_scalef32_pk32_f32_fp6 v[0:31], v[38:43], 1.0
	v_pk_fma_f32 v[38:39], v[0:1], s[2:3], v[50:51] op_sel_hi:[1,0,1]
	v_pk_fma_f32 v[40:41], v[2:3], s[2:3], v[52:53] op_sel_hi:[1,0,1]
	v_pk_fma_f32 v[42:43], v[4:5], s[2:3], v[54:55] op_sel_hi:[1,0,1]
	v_pk_fma_f32 v[50:51], v[6:7], s[2:3], v[62:63] op_sel_hi:[1,0,1]
	v_pk_fma_f32 v[52:53], v[8:9], s[2:3], v[64:65] op_sel_hi:[1,0,1]
	v_pk_fma_f32 v[54:55], v[10:11], s[2:3], v[66:67] op_sel_hi:[1,0,1]
	v_pk_fma_f32 v[62:63], v[12:13], s[2:3], v[164:165] op_sel_hi:[1,0,1]
	v_pk_fma_f32 v[64:65], v[14:15], s[2:3], v[166:167] op_sel_hi:[1,0,1]
	v_pk_fma_f32 v[66:67], v[16:17], s[2:3], v[168:169] op_sel_hi:[1,0,1]
	v_pk_fma_f32 v[162:163], v[18:19], s[2:3], v[162:163] op_sel_hi:[1,0,1]
	v_pk_fma_f32 v[160:161], v[20:21], s[2:3], v[160:161] op_sel_hi:[1,0,1]
	v_pk_fma_f32 v[158:159], v[22:23], s[2:3], v[158:159] op_sel_hi:[1,0,1]
	v_pk_fma_f32 v[156:157], v[24:25], s[2:3], v[156:157] op_sel_hi:[1,0,1]
	v_pk_fma_f32 v[154:155], v[26:27], s[2:3], v[154:155] op_sel_hi:[1,0,1]
	v_pk_fma_f32 v[152:153], v[28:29], s[2:3], v[152:153] op_sel_hi:[1,0,1]
	v_pk_fma_f32 v[150:151], v[30:31], s[2:3], v[150:151] op_sel_hi:[1,0,1]
	v_readlane_b32 s2, v211, 19
	s_waitcnt vmcnt(16)
	v_cvt_scalef32_pk32_f32_fp6 v[0:31], v[32:37], 1.0
	v_pk_fma_f32 v[164:165], v[0:1], s[2:3], v[38:39] op_sel_hi:[1,0,1]
	v_pk_fma_f32 v[166:167], v[2:3], s[2:3], v[40:41] op_sel_hi:[1,0,1]
	v_pk_fma_f32 v[168:169], v[4:5], s[2:3], v[42:43] op_sel_hi:[1,0,1]
	v_pk_fma_f32 v[170:171], v[6:7], s[2:3], v[50:51] op_sel_hi:[1,0,1]
	v_pk_fma_f32 v[172:173], v[8:9], s[2:3], v[52:53] op_sel_hi:[1,0,1]
	v_pk_fma_f32 v[174:175], v[10:11], s[2:3], v[54:55] op_sel_hi:[1,0,1]
	v_pk_fma_f32 v[176:177], v[12:13], s[2:3], v[62:63] op_sel_hi:[1,0,1]
	v_pk_fma_f32 v[178:179], v[14:15], s[2:3], v[64:65] op_sel_hi:[1,0,1]
	v_pk_fma_f32 v[180:181], v[16:17], s[2:3], v[66:67] op_sel_hi:[1,0,1]
	v_pk_fma_f32 v[162:163], v[18:19], s[2:3], v[162:163] op_sel_hi:[1,0,1]
	v_pk_fma_f32 v[160:161], v[20:21], s[2:3], v[160:161] op_sel_hi:[1,0,1]
	v_pk_fma_f32 v[158:159], v[22:23], s[2:3], v[158:159] op_sel_hi:[1,0,1]
	v_pk_fma_f32 v[156:157], v[24:25], s[2:3], v[156:157] op_sel_hi:[1,0,1]
	v_pk_fma_f32 v[154:155], v[26:27], s[2:3], v[154:155] op_sel_hi:[1,0,1]
	v_pk_fma_f32 v[152:153], v[28:29], s[2:3], v[152:153] op_sel_hi:[1,0,1]
	v_pk_fma_f32 v[150:151], v[30:31], s[2:3], v[150:151] op_sel_hi:[1,0,1]
	v_readlane_b32 s2, v240, 28
	v_readlane_b32 s3, v240, 29
	v_readlane_b32 s100, v240, 30
	v_readlane_b32 s101, v240, 31
	s_nop 1
	buffer_load_dwordx4 v[62:65], v129, s[44:47], s2 offen nt
	buffer_load_dwordx2 v[66:67], v210, s[44:47], s2 offen nt
	buffer_load_dwordx4 v[50:53], v129, s[44:47], s3 offen nt
	buffer_load_dwordx2 v[54:55], v210, s[44:47], s3 offen nt
	buffer_load_dwordx4 v[38:41], v129, s[44:47], s100 offen nt
	buffer_load_dwordx2 v[42:43], v210, s[44:47], s100 offen nt
	buffer_load_dwordx4 v[32:35], v129, s[44:47], s101 offen nt
	buffer_load_dwordx2 v[36:37], v210, s[44:47], s101 offen nt
	v_readlane_b32 s2, v211, 20
	s_waitcnt vmcnt(22)
	v_cvt_scalef32_pk32_f32_fp6 v[0:31], v[98:103], 1.0
	v_pk_fma_f32 v[98:99], v[0:1], s[2:3], v[164:165] op_sel_hi:[1,0,1]
	v_pk_fma_f32 v[100:101], v[2:3], s[2:3], v[166:167] op_sel_hi:[1,0,1]
	v_pk_fma_f32 v[102:103], v[4:5], s[2:3], v[168:169] op_sel_hi:[1,0,1]
	v_pk_fma_f32 v[164:165], v[6:7], s[2:3], v[170:171] op_sel_hi:[1,0,1]
	v_pk_fma_f32 v[166:167], v[8:9], s[2:3], v[172:173] op_sel_hi:[1,0,1]
	v_pk_fma_f32 v[168:169], v[10:11], s[2:3], v[174:175] op_sel_hi:[1,0,1]
	v_pk_fma_f32 v[170:171], v[12:13], s[2:3], v[176:177] op_sel_hi:[1,0,1]
	v_pk_fma_f32 v[172:173], v[14:15], s[2:3], v[178:179] op_sel_hi:[1,0,1]
	v_pk_fma_f32 v[174:175], v[16:17], s[2:3], v[180:181] op_sel_hi:[1,0,1]
	v_pk_fma_f32 v[162:163], v[18:19], s[2:3], v[162:163] op_sel_hi:[1,0,1]
	v_pk_fma_f32 v[160:161], v[20:21], s[2:3], v[160:161] op_sel_hi:[1,0,1]
	v_pk_fma_f32 v[158:159], v[22:23], s[2:3], v[158:159] op_sel_hi:[1,0,1]
	v_pk_fma_f32 v[156:157], v[24:25], s[2:3], v[156:157] op_sel_hi:[1,0,1]
	v_pk_fma_f32 v[154:155], v[26:27], s[2:3], v[154:155] op_sel_hi:[1,0,1]
	v_pk_fma_f32 v[152:153], v[28:29], s[2:3], v[152:153] op_sel_hi:[1,0,1]
	v_pk_fma_f32 v[150:151], v[30:31], s[2:3], v[150:151] op_sel_hi:[1,0,1]
	v_readlane_b32 s2, v211, 21
	s_waitcnt vmcnt(20)
	v_cvt_scalef32_pk32_f32_fp6 v[0:31], v[92:97], 1.0
	v_pk_fma_f32 v[92:93], v[0:1], s[2:3], v[98:99] op_sel_hi:[1,0,1]
	v_pk_fma_f32 v[94:95], v[2:3], s[2:3], v[100:101] op_sel_hi:[1,0,1]
	v_pk_fma_f32 v[96:97], v[4:5], s[2:3], v[102:103] op_sel_hi:[1,0,1]
	v_pk_fma_f32 v[98:99], v[6:7], s[2:3], v[164:165] op_sel_hi:[1,0,1]
	v_pk_fma_f32 v[100:101], v[8:9], s[2:3], v[166:167] op_sel_hi:[1,0,1]
	v_pk_fma_f32 v[102:103], v[10:11], s[2:3], v[168:169] op_sel_hi:[1,0,1]
	v_pk_fma_f32 v[164:165], v[12:13], s[2:3], v[170:171] op_sel_hi:[1,0,1]
	v_pk_fma_f32 v[166:167], v[14:15], s[2:3], v[172:173] op_sel_hi:[1,0,1]
	v_pk_fma_f32 v[168:169], v[16:17], s[2:3], v[174:175] op_sel_hi:[1,0,1]
	v_pk_fma_f32 v[162:163], v[18:19], s[2:3], v[162:163] op_sel_hi:[1,0,1]
	v_pk_fma_f32 v[160:161], v[20:21], s[2:3], v[160:161] op_sel_hi:[1,0,1]
	v_pk_fma_f32 v[158:159], v[22:23], s[2:3], v[158:159] op_sel_hi:[1,0,1]
	v_pk_fma_f32 v[156:157], v[24:25], s[2:3], v[156:157] op_sel_hi:[1,0,1]
	v_pk_fma_f32 v[154:155], v[26:27], s[2:3], v[154:155] op_sel_hi:[1,0,1]
	v_pk_fma_f32 v[152:153], v[28:29], s[2:3], v[152:153] op_sel_hi:[1,0,1]
	v_pk_fma_f32 v[150:151], v[30:31], s[2:3], v[150:151] op_sel_hi:[1,0,1]
	v_readlane_b32 s2, v211, 22
	s_waitcnt vmcnt(18)
	v_cvt_scalef32_pk32_f32_fp6 v[0:31], v[86:91], 1.0
	v_pk_fma_f32 v[86:87], v[0:1], s[2:3], v[92:93] op_sel_hi:[1,0,1]
	v_pk_fma_f32 v[88:89], v[2:3], s[2:3], v[94:95] op_sel_hi:[1,0,1]
	v_pk_fma_f32 v[90:91], v[4:5], s[2:3], v[96:97] op_sel_hi:[1,0,1]
	v_pk_fma_f32 v[92:93], v[6:7], s[2:3], v[98:99] op_sel_hi:[1,0,1]
	v_pk_fma_f32 v[94:95], v[8:9], s[2:3], v[100:101] op_sel_hi:[1,0,1]
	v_pk_fma_f32 v[96:97], v[10:11], s[2:3], v[102:103] op_sel_hi:[1,0,1]
	v_pk_fma_f32 v[98:99], v[12:13], s[2:3], v[164:165] op_sel_hi:[1,0,1]
	v_pk_fma_f32 v[100:101], v[14:15], s[2:3], v[166:167] op_sel_hi:[1,0,1]
	v_pk_fma_f32 v[102:103], v[16:17], s[2:3], v[168:169] op_sel_hi:[1,0,1]
	v_pk_fma_f32 v[162:163], v[18:19], s[2:3], v[162:163] op_sel_hi:[1,0,1]
	v_pk_fma_f32 v[160:161], v[20:21], s[2:3], v[160:161] op_sel_hi:[1,0,1]
	v_pk_fma_f32 v[158:159], v[22:23], s[2:3], v[158:159] op_sel_hi:[1,0,1]
	v_pk_fma_f32 v[156:157], v[24:25], s[2:3], v[156:157] op_sel_hi:[1,0,1]
	v_pk_fma_f32 v[154:155], v[26:27], s[2:3], v[154:155] op_sel_hi:[1,0,1]
	v_pk_fma_f32 v[152:153], v[28:29], s[2:3], v[152:153] op_sel_hi:[1,0,1]
	v_pk_fma_f32 v[150:151], v[30:31], s[2:3], v[150:151] op_sel_hi:[1,0,1]
	v_readlane_b32 s2, v211, 23
	s_waitcnt vmcnt(16)
	v_cvt_scalef32_pk32_f32_fp6 v[0:31], v[80:85], 1.0
	v_pk_fma_f32 v[180:181], v[0:1], s[2:3], v[86:87] op_sel_hi:[1,0,1]
	v_pk_fma_f32 v[178:179], v[2:3], s[2:3], v[88:89] op_sel_hi:[1,0,1]
	v_pk_fma_f32 v[176:177], v[4:5], s[2:3], v[90:91] op_sel_hi:[1,0,1]
	v_pk_fma_f32 v[174:175], v[6:7], s[2:3], v[92:93] op_sel_hi:[1,0,1]
	v_pk_fma_f32 v[172:173], v[8:9], s[2:3], v[94:95] op_sel_hi:[1,0,1]
	v_pk_fma_f32 v[170:171], v[10:11], s[2:3], v[96:97] op_sel_hi:[1,0,1]
	v_pk_fma_f32 v[168:169], v[12:13], s[2:3], v[98:99] op_sel_hi:[1,0,1]
	v_pk_fma_f32 v[166:167], v[14:15], s[2:3], v[100:101] op_sel_hi:[1,0,1]
	v_pk_fma_f32 v[164:165], v[16:17], s[2:3], v[102:103] op_sel_hi:[1,0,1]
	v_pk_fma_f32 v[162:163], v[18:19], s[2:3], v[162:163] op_sel_hi:[1,0,1]
	v_pk_fma_f32 v[160:161], v[20:21], s[2:3], v[160:161] op_sel_hi:[1,0,1]
	v_pk_fma_f32 v[158:159], v[22:23], s[2:3], v[158:159] op_sel_hi:[1,0,1]
	v_pk_fma_f32 v[156:157], v[24:25], s[2:3], v[156:157] op_sel_hi:[1,0,1]
	v_pk_fma_f32 v[154:155], v[26:27], s[2:3], v[154:155] op_sel_hi:[1,0,1]
	v_pk_fma_f32 v[152:153], v[28:29], s[2:3], v[152:153] op_sel_hi:[1,0,1]
	v_pk_fma_f32 v[150:151], v[30:31], s[2:3], v[150:151] op_sel_hi:[1,0,1]
	v_readlane_b32 s2, v240, 32
	v_readlane_b32 s3, v240, 33
	v_readlane_b32 s100, v240, 34
	v_readlane_b32 s101, v240, 35
	s_nop 1
	buffer_load_dwordx4 v[98:101], v129, s[44:47], s2 offen nt
	buffer_load_dwordx2 v[102:103], v210, s[44:47], s2 offen nt
	buffer_load_dwordx4 v[92:95], v129, s[44:47], s3 offen nt
	buffer_load_dwordx2 v[96:97], v210, s[44:47], s3 offen nt
	buffer_load_dwordx4 v[86:89], v129, s[44:47], s100 offen nt
	buffer_load_dwordx2 v[90:91], v210, s[44:47], s100 offen nt
	buffer_load_dwordx4 v[80:83], v129, s[44:47], s101 offen nt
	buffer_load_dwordx2 v[84:85], v210, s[44:47], s101 offen nt
	v_readlane_b32 s2, v211, 24
	s_waitcnt vmcnt(22)
	v_cvt_scalef32_pk32_f32_fp6 v[0:31], v[74:79], 1.0
	v_pk_fma_f32 v[74:75], v[0:1], s[2:3], v[180:181] op_sel_hi:[1,0,1]
	v_pk_fma_f32 v[76:77], v[2:3], s[2:3], v[178:179] op_sel_hi:[1,0,1]
	v_pk_fma_f32 v[78:79], v[4:5], s[2:3], v[176:177] op_sel_hi:[1,0,1]
	v_pk_fma_f32 v[174:175], v[6:7], s[2:3], v[174:175] op_sel_hi:[1,0,1]
	v_pk_fma_f32 v[172:173], v[8:9], s[2:3], v[172:173] op_sel_hi:[1,0,1]
	v_pk_fma_f32 v[170:171], v[10:11], s[2:3], v[170:171] op_sel_hi:[1,0,1]
	v_pk_fma_f32 v[168:169], v[12:13], s[2:3], v[168:169] op_sel_hi:[1,0,1]
	v_pk_fma_f32 v[166:167], v[14:15], s[2:3], v[166:167] op_sel_hi:[1,0,1]
	v_pk_fma_f32 v[164:165], v[16:17], s[2:3], v[164:165] op_sel_hi:[1,0,1]
	v_pk_fma_f32 v[162:163], v[18:19], s[2:3], v[162:163] op_sel_hi:[1,0,1]
	v_pk_fma_f32 v[160:161], v[20:21], s[2:3], v[160:161] op_sel_hi:[1,0,1]
	v_pk_fma_f32 v[158:159], v[22:23], s[2:3], v[158:159] op_sel_hi:[1,0,1]
	v_pk_fma_f32 v[156:157], v[24:25], s[2:3], v[156:157] op_sel_hi:[1,0,1]
	v_pk_fma_f32 v[154:155], v[26:27], s[2:3], v[154:155] op_sel_hi:[1,0,1]
	v_pk_fma_f32 v[152:153], v[28:29], s[2:3], v[152:153] op_sel_hi:[1,0,1]
	v_pk_fma_f32 v[150:151], v[30:31], s[2:3], v[150:151] op_sel_hi:[1,0,1]
	v_readlane_b32 s2, v211, 25
	s_waitcnt vmcnt(20)
	v_cvt_scalef32_pk32_f32_fp6 v[0:31], v[68:73], 1.0
	v_pk_fma_f32 v[68:69], v[0:1], s[2:3], v[74:75] op_sel_hi:[1,0,1]
	v_pk_fma_f32 v[70:71], v[2:3], s[2:3], v[76:77] op_sel_hi:[1,0,1]
	v_pk_fma_f32 v[72:73], v[4:5], s[2:3], v[78:79] op_sel_hi:[1,0,1]
	v_pk_fma_f32 v[74:75], v[6:7], s[2:3], v[174:175] op_sel_hi:[1,0,1]
	v_pk_fma_f32 v[76:77], v[8:9], s[2:3], v[172:173] op_sel_hi:[1,0,1]
	v_pk_fma_f32 v[78:79], v[10:11], s[2:3], v[170:171] op_sel_hi:[1,0,1]
	v_pk_fma_f32 v[168:169], v[12:13], s[2:3], v[168:169] op_sel_hi:[1,0,1]
	v_pk_fma_f32 v[166:167], v[14:15], s[2:3], v[166:167] op_sel_hi:[1,0,1]
	v_pk_fma_f32 v[164:165], v[16:17], s[2:3], v[164:165] op_sel_hi:[1,0,1]
	v_pk_fma_f32 v[162:163], v[18:19], s[2:3], v[162:163] op_sel_hi:[1,0,1]
	v_pk_fma_f32 v[160:161], v[20:21], s[2:3], v[160:161] op_sel_hi:[1,0,1]
	v_pk_fma_f32 v[158:159], v[22:23], s[2:3], v[158:159] op_sel_hi:[1,0,1]
	v_pk_fma_f32 v[156:157], v[24:25], s[2:3], v[156:157] op_sel_hi:[1,0,1]
	v_pk_fma_f32 v[154:155], v[26:27], s[2:3], v[154:155] op_sel_hi:[1,0,1]
	v_pk_fma_f32 v[152:153], v[28:29], s[2:3], v[152:153] op_sel_hi:[1,0,1]
	v_pk_fma_f32 v[150:151], v[30:31], s[2:3], v[150:151] op_sel_hi:[1,0,1]
	v_readlane_b32 s2, v211, 26
	s_waitcnt vmcnt(18)
	v_cvt_scalef32_pk32_f32_fp6 v[0:31], v[56:61], 1.0
	v_pk_fma_f32 v[56:57], v[0:1], s[2:3], v[68:69] op_sel_hi:[1,0,1]
	v_pk_fma_f32 v[58:59], v[2:3], s[2:3], v[70:71] op_sel_hi:[1,0,1]
	v_pk_fma_f32 v[60:61], v[4:5], s[2:3], v[72:73] op_sel_hi:[1,0,1]
	v_pk_fma_f32 v[68:69], v[6:7], s[2:3], v[74:75] op_sel_hi:[1,0,1]
	v_pk_fma_f32 v[70:71], v[8:9], s[2:3], v[76:77] op_sel_hi:[1,0,1]
	v_pk_fma_f32 v[72:73], v[10:11], s[2:3], v[78:79] op_sel_hi:[1,0,1]
	v_pk_fma_f32 v[74:75], v[12:13], s[2:3], v[168:169] op_sel_hi:[1,0,1]
	v_pk_fma_f32 v[76:77], v[14:15], s[2:3], v[166:167] op_sel_hi:[1,0,1]
	v_pk_fma_f32 v[78:79], v[16:17], s[2:3], v[164:165] op_sel_hi:[1,0,1]
	v_pk_fma_f32 v[162:163], v[18:19], s[2:3], v[162:163] op_sel_hi:[1,0,1]
	v_pk_fma_f32 v[160:161], v[20:21], s[2:3], v[160:161] op_sel_hi:[1,0,1]
	v_pk_fma_f32 v[158:159], v[22:23], s[2:3], v[158:159] op_sel_hi:[1,0,1]
	v_pk_fma_f32 v[156:157], v[24:25], s[2:3], v[156:157] op_sel_hi:[1,0,1]
	v_pk_fma_f32 v[154:155], v[26:27], s[2:3], v[154:155] op_sel_hi:[1,0,1]
	v_pk_fma_f32 v[152:153], v[28:29], s[2:3], v[152:153] op_sel_hi:[1,0,1]
	v_pk_fma_f32 v[150:151], v[30:31], s[2:3], v[150:151] op_sel_hi:[1,0,1]
	v_readlane_b32 s2, v211, 27
	s_waitcnt vmcnt(16)
	v_cvt_scalef32_pk32_f32_fp6 v[0:31], v[44:49], 1.0
	v_pk_fma_f32 v[164:165], v[0:1], s[2:3], v[56:57] op_sel_hi:[1,0,1]
	v_pk_fma_f32 v[166:167], v[2:3], s[2:3], v[58:59] op_sel_hi:[1,0,1]
	v_pk_fma_f32 v[168:169], v[4:5], s[2:3], v[60:61] op_sel_hi:[1,0,1]
	v_pk_fma_f32 v[170:171], v[6:7], s[2:3], v[68:69] op_sel_hi:[1,0,1]
	v_pk_fma_f32 v[172:173], v[8:9], s[2:3], v[70:71] op_sel_hi:[1,0,1]
	v_pk_fma_f32 v[174:175], v[10:11], s[2:3], v[72:73] op_sel_hi:[1,0,1]
	v_pk_fma_f32 v[176:177], v[12:13], s[2:3], v[74:75] op_sel_hi:[1,0,1]
	v_pk_fma_f32 v[178:179], v[14:15], s[2:3], v[76:77] op_sel_hi:[1,0,1]
	v_pk_fma_f32 v[180:181], v[16:17], s[2:3], v[78:79] op_sel_hi:[1,0,1]
	v_pk_fma_f32 v[162:163], v[18:19], s[2:3], v[162:163] op_sel_hi:[1,0,1]
	v_pk_fma_f32 v[160:161], v[20:21], s[2:3], v[160:161] op_sel_hi:[1,0,1]
	v_pk_fma_f32 v[158:159], v[22:23], s[2:3], v[158:159] op_sel_hi:[1,0,1]
	v_pk_fma_f32 v[156:157], v[24:25], s[2:3], v[156:157] op_sel_hi:[1,0,1]
	v_pk_fma_f32 v[154:155], v[26:27], s[2:3], v[154:155] op_sel_hi:[1,0,1]
	v_pk_fma_f32 v[152:153], v[28:29], s[2:3], v[152:153] op_sel_hi:[1,0,1]
	v_pk_fma_f32 v[150:151], v[30:31], s[2:3], v[150:151] op_sel_hi:[1,0,1]
	v_readlane_b32 s2, v240, 36
	v_readlane_b32 s3, v240, 37
	v_readlane_b32 s100, v240, 38
	v_readlane_b32 s101, v240, 39
	s_nop 1
	buffer_load_dwordx4 v[74:77], v129, s[44:47], s2 offen nt
	buffer_load_dwordx2 v[78:79], v210, s[44:47], s2 offen nt
	buffer_load_dwordx4 v[68:71], v129, s[44:47], s3 offen nt
	buffer_load_dwordx2 v[72:73], v210, s[44:47], s3 offen nt
	buffer_load_dwordx4 v[56:59], v129, s[44:47], s100 offen nt
	buffer_load_dwordx2 v[60:61], v210, s[44:47], s100 offen nt
	buffer_load_dwordx4 v[44:47], v129, s[44:47], s101 offen nt
	buffer_load_dwordx2 v[48:49], v210, s[44:47], s101 offen nt
	v_readlane_b32 s2, v211, 28
	s_waitcnt vmcnt(22)
	v_cvt_scalef32_pk32_f32_fp6 v[0:31], v[62:67], 1.0
	v_pk_fma_f32 v[62:63], v[0:1], s[2:3], v[164:165] op_sel_hi:[1,0,1]
	v_pk_fma_f32 v[64:65], v[2:3], s[2:3], v[166:167] op_sel_hi:[1,0,1]
	v_pk_fma_f32 v[66:67], v[4:5], s[2:3], v[168:169] op_sel_hi:[1,0,1]
	v_pk_fma_f32 v[164:165], v[6:7], s[2:3], v[170:171] op_sel_hi:[1,0,1]
	v_pk_fma_f32 v[166:167], v[8:9], s[2:3], v[172:173] op_sel_hi:[1,0,1]
	v_pk_fma_f32 v[168:169], v[10:11], s[2:3], v[174:175] op_sel_hi:[1,0,1]
	v_pk_fma_f32 v[170:171], v[12:13], s[2:3], v[176:177] op_sel_hi:[1,0,1]
	v_pk_fma_f32 v[172:173], v[14:15], s[2:3], v[178:179] op_sel_hi:[1,0,1]
	v_pk_fma_f32 v[174:175], v[16:17], s[2:3], v[180:181] op_sel_hi:[1,0,1]
	v_pk_fma_f32 v[162:163], v[18:19], s[2:3], v[162:163] op_sel_hi:[1,0,1]
	v_pk_fma_f32 v[160:161], v[20:21], s[2:3], v[160:161] op_sel_hi:[1,0,1]
	v_pk_fma_f32 v[158:159], v[22:23], s[2:3], v[158:159] op_sel_hi:[1,0,1]
	v_pk_fma_f32 v[156:157], v[24:25], s[2:3], v[156:157] op_sel_hi:[1,0,1]
	v_pk_fma_f32 v[154:155], v[26:27], s[2:3], v[154:155] op_sel_hi:[1,0,1]
	v_pk_fma_f32 v[152:153], v[28:29], s[2:3], v[152:153] op_sel_hi:[1,0,1]
	v_pk_fma_f32 v[150:151], v[30:31], s[2:3], v[150:151] op_sel_hi:[1,0,1]
	v_readlane_b32 s2, v211, 29
	s_waitcnt vmcnt(20)
	v_cvt_scalef32_pk32_f32_fp6 v[0:31], v[50:55], 1.0
	v_pk_fma_f32 v[50:51], v[0:1], s[2:3], v[62:63] op_sel_hi:[1,0,1]
	v_pk_fma_f32 v[52:53], v[2:3], s[2:3], v[64:65] op_sel_hi:[1,0,1]
	v_pk_fma_f32 v[54:55], v[4:5], s[2:3], v[66:67] op_sel_hi:[1,0,1]
	v_pk_fma_f32 v[62:63], v[6:7], s[2:3], v[164:165] op_sel_hi:[1,0,1]
	v_pk_fma_f32 v[64:65], v[8:9], s[2:3], v[166:167] op_sel_hi:[1,0,1]
	v_pk_fma_f32 v[66:67], v[10:11], s[2:3], v[168:169] op_sel_hi:[1,0,1]
	v_pk_fma_f32 v[164:165], v[12:13], s[2:3], v[170:171] op_sel_hi:[1,0,1]
	v_pk_fma_f32 v[166:167], v[14:15], s[2:3], v[172:173] op_sel_hi:[1,0,1]
	v_pk_fma_f32 v[168:169], v[16:17], s[2:3], v[174:175] op_sel_hi:[1,0,1]
	v_pk_fma_f32 v[162:163], v[18:19], s[2:3], v[162:163] op_sel_hi:[1,0,1]
	v_pk_fma_f32 v[160:161], v[20:21], s[2:3], v[160:161] op_sel_hi:[1,0,1]
	v_pk_fma_f32 v[158:159], v[22:23], s[2:3], v[158:159] op_sel_hi:[1,0,1]
	v_pk_fma_f32 v[156:157], v[24:25], s[2:3], v[156:157] op_sel_hi:[1,0,1]
	v_pk_fma_f32 v[154:155], v[26:27], s[2:3], v[154:155] op_sel_hi:[1,0,1]
	v_pk_fma_f32 v[152:153], v[28:29], s[2:3], v[152:153] op_sel_hi:[1,0,1]
	v_pk_fma_f32 v[150:151], v[30:31], s[2:3], v[150:151] op_sel_hi:[1,0,1]
	v_readlane_b32 s2, v211, 30
	s_waitcnt vmcnt(18)
	v_cvt_scalef32_pk32_f32_fp6 v[0:31], v[38:43], 1.0
	v_pk_fma_f32 v[38:39], v[0:1], s[2:3], v[50:51] op_sel_hi:[1,0,1]
	v_pk_fma_f32 v[40:41], v[2:3], s[2:3], v[52:53] op_sel_hi:[1,0,1]
	v_pk_fma_f32 v[42:43], v[4:5], s[2:3], v[54:55] op_sel_hi:[1,0,1]
	v_pk_fma_f32 v[50:51], v[6:7], s[2:3], v[62:63] op_sel_hi:[1,0,1]
	v_pk_fma_f32 v[52:53], v[8:9], s[2:3], v[64:65] op_sel_hi:[1,0,1]
	v_pk_fma_f32 v[54:55], v[10:11], s[2:3], v[66:67] op_sel_hi:[1,0,1]
	v_pk_fma_f32 v[62:63], v[12:13], s[2:3], v[164:165] op_sel_hi:[1,0,1]
	v_pk_fma_f32 v[64:65], v[14:15], s[2:3], v[166:167] op_sel_hi:[1,0,1]
	v_pk_fma_f32 v[66:67], v[16:17], s[2:3], v[168:169] op_sel_hi:[1,0,1]
	v_pk_fma_f32 v[162:163], v[18:19], s[2:3], v[162:163] op_sel_hi:[1,0,1]
	v_pk_fma_f32 v[160:161], v[20:21], s[2:3], v[160:161] op_sel_hi:[1,0,1]
	v_pk_fma_f32 v[158:159], v[22:23], s[2:3], v[158:159] op_sel_hi:[1,0,1]
	v_pk_fma_f32 v[156:157], v[24:25], s[2:3], v[156:157] op_sel_hi:[1,0,1]
	v_pk_fma_f32 v[154:155], v[26:27], s[2:3], v[154:155] op_sel_hi:[1,0,1]
	v_pk_fma_f32 v[152:153], v[28:29], s[2:3], v[152:153] op_sel_hi:[1,0,1]
	v_pk_fma_f32 v[150:151], v[30:31], s[2:3], v[150:151] op_sel_hi:[1,0,1]
	v_readlane_b32 s2, v211, 31
	s_waitcnt vmcnt(16)
	v_cvt_scalef32_pk32_f32_fp6 v[0:31], v[32:37], 1.0
	v_pk_fma_f32 v[164:165], v[0:1], s[2:3], v[38:39] op_sel_hi:[1,0,1]
	v_pk_fma_f32 v[166:167], v[2:3], s[2:3], v[40:41] op_sel_hi:[1,0,1]
	v_pk_fma_f32 v[168:169], v[4:5], s[2:3], v[42:43] op_sel_hi:[1,0,1]
	v_pk_fma_f32 v[170:171], v[6:7], s[2:3], v[50:51] op_sel_hi:[1,0,1]
	v_pk_fma_f32 v[172:173], v[8:9], s[2:3], v[52:53] op_sel_hi:[1,0,1]
	v_pk_fma_f32 v[174:175], v[10:11], s[2:3], v[54:55] op_sel_hi:[1,0,1]
	v_pk_fma_f32 v[176:177], v[12:13], s[2:3], v[62:63] op_sel_hi:[1,0,1]
	v_pk_fma_f32 v[178:179], v[14:15], s[2:3], v[64:65] op_sel_hi:[1,0,1]
	v_pk_fma_f32 v[180:181], v[16:17], s[2:3], v[66:67] op_sel_hi:[1,0,1]
	v_pk_fma_f32 v[162:163], v[18:19], s[2:3], v[162:163] op_sel_hi:[1,0,1]
	v_pk_fma_f32 v[160:161], v[20:21], s[2:3], v[160:161] op_sel_hi:[1,0,1]
	v_pk_fma_f32 v[158:159], v[22:23], s[2:3], v[158:159] op_sel_hi:[1,0,1]
	v_pk_fma_f32 v[156:157], v[24:25], s[2:3], v[156:157] op_sel_hi:[1,0,1]
	v_pk_fma_f32 v[154:155], v[26:27], s[2:3], v[154:155] op_sel_hi:[1,0,1]
	v_pk_fma_f32 v[152:153], v[28:29], s[2:3], v[152:153] op_sel_hi:[1,0,1]
	v_pk_fma_f32 v[150:151], v[30:31], s[2:3], v[150:151] op_sel_hi:[1,0,1]
	v_readlane_b32 s2, v240, 40
	v_readlane_b32 s3, v240, 41
	v_readlane_b32 s100, v240, 42
	v_readlane_b32 s101, v240, 43
	s_nop 1
	buffer_load_dwordx4 v[62:65], v129, s[44:47], s2 offen nt
	buffer_load_dwordx2 v[66:67], v210, s[44:47], s2 offen nt
	buffer_load_dwordx4 v[50:53], v129, s[44:47], s3 offen nt
	buffer_load_dwordx2 v[54:55], v210, s[44:47], s3 offen nt
	buffer_load_dwordx4 v[38:41], v129, s[44:47], s100 offen nt
	buffer_load_dwordx2 v[42:43], v210, s[44:47], s100 offen nt
	buffer_load_dwordx4 v[32:35], v129, s[44:47], s101 offen nt
	buffer_load_dwordx2 v[36:37], v210, s[44:47], s101 offen nt
	v_readlane_b32 s2, v211, 32
	s_waitcnt vmcnt(22)
	v_cvt_scalef32_pk32_f32_fp6 v[0:31], v[98:103], 1.0
	v_pk_fma_f32 v[98:99], v[0:1], s[2:3], v[164:165] op_sel_hi:[1,0,1]
	v_pk_fma_f32 v[100:101], v[2:3], s[2:3], v[166:167] op_sel_hi:[1,0,1]
	v_pk_fma_f32 v[102:103], v[4:5], s[2:3], v[168:169] op_sel_hi:[1,0,1]
	v_pk_fma_f32 v[164:165], v[6:7], s[2:3], v[170:171] op_sel_hi:[1,0,1]
	v_pk_fma_f32 v[166:167], v[8:9], s[2:3], v[172:173] op_sel_hi:[1,0,1]
	v_pk_fma_f32 v[168:169], v[10:11], s[2:3], v[174:175] op_sel_hi:[1,0,1]
	v_pk_fma_f32 v[170:171], v[12:13], s[2:3], v[176:177] op_sel_hi:[1,0,1]
	v_pk_fma_f32 v[172:173], v[14:15], s[2:3], v[178:179] op_sel_hi:[1,0,1]
	v_pk_fma_f32 v[174:175], v[16:17], s[2:3], v[180:181] op_sel_hi:[1,0,1]
	v_pk_fma_f32 v[162:163], v[18:19], s[2:3], v[162:163] op_sel_hi:[1,0,1]
	v_pk_fma_f32 v[160:161], v[20:21], s[2:3], v[160:161] op_sel_hi:[1,0,1]
	v_pk_fma_f32 v[158:159], v[22:23], s[2:3], v[158:159] op_sel_hi:[1,0,1]
	v_pk_fma_f32 v[156:157], v[24:25], s[2:3], v[156:157] op_sel_hi:[1,0,1]
	v_pk_fma_f32 v[154:155], v[26:27], s[2:3], v[154:155] op_sel_hi:[1,0,1]
	v_pk_fma_f32 v[152:153], v[28:29], s[2:3], v[152:153] op_sel_hi:[1,0,1]
	v_pk_fma_f32 v[150:151], v[30:31], s[2:3], v[150:151] op_sel_hi:[1,0,1]
	v_readlane_b32 s2, v211, 33
	s_waitcnt vmcnt(20)
	v_cvt_scalef32_pk32_f32_fp6 v[0:31], v[92:97], 1.0
	v_pk_fma_f32 v[92:93], v[0:1], s[2:3], v[98:99] op_sel_hi:[1,0,1]
	v_pk_fma_f32 v[94:95], v[2:3], s[2:3], v[100:101] op_sel_hi:[1,0,1]
	v_pk_fma_f32 v[96:97], v[4:5], s[2:3], v[102:103] op_sel_hi:[1,0,1]
	v_pk_fma_f32 v[98:99], v[6:7], s[2:3], v[164:165] op_sel_hi:[1,0,1]
	v_pk_fma_f32 v[100:101], v[8:9], s[2:3], v[166:167] op_sel_hi:[1,0,1]
	v_pk_fma_f32 v[102:103], v[10:11], s[2:3], v[168:169] op_sel_hi:[1,0,1]
	v_pk_fma_f32 v[164:165], v[12:13], s[2:3], v[170:171] op_sel_hi:[1,0,1]
	v_pk_fma_f32 v[166:167], v[14:15], s[2:3], v[172:173] op_sel_hi:[1,0,1]
	v_pk_fma_f32 v[168:169], v[16:17], s[2:3], v[174:175] op_sel_hi:[1,0,1]
	v_pk_fma_f32 v[162:163], v[18:19], s[2:3], v[162:163] op_sel_hi:[1,0,1]
	v_pk_fma_f32 v[160:161], v[20:21], s[2:3], v[160:161] op_sel_hi:[1,0,1]
	v_pk_fma_f32 v[158:159], v[22:23], s[2:3], v[158:159] op_sel_hi:[1,0,1]
	v_pk_fma_f32 v[156:157], v[24:25], s[2:3], v[156:157] op_sel_hi:[1,0,1]
	v_pk_fma_f32 v[154:155], v[26:27], s[2:3], v[154:155] op_sel_hi:[1,0,1]
	v_pk_fma_f32 v[152:153], v[28:29], s[2:3], v[152:153] op_sel_hi:[1,0,1]
	v_pk_fma_f32 v[150:151], v[30:31], s[2:3], v[150:151] op_sel_hi:[1,0,1]
	v_readlane_b32 s2, v211, 34
	s_waitcnt vmcnt(18)
	v_cvt_scalef32_pk32_f32_fp6 v[0:31], v[86:91], 1.0
	v_pk_fma_f32 v[86:87], v[0:1], s[2:3], v[92:93] op_sel_hi:[1,0,1]
	v_pk_fma_f32 v[88:89], v[2:3], s[2:3], v[94:95] op_sel_hi:[1,0,1]
	v_pk_fma_f32 v[90:91], v[4:5], s[2:3], v[96:97] op_sel_hi:[1,0,1]
	v_pk_fma_f32 v[92:93], v[6:7], s[2:3], v[98:99] op_sel_hi:[1,0,1]
	v_pk_fma_f32 v[94:95], v[8:9], s[2:3], v[100:101] op_sel_hi:[1,0,1]
	v_pk_fma_f32 v[96:97], v[10:11], s[2:3], v[102:103] op_sel_hi:[1,0,1]
	v_pk_fma_f32 v[98:99], v[12:13], s[2:3], v[164:165] op_sel_hi:[1,0,1]
	v_pk_fma_f32 v[100:101], v[14:15], s[2:3], v[166:167] op_sel_hi:[1,0,1]
	v_pk_fma_f32 v[102:103], v[16:17], s[2:3], v[168:169] op_sel_hi:[1,0,1]
	v_pk_fma_f32 v[162:163], v[18:19], s[2:3], v[162:163] op_sel_hi:[1,0,1]
	v_pk_fma_f32 v[160:161], v[20:21], s[2:3], v[160:161] op_sel_hi:[1,0,1]
	v_pk_fma_f32 v[158:159], v[22:23], s[2:3], v[158:159] op_sel_hi:[1,0,1]
	v_pk_fma_f32 v[156:157], v[24:25], s[2:3], v[156:157] op_sel_hi:[1,0,1]
	v_pk_fma_f32 v[154:155], v[26:27], s[2:3], v[154:155] op_sel_hi:[1,0,1]
	v_pk_fma_f32 v[152:153], v[28:29], s[2:3], v[152:153] op_sel_hi:[1,0,1]
	v_pk_fma_f32 v[150:151], v[30:31], s[2:3], v[150:151] op_sel_hi:[1,0,1]
	v_readlane_b32 s2, v211, 35
	s_waitcnt vmcnt(16)
	v_cvt_scalef32_pk32_f32_fp6 v[0:31], v[80:85], 1.0
	v_pk_fma_f32 v[180:181], v[0:1], s[2:3], v[86:87] op_sel_hi:[1,0,1]
	v_pk_fma_f32 v[178:179], v[2:3], s[2:3], v[88:89] op_sel_hi:[1,0,1]
	v_pk_fma_f32 v[176:177], v[4:5], s[2:3], v[90:91] op_sel_hi:[1,0,1]
	v_pk_fma_f32 v[174:175], v[6:7], s[2:3], v[92:93] op_sel_hi:[1,0,1]
	v_pk_fma_f32 v[172:173], v[8:9], s[2:3], v[94:95] op_sel_hi:[1,0,1]
	v_pk_fma_f32 v[170:171], v[10:11], s[2:3], v[96:97] op_sel_hi:[1,0,1]
	v_pk_fma_f32 v[168:169], v[12:13], s[2:3], v[98:99] op_sel_hi:[1,0,1]
	v_pk_fma_f32 v[166:167], v[14:15], s[2:3], v[100:101] op_sel_hi:[1,0,1]
	v_pk_fma_f32 v[164:165], v[16:17], s[2:3], v[102:103] op_sel_hi:[1,0,1]
	v_pk_fma_f32 v[162:163], v[18:19], s[2:3], v[162:163] op_sel_hi:[1,0,1]
	v_pk_fma_f32 v[160:161], v[20:21], s[2:3], v[160:161] op_sel_hi:[1,0,1]
	v_pk_fma_f32 v[158:159], v[22:23], s[2:3], v[158:159] op_sel_hi:[1,0,1]
	v_pk_fma_f32 v[156:157], v[24:25], s[2:3], v[156:157] op_sel_hi:[1,0,1]
	v_pk_fma_f32 v[154:155], v[26:27], s[2:3], v[154:155] op_sel_hi:[1,0,1]
	v_pk_fma_f32 v[152:153], v[28:29], s[2:3], v[152:153] op_sel_hi:[1,0,1]
	v_pk_fma_f32 v[150:151], v[30:31], s[2:3], v[150:151] op_sel_hi:[1,0,1]
	v_readlane_b32 s2, v240, 44
	v_readlane_b32 s3, v240, 45
	v_readlane_b32 s100, v240, 46
	v_readlane_b32 s101, v240, 47
	s_nop 1
	buffer_load_dwordx4 v[98:101], v129, s[44:47], s2 offen nt
	buffer_load_dwordx2 v[102:103], v210, s[44:47], s2 offen nt
	buffer_load_dwordx4 v[92:95], v129, s[44:47], s3 offen nt
	buffer_load_dwordx2 v[96:97], v210, s[44:47], s3 offen nt
	buffer_load_dwordx4 v[86:89], v129, s[44:47], s100 offen nt
	buffer_load_dwordx2 v[90:91], v210, s[44:47], s100 offen nt
	buffer_load_dwordx4 v[80:83], v129, s[44:47], s101 offen nt
	buffer_load_dwordx2 v[84:85], v210, s[44:47], s101 offen nt
	v_readlane_b32 s2, v211, 36
	s_waitcnt vmcnt(22)
	v_cvt_scalef32_pk32_f32_fp6 v[0:31], v[74:79], 1.0
	v_pk_fma_f32 v[74:75], v[0:1], s[2:3], v[180:181] op_sel_hi:[1,0,1]
	v_pk_fma_f32 v[76:77], v[2:3], s[2:3], v[178:179] op_sel_hi:[1,0,1]
	v_pk_fma_f32 v[78:79], v[4:5], s[2:3], v[176:177] op_sel_hi:[1,0,1]
	v_pk_fma_f32 v[174:175], v[6:7], s[2:3], v[174:175] op_sel_hi:[1,0,1]
	v_pk_fma_f32 v[172:173], v[8:9], s[2:3], v[172:173] op_sel_hi:[1,0,1]
	v_pk_fma_f32 v[170:171], v[10:11], s[2:3], v[170:171] op_sel_hi:[1,0,1]
	v_pk_fma_f32 v[168:169], v[12:13], s[2:3], v[168:169] op_sel_hi:[1,0,1]
	v_pk_fma_f32 v[166:167], v[14:15], s[2:3], v[166:167] op_sel_hi:[1,0,1]
	v_pk_fma_f32 v[164:165], v[16:17], s[2:3], v[164:165] op_sel_hi:[1,0,1]
	v_pk_fma_f32 v[162:163], v[18:19], s[2:3], v[162:163] op_sel_hi:[1,0,1]
	v_pk_fma_f32 v[160:161], v[20:21], s[2:3], v[160:161] op_sel_hi:[1,0,1]
	v_pk_fma_f32 v[158:159], v[22:23], s[2:3], v[158:159] op_sel_hi:[1,0,1]
	v_pk_fma_f32 v[156:157], v[24:25], s[2:3], v[156:157] op_sel_hi:[1,0,1]
	v_pk_fma_f32 v[154:155], v[26:27], s[2:3], v[154:155] op_sel_hi:[1,0,1]
	v_pk_fma_f32 v[152:153], v[28:29], s[2:3], v[152:153] op_sel_hi:[1,0,1]
	v_pk_fma_f32 v[150:151], v[30:31], s[2:3], v[150:151] op_sel_hi:[1,0,1]
	v_readlane_b32 s2, v211, 37
	s_waitcnt vmcnt(20)
	v_cvt_scalef32_pk32_f32_fp6 v[0:31], v[68:73], 1.0
	v_pk_fma_f32 v[68:69], v[0:1], s[2:3], v[74:75] op_sel_hi:[1,0,1]
	v_pk_fma_f32 v[70:71], v[2:3], s[2:3], v[76:77] op_sel_hi:[1,0,1]
	v_pk_fma_f32 v[72:73], v[4:5], s[2:3], v[78:79] op_sel_hi:[1,0,1]
	v_pk_fma_f32 v[74:75], v[6:7], s[2:3], v[174:175] op_sel_hi:[1,0,1]
	v_pk_fma_f32 v[76:77], v[8:9], s[2:3], v[172:173] op_sel_hi:[1,0,1]
	v_pk_fma_f32 v[78:79], v[10:11], s[2:3], v[170:171] op_sel_hi:[1,0,1]
	v_pk_fma_f32 v[168:169], v[12:13], s[2:3], v[168:169] op_sel_hi:[1,0,1]
	v_pk_fma_f32 v[166:167], v[14:15], s[2:3], v[166:167] op_sel_hi:[1,0,1]
	v_pk_fma_f32 v[164:165], v[16:17], s[2:3], v[164:165] op_sel_hi:[1,0,1]
	v_pk_fma_f32 v[162:163], v[18:19], s[2:3], v[162:163] op_sel_hi:[1,0,1]
	v_pk_fma_f32 v[160:161], v[20:21], s[2:3], v[160:161] op_sel_hi:[1,0,1]
	v_pk_fma_f32 v[158:159], v[22:23], s[2:3], v[158:159] op_sel_hi:[1,0,1]
	v_pk_fma_f32 v[156:157], v[24:25], s[2:3], v[156:157] op_sel_hi:[1,0,1]
	v_pk_fma_f32 v[154:155], v[26:27], s[2:3], v[154:155] op_sel_hi:[1,0,1]
	v_pk_fma_f32 v[152:153], v[28:29], s[2:3], v[152:153] op_sel_hi:[1,0,1]
	v_pk_fma_f32 v[150:151], v[30:31], s[2:3], v[150:151] op_sel_hi:[1,0,1]
	v_readlane_b32 s2, v211, 38
	s_waitcnt vmcnt(18)
	v_cvt_scalef32_pk32_f32_fp6 v[0:31], v[56:61], 1.0
	v_pk_fma_f32 v[56:57], v[0:1], s[2:3], v[68:69] op_sel_hi:[1,0,1]
	v_pk_fma_f32 v[58:59], v[2:3], s[2:3], v[70:71] op_sel_hi:[1,0,1]
	v_pk_fma_f32 v[60:61], v[4:5], s[2:3], v[72:73] op_sel_hi:[1,0,1]
	v_pk_fma_f32 v[68:69], v[6:7], s[2:3], v[74:75] op_sel_hi:[1,0,1]
	v_pk_fma_f32 v[70:71], v[8:9], s[2:3], v[76:77] op_sel_hi:[1,0,1]
	v_pk_fma_f32 v[72:73], v[10:11], s[2:3], v[78:79] op_sel_hi:[1,0,1]
	v_pk_fma_f32 v[74:75], v[12:13], s[2:3], v[168:169] op_sel_hi:[1,0,1]
	v_pk_fma_f32 v[76:77], v[14:15], s[2:3], v[166:167] op_sel_hi:[1,0,1]
	v_pk_fma_f32 v[78:79], v[16:17], s[2:3], v[164:165] op_sel_hi:[1,0,1]
	v_pk_fma_f32 v[162:163], v[18:19], s[2:3], v[162:163] op_sel_hi:[1,0,1]
	v_pk_fma_f32 v[160:161], v[20:21], s[2:3], v[160:161] op_sel_hi:[1,0,1]
	v_pk_fma_f32 v[158:159], v[22:23], s[2:3], v[158:159] op_sel_hi:[1,0,1]
	v_pk_fma_f32 v[156:157], v[24:25], s[2:3], v[156:157] op_sel_hi:[1,0,1]
	v_pk_fma_f32 v[154:155], v[26:27], s[2:3], v[154:155] op_sel_hi:[1,0,1]
	v_pk_fma_f32 v[152:153], v[28:29], s[2:3], v[152:153] op_sel_hi:[1,0,1]
	v_pk_fma_f32 v[150:151], v[30:31], s[2:3], v[150:151] op_sel_hi:[1,0,1]
	v_readlane_b32 s2, v211, 39
	s_waitcnt vmcnt(16)
	v_cvt_scalef32_pk32_f32_fp6 v[0:31], v[44:49], 1.0
	v_pk_fma_f32 v[164:165], v[0:1], s[2:3], v[56:57] op_sel_hi:[1,0,1]
	v_pk_fma_f32 v[166:167], v[2:3], s[2:3], v[58:59] op_sel_hi:[1,0,1]
	v_pk_fma_f32 v[168:169], v[4:5], s[2:3], v[60:61] op_sel_hi:[1,0,1]
	v_pk_fma_f32 v[170:171], v[6:7], s[2:3], v[68:69] op_sel_hi:[1,0,1]
	v_pk_fma_f32 v[172:173], v[8:9], s[2:3], v[70:71] op_sel_hi:[1,0,1]
	v_pk_fma_f32 v[174:175], v[10:11], s[2:3], v[72:73] op_sel_hi:[1,0,1]
	v_pk_fma_f32 v[176:177], v[12:13], s[2:3], v[74:75] op_sel_hi:[1,0,1]
	v_pk_fma_f32 v[178:179], v[14:15], s[2:3], v[76:77] op_sel_hi:[1,0,1]
	v_pk_fma_f32 v[180:181], v[16:17], s[2:3], v[78:79] op_sel_hi:[1,0,1]
	v_pk_fma_f32 v[162:163], v[18:19], s[2:3], v[162:163] op_sel_hi:[1,0,1]
	v_pk_fma_f32 v[160:161], v[20:21], s[2:3], v[160:161] op_sel_hi:[1,0,1]
	v_pk_fma_f32 v[158:159], v[22:23], s[2:3], v[158:159] op_sel_hi:[1,0,1]
	v_pk_fma_f32 v[156:157], v[24:25], s[2:3], v[156:157] op_sel_hi:[1,0,1]
	v_pk_fma_f32 v[154:155], v[26:27], s[2:3], v[154:155] op_sel_hi:[1,0,1]
	v_pk_fma_f32 v[152:153], v[28:29], s[2:3], v[152:153] op_sel_hi:[1,0,1]
	v_pk_fma_f32 v[150:151], v[30:31], s[2:3], v[150:151] op_sel_hi:[1,0,1]
	v_readlane_b32 s2, v240, 48
	v_readlane_b32 s3, v240, 49
	v_readlane_b32 s100, v240, 50
	v_readlane_b32 s101, v240, 51
	s_nop 1
	buffer_load_dwordx4 v[74:77], v129, s[44:47], s2 offen nt
	buffer_load_dwordx2 v[78:79], v210, s[44:47], s2 offen nt
	buffer_load_dwordx4 v[68:71], v129, s[44:47], s3 offen nt
	buffer_load_dwordx2 v[72:73], v210, s[44:47], s3 offen nt
	buffer_load_dwordx4 v[56:59], v129, s[44:47], s100 offen nt
	buffer_load_dwordx2 v[60:61], v210, s[44:47], s100 offen nt
	buffer_load_dwordx4 v[44:47], v129, s[44:47], s101 offen nt
	buffer_load_dwordx2 v[48:49], v210, s[44:47], s101 offen nt
	v_readlane_b32 s2, v211, 40
	s_waitcnt vmcnt(22)
	v_cvt_scalef32_pk32_f32_fp6 v[0:31], v[62:67], 1.0
	v_pk_fma_f32 v[62:63], v[0:1], s[2:3], v[164:165] op_sel_hi:[1,0,1]
	v_pk_fma_f32 v[64:65], v[2:3], s[2:3], v[166:167] op_sel_hi:[1,0,1]
	v_pk_fma_f32 v[66:67], v[4:5], s[2:3], v[168:169] op_sel_hi:[1,0,1]
	v_pk_fma_f32 v[164:165], v[6:7], s[2:3], v[170:171] op_sel_hi:[1,0,1]
	v_pk_fma_f32 v[166:167], v[8:9], s[2:3], v[172:173] op_sel_hi:[1,0,1]
	v_pk_fma_f32 v[168:169], v[10:11], s[2:3], v[174:175] op_sel_hi:[1,0,1]
	v_pk_fma_f32 v[170:171], v[12:13], s[2:3], v[176:177] op_sel_hi:[1,0,1]
	v_pk_fma_f32 v[172:173], v[14:15], s[2:3], v[178:179] op_sel_hi:[1,0,1]
	v_pk_fma_f32 v[174:175], v[16:17], s[2:3], v[180:181] op_sel_hi:[1,0,1]
	v_pk_fma_f32 v[162:163], v[18:19], s[2:3], v[162:163] op_sel_hi:[1,0,1]
	v_pk_fma_f32 v[160:161], v[20:21], s[2:3], v[160:161] op_sel_hi:[1,0,1]
	v_pk_fma_f32 v[158:159], v[22:23], s[2:3], v[158:159] op_sel_hi:[1,0,1]
	v_pk_fma_f32 v[156:157], v[24:25], s[2:3], v[156:157] op_sel_hi:[1,0,1]
	v_pk_fma_f32 v[154:155], v[26:27], s[2:3], v[154:155] op_sel_hi:[1,0,1]
	v_pk_fma_f32 v[152:153], v[28:29], s[2:3], v[152:153] op_sel_hi:[1,0,1]
	v_pk_fma_f32 v[150:151], v[30:31], s[2:3], v[150:151] op_sel_hi:[1,0,1]
	v_readlane_b32 s2, v211, 41
	s_waitcnt vmcnt(20)
	v_cvt_scalef32_pk32_f32_fp6 v[0:31], v[50:55], 1.0
	v_pk_fma_f32 v[50:51], v[0:1], s[2:3], v[62:63] op_sel_hi:[1,0,1]
	v_pk_fma_f32 v[52:53], v[2:3], s[2:3], v[64:65] op_sel_hi:[1,0,1]
	v_pk_fma_f32 v[54:55], v[4:5], s[2:3], v[66:67] op_sel_hi:[1,0,1]
	v_pk_fma_f32 v[62:63], v[6:7], s[2:3], v[164:165] op_sel_hi:[1,0,1]
	v_pk_fma_f32 v[64:65], v[8:9], s[2:3], v[166:167] op_sel_hi:[1,0,1]
	v_pk_fma_f32 v[66:67], v[10:11], s[2:3], v[168:169] op_sel_hi:[1,0,1]
	v_pk_fma_f32 v[164:165], v[12:13], s[2:3], v[170:171] op_sel_hi:[1,0,1]
	v_pk_fma_f32 v[166:167], v[14:15], s[2:3], v[172:173] op_sel_hi:[1,0,1]
	v_pk_fma_f32 v[168:169], v[16:17], s[2:3], v[174:175] op_sel_hi:[1,0,1]
	v_pk_fma_f32 v[162:163], v[18:19], s[2:3], v[162:163] op_sel_hi:[1,0,1]
	v_pk_fma_f32 v[160:161], v[20:21], s[2:3], v[160:161] op_sel_hi:[1,0,1]
	v_pk_fma_f32 v[158:159], v[22:23], s[2:3], v[158:159] op_sel_hi:[1,0,1]
	v_pk_fma_f32 v[156:157], v[24:25], s[2:3], v[156:157] op_sel_hi:[1,0,1]
	v_pk_fma_f32 v[154:155], v[26:27], s[2:3], v[154:155] op_sel_hi:[1,0,1]
	v_pk_fma_f32 v[152:153], v[28:29], s[2:3], v[152:153] op_sel_hi:[1,0,1]
	v_pk_fma_f32 v[150:151], v[30:31], s[2:3], v[150:151] op_sel_hi:[1,0,1]
	v_readlane_b32 s2, v211, 42
	s_waitcnt vmcnt(18)
	v_cvt_scalef32_pk32_f32_fp6 v[0:31], v[38:43], 1.0
	v_pk_fma_f32 v[38:39], v[0:1], s[2:3], v[50:51] op_sel_hi:[1,0,1]
	v_pk_fma_f32 v[40:41], v[2:3], s[2:3], v[52:53] op_sel_hi:[1,0,1]
	v_pk_fma_f32 v[42:43], v[4:5], s[2:3], v[54:55] op_sel_hi:[1,0,1]
	v_pk_fma_f32 v[50:51], v[6:7], s[2:3], v[62:63] op_sel_hi:[1,0,1]
	v_pk_fma_f32 v[52:53], v[8:9], s[2:3], v[64:65] op_sel_hi:[1,0,1]
	v_pk_fma_f32 v[54:55], v[10:11], s[2:3], v[66:67] op_sel_hi:[1,0,1]
	v_pk_fma_f32 v[62:63], v[12:13], s[2:3], v[164:165] op_sel_hi:[1,0,1]
	v_pk_fma_f32 v[64:65], v[14:15], s[2:3], v[166:167] op_sel_hi:[1,0,1]
	v_pk_fma_f32 v[66:67], v[16:17], s[2:3], v[168:169] op_sel_hi:[1,0,1]
	v_pk_fma_f32 v[162:163], v[18:19], s[2:3], v[162:163] op_sel_hi:[1,0,1]
	v_pk_fma_f32 v[160:161], v[20:21], s[2:3], v[160:161] op_sel_hi:[1,0,1]
	v_pk_fma_f32 v[158:159], v[22:23], s[2:3], v[158:159] op_sel_hi:[1,0,1]
	v_pk_fma_f32 v[156:157], v[24:25], s[2:3], v[156:157] op_sel_hi:[1,0,1]
	v_pk_fma_f32 v[154:155], v[26:27], s[2:3], v[154:155] op_sel_hi:[1,0,1]
	v_pk_fma_f32 v[152:153], v[28:29], s[2:3], v[152:153] op_sel_hi:[1,0,1]
	v_pk_fma_f32 v[150:151], v[30:31], s[2:3], v[150:151] op_sel_hi:[1,0,1]
	v_readlane_b32 s2, v211, 43
	s_waitcnt vmcnt(16)
	v_cvt_scalef32_pk32_f32_fp6 v[0:31], v[32:37], 1.0
	v_pk_fma_f32 v[164:165], v[0:1], s[2:3], v[38:39] op_sel_hi:[1,0,1]
	v_pk_fma_f32 v[166:167], v[2:3], s[2:3], v[40:41] op_sel_hi:[1,0,1]
	v_pk_fma_f32 v[168:169], v[4:5], s[2:3], v[42:43] op_sel_hi:[1,0,1]
	v_pk_fma_f32 v[170:171], v[6:7], s[2:3], v[50:51] op_sel_hi:[1,0,1]
	v_pk_fma_f32 v[172:173], v[8:9], s[2:3], v[52:53] op_sel_hi:[1,0,1]
	v_pk_fma_f32 v[174:175], v[10:11], s[2:3], v[54:55] op_sel_hi:[1,0,1]
	v_pk_fma_f32 v[176:177], v[12:13], s[2:3], v[62:63] op_sel_hi:[1,0,1]
	v_pk_fma_f32 v[178:179], v[14:15], s[2:3], v[64:65] op_sel_hi:[1,0,1]
	v_pk_fma_f32 v[180:181], v[16:17], s[2:3], v[66:67] op_sel_hi:[1,0,1]
	v_pk_fma_f32 v[162:163], v[18:19], s[2:3], v[162:163] op_sel_hi:[1,0,1]
	v_pk_fma_f32 v[160:161], v[20:21], s[2:3], v[160:161] op_sel_hi:[1,0,1]
	v_pk_fma_f32 v[158:159], v[22:23], s[2:3], v[158:159] op_sel_hi:[1,0,1]
	v_pk_fma_f32 v[156:157], v[24:25], s[2:3], v[156:157] op_sel_hi:[1,0,1]
	v_pk_fma_f32 v[154:155], v[26:27], s[2:3], v[154:155] op_sel_hi:[1,0,1]
	v_pk_fma_f32 v[152:153], v[28:29], s[2:3], v[152:153] op_sel_hi:[1,0,1]
	v_pk_fma_f32 v[150:151], v[30:31], s[2:3], v[150:151] op_sel_hi:[1,0,1]
	v_readlane_b32 s2, v240, 52
	v_readlane_b32 s3, v240, 53
	v_readlane_b32 s100, v240, 54
	v_readlane_b32 s101, v240, 55
	s_nop 1
	buffer_load_dwordx4 v[62:65], v129, s[44:47], s2 offen nt
	buffer_load_dwordx2 v[66:67], v210, s[44:47], s2 offen nt
	buffer_load_dwordx4 v[50:53], v129, s[44:47], s3 offen nt
	buffer_load_dwordx2 v[54:55], v210, s[44:47], s3 offen nt
	buffer_load_dwordx4 v[38:41], v129, s[44:47], s100 offen nt
	buffer_load_dwordx2 v[42:43], v210, s[44:47], s100 offen nt
	buffer_load_dwordx4 v[32:35], v129, s[44:47], s101 offen nt
	buffer_load_dwordx2 v[36:37], v210, s[44:47], s101 offen nt
	v_readlane_b32 s2, v211, 44
	s_waitcnt vmcnt(22)
	v_cvt_scalef32_pk32_f32_fp6 v[0:31], v[98:103], 1.0
	v_pk_fma_f32 v[98:99], v[0:1], s[2:3], v[164:165] op_sel_hi:[1,0,1]
	v_pk_fma_f32 v[100:101], v[2:3], s[2:3], v[166:167] op_sel_hi:[1,0,1]
	v_pk_fma_f32 v[102:103], v[4:5], s[2:3], v[168:169] op_sel_hi:[1,0,1]
	v_pk_fma_f32 v[164:165], v[6:7], s[2:3], v[170:171] op_sel_hi:[1,0,1]
	v_pk_fma_f32 v[166:167], v[8:9], s[2:3], v[172:173] op_sel_hi:[1,0,1]
	v_pk_fma_f32 v[168:169], v[10:11], s[2:3], v[174:175] op_sel_hi:[1,0,1]
	v_pk_fma_f32 v[170:171], v[12:13], s[2:3], v[176:177] op_sel_hi:[1,0,1]
	v_pk_fma_f32 v[172:173], v[14:15], s[2:3], v[178:179] op_sel_hi:[1,0,1]
	v_pk_fma_f32 v[174:175], v[16:17], s[2:3], v[180:181] op_sel_hi:[1,0,1]
	v_pk_fma_f32 v[162:163], v[18:19], s[2:3], v[162:163] op_sel_hi:[1,0,1]
	v_pk_fma_f32 v[160:161], v[20:21], s[2:3], v[160:161] op_sel_hi:[1,0,1]
	v_pk_fma_f32 v[158:159], v[22:23], s[2:3], v[158:159] op_sel_hi:[1,0,1]
	v_pk_fma_f32 v[156:157], v[24:25], s[2:3], v[156:157] op_sel_hi:[1,0,1]
	v_pk_fma_f32 v[154:155], v[26:27], s[2:3], v[154:155] op_sel_hi:[1,0,1]
	v_pk_fma_f32 v[152:153], v[28:29], s[2:3], v[152:153] op_sel_hi:[1,0,1]
	v_pk_fma_f32 v[150:151], v[30:31], s[2:3], v[150:151] op_sel_hi:[1,0,1]
	v_readlane_b32 s2, v211, 45
	s_waitcnt vmcnt(20)
	v_cvt_scalef32_pk32_f32_fp6 v[0:31], v[92:97], 1.0
	v_pk_fma_f32 v[92:93], v[0:1], s[2:3], v[98:99] op_sel_hi:[1,0,1]
	v_pk_fma_f32 v[94:95], v[2:3], s[2:3], v[100:101] op_sel_hi:[1,0,1]
	v_pk_fma_f32 v[96:97], v[4:5], s[2:3], v[102:103] op_sel_hi:[1,0,1]
	v_pk_fma_f32 v[98:99], v[6:7], s[2:3], v[164:165] op_sel_hi:[1,0,1]
	v_pk_fma_f32 v[100:101], v[8:9], s[2:3], v[166:167] op_sel_hi:[1,0,1]
	v_pk_fma_f32 v[102:103], v[10:11], s[2:3], v[168:169] op_sel_hi:[1,0,1]
	v_pk_fma_f32 v[164:165], v[12:13], s[2:3], v[170:171] op_sel_hi:[1,0,1]
	v_pk_fma_f32 v[166:167], v[14:15], s[2:3], v[172:173] op_sel_hi:[1,0,1]
	v_pk_fma_f32 v[168:169], v[16:17], s[2:3], v[174:175] op_sel_hi:[1,0,1]
	v_pk_fma_f32 v[162:163], v[18:19], s[2:3], v[162:163] op_sel_hi:[1,0,1]
	v_pk_fma_f32 v[160:161], v[20:21], s[2:3], v[160:161] op_sel_hi:[1,0,1]
	v_pk_fma_f32 v[158:159], v[22:23], s[2:3], v[158:159] op_sel_hi:[1,0,1]
	v_pk_fma_f32 v[156:157], v[24:25], s[2:3], v[156:157] op_sel_hi:[1,0,1]
	v_pk_fma_f32 v[154:155], v[26:27], s[2:3], v[154:155] op_sel_hi:[1,0,1]
	v_pk_fma_f32 v[152:153], v[28:29], s[2:3], v[152:153] op_sel_hi:[1,0,1]
	v_pk_fma_f32 v[150:151], v[30:31], s[2:3], v[150:151] op_sel_hi:[1,0,1]
	v_readlane_b32 s2, v211, 46
	s_waitcnt vmcnt(18)
	v_cvt_scalef32_pk32_f32_fp6 v[0:31], v[86:91], 1.0
	v_pk_fma_f32 v[86:87], v[0:1], s[2:3], v[92:93] op_sel_hi:[1,0,1]
	v_pk_fma_f32 v[88:89], v[2:3], s[2:3], v[94:95] op_sel_hi:[1,0,1]
	v_pk_fma_f32 v[90:91], v[4:5], s[2:3], v[96:97] op_sel_hi:[1,0,1]
	v_pk_fma_f32 v[92:93], v[6:7], s[2:3], v[98:99] op_sel_hi:[1,0,1]
	v_pk_fma_f32 v[94:95], v[8:9], s[2:3], v[100:101] op_sel_hi:[1,0,1]
	v_pk_fma_f32 v[96:97], v[10:11], s[2:3], v[102:103] op_sel_hi:[1,0,1]
	v_pk_fma_f32 v[98:99], v[12:13], s[2:3], v[164:165] op_sel_hi:[1,0,1]
	v_pk_fma_f32 v[100:101], v[14:15], s[2:3], v[166:167] op_sel_hi:[1,0,1]
	v_pk_fma_f32 v[102:103], v[16:17], s[2:3], v[168:169] op_sel_hi:[1,0,1]
	v_pk_fma_f32 v[162:163], v[18:19], s[2:3], v[162:163] op_sel_hi:[1,0,1]
	v_pk_fma_f32 v[160:161], v[20:21], s[2:3], v[160:161] op_sel_hi:[1,0,1]
	v_pk_fma_f32 v[158:159], v[22:23], s[2:3], v[158:159] op_sel_hi:[1,0,1]
	v_pk_fma_f32 v[156:157], v[24:25], s[2:3], v[156:157] op_sel_hi:[1,0,1]
	v_pk_fma_f32 v[154:155], v[26:27], s[2:3], v[154:155] op_sel_hi:[1,0,1]
	v_pk_fma_f32 v[152:153], v[28:29], s[2:3], v[152:153] op_sel_hi:[1,0,1]
	v_pk_fma_f32 v[150:151], v[30:31], s[2:3], v[150:151] op_sel_hi:[1,0,1]
	v_readlane_b32 s2, v211, 47
	s_waitcnt vmcnt(16)
	v_cvt_scalef32_pk32_f32_fp6 v[0:31], v[80:85], 1.0
	v_pk_fma_f32 v[180:181], v[0:1], s[2:3], v[86:87] op_sel_hi:[1,0,1]
	v_pk_fma_f32 v[178:179], v[2:3], s[2:3], v[88:89] op_sel_hi:[1,0,1]
	v_pk_fma_f32 v[176:177], v[4:5], s[2:3], v[90:91] op_sel_hi:[1,0,1]
	v_pk_fma_f32 v[174:175], v[6:7], s[2:3], v[92:93] op_sel_hi:[1,0,1]
	v_pk_fma_f32 v[172:173], v[8:9], s[2:3], v[94:95] op_sel_hi:[1,0,1]
	v_pk_fma_f32 v[170:171], v[10:11], s[2:3], v[96:97] op_sel_hi:[1,0,1]
	v_pk_fma_f32 v[168:169], v[12:13], s[2:3], v[98:99] op_sel_hi:[1,0,1]
	v_pk_fma_f32 v[166:167], v[14:15], s[2:3], v[100:101] op_sel_hi:[1,0,1]
	v_pk_fma_f32 v[164:165], v[16:17], s[2:3], v[102:103] op_sel_hi:[1,0,1]
	v_pk_fma_f32 v[162:163], v[18:19], s[2:3], v[162:163] op_sel_hi:[1,0,1]
	v_pk_fma_f32 v[160:161], v[20:21], s[2:3], v[160:161] op_sel_hi:[1,0,1]
	v_pk_fma_f32 v[158:159], v[22:23], s[2:3], v[158:159] op_sel_hi:[1,0,1]
	v_pk_fma_f32 v[156:157], v[24:25], s[2:3], v[156:157] op_sel_hi:[1,0,1]
	v_pk_fma_f32 v[154:155], v[26:27], s[2:3], v[154:155] op_sel_hi:[1,0,1]
	v_pk_fma_f32 v[152:153], v[28:29], s[2:3], v[152:153] op_sel_hi:[1,0,1]
	v_pk_fma_f32 v[150:151], v[30:31], s[2:3], v[150:151] op_sel_hi:[1,0,1]
	v_readlane_b32 s2, v240, 56
	v_readlane_b32 s3, v240, 57
	v_readlane_b32 s100, v240, 58
	v_readlane_b32 s101, v240, 59
	s_nop 1
	buffer_load_dwordx4 v[98:101], v129, s[44:47], s2 offen nt
	buffer_load_dwordx2 v[102:103], v210, s[44:47], s2 offen nt
	buffer_load_dwordx4 v[92:95], v129, s[44:47], s3 offen nt
	buffer_load_dwordx2 v[96:97], v210, s[44:47], s3 offen nt
	buffer_load_dwordx4 v[86:89], v129, s[44:47], s100 offen nt
	buffer_load_dwordx2 v[90:91], v210, s[44:47], s100 offen nt
	buffer_load_dwordx4 v[80:83], v129, s[44:47], s101 offen nt
	buffer_load_dwordx2 v[84:85], v210, s[44:47], s101 offen nt
	v_readlane_b32 s2, v211, 48
	s_waitcnt vmcnt(22)
	v_cvt_scalef32_pk32_f32_fp6 v[0:31], v[74:79], 1.0
	v_pk_fma_f32 v[74:75], v[0:1], s[2:3], v[180:181] op_sel_hi:[1,0,1]
	v_pk_fma_f32 v[76:77], v[2:3], s[2:3], v[178:179] op_sel_hi:[1,0,1]
	v_pk_fma_f32 v[78:79], v[4:5], s[2:3], v[176:177] op_sel_hi:[1,0,1]
	v_pk_fma_f32 v[174:175], v[6:7], s[2:3], v[174:175] op_sel_hi:[1,0,1]
	v_pk_fma_f32 v[172:173], v[8:9], s[2:3], v[172:173] op_sel_hi:[1,0,1]
	v_pk_fma_f32 v[170:171], v[10:11], s[2:3], v[170:171] op_sel_hi:[1,0,1]
	v_pk_fma_f32 v[168:169], v[12:13], s[2:3], v[168:169] op_sel_hi:[1,0,1]
	v_pk_fma_f32 v[166:167], v[14:15], s[2:3], v[166:167] op_sel_hi:[1,0,1]
	v_pk_fma_f32 v[164:165], v[16:17], s[2:3], v[164:165] op_sel_hi:[1,0,1]
	v_pk_fma_f32 v[162:163], v[18:19], s[2:3], v[162:163] op_sel_hi:[1,0,1]
	v_pk_fma_f32 v[160:161], v[20:21], s[2:3], v[160:161] op_sel_hi:[1,0,1]
	v_pk_fma_f32 v[158:159], v[22:23], s[2:3], v[158:159] op_sel_hi:[1,0,1]
	v_pk_fma_f32 v[156:157], v[24:25], s[2:3], v[156:157] op_sel_hi:[1,0,1]
	v_pk_fma_f32 v[154:155], v[26:27], s[2:3], v[154:155] op_sel_hi:[1,0,1]
	v_pk_fma_f32 v[152:153], v[28:29], s[2:3], v[152:153] op_sel_hi:[1,0,1]
	v_pk_fma_f32 v[150:151], v[30:31], s[2:3], v[150:151] op_sel_hi:[1,0,1]
	v_readlane_b32 s2, v211, 49
	s_waitcnt vmcnt(20)
	v_cvt_scalef32_pk32_f32_fp6 v[0:31], v[68:73], 1.0
	v_pk_fma_f32 v[68:69], v[0:1], s[2:3], v[74:75] op_sel_hi:[1,0,1]
	v_pk_fma_f32 v[70:71], v[2:3], s[2:3], v[76:77] op_sel_hi:[1,0,1]
	v_pk_fma_f32 v[72:73], v[4:5], s[2:3], v[78:79] op_sel_hi:[1,0,1]
	v_pk_fma_f32 v[74:75], v[6:7], s[2:3], v[174:175] op_sel_hi:[1,0,1]
	v_pk_fma_f32 v[76:77], v[8:9], s[2:3], v[172:173] op_sel_hi:[1,0,1]
	v_pk_fma_f32 v[78:79], v[10:11], s[2:3], v[170:171] op_sel_hi:[1,0,1]
	v_pk_fma_f32 v[168:169], v[12:13], s[2:3], v[168:169] op_sel_hi:[1,0,1]
	v_pk_fma_f32 v[166:167], v[14:15], s[2:3], v[166:167] op_sel_hi:[1,0,1]
	v_pk_fma_f32 v[164:165], v[16:17], s[2:3], v[164:165] op_sel_hi:[1,0,1]
	v_pk_fma_f32 v[162:163], v[18:19], s[2:3], v[162:163] op_sel_hi:[1,0,1]
	v_pk_fma_f32 v[160:161], v[20:21], s[2:3], v[160:161] op_sel_hi:[1,0,1]
	v_pk_fma_f32 v[158:159], v[22:23], s[2:3], v[158:159] op_sel_hi:[1,0,1]
	v_pk_fma_f32 v[156:157], v[24:25], s[2:3], v[156:157] op_sel_hi:[1,0,1]
	v_pk_fma_f32 v[154:155], v[26:27], s[2:3], v[154:155] op_sel_hi:[1,0,1]
	v_pk_fma_f32 v[152:153], v[28:29], s[2:3], v[152:153] op_sel_hi:[1,0,1]
	v_pk_fma_f32 v[150:151], v[30:31], s[2:3], v[150:151] op_sel_hi:[1,0,1]
	v_readlane_b32 s2, v211, 50
	s_waitcnt vmcnt(18)
	v_cvt_scalef32_pk32_f32_fp6 v[0:31], v[56:61], 1.0
	v_pk_fma_f32 v[56:57], v[0:1], s[2:3], v[68:69] op_sel_hi:[1,0,1]
	v_pk_fma_f32 v[58:59], v[2:3], s[2:3], v[70:71] op_sel_hi:[1,0,1]
	v_pk_fma_f32 v[60:61], v[4:5], s[2:3], v[72:73] op_sel_hi:[1,0,1]
	v_pk_fma_f32 v[68:69], v[6:7], s[2:3], v[74:75] op_sel_hi:[1,0,1]
	v_pk_fma_f32 v[70:71], v[8:9], s[2:3], v[76:77] op_sel_hi:[1,0,1]
	v_pk_fma_f32 v[72:73], v[10:11], s[2:3], v[78:79] op_sel_hi:[1,0,1]
	v_pk_fma_f32 v[74:75], v[12:13], s[2:3], v[168:169] op_sel_hi:[1,0,1]
	v_pk_fma_f32 v[76:77], v[14:15], s[2:3], v[166:167] op_sel_hi:[1,0,1]
	v_pk_fma_f32 v[78:79], v[16:17], s[2:3], v[164:165] op_sel_hi:[1,0,1]
	v_pk_fma_f32 v[162:163], v[18:19], s[2:3], v[162:163] op_sel_hi:[1,0,1]
	v_pk_fma_f32 v[160:161], v[20:21], s[2:3], v[160:161] op_sel_hi:[1,0,1]
	v_pk_fma_f32 v[158:159], v[22:23], s[2:3], v[158:159] op_sel_hi:[1,0,1]
	v_pk_fma_f32 v[156:157], v[24:25], s[2:3], v[156:157] op_sel_hi:[1,0,1]
	v_pk_fma_f32 v[154:155], v[26:27], s[2:3], v[154:155] op_sel_hi:[1,0,1]
	v_pk_fma_f32 v[152:153], v[28:29], s[2:3], v[152:153] op_sel_hi:[1,0,1]
	v_pk_fma_f32 v[150:151], v[30:31], s[2:3], v[150:151] op_sel_hi:[1,0,1]
	v_readlane_b32 s2, v211, 51
	s_waitcnt vmcnt(16)
	v_cvt_scalef32_pk32_f32_fp6 v[0:31], v[44:49], 1.0
	v_pk_fma_f32 v[164:165], v[0:1], s[2:3], v[56:57] op_sel_hi:[1,0,1]
	v_pk_fma_f32 v[166:167], v[2:3], s[2:3], v[58:59] op_sel_hi:[1,0,1]
	v_pk_fma_f32 v[168:169], v[4:5], s[2:3], v[60:61] op_sel_hi:[1,0,1]
	v_pk_fma_f32 v[170:171], v[6:7], s[2:3], v[68:69] op_sel_hi:[1,0,1]
	v_pk_fma_f32 v[172:173], v[8:9], s[2:3], v[70:71] op_sel_hi:[1,0,1]
	v_pk_fma_f32 v[174:175], v[10:11], s[2:3], v[72:73] op_sel_hi:[1,0,1]
	v_pk_fma_f32 v[176:177], v[12:13], s[2:3], v[74:75] op_sel_hi:[1,0,1]
	v_pk_fma_f32 v[178:179], v[14:15], s[2:3], v[76:77] op_sel_hi:[1,0,1]
	v_pk_fma_f32 v[180:181], v[16:17], s[2:3], v[78:79] op_sel_hi:[1,0,1]
	v_pk_fma_f32 v[162:163], v[18:19], s[2:3], v[162:163] op_sel_hi:[1,0,1]
	v_pk_fma_f32 v[160:161], v[20:21], s[2:3], v[160:161] op_sel_hi:[1,0,1]
	v_pk_fma_f32 v[158:159], v[22:23], s[2:3], v[158:159] op_sel_hi:[1,0,1]
	v_pk_fma_f32 v[156:157], v[24:25], s[2:3], v[156:157] op_sel_hi:[1,0,1]
	v_pk_fma_f32 v[154:155], v[26:27], s[2:3], v[154:155] op_sel_hi:[1,0,1]
	v_pk_fma_f32 v[152:153], v[28:29], s[2:3], v[152:153] op_sel_hi:[1,0,1]
	v_pk_fma_f32 v[150:151], v[30:31], s[2:3], v[150:151] op_sel_hi:[1,0,1]
	v_readlane_b32 s2, v240, 60
	v_readlane_b32 s3, v240, 61
	v_readlane_b32 s100, v240, 62
	v_readlane_b32 s101, v240, 63
	s_nop 1
	buffer_load_dwordx4 v[74:77], v129, s[44:47], s2 offen nt
	buffer_load_dwordx2 v[78:79], v210, s[44:47], s2 offen nt
	buffer_load_dwordx4 v[68:71], v129, s[44:47], s3 offen nt
	buffer_load_dwordx2 v[72:73], v210, s[44:47], s3 offen nt
	buffer_load_dwordx4 v[56:59], v129, s[44:47], s100 offen nt
	buffer_load_dwordx2 v[60:61], v210, s[44:47], s100 offen nt
	buffer_load_dwordx4 v[44:47], v129, s[44:47], s101 offen nt
	buffer_load_dwordx2 v[48:49], v210, s[44:47], s101 offen nt
	v_readlane_b32 s2, v211, 52
	s_waitcnt vmcnt(22)
	v_cvt_scalef32_pk32_f32_fp6 v[0:31], v[62:67], 1.0
	v_pk_fma_f32 v[62:63], v[0:1], s[2:3], v[164:165] op_sel_hi:[1,0,1]
	v_pk_fma_f32 v[64:65], v[2:3], s[2:3], v[166:167] op_sel_hi:[1,0,1]
	v_pk_fma_f32 v[66:67], v[4:5], s[2:3], v[168:169] op_sel_hi:[1,0,1]
	v_pk_fma_f32 v[164:165], v[6:7], s[2:3], v[170:171] op_sel_hi:[1,0,1]
	v_pk_fma_f32 v[166:167], v[8:9], s[2:3], v[172:173] op_sel_hi:[1,0,1]
	v_pk_fma_f32 v[168:169], v[10:11], s[2:3], v[174:175] op_sel_hi:[1,0,1]
	v_pk_fma_f32 v[170:171], v[12:13], s[2:3], v[176:177] op_sel_hi:[1,0,1]
	v_pk_fma_f32 v[172:173], v[14:15], s[2:3], v[178:179] op_sel_hi:[1,0,1]
	v_pk_fma_f32 v[174:175], v[16:17], s[2:3], v[180:181] op_sel_hi:[1,0,1]
	v_pk_fma_f32 v[162:163], v[18:19], s[2:3], v[162:163] op_sel_hi:[1,0,1]
	v_pk_fma_f32 v[160:161], v[20:21], s[2:3], v[160:161] op_sel_hi:[1,0,1]
	v_pk_fma_f32 v[158:159], v[22:23], s[2:3], v[158:159] op_sel_hi:[1,0,1]
	v_pk_fma_f32 v[156:157], v[24:25], s[2:3], v[156:157] op_sel_hi:[1,0,1]
	v_pk_fma_f32 v[154:155], v[26:27], s[2:3], v[154:155] op_sel_hi:[1,0,1]
	v_pk_fma_f32 v[152:153], v[28:29], s[2:3], v[152:153] op_sel_hi:[1,0,1]
	v_pk_fma_f32 v[150:151], v[30:31], s[2:3], v[150:151] op_sel_hi:[1,0,1]
	v_readlane_b32 s2, v211, 53
	s_waitcnt vmcnt(20)
	v_cvt_scalef32_pk32_f32_fp6 v[0:31], v[50:55], 1.0
	v_pk_fma_f32 v[50:51], v[0:1], s[2:3], v[62:63] op_sel_hi:[1,0,1]
	v_pk_fma_f32 v[52:53], v[2:3], s[2:3], v[64:65] op_sel_hi:[1,0,1]
	v_pk_fma_f32 v[54:55], v[4:5], s[2:3], v[66:67] op_sel_hi:[1,0,1]
	v_pk_fma_f32 v[62:63], v[6:7], s[2:3], v[164:165] op_sel_hi:[1,0,1]
	v_pk_fma_f32 v[64:65], v[8:9], s[2:3], v[166:167] op_sel_hi:[1,0,1]
	v_pk_fma_f32 v[66:67], v[10:11], s[2:3], v[168:169] op_sel_hi:[1,0,1]
	v_pk_fma_f32 v[164:165], v[12:13], s[2:3], v[170:171] op_sel_hi:[1,0,1]
	v_pk_fma_f32 v[166:167], v[14:15], s[2:3], v[172:173] op_sel_hi:[1,0,1]
	v_pk_fma_f32 v[168:169], v[16:17], s[2:3], v[174:175] op_sel_hi:[1,0,1]
	v_pk_fma_f32 v[162:163], v[18:19], s[2:3], v[162:163] op_sel_hi:[1,0,1]
	v_pk_fma_f32 v[160:161], v[20:21], s[2:3], v[160:161] op_sel_hi:[1,0,1]
	v_pk_fma_f32 v[158:159], v[22:23], s[2:3], v[158:159] op_sel_hi:[1,0,1]
	v_pk_fma_f32 v[156:157], v[24:25], s[2:3], v[156:157] op_sel_hi:[1,0,1]
	v_pk_fma_f32 v[154:155], v[26:27], s[2:3], v[154:155] op_sel_hi:[1,0,1]
	v_pk_fma_f32 v[152:153], v[28:29], s[2:3], v[152:153] op_sel_hi:[1,0,1]
	v_pk_fma_f32 v[150:151], v[30:31], s[2:3], v[150:151] op_sel_hi:[1,0,1]
	v_readlane_b32 s2, v211, 54
	s_waitcnt vmcnt(18)
	v_cvt_scalef32_pk32_f32_fp6 v[0:31], v[38:43], 1.0
	v_pk_fma_f32 v[38:39], v[0:1], s[2:3], v[50:51] op_sel_hi:[1,0,1]
	v_pk_fma_f32 v[40:41], v[2:3], s[2:3], v[52:53] op_sel_hi:[1,0,1]
	v_pk_fma_f32 v[42:43], v[4:5], s[2:3], v[54:55] op_sel_hi:[1,0,1]
	v_pk_fma_f32 v[50:51], v[6:7], s[2:3], v[62:63] op_sel_hi:[1,0,1]
	v_pk_fma_f32 v[52:53], v[8:9], s[2:3], v[64:65] op_sel_hi:[1,0,1]
	v_pk_fma_f32 v[54:55], v[10:11], s[2:3], v[66:67] op_sel_hi:[1,0,1]
	v_pk_fma_f32 v[62:63], v[12:13], s[2:3], v[164:165] op_sel_hi:[1,0,1]
	v_pk_fma_f32 v[64:65], v[14:15], s[2:3], v[166:167] op_sel_hi:[1,0,1]
	v_pk_fma_f32 v[66:67], v[16:17], s[2:3], v[168:169] op_sel_hi:[1,0,1]
	v_pk_fma_f32 v[162:163], v[18:19], s[2:3], v[162:163] op_sel_hi:[1,0,1]
	v_pk_fma_f32 v[160:161], v[20:21], s[2:3], v[160:161] op_sel_hi:[1,0,1]
	v_pk_fma_f32 v[158:159], v[22:23], s[2:3], v[158:159] op_sel_hi:[1,0,1]
	v_pk_fma_f32 v[156:157], v[24:25], s[2:3], v[156:157] op_sel_hi:[1,0,1]
	v_pk_fma_f32 v[154:155], v[26:27], s[2:3], v[154:155] op_sel_hi:[1,0,1]
	v_pk_fma_f32 v[152:153], v[28:29], s[2:3], v[152:153] op_sel_hi:[1,0,1]
	v_pk_fma_f32 v[150:151], v[30:31], s[2:3], v[150:151] op_sel_hi:[1,0,1]
	v_readlane_b32 s2, v211, 55
	s_waitcnt vmcnt(16)
	v_cvt_scalef32_pk32_f32_fp6 v[0:31], v[32:37], 1.0
	v_pk_fma_f32 v[164:165], v[0:1], s[2:3], v[38:39] op_sel_hi:[1,0,1]
	v_pk_fma_f32 v[166:167], v[2:3], s[2:3], v[40:41] op_sel_hi:[1,0,1]
	v_pk_fma_f32 v[168:169], v[4:5], s[2:3], v[42:43] op_sel_hi:[1,0,1]
	v_pk_fma_f32 v[170:171], v[6:7], s[2:3], v[50:51] op_sel_hi:[1,0,1]
	v_pk_fma_f32 v[172:173], v[8:9], s[2:3], v[52:53] op_sel_hi:[1,0,1]
	v_pk_fma_f32 v[174:175], v[10:11], s[2:3], v[54:55] op_sel_hi:[1,0,1]
	v_pk_fma_f32 v[176:177], v[12:13], s[2:3], v[62:63] op_sel_hi:[1,0,1]
	v_pk_fma_f32 v[178:179], v[14:15], s[2:3], v[64:65] op_sel_hi:[1,0,1]
	v_pk_fma_f32 v[180:181], v[16:17], s[2:3], v[66:67] op_sel_hi:[1,0,1]
	v_pk_fma_f32 v[162:163], v[18:19], s[2:3], v[162:163] op_sel_hi:[1,0,1]
	v_pk_fma_f32 v[160:161], v[20:21], s[2:3], v[160:161] op_sel_hi:[1,0,1]
	v_pk_fma_f32 v[158:159], v[22:23], s[2:3], v[158:159] op_sel_hi:[1,0,1]
	v_pk_fma_f32 v[156:157], v[24:25], s[2:3], v[156:157] op_sel_hi:[1,0,1]
	v_pk_fma_f32 v[154:155], v[26:27], s[2:3], v[154:155] op_sel_hi:[1,0,1]
	v_pk_fma_f32 v[152:153], v[28:29], s[2:3], v[152:153] op_sel_hi:[1,0,1]
	v_pk_fma_f32 v[150:151], v[30:31], s[2:3], v[150:151] op_sel_hi:[1,0,1]
	v_readlane_b32 s2, v241, 0
	v_readlane_b32 s3, v241, 1
	v_readlane_b32 s100, v241, 2
	v_readlane_b32 s101, v241, 3
	s_nop 1
	buffer_load_dwordx4 v[62:65], v129, s[44:47], s2 offen nt
	buffer_load_dwordx2 v[66:67], v210, s[44:47], s2 offen nt
	buffer_load_dwordx4 v[50:53], v129, s[44:47], s3 offen nt
	buffer_load_dwordx2 v[54:55], v210, s[44:47], s3 offen nt
	buffer_load_dwordx4 v[38:41], v129, s[44:47], s100 offen nt
	buffer_load_dwordx2 v[42:43], v210, s[44:47], s100 offen nt
	buffer_load_dwordx4 v[32:35], v129, s[44:47], s101 offen nt
	buffer_load_dwordx2 v[36:37], v210, s[44:47], s101 offen nt
	v_readlane_b32 s2, v211, 56
	s_waitcnt vmcnt(22)
	v_cvt_scalef32_pk32_f32_fp6 v[0:31], v[98:103], 1.0
	v_pk_fma_f32 v[98:99], v[0:1], s[2:3], v[164:165] op_sel_hi:[1,0,1]
	v_pk_fma_f32 v[100:101], v[2:3], s[2:3], v[166:167] op_sel_hi:[1,0,1]
	v_pk_fma_f32 v[102:103], v[4:5], s[2:3], v[168:169] op_sel_hi:[1,0,1]
	v_pk_fma_f32 v[164:165], v[6:7], s[2:3], v[170:171] op_sel_hi:[1,0,1]
	v_pk_fma_f32 v[166:167], v[8:9], s[2:3], v[172:173] op_sel_hi:[1,0,1]
	v_pk_fma_f32 v[168:169], v[10:11], s[2:3], v[174:175] op_sel_hi:[1,0,1]
	v_pk_fma_f32 v[170:171], v[12:13], s[2:3], v[176:177] op_sel_hi:[1,0,1]
	v_pk_fma_f32 v[172:173], v[14:15], s[2:3], v[178:179] op_sel_hi:[1,0,1]
	v_pk_fma_f32 v[174:175], v[16:17], s[2:3], v[180:181] op_sel_hi:[1,0,1]
	v_pk_fma_f32 v[162:163], v[18:19], s[2:3], v[162:163] op_sel_hi:[1,0,1]
	v_pk_fma_f32 v[160:161], v[20:21], s[2:3], v[160:161] op_sel_hi:[1,0,1]
	v_pk_fma_f32 v[158:159], v[22:23], s[2:3], v[158:159] op_sel_hi:[1,0,1]
	v_pk_fma_f32 v[156:157], v[24:25], s[2:3], v[156:157] op_sel_hi:[1,0,1]
	v_pk_fma_f32 v[154:155], v[26:27], s[2:3], v[154:155] op_sel_hi:[1,0,1]
	v_pk_fma_f32 v[152:153], v[28:29], s[2:3], v[152:153] op_sel_hi:[1,0,1]
	v_pk_fma_f32 v[150:151], v[30:31], s[2:3], v[150:151] op_sel_hi:[1,0,1]
	v_readlane_b32 s2, v211, 57
	s_waitcnt vmcnt(20)
	v_cvt_scalef32_pk32_f32_fp6 v[0:31], v[92:97], 1.0
	v_pk_fma_f32 v[92:93], v[0:1], s[2:3], v[98:99] op_sel_hi:[1,0,1]
	v_pk_fma_f32 v[94:95], v[2:3], s[2:3], v[100:101] op_sel_hi:[1,0,1]
	v_pk_fma_f32 v[96:97], v[4:5], s[2:3], v[102:103] op_sel_hi:[1,0,1]
	v_pk_fma_f32 v[98:99], v[6:7], s[2:3], v[164:165] op_sel_hi:[1,0,1]
	v_pk_fma_f32 v[100:101], v[8:9], s[2:3], v[166:167] op_sel_hi:[1,0,1]
	v_pk_fma_f32 v[102:103], v[10:11], s[2:3], v[168:169] op_sel_hi:[1,0,1]
	v_pk_fma_f32 v[164:165], v[12:13], s[2:3], v[170:171] op_sel_hi:[1,0,1]
	v_pk_fma_f32 v[166:167], v[14:15], s[2:3], v[172:173] op_sel_hi:[1,0,1]
	v_pk_fma_f32 v[168:169], v[16:17], s[2:3], v[174:175] op_sel_hi:[1,0,1]
	v_pk_fma_f32 v[162:163], v[18:19], s[2:3], v[162:163] op_sel_hi:[1,0,1]
	v_pk_fma_f32 v[160:161], v[20:21], s[2:3], v[160:161] op_sel_hi:[1,0,1]
	v_pk_fma_f32 v[158:159], v[22:23], s[2:3], v[158:159] op_sel_hi:[1,0,1]
	v_pk_fma_f32 v[156:157], v[24:25], s[2:3], v[156:157] op_sel_hi:[1,0,1]
	v_pk_fma_f32 v[154:155], v[26:27], s[2:3], v[154:155] op_sel_hi:[1,0,1]
	v_pk_fma_f32 v[152:153], v[28:29], s[2:3], v[152:153] op_sel_hi:[1,0,1]
	v_pk_fma_f32 v[150:151], v[30:31], s[2:3], v[150:151] op_sel_hi:[1,0,1]
	v_readlane_b32 s2, v211, 58
	s_waitcnt vmcnt(18)
	v_cvt_scalef32_pk32_f32_fp6 v[0:31], v[86:91], 1.0
	v_pk_fma_f32 v[86:87], v[0:1], s[2:3], v[92:93] op_sel_hi:[1,0,1]
	v_pk_fma_f32 v[88:89], v[2:3], s[2:3], v[94:95] op_sel_hi:[1,0,1]
	v_pk_fma_f32 v[90:91], v[4:5], s[2:3], v[96:97] op_sel_hi:[1,0,1]
	v_pk_fma_f32 v[92:93], v[6:7], s[2:3], v[98:99] op_sel_hi:[1,0,1]
	v_pk_fma_f32 v[94:95], v[8:9], s[2:3], v[100:101] op_sel_hi:[1,0,1]
	v_pk_fma_f32 v[96:97], v[10:11], s[2:3], v[102:103] op_sel_hi:[1,0,1]
	v_pk_fma_f32 v[98:99], v[12:13], s[2:3], v[164:165] op_sel_hi:[1,0,1]
	v_pk_fma_f32 v[100:101], v[14:15], s[2:3], v[166:167] op_sel_hi:[1,0,1]
	v_pk_fma_f32 v[102:103], v[16:17], s[2:3], v[168:169] op_sel_hi:[1,0,1]
	v_pk_fma_f32 v[162:163], v[18:19], s[2:3], v[162:163] op_sel_hi:[1,0,1]
	v_pk_fma_f32 v[160:161], v[20:21], s[2:3], v[160:161] op_sel_hi:[1,0,1]
	v_pk_fma_f32 v[158:159], v[22:23], s[2:3], v[158:159] op_sel_hi:[1,0,1]
	v_pk_fma_f32 v[156:157], v[24:25], s[2:3], v[156:157] op_sel_hi:[1,0,1]
	v_pk_fma_f32 v[154:155], v[26:27], s[2:3], v[154:155] op_sel_hi:[1,0,1]
	v_pk_fma_f32 v[152:153], v[28:29], s[2:3], v[152:153] op_sel_hi:[1,0,1]
	v_pk_fma_f32 v[150:151], v[30:31], s[2:3], v[150:151] op_sel_hi:[1,0,1]
	v_readlane_b32 s2, v211, 59
	s_waitcnt vmcnt(16)
	v_cvt_scalef32_pk32_f32_fp6 v[0:31], v[80:85], 1.0
	v_pk_fma_f32 v[180:181], v[0:1], s[2:3], v[86:87] op_sel_hi:[1,0,1]
	v_pk_fma_f32 v[178:179], v[2:3], s[2:3], v[88:89] op_sel_hi:[1,0,1]
	v_pk_fma_f32 v[176:177], v[4:5], s[2:3], v[90:91] op_sel_hi:[1,0,1]
	v_pk_fma_f32 v[174:175], v[6:7], s[2:3], v[92:93] op_sel_hi:[1,0,1]
	v_pk_fma_f32 v[172:173], v[8:9], s[2:3], v[94:95] op_sel_hi:[1,0,1]
	v_pk_fma_f32 v[170:171], v[10:11], s[2:3], v[96:97] op_sel_hi:[1,0,1]
	v_pk_fma_f32 v[168:169], v[12:13], s[2:3], v[98:99] op_sel_hi:[1,0,1]
	v_pk_fma_f32 v[166:167], v[14:15], s[2:3], v[100:101] op_sel_hi:[1,0,1]
	v_pk_fma_f32 v[164:165], v[16:17], s[2:3], v[102:103] op_sel_hi:[1,0,1]
	v_pk_fma_f32 v[162:163], v[18:19], s[2:3], v[162:163] op_sel_hi:[1,0,1]
	v_pk_fma_f32 v[160:161], v[20:21], s[2:3], v[160:161] op_sel_hi:[1,0,1]
	v_pk_fma_f32 v[158:159], v[22:23], s[2:3], v[158:159] op_sel_hi:[1,0,1]
	v_pk_fma_f32 v[156:157], v[24:25], s[2:3], v[156:157] op_sel_hi:[1,0,1]
	v_pk_fma_f32 v[154:155], v[26:27], s[2:3], v[154:155] op_sel_hi:[1,0,1]
	v_pk_fma_f32 v[152:153], v[28:29], s[2:3], v[152:153] op_sel_hi:[1,0,1]
	v_pk_fma_f32 v[150:151], v[30:31], s[2:3], v[150:151] op_sel_hi:[1,0,1]
	v_readlane_b32 s2, v241, 4
	v_readlane_b32 s3, v241, 5
	v_readlane_b32 s100, v241, 6
	v_readlane_b32 s101, v241, 7
	s_nop 1
	buffer_load_dwordx4 v[98:101], v129, s[44:47], s2 offen nt
	buffer_load_dwordx2 v[102:103], v210, s[44:47], s2 offen nt
	buffer_load_dwordx4 v[92:95], v129, s[44:47], s3 offen nt
	buffer_load_dwordx2 v[96:97], v210, s[44:47], s3 offen nt
	buffer_load_dwordx4 v[86:89], v129, s[44:47], s100 offen nt
	buffer_load_dwordx2 v[90:91], v210, s[44:47], s100 offen nt
	buffer_load_dwordx4 v[80:83], v129, s[44:47], s101 offen nt
	buffer_load_dwordx2 v[84:85], v210, s[44:47], s101 offen nt
	v_readlane_b32 s2, v211, 60
	s_waitcnt vmcnt(22)
	v_cvt_scalef32_pk32_f32_fp6 v[0:31], v[74:79], 1.0
	v_pk_fma_f32 v[74:75], v[0:1], s[2:3], v[180:181] op_sel_hi:[1,0,1]
	v_pk_fma_f32 v[76:77], v[2:3], s[2:3], v[178:179] op_sel_hi:[1,0,1]
	v_pk_fma_f32 v[78:79], v[4:5], s[2:3], v[176:177] op_sel_hi:[1,0,1]
	v_pk_fma_f32 v[174:175], v[6:7], s[2:3], v[174:175] op_sel_hi:[1,0,1]
	v_pk_fma_f32 v[172:173], v[8:9], s[2:3], v[172:173] op_sel_hi:[1,0,1]
	v_pk_fma_f32 v[170:171], v[10:11], s[2:3], v[170:171] op_sel_hi:[1,0,1]
	v_pk_fma_f32 v[168:169], v[12:13], s[2:3], v[168:169] op_sel_hi:[1,0,1]
	v_pk_fma_f32 v[166:167], v[14:15], s[2:3], v[166:167] op_sel_hi:[1,0,1]
	v_pk_fma_f32 v[164:165], v[16:17], s[2:3], v[164:165] op_sel_hi:[1,0,1]
	v_pk_fma_f32 v[162:163], v[18:19], s[2:3], v[162:163] op_sel_hi:[1,0,1]
	v_pk_fma_f32 v[160:161], v[20:21], s[2:3], v[160:161] op_sel_hi:[1,0,1]
	v_pk_fma_f32 v[158:159], v[22:23], s[2:3], v[158:159] op_sel_hi:[1,0,1]
	v_pk_fma_f32 v[156:157], v[24:25], s[2:3], v[156:157] op_sel_hi:[1,0,1]
	v_pk_fma_f32 v[154:155], v[26:27], s[2:3], v[154:155] op_sel_hi:[1,0,1]
	v_pk_fma_f32 v[152:153], v[28:29], s[2:3], v[152:153] op_sel_hi:[1,0,1]
	v_pk_fma_f32 v[150:151], v[30:31], s[2:3], v[150:151] op_sel_hi:[1,0,1]
	v_readlane_b32 s2, v211, 61
	s_waitcnt vmcnt(20)
	v_cvt_scalef32_pk32_f32_fp6 v[0:31], v[68:73], 1.0
	v_pk_fma_f32 v[68:69], v[0:1], s[2:3], v[74:75] op_sel_hi:[1,0,1]
	v_pk_fma_f32 v[70:71], v[2:3], s[2:3], v[76:77] op_sel_hi:[1,0,1]
	v_pk_fma_f32 v[72:73], v[4:5], s[2:3], v[78:79] op_sel_hi:[1,0,1]
	v_pk_fma_f32 v[74:75], v[6:7], s[2:3], v[174:175] op_sel_hi:[1,0,1]
	v_pk_fma_f32 v[76:77], v[8:9], s[2:3], v[172:173] op_sel_hi:[1,0,1]
	v_pk_fma_f32 v[78:79], v[10:11], s[2:3], v[170:171] op_sel_hi:[1,0,1]
	v_pk_fma_f32 v[168:169], v[12:13], s[2:3], v[168:169] op_sel_hi:[1,0,1]
	v_pk_fma_f32 v[166:167], v[14:15], s[2:3], v[166:167] op_sel_hi:[1,0,1]
	v_pk_fma_f32 v[164:165], v[16:17], s[2:3], v[164:165] op_sel_hi:[1,0,1]
	v_pk_fma_f32 v[162:163], v[18:19], s[2:3], v[162:163] op_sel_hi:[1,0,1]
	v_pk_fma_f32 v[160:161], v[20:21], s[2:3], v[160:161] op_sel_hi:[1,0,1]
	v_pk_fma_f32 v[158:159], v[22:23], s[2:3], v[158:159] op_sel_hi:[1,0,1]
	v_pk_fma_f32 v[156:157], v[24:25], s[2:3], v[156:157] op_sel_hi:[1,0,1]
	v_pk_fma_f32 v[154:155], v[26:27], s[2:3], v[154:155] op_sel_hi:[1,0,1]
	v_pk_fma_f32 v[152:153], v[28:29], s[2:3], v[152:153] op_sel_hi:[1,0,1]
	v_pk_fma_f32 v[150:151], v[30:31], s[2:3], v[150:151] op_sel_hi:[1,0,1]
	v_readlane_b32 s2, v211, 62
	s_waitcnt vmcnt(18)
	v_cvt_scalef32_pk32_f32_fp6 v[0:31], v[56:61], 1.0
	v_pk_fma_f32 v[56:57], v[0:1], s[2:3], v[68:69] op_sel_hi:[1,0,1]
	v_pk_fma_f32 v[58:59], v[2:3], s[2:3], v[70:71] op_sel_hi:[1,0,1]
	v_pk_fma_f32 v[60:61], v[4:5], s[2:3], v[72:73] op_sel_hi:[1,0,1]
	v_pk_fma_f32 v[68:69], v[6:7], s[2:3], v[74:75] op_sel_hi:[1,0,1]
	v_pk_fma_f32 v[70:71], v[8:9], s[2:3], v[76:77] op_sel_hi:[1,0,1]
	v_pk_fma_f32 v[72:73], v[10:11], s[2:3], v[78:79] op_sel_hi:[1,0,1]
	v_pk_fma_f32 v[74:75], v[12:13], s[2:3], v[168:169] op_sel_hi:[1,0,1]
	v_pk_fma_f32 v[76:77], v[14:15], s[2:3], v[166:167] op_sel_hi:[1,0,1]
	v_pk_fma_f32 v[78:79], v[16:17], s[2:3], v[164:165] op_sel_hi:[1,0,1]
	v_pk_fma_f32 v[162:163], v[18:19], s[2:3], v[162:163] op_sel_hi:[1,0,1]
	v_pk_fma_f32 v[160:161], v[20:21], s[2:3], v[160:161] op_sel_hi:[1,0,1]
	v_pk_fma_f32 v[158:159], v[22:23], s[2:3], v[158:159] op_sel_hi:[1,0,1]
	v_pk_fma_f32 v[156:157], v[24:25], s[2:3], v[156:157] op_sel_hi:[1,0,1]
	v_pk_fma_f32 v[154:155], v[26:27], s[2:3], v[154:155] op_sel_hi:[1,0,1]
	v_pk_fma_f32 v[152:153], v[28:29], s[2:3], v[152:153] op_sel_hi:[1,0,1]
	v_pk_fma_f32 v[150:151], v[30:31], s[2:3], v[150:151] op_sel_hi:[1,0,1]
	v_readlane_b32 s2, v211, 63
	s_waitcnt vmcnt(16)
	v_cvt_scalef32_pk32_f32_fp6 v[0:31], v[44:49], 1.0
	v_pk_fma_f32 v[164:165], v[0:1], s[2:3], v[56:57] op_sel_hi:[1,0,1]
	v_pk_fma_f32 v[166:167], v[2:3], s[2:3], v[58:59] op_sel_hi:[1,0,1]
	v_pk_fma_f32 v[168:169], v[4:5], s[2:3], v[60:61] op_sel_hi:[1,0,1]
	v_pk_fma_f32 v[170:171], v[6:7], s[2:3], v[68:69] op_sel_hi:[1,0,1]
	v_pk_fma_f32 v[172:173], v[8:9], s[2:3], v[70:71] op_sel_hi:[1,0,1]
	v_pk_fma_f32 v[174:175], v[10:11], s[2:3], v[72:73] op_sel_hi:[1,0,1]
	v_pk_fma_f32 v[176:177], v[12:13], s[2:3], v[74:75] op_sel_hi:[1,0,1]
	v_pk_fma_f32 v[178:179], v[14:15], s[2:3], v[76:77] op_sel_hi:[1,0,1]
	v_pk_fma_f32 v[180:181], v[16:17], s[2:3], v[78:79] op_sel_hi:[1,0,1]
	v_pk_fma_f32 v[162:163], v[18:19], s[2:3], v[162:163] op_sel_hi:[1,0,1]
	v_pk_fma_f32 v[160:161], v[20:21], s[2:3], v[160:161] op_sel_hi:[1,0,1]
	v_pk_fma_f32 v[158:159], v[22:23], s[2:3], v[158:159] op_sel_hi:[1,0,1]
	v_pk_fma_f32 v[156:157], v[24:25], s[2:3], v[156:157] op_sel_hi:[1,0,1]
	v_pk_fma_f32 v[154:155], v[26:27], s[2:3], v[154:155] op_sel_hi:[1,0,1]
	v_pk_fma_f32 v[152:153], v[28:29], s[2:3], v[152:153] op_sel_hi:[1,0,1]
	v_pk_fma_f32 v[150:151], v[30:31], s[2:3], v[150:151] op_sel_hi:[1,0,1]
	v_readlane_b32 s2, v241, 8
	v_readlane_b32 s3, v241, 9
	v_readlane_b32 s100, v241, 10
	v_readlane_b32 s101, v241, 11
	s_nop 1
	buffer_load_dwordx4 v[74:77], v129, s[44:47], s2 offen nt
	buffer_load_dwordx2 v[78:79], v210, s[44:47], s2 offen nt
	buffer_load_dwordx4 v[68:71], v129, s[44:47], s3 offen nt
	buffer_load_dwordx2 v[72:73], v210, s[44:47], s3 offen nt
	buffer_load_dwordx4 v[56:59], v129, s[44:47], s100 offen nt
	buffer_load_dwordx2 v[60:61], v210, s[44:47], s100 offen nt
	buffer_load_dwordx4 v[44:47], v129, s[44:47], s101 offen nt
	buffer_load_dwordx2 v[48:49], v210, s[44:47], s101 offen nt
	v_readlane_b32 s2, v131, 0
	s_waitcnt vmcnt(22)
	v_cvt_scalef32_pk32_f32_fp6 v[0:31], v[62:67], 1.0
	v_pk_fma_f32 v[62:63], v[0:1], s[2:3], v[164:165] op_sel_hi:[1,0,1]
	v_pk_fma_f32 v[64:65], v[2:3], s[2:3], v[166:167] op_sel_hi:[1,0,1]
	v_pk_fma_f32 v[66:67], v[4:5], s[2:3], v[168:169] op_sel_hi:[1,0,1]
	v_pk_fma_f32 v[164:165], v[6:7], s[2:3], v[170:171] op_sel_hi:[1,0,1]
	v_pk_fma_f32 v[166:167], v[8:9], s[2:3], v[172:173] op_sel_hi:[1,0,1]
	v_pk_fma_f32 v[168:169], v[10:11], s[2:3], v[174:175] op_sel_hi:[1,0,1]
	v_pk_fma_f32 v[170:171], v[12:13], s[2:3], v[176:177] op_sel_hi:[1,0,1]
	v_pk_fma_f32 v[172:173], v[14:15], s[2:3], v[178:179] op_sel_hi:[1,0,1]
	v_pk_fma_f32 v[174:175], v[16:17], s[2:3], v[180:181] op_sel_hi:[1,0,1]
	v_pk_fma_f32 v[162:163], v[18:19], s[2:3], v[162:163] op_sel_hi:[1,0,1]
	v_pk_fma_f32 v[160:161], v[20:21], s[2:3], v[160:161] op_sel_hi:[1,0,1]
	v_pk_fma_f32 v[158:159], v[22:23], s[2:3], v[158:159] op_sel_hi:[1,0,1]
	v_pk_fma_f32 v[156:157], v[24:25], s[2:3], v[156:157] op_sel_hi:[1,0,1]
	v_pk_fma_f32 v[154:155], v[26:27], s[2:3], v[154:155] op_sel_hi:[1,0,1]
	v_pk_fma_f32 v[152:153], v[28:29], s[2:3], v[152:153] op_sel_hi:[1,0,1]
	v_pk_fma_f32 v[150:151], v[30:31], s[2:3], v[150:151] op_sel_hi:[1,0,1]
	v_readlane_b32 s2, v131, 1
	s_waitcnt vmcnt(20)
	v_cvt_scalef32_pk32_f32_fp6 v[0:31], v[50:55], 1.0
	v_pk_fma_f32 v[50:51], v[0:1], s[2:3], v[62:63] op_sel_hi:[1,0,1]
	v_pk_fma_f32 v[52:53], v[2:3], s[2:3], v[64:65] op_sel_hi:[1,0,1]
	v_pk_fma_f32 v[54:55], v[4:5], s[2:3], v[66:67] op_sel_hi:[1,0,1]
	v_pk_fma_f32 v[62:63], v[6:7], s[2:3], v[164:165] op_sel_hi:[1,0,1]
	v_pk_fma_f32 v[64:65], v[8:9], s[2:3], v[166:167] op_sel_hi:[1,0,1]
	v_pk_fma_f32 v[66:67], v[10:11], s[2:3], v[168:169] op_sel_hi:[1,0,1]
	v_pk_fma_f32 v[164:165], v[12:13], s[2:3], v[170:171] op_sel_hi:[1,0,1]
	v_pk_fma_f32 v[166:167], v[14:15], s[2:3], v[172:173] op_sel_hi:[1,0,1]
	v_pk_fma_f32 v[168:169], v[16:17], s[2:3], v[174:175] op_sel_hi:[1,0,1]
	v_pk_fma_f32 v[162:163], v[18:19], s[2:3], v[162:163] op_sel_hi:[1,0,1]
	v_pk_fma_f32 v[160:161], v[20:21], s[2:3], v[160:161] op_sel_hi:[1,0,1]
	v_pk_fma_f32 v[158:159], v[22:23], s[2:3], v[158:159] op_sel_hi:[1,0,1]
	v_pk_fma_f32 v[156:157], v[24:25], s[2:3], v[156:157] op_sel_hi:[1,0,1]
	v_pk_fma_f32 v[154:155], v[26:27], s[2:3], v[154:155] op_sel_hi:[1,0,1]
	v_pk_fma_f32 v[152:153], v[28:29], s[2:3], v[152:153] op_sel_hi:[1,0,1]
	v_pk_fma_f32 v[150:151], v[30:31], s[2:3], v[150:151] op_sel_hi:[1,0,1]
	v_readlane_b32 s2, v131, 2
	s_waitcnt vmcnt(18)
	v_cvt_scalef32_pk32_f32_fp6 v[0:31], v[38:43], 1.0
	v_pk_fma_f32 v[38:39], v[0:1], s[2:3], v[50:51] op_sel_hi:[1,0,1]
	v_pk_fma_f32 v[40:41], v[2:3], s[2:3], v[52:53] op_sel_hi:[1,0,1]
	v_pk_fma_f32 v[42:43], v[4:5], s[2:3], v[54:55] op_sel_hi:[1,0,1]
	v_pk_fma_f32 v[50:51], v[6:7], s[2:3], v[62:63] op_sel_hi:[1,0,1]
	v_pk_fma_f32 v[52:53], v[8:9], s[2:3], v[64:65] op_sel_hi:[1,0,1]
	v_pk_fma_f32 v[54:55], v[10:11], s[2:3], v[66:67] op_sel_hi:[1,0,1]
	v_pk_fma_f32 v[62:63], v[12:13], s[2:3], v[164:165] op_sel_hi:[1,0,1]
	v_pk_fma_f32 v[64:65], v[14:15], s[2:3], v[166:167] op_sel_hi:[1,0,1]
	v_pk_fma_f32 v[66:67], v[16:17], s[2:3], v[168:169] op_sel_hi:[1,0,1]
	v_pk_fma_f32 v[162:163], v[18:19], s[2:3], v[162:163] op_sel_hi:[1,0,1]
	v_pk_fma_f32 v[160:161], v[20:21], s[2:3], v[160:161] op_sel_hi:[1,0,1]
	v_pk_fma_f32 v[158:159], v[22:23], s[2:3], v[158:159] op_sel_hi:[1,0,1]
	v_pk_fma_f32 v[156:157], v[24:25], s[2:3], v[156:157] op_sel_hi:[1,0,1]
	v_pk_fma_f32 v[154:155], v[26:27], s[2:3], v[154:155] op_sel_hi:[1,0,1]
	v_pk_fma_f32 v[152:153], v[28:29], s[2:3], v[152:153] op_sel_hi:[1,0,1]
	v_pk_fma_f32 v[150:151], v[30:31], s[2:3], v[150:151] op_sel_hi:[1,0,1]
	v_readlane_b32 s2, v131, 3
	s_waitcnt vmcnt(16)
	v_cvt_scalef32_pk32_f32_fp6 v[0:31], v[32:37], 1.0
	v_pk_fma_f32 v[164:165], v[0:1], s[2:3], v[38:39] op_sel_hi:[1,0,1]
	v_pk_fma_f32 v[166:167], v[2:3], s[2:3], v[40:41] op_sel_hi:[1,0,1]
	v_pk_fma_f32 v[168:169], v[4:5], s[2:3], v[42:43] op_sel_hi:[1,0,1]
	v_pk_fma_f32 v[170:171], v[6:7], s[2:3], v[50:51] op_sel_hi:[1,0,1]
	v_pk_fma_f32 v[172:173], v[8:9], s[2:3], v[52:53] op_sel_hi:[1,0,1]
	v_pk_fma_f32 v[174:175], v[10:11], s[2:3], v[54:55] op_sel_hi:[1,0,1]
	v_pk_fma_f32 v[176:177], v[12:13], s[2:3], v[62:63] op_sel_hi:[1,0,1]
	v_pk_fma_f32 v[178:179], v[14:15], s[2:3], v[64:65] op_sel_hi:[1,0,1]
	v_pk_fma_f32 v[180:181], v[16:17], s[2:3], v[66:67] op_sel_hi:[1,0,1]
	v_pk_fma_f32 v[162:163], v[18:19], s[2:3], v[162:163] op_sel_hi:[1,0,1]
	v_pk_fma_f32 v[160:161], v[20:21], s[2:3], v[160:161] op_sel_hi:[1,0,1]
	v_pk_fma_f32 v[158:159], v[22:23], s[2:3], v[158:159] op_sel_hi:[1,0,1]
	v_pk_fma_f32 v[156:157], v[24:25], s[2:3], v[156:157] op_sel_hi:[1,0,1]
	v_pk_fma_f32 v[154:155], v[26:27], s[2:3], v[154:155] op_sel_hi:[1,0,1]
	v_pk_fma_f32 v[152:153], v[28:29], s[2:3], v[152:153] op_sel_hi:[1,0,1]
	v_pk_fma_f32 v[150:151], v[30:31], s[2:3], v[150:151] op_sel_hi:[1,0,1]
	v_readlane_b32 s2, v241, 12
	v_readlane_b32 s3, v241, 13
	v_readlane_b32 s100, v241, 14
	v_readlane_b32 s101, v241, 15
	s_nop 1
	buffer_load_dwordx4 v[62:65], v129, s[44:47], s2 offen nt
	buffer_load_dwordx2 v[66:67], v210, s[44:47], s2 offen nt
	buffer_load_dwordx4 v[50:53], v129, s[44:47], s3 offen nt
	buffer_load_dwordx2 v[54:55], v210, s[44:47], s3 offen nt
	buffer_load_dwordx4 v[38:41], v129, s[44:47], s100 offen nt
	buffer_load_dwordx2 v[42:43], v210, s[44:47], s100 offen nt
	buffer_load_dwordx4 v[32:35], v129, s[44:47], s101 offen nt
	buffer_load_dwordx2 v[36:37], v210, s[44:47], s101 offen nt
	v_readlane_b32 s2, v131, 4
	s_waitcnt vmcnt(22)
	v_cvt_scalef32_pk32_f32_fp6 v[0:31], v[98:103], 1.0
	v_pk_fma_f32 v[98:99], v[0:1], s[2:3], v[164:165] op_sel_hi:[1,0,1]
	v_pk_fma_f32 v[100:101], v[2:3], s[2:3], v[166:167] op_sel_hi:[1,0,1]
	v_pk_fma_f32 v[102:103], v[4:5], s[2:3], v[168:169] op_sel_hi:[1,0,1]
	v_pk_fma_f32 v[164:165], v[6:7], s[2:3], v[170:171] op_sel_hi:[1,0,1]
	v_pk_fma_f32 v[166:167], v[8:9], s[2:3], v[172:173] op_sel_hi:[1,0,1]
	v_pk_fma_f32 v[168:169], v[10:11], s[2:3], v[174:175] op_sel_hi:[1,0,1]
	v_pk_fma_f32 v[170:171], v[12:13], s[2:3], v[176:177] op_sel_hi:[1,0,1]
	v_pk_fma_f32 v[172:173], v[14:15], s[2:3], v[178:179] op_sel_hi:[1,0,1]
	v_pk_fma_f32 v[174:175], v[16:17], s[2:3], v[180:181] op_sel_hi:[1,0,1]
	v_pk_fma_f32 v[162:163], v[18:19], s[2:3], v[162:163] op_sel_hi:[1,0,1]
	v_pk_fma_f32 v[160:161], v[20:21], s[2:3], v[160:161] op_sel_hi:[1,0,1]
	v_pk_fma_f32 v[158:159], v[22:23], s[2:3], v[158:159] op_sel_hi:[1,0,1]
	v_pk_fma_f32 v[156:157], v[24:25], s[2:3], v[156:157] op_sel_hi:[1,0,1]
	v_pk_fma_f32 v[154:155], v[26:27], s[2:3], v[154:155] op_sel_hi:[1,0,1]
	v_pk_fma_f32 v[152:153], v[28:29], s[2:3], v[152:153] op_sel_hi:[1,0,1]
	v_pk_fma_f32 v[150:151], v[30:31], s[2:3], v[150:151] op_sel_hi:[1,0,1]
	v_readlane_b32 s2, v131, 5
	s_waitcnt vmcnt(20)
	v_cvt_scalef32_pk32_f32_fp6 v[0:31], v[92:97], 1.0
	v_pk_fma_f32 v[92:93], v[0:1], s[2:3], v[98:99] op_sel_hi:[1,0,1]
	v_pk_fma_f32 v[94:95], v[2:3], s[2:3], v[100:101] op_sel_hi:[1,0,1]
	v_pk_fma_f32 v[96:97], v[4:5], s[2:3], v[102:103] op_sel_hi:[1,0,1]
	v_pk_fma_f32 v[98:99], v[6:7], s[2:3], v[164:165] op_sel_hi:[1,0,1]
	v_pk_fma_f32 v[100:101], v[8:9], s[2:3], v[166:167] op_sel_hi:[1,0,1]
	v_pk_fma_f32 v[102:103], v[10:11], s[2:3], v[168:169] op_sel_hi:[1,0,1]
	v_pk_fma_f32 v[164:165], v[12:13], s[2:3], v[170:171] op_sel_hi:[1,0,1]
	v_pk_fma_f32 v[166:167], v[14:15], s[2:3], v[172:173] op_sel_hi:[1,0,1]
	v_pk_fma_f32 v[168:169], v[16:17], s[2:3], v[174:175] op_sel_hi:[1,0,1]
	v_pk_fma_f32 v[162:163], v[18:19], s[2:3], v[162:163] op_sel_hi:[1,0,1]
	v_pk_fma_f32 v[160:161], v[20:21], s[2:3], v[160:161] op_sel_hi:[1,0,1]
	v_pk_fma_f32 v[158:159], v[22:23], s[2:3], v[158:159] op_sel_hi:[1,0,1]
	v_pk_fma_f32 v[156:157], v[24:25], s[2:3], v[156:157] op_sel_hi:[1,0,1]
	v_pk_fma_f32 v[154:155], v[26:27], s[2:3], v[154:155] op_sel_hi:[1,0,1]
	v_pk_fma_f32 v[152:153], v[28:29], s[2:3], v[152:153] op_sel_hi:[1,0,1]
	v_pk_fma_f32 v[150:151], v[30:31], s[2:3], v[150:151] op_sel_hi:[1,0,1]
	v_readlane_b32 s2, v131, 6
	s_waitcnt vmcnt(18)
	v_cvt_scalef32_pk32_f32_fp6 v[0:31], v[86:91], 1.0
	v_pk_fma_f32 v[86:87], v[0:1], s[2:3], v[92:93] op_sel_hi:[1,0,1]
	v_pk_fma_f32 v[88:89], v[2:3], s[2:3], v[94:95] op_sel_hi:[1,0,1]
	v_pk_fma_f32 v[90:91], v[4:5], s[2:3], v[96:97] op_sel_hi:[1,0,1]
	v_pk_fma_f32 v[92:93], v[6:7], s[2:3], v[98:99] op_sel_hi:[1,0,1]
	v_pk_fma_f32 v[94:95], v[8:9], s[2:3], v[100:101] op_sel_hi:[1,0,1]
	v_pk_fma_f32 v[96:97], v[10:11], s[2:3], v[102:103] op_sel_hi:[1,0,1]
	v_pk_fma_f32 v[98:99], v[12:13], s[2:3], v[164:165] op_sel_hi:[1,0,1]
	v_pk_fma_f32 v[100:101], v[14:15], s[2:3], v[166:167] op_sel_hi:[1,0,1]
	v_pk_fma_f32 v[102:103], v[16:17], s[2:3], v[168:169] op_sel_hi:[1,0,1]
	v_pk_fma_f32 v[162:163], v[18:19], s[2:3], v[162:163] op_sel_hi:[1,0,1]
	v_pk_fma_f32 v[160:161], v[20:21], s[2:3], v[160:161] op_sel_hi:[1,0,1]
	v_pk_fma_f32 v[158:159], v[22:23], s[2:3], v[158:159] op_sel_hi:[1,0,1]
	v_pk_fma_f32 v[156:157], v[24:25], s[2:3], v[156:157] op_sel_hi:[1,0,1]
	v_pk_fma_f32 v[154:155], v[26:27], s[2:3], v[154:155] op_sel_hi:[1,0,1]
	v_pk_fma_f32 v[152:153], v[28:29], s[2:3], v[152:153] op_sel_hi:[1,0,1]
	v_pk_fma_f32 v[150:151], v[30:31], s[2:3], v[150:151] op_sel_hi:[1,0,1]
	v_readlane_b32 s2, v131, 7
	s_waitcnt vmcnt(16)
	v_cvt_scalef32_pk32_f32_fp6 v[0:31], v[80:85], 1.0
	v_pk_fma_f32 v[180:181], v[0:1], s[2:3], v[86:87] op_sel_hi:[1,0,1]
	v_pk_fma_f32 v[178:179], v[2:3], s[2:3], v[88:89] op_sel_hi:[1,0,1]
	v_pk_fma_f32 v[176:177], v[4:5], s[2:3], v[90:91] op_sel_hi:[1,0,1]
	v_pk_fma_f32 v[174:175], v[6:7], s[2:3], v[92:93] op_sel_hi:[1,0,1]
	v_pk_fma_f32 v[172:173], v[8:9], s[2:3], v[94:95] op_sel_hi:[1,0,1]
	v_pk_fma_f32 v[170:171], v[10:11], s[2:3], v[96:97] op_sel_hi:[1,0,1]
	v_pk_fma_f32 v[168:169], v[12:13], s[2:3], v[98:99] op_sel_hi:[1,0,1]
	v_pk_fma_f32 v[166:167], v[14:15], s[2:3], v[100:101] op_sel_hi:[1,0,1]
	v_pk_fma_f32 v[164:165], v[16:17], s[2:3], v[102:103] op_sel_hi:[1,0,1]
	v_pk_fma_f32 v[162:163], v[18:19], s[2:3], v[162:163] op_sel_hi:[1,0,1]
	v_pk_fma_f32 v[160:161], v[20:21], s[2:3], v[160:161] op_sel_hi:[1,0,1]
	v_pk_fma_f32 v[158:159], v[22:23], s[2:3], v[158:159] op_sel_hi:[1,0,1]
	v_pk_fma_f32 v[156:157], v[24:25], s[2:3], v[156:157] op_sel_hi:[1,0,1]
	v_pk_fma_f32 v[154:155], v[26:27], s[2:3], v[154:155] op_sel_hi:[1,0,1]
	v_pk_fma_f32 v[152:153], v[28:29], s[2:3], v[152:153] op_sel_hi:[1,0,1]
	v_pk_fma_f32 v[150:151], v[30:31], s[2:3], v[150:151] op_sel_hi:[1,0,1]
	v_readlane_b32 s2, v241, 16
	v_readlane_b32 s3, v241, 17
	v_readlane_b32 s100, v241, 18
	v_readlane_b32 s101, v241, 19
	s_nop 1
	buffer_load_dwordx4 v[98:101], v129, s[44:47], s2 offen nt
	buffer_load_dwordx2 v[102:103], v210, s[44:47], s2 offen nt
	buffer_load_dwordx4 v[92:95], v129, s[44:47], s3 offen nt
	buffer_load_dwordx2 v[96:97], v210, s[44:47], s3 offen nt
	buffer_load_dwordx4 v[86:89], v129, s[44:47], s100 offen nt
	buffer_load_dwordx2 v[90:91], v210, s[44:47], s100 offen nt
	buffer_load_dwordx4 v[80:83], v129, s[44:47], s101 offen nt
	buffer_load_dwordx2 v[84:85], v210, s[44:47], s101 offen nt
	v_readlane_b32 s2, v131, 8
	s_waitcnt vmcnt(22)
	v_cvt_scalef32_pk32_f32_fp6 v[0:31], v[74:79], 1.0
	v_pk_fma_f32 v[74:75], v[0:1], s[2:3], v[180:181] op_sel_hi:[1,0,1]
	v_pk_fma_f32 v[76:77], v[2:3], s[2:3], v[178:179] op_sel_hi:[1,0,1]
	v_pk_fma_f32 v[78:79], v[4:5], s[2:3], v[176:177] op_sel_hi:[1,0,1]
	v_pk_fma_f32 v[174:175], v[6:7], s[2:3], v[174:175] op_sel_hi:[1,0,1]
	v_pk_fma_f32 v[172:173], v[8:9], s[2:3], v[172:173] op_sel_hi:[1,0,1]
	v_pk_fma_f32 v[170:171], v[10:11], s[2:3], v[170:171] op_sel_hi:[1,0,1]
	v_pk_fma_f32 v[168:169], v[12:13], s[2:3], v[168:169] op_sel_hi:[1,0,1]
	v_pk_fma_f32 v[166:167], v[14:15], s[2:3], v[166:167] op_sel_hi:[1,0,1]
	v_pk_fma_f32 v[164:165], v[16:17], s[2:3], v[164:165] op_sel_hi:[1,0,1]
	v_pk_fma_f32 v[162:163], v[18:19], s[2:3], v[162:163] op_sel_hi:[1,0,1]
	v_pk_fma_f32 v[160:161], v[20:21], s[2:3], v[160:161] op_sel_hi:[1,0,1]
	v_pk_fma_f32 v[158:159], v[22:23], s[2:3], v[158:159] op_sel_hi:[1,0,1]
	v_pk_fma_f32 v[156:157], v[24:25], s[2:3], v[156:157] op_sel_hi:[1,0,1]
	v_pk_fma_f32 v[154:155], v[26:27], s[2:3], v[154:155] op_sel_hi:[1,0,1]
	v_pk_fma_f32 v[152:153], v[28:29], s[2:3], v[152:153] op_sel_hi:[1,0,1]
	v_pk_fma_f32 v[150:151], v[30:31], s[2:3], v[150:151] op_sel_hi:[1,0,1]
	v_readlane_b32 s2, v131, 9
	s_waitcnt vmcnt(20)
	v_cvt_scalef32_pk32_f32_fp6 v[0:31], v[68:73], 1.0
	v_pk_fma_f32 v[68:69], v[0:1], s[2:3], v[74:75] op_sel_hi:[1,0,1]
	v_pk_fma_f32 v[70:71], v[2:3], s[2:3], v[76:77] op_sel_hi:[1,0,1]
	v_pk_fma_f32 v[72:73], v[4:5], s[2:3], v[78:79] op_sel_hi:[1,0,1]
	v_pk_fma_f32 v[74:75], v[6:7], s[2:3], v[174:175] op_sel_hi:[1,0,1]
	v_pk_fma_f32 v[76:77], v[8:9], s[2:3], v[172:173] op_sel_hi:[1,0,1]
	v_pk_fma_f32 v[78:79], v[10:11], s[2:3], v[170:171] op_sel_hi:[1,0,1]
	v_pk_fma_f32 v[168:169], v[12:13], s[2:3], v[168:169] op_sel_hi:[1,0,1]
	v_pk_fma_f32 v[166:167], v[14:15], s[2:3], v[166:167] op_sel_hi:[1,0,1]
	v_pk_fma_f32 v[164:165], v[16:17], s[2:3], v[164:165] op_sel_hi:[1,0,1]
	v_pk_fma_f32 v[162:163], v[18:19], s[2:3], v[162:163] op_sel_hi:[1,0,1]
	v_pk_fma_f32 v[160:161], v[20:21], s[2:3], v[160:161] op_sel_hi:[1,0,1]
	v_pk_fma_f32 v[158:159], v[22:23], s[2:3], v[158:159] op_sel_hi:[1,0,1]
	v_pk_fma_f32 v[156:157], v[24:25], s[2:3], v[156:157] op_sel_hi:[1,0,1]
	v_pk_fma_f32 v[154:155], v[26:27], s[2:3], v[154:155] op_sel_hi:[1,0,1]
	v_pk_fma_f32 v[152:153], v[28:29], s[2:3], v[152:153] op_sel_hi:[1,0,1]
	v_pk_fma_f32 v[150:151], v[30:31], s[2:3], v[150:151] op_sel_hi:[1,0,1]
	v_readlane_b32 s2, v131, 10
	s_waitcnt vmcnt(18)
	v_cvt_scalef32_pk32_f32_fp6 v[0:31], v[56:61], 1.0
	v_pk_fma_f32 v[56:57], v[0:1], s[2:3], v[68:69] op_sel_hi:[1,0,1]
	v_pk_fma_f32 v[58:59], v[2:3], s[2:3], v[70:71] op_sel_hi:[1,0,1]
	v_pk_fma_f32 v[60:61], v[4:5], s[2:3], v[72:73] op_sel_hi:[1,0,1]
	v_pk_fma_f32 v[68:69], v[6:7], s[2:3], v[74:75] op_sel_hi:[1,0,1]
	v_pk_fma_f32 v[70:71], v[8:9], s[2:3], v[76:77] op_sel_hi:[1,0,1]
	v_pk_fma_f32 v[72:73], v[10:11], s[2:3], v[78:79] op_sel_hi:[1,0,1]
	v_pk_fma_f32 v[74:75], v[12:13], s[2:3], v[168:169] op_sel_hi:[1,0,1]
	v_pk_fma_f32 v[76:77], v[14:15], s[2:3], v[166:167] op_sel_hi:[1,0,1]
	v_pk_fma_f32 v[78:79], v[16:17], s[2:3], v[164:165] op_sel_hi:[1,0,1]
	v_pk_fma_f32 v[162:163], v[18:19], s[2:3], v[162:163] op_sel_hi:[1,0,1]
	v_pk_fma_f32 v[160:161], v[20:21], s[2:3], v[160:161] op_sel_hi:[1,0,1]
	v_pk_fma_f32 v[158:159], v[22:23], s[2:3], v[158:159] op_sel_hi:[1,0,1]
	v_pk_fma_f32 v[156:157], v[24:25], s[2:3], v[156:157] op_sel_hi:[1,0,1]
	v_pk_fma_f32 v[154:155], v[26:27], s[2:3], v[154:155] op_sel_hi:[1,0,1]
	v_pk_fma_f32 v[152:153], v[28:29], s[2:3], v[152:153] op_sel_hi:[1,0,1]
	v_pk_fma_f32 v[150:151], v[30:31], s[2:3], v[150:151] op_sel_hi:[1,0,1]
	v_readlane_b32 s2, v131, 11
	s_waitcnt vmcnt(16)
	v_cvt_scalef32_pk32_f32_fp6 v[0:31], v[44:49], 1.0
	v_pk_fma_f32 v[164:165], v[0:1], s[2:3], v[56:57] op_sel_hi:[1,0,1]
	v_pk_fma_f32 v[166:167], v[2:3], s[2:3], v[58:59] op_sel_hi:[1,0,1]
	v_pk_fma_f32 v[168:169], v[4:5], s[2:3], v[60:61] op_sel_hi:[1,0,1]
	v_pk_fma_f32 v[170:171], v[6:7], s[2:3], v[68:69] op_sel_hi:[1,0,1]
	v_pk_fma_f32 v[172:173], v[8:9], s[2:3], v[70:71] op_sel_hi:[1,0,1]
	v_pk_fma_f32 v[174:175], v[10:11], s[2:3], v[72:73] op_sel_hi:[1,0,1]
	v_pk_fma_f32 v[176:177], v[12:13], s[2:3], v[74:75] op_sel_hi:[1,0,1]
	v_pk_fma_f32 v[178:179], v[14:15], s[2:3], v[76:77] op_sel_hi:[1,0,1]
	v_pk_fma_f32 v[180:181], v[16:17], s[2:3], v[78:79] op_sel_hi:[1,0,1]
	v_pk_fma_f32 v[162:163], v[18:19], s[2:3], v[162:163] op_sel_hi:[1,0,1]
	v_pk_fma_f32 v[160:161], v[20:21], s[2:3], v[160:161] op_sel_hi:[1,0,1]
	v_pk_fma_f32 v[158:159], v[22:23], s[2:3], v[158:159] op_sel_hi:[1,0,1]
	v_pk_fma_f32 v[156:157], v[24:25], s[2:3], v[156:157] op_sel_hi:[1,0,1]
	v_pk_fma_f32 v[154:155], v[26:27], s[2:3], v[154:155] op_sel_hi:[1,0,1]
	v_pk_fma_f32 v[152:153], v[28:29], s[2:3], v[152:153] op_sel_hi:[1,0,1]
	v_pk_fma_f32 v[150:151], v[30:31], s[2:3], v[150:151] op_sel_hi:[1,0,1]
	v_readlane_b32 s2, v241, 20
	v_readlane_b32 s3, v241, 21
	v_readlane_b32 s100, v241, 22
	v_readlane_b32 s101, v241, 23
	s_nop 1
	buffer_load_dwordx4 v[74:77], v129, s[44:47], s2 offen nt
	buffer_load_dwordx2 v[78:79], v210, s[44:47], s2 offen nt
	buffer_load_dwordx4 v[68:71], v129, s[44:47], s3 offen nt
	buffer_load_dwordx2 v[72:73], v210, s[44:47], s3 offen nt
	buffer_load_dwordx4 v[56:59], v129, s[44:47], s100 offen nt
	buffer_load_dwordx2 v[60:61], v210, s[44:47], s100 offen nt
	buffer_load_dwordx4 v[44:47], v129, s[44:47], s101 offen nt
	buffer_load_dwordx2 v[48:49], v210, s[44:47], s101 offen nt
	v_readlane_b32 s2, v131, 12
	s_waitcnt vmcnt(22)
	v_cvt_scalef32_pk32_f32_fp6 v[0:31], v[62:67], 1.0
	v_pk_fma_f32 v[62:63], v[0:1], s[2:3], v[164:165] op_sel_hi:[1,0,1]
	v_pk_fma_f32 v[64:65], v[2:3], s[2:3], v[166:167] op_sel_hi:[1,0,1]
	v_pk_fma_f32 v[66:67], v[4:5], s[2:3], v[168:169] op_sel_hi:[1,0,1]
	v_pk_fma_f32 v[164:165], v[6:7], s[2:3], v[170:171] op_sel_hi:[1,0,1]
	v_pk_fma_f32 v[166:167], v[8:9], s[2:3], v[172:173] op_sel_hi:[1,0,1]
	v_pk_fma_f32 v[168:169], v[10:11], s[2:3], v[174:175] op_sel_hi:[1,0,1]
	v_pk_fma_f32 v[170:171], v[12:13], s[2:3], v[176:177] op_sel_hi:[1,0,1]
	v_pk_fma_f32 v[172:173], v[14:15], s[2:3], v[178:179] op_sel_hi:[1,0,1]
	v_pk_fma_f32 v[174:175], v[16:17], s[2:3], v[180:181] op_sel_hi:[1,0,1]
	v_pk_fma_f32 v[162:163], v[18:19], s[2:3], v[162:163] op_sel_hi:[1,0,1]
	v_pk_fma_f32 v[160:161], v[20:21], s[2:3], v[160:161] op_sel_hi:[1,0,1]
	v_pk_fma_f32 v[158:159], v[22:23], s[2:3], v[158:159] op_sel_hi:[1,0,1]
	v_pk_fma_f32 v[156:157], v[24:25], s[2:3], v[156:157] op_sel_hi:[1,0,1]
	v_pk_fma_f32 v[154:155], v[26:27], s[2:3], v[154:155] op_sel_hi:[1,0,1]
	v_pk_fma_f32 v[152:153], v[28:29], s[2:3], v[152:153] op_sel_hi:[1,0,1]
	v_pk_fma_f32 v[150:151], v[30:31], s[2:3], v[150:151] op_sel_hi:[1,0,1]
	v_readlane_b32 s2, v131, 13
	s_waitcnt vmcnt(20)
	v_cvt_scalef32_pk32_f32_fp6 v[0:31], v[50:55], 1.0
	v_pk_fma_f32 v[50:51], v[0:1], s[2:3], v[62:63] op_sel_hi:[1,0,1]
	v_pk_fma_f32 v[52:53], v[2:3], s[2:3], v[64:65] op_sel_hi:[1,0,1]
	v_pk_fma_f32 v[54:55], v[4:5], s[2:3], v[66:67] op_sel_hi:[1,0,1]
	v_pk_fma_f32 v[62:63], v[6:7], s[2:3], v[164:165] op_sel_hi:[1,0,1]
	v_pk_fma_f32 v[64:65], v[8:9], s[2:3], v[166:167] op_sel_hi:[1,0,1]
	v_pk_fma_f32 v[66:67], v[10:11], s[2:3], v[168:169] op_sel_hi:[1,0,1]
	v_pk_fma_f32 v[164:165], v[12:13], s[2:3], v[170:171] op_sel_hi:[1,0,1]
	v_pk_fma_f32 v[166:167], v[14:15], s[2:3], v[172:173] op_sel_hi:[1,0,1]
	v_pk_fma_f32 v[168:169], v[16:17], s[2:3], v[174:175] op_sel_hi:[1,0,1]
	v_pk_fma_f32 v[162:163], v[18:19], s[2:3], v[162:163] op_sel_hi:[1,0,1]
	v_pk_fma_f32 v[160:161], v[20:21], s[2:3], v[160:161] op_sel_hi:[1,0,1]
	v_pk_fma_f32 v[158:159], v[22:23], s[2:3], v[158:159] op_sel_hi:[1,0,1]
	v_pk_fma_f32 v[156:157], v[24:25], s[2:3], v[156:157] op_sel_hi:[1,0,1]
	v_pk_fma_f32 v[154:155], v[26:27], s[2:3], v[154:155] op_sel_hi:[1,0,1]
	v_pk_fma_f32 v[152:153], v[28:29], s[2:3], v[152:153] op_sel_hi:[1,0,1]
	v_pk_fma_f32 v[150:151], v[30:31], s[2:3], v[150:151] op_sel_hi:[1,0,1]
	v_readlane_b32 s2, v131, 14
	s_waitcnt vmcnt(18)
	v_cvt_scalef32_pk32_f32_fp6 v[0:31], v[38:43], 1.0
	v_pk_fma_f32 v[38:39], v[0:1], s[2:3], v[50:51] op_sel_hi:[1,0,1]
	v_pk_fma_f32 v[40:41], v[2:3], s[2:3], v[52:53] op_sel_hi:[1,0,1]
	v_pk_fma_f32 v[42:43], v[4:5], s[2:3], v[54:55] op_sel_hi:[1,0,1]
	v_pk_fma_f32 v[50:51], v[6:7], s[2:3], v[62:63] op_sel_hi:[1,0,1]
	v_pk_fma_f32 v[52:53], v[8:9], s[2:3], v[64:65] op_sel_hi:[1,0,1]
	v_pk_fma_f32 v[54:55], v[10:11], s[2:3], v[66:67] op_sel_hi:[1,0,1]
	v_pk_fma_f32 v[62:63], v[12:13], s[2:3], v[164:165] op_sel_hi:[1,0,1]
	v_pk_fma_f32 v[64:65], v[14:15], s[2:3], v[166:167] op_sel_hi:[1,0,1]
	v_pk_fma_f32 v[66:67], v[16:17], s[2:3], v[168:169] op_sel_hi:[1,0,1]
	v_pk_fma_f32 v[162:163], v[18:19], s[2:3], v[162:163] op_sel_hi:[1,0,1]
	v_pk_fma_f32 v[160:161], v[20:21], s[2:3], v[160:161] op_sel_hi:[1,0,1]
	v_pk_fma_f32 v[158:159], v[22:23], s[2:3], v[158:159] op_sel_hi:[1,0,1]
	v_pk_fma_f32 v[156:157], v[24:25], s[2:3], v[156:157] op_sel_hi:[1,0,1]
	v_pk_fma_f32 v[154:155], v[26:27], s[2:3], v[154:155] op_sel_hi:[1,0,1]
	v_pk_fma_f32 v[152:153], v[28:29], s[2:3], v[152:153] op_sel_hi:[1,0,1]
	v_pk_fma_f32 v[150:151], v[30:31], s[2:3], v[150:151] op_sel_hi:[1,0,1]
	v_readlane_b32 s2, v131, 15
	s_waitcnt vmcnt(16)
	v_cvt_scalef32_pk32_f32_fp6 v[0:31], v[32:37], 1.0
	v_pk_fma_f32 v[164:165], v[0:1], s[2:3], v[38:39] op_sel_hi:[1,0,1]
	v_pk_fma_f32 v[166:167], v[2:3], s[2:3], v[40:41] op_sel_hi:[1,0,1]
	v_pk_fma_f32 v[168:169], v[4:5], s[2:3], v[42:43] op_sel_hi:[1,0,1]
	v_pk_fma_f32 v[170:171], v[6:7], s[2:3], v[50:51] op_sel_hi:[1,0,1]
	v_pk_fma_f32 v[172:173], v[8:9], s[2:3], v[52:53] op_sel_hi:[1,0,1]
	v_pk_fma_f32 v[174:175], v[10:11], s[2:3], v[54:55] op_sel_hi:[1,0,1]
	v_pk_fma_f32 v[176:177], v[12:13], s[2:3], v[62:63] op_sel_hi:[1,0,1]
	v_pk_fma_f32 v[178:179], v[14:15], s[2:3], v[64:65] op_sel_hi:[1,0,1]
	v_pk_fma_f32 v[180:181], v[16:17], s[2:3], v[66:67] op_sel_hi:[1,0,1]
	v_pk_fma_f32 v[162:163], v[18:19], s[2:3], v[162:163] op_sel_hi:[1,0,1]
	v_pk_fma_f32 v[160:161], v[20:21], s[2:3], v[160:161] op_sel_hi:[1,0,1]
	v_pk_fma_f32 v[158:159], v[22:23], s[2:3], v[158:159] op_sel_hi:[1,0,1]
	v_pk_fma_f32 v[156:157], v[24:25], s[2:3], v[156:157] op_sel_hi:[1,0,1]
	v_pk_fma_f32 v[154:155], v[26:27], s[2:3], v[154:155] op_sel_hi:[1,0,1]
	v_pk_fma_f32 v[152:153], v[28:29], s[2:3], v[152:153] op_sel_hi:[1,0,1]
	v_pk_fma_f32 v[150:151], v[30:31], s[2:3], v[150:151] op_sel_hi:[1,0,1]
	v_readlane_b32 s2, v241, 24
	v_readlane_b32 s3, v241, 25
	v_readlane_b32 s100, v241, 26
	v_readlane_b32 s101, v241, 27
	s_nop 1
	buffer_load_dwordx4 v[62:65], v129, s[44:47], s2 offen nt
	buffer_load_dwordx2 v[66:67], v210, s[44:47], s2 offen nt
	buffer_load_dwordx4 v[50:53], v129, s[44:47], s3 offen nt
	buffer_load_dwordx2 v[54:55], v210, s[44:47], s3 offen nt
	buffer_load_dwordx4 v[38:41], v129, s[44:47], s100 offen nt
	buffer_load_dwordx2 v[42:43], v210, s[44:47], s100 offen nt
	buffer_load_dwordx4 v[32:35], v129, s[44:47], s101 offen nt
	buffer_load_dwordx2 v[36:37], v210, s[44:47], s101 offen nt
	v_readlane_b32 s2, v131, 16
	s_waitcnt vmcnt(22)
	v_cvt_scalef32_pk32_f32_fp6 v[0:31], v[98:103], 1.0
	v_pk_fma_f32 v[98:99], v[0:1], s[2:3], v[164:165] op_sel_hi:[1,0,1]
	v_pk_fma_f32 v[100:101], v[2:3], s[2:3], v[166:167] op_sel_hi:[1,0,1]
	v_pk_fma_f32 v[102:103], v[4:5], s[2:3], v[168:169] op_sel_hi:[1,0,1]
	v_pk_fma_f32 v[164:165], v[6:7], s[2:3], v[170:171] op_sel_hi:[1,0,1]
	v_pk_fma_f32 v[166:167], v[8:9], s[2:3], v[172:173] op_sel_hi:[1,0,1]
	v_pk_fma_f32 v[168:169], v[10:11], s[2:3], v[174:175] op_sel_hi:[1,0,1]
	v_pk_fma_f32 v[170:171], v[12:13], s[2:3], v[176:177] op_sel_hi:[1,0,1]
	v_pk_fma_f32 v[172:173], v[14:15], s[2:3], v[178:179] op_sel_hi:[1,0,1]
	v_pk_fma_f32 v[174:175], v[16:17], s[2:3], v[180:181] op_sel_hi:[1,0,1]
	v_pk_fma_f32 v[162:163], v[18:19], s[2:3], v[162:163] op_sel_hi:[1,0,1]
	v_pk_fma_f32 v[160:161], v[20:21], s[2:3], v[160:161] op_sel_hi:[1,0,1]
	v_pk_fma_f32 v[158:159], v[22:23], s[2:3], v[158:159] op_sel_hi:[1,0,1]
	v_pk_fma_f32 v[156:157], v[24:25], s[2:3], v[156:157] op_sel_hi:[1,0,1]
	v_pk_fma_f32 v[154:155], v[26:27], s[2:3], v[154:155] op_sel_hi:[1,0,1]
	v_pk_fma_f32 v[152:153], v[28:29], s[2:3], v[152:153] op_sel_hi:[1,0,1]
	v_pk_fma_f32 v[150:151], v[30:31], s[2:3], v[150:151] op_sel_hi:[1,0,1]
	v_readlane_b32 s2, v131, 17
	s_waitcnt vmcnt(20)
	v_cvt_scalef32_pk32_f32_fp6 v[0:31], v[92:97], 1.0
	v_pk_fma_f32 v[92:93], v[0:1], s[2:3], v[98:99] op_sel_hi:[1,0,1]
	v_pk_fma_f32 v[94:95], v[2:3], s[2:3], v[100:101] op_sel_hi:[1,0,1]
	v_pk_fma_f32 v[96:97], v[4:5], s[2:3], v[102:103] op_sel_hi:[1,0,1]
	v_pk_fma_f32 v[98:99], v[6:7], s[2:3], v[164:165] op_sel_hi:[1,0,1]
	v_pk_fma_f32 v[100:101], v[8:9], s[2:3], v[166:167] op_sel_hi:[1,0,1]
	v_pk_fma_f32 v[102:103], v[10:11], s[2:3], v[168:169] op_sel_hi:[1,0,1]
	v_pk_fma_f32 v[164:165], v[12:13], s[2:3], v[170:171] op_sel_hi:[1,0,1]
	v_pk_fma_f32 v[166:167], v[14:15], s[2:3], v[172:173] op_sel_hi:[1,0,1]
	v_pk_fma_f32 v[168:169], v[16:17], s[2:3], v[174:175] op_sel_hi:[1,0,1]
	v_pk_fma_f32 v[162:163], v[18:19], s[2:3], v[162:163] op_sel_hi:[1,0,1]
	v_pk_fma_f32 v[160:161], v[20:21], s[2:3], v[160:161] op_sel_hi:[1,0,1]
	v_pk_fma_f32 v[158:159], v[22:23], s[2:3], v[158:159] op_sel_hi:[1,0,1]
	v_pk_fma_f32 v[156:157], v[24:25], s[2:3], v[156:157] op_sel_hi:[1,0,1]
	v_pk_fma_f32 v[154:155], v[26:27], s[2:3], v[154:155] op_sel_hi:[1,0,1]
	v_pk_fma_f32 v[152:153], v[28:29], s[2:3], v[152:153] op_sel_hi:[1,0,1]
	v_pk_fma_f32 v[150:151], v[30:31], s[2:3], v[150:151] op_sel_hi:[1,0,1]
	v_readlane_b32 s2, v131, 18
	s_waitcnt vmcnt(18)
	v_cvt_scalef32_pk32_f32_fp6 v[0:31], v[86:91], 1.0
	v_pk_fma_f32 v[86:87], v[0:1], s[2:3], v[92:93] op_sel_hi:[1,0,1]
	v_pk_fma_f32 v[88:89], v[2:3], s[2:3], v[94:95] op_sel_hi:[1,0,1]
	v_pk_fma_f32 v[90:91], v[4:5], s[2:3], v[96:97] op_sel_hi:[1,0,1]
	v_pk_fma_f32 v[92:93], v[6:7], s[2:3], v[98:99] op_sel_hi:[1,0,1]
	v_pk_fma_f32 v[94:95], v[8:9], s[2:3], v[100:101] op_sel_hi:[1,0,1]
	v_pk_fma_f32 v[96:97], v[10:11], s[2:3], v[102:103] op_sel_hi:[1,0,1]
	v_pk_fma_f32 v[98:99], v[12:13], s[2:3], v[164:165] op_sel_hi:[1,0,1]
	v_pk_fma_f32 v[100:101], v[14:15], s[2:3], v[166:167] op_sel_hi:[1,0,1]
	v_pk_fma_f32 v[102:103], v[16:17], s[2:3], v[168:169] op_sel_hi:[1,0,1]
	v_pk_fma_f32 v[162:163], v[18:19], s[2:3], v[162:163] op_sel_hi:[1,0,1]
	v_pk_fma_f32 v[160:161], v[20:21], s[2:3], v[160:161] op_sel_hi:[1,0,1]
	v_pk_fma_f32 v[158:159], v[22:23], s[2:3], v[158:159] op_sel_hi:[1,0,1]
	v_pk_fma_f32 v[156:157], v[24:25], s[2:3], v[156:157] op_sel_hi:[1,0,1]
	v_pk_fma_f32 v[154:155], v[26:27], s[2:3], v[154:155] op_sel_hi:[1,0,1]
	v_pk_fma_f32 v[152:153], v[28:29], s[2:3], v[152:153] op_sel_hi:[1,0,1]
	v_pk_fma_f32 v[150:151], v[30:31], s[2:3], v[150:151] op_sel_hi:[1,0,1]
	v_readlane_b32 s2, v131, 19
	s_waitcnt vmcnt(16)
	v_cvt_scalef32_pk32_f32_fp6 v[0:31], v[80:85], 1.0
	v_pk_fma_f32 v[180:181], v[0:1], s[2:3], v[86:87] op_sel_hi:[1,0,1]
	v_pk_fma_f32 v[178:179], v[2:3], s[2:3], v[88:89] op_sel_hi:[1,0,1]
	v_pk_fma_f32 v[176:177], v[4:5], s[2:3], v[90:91] op_sel_hi:[1,0,1]
	v_pk_fma_f32 v[174:175], v[6:7], s[2:3], v[92:93] op_sel_hi:[1,0,1]
	v_pk_fma_f32 v[172:173], v[8:9], s[2:3], v[94:95] op_sel_hi:[1,0,1]
	v_pk_fma_f32 v[170:171], v[10:11], s[2:3], v[96:97] op_sel_hi:[1,0,1]
	v_pk_fma_f32 v[168:169], v[12:13], s[2:3], v[98:99] op_sel_hi:[1,0,1]
	v_pk_fma_f32 v[166:167], v[14:15], s[2:3], v[100:101] op_sel_hi:[1,0,1]
	v_pk_fma_f32 v[164:165], v[16:17], s[2:3], v[102:103] op_sel_hi:[1,0,1]
	v_pk_fma_f32 v[162:163], v[18:19], s[2:3], v[162:163] op_sel_hi:[1,0,1]
	v_pk_fma_f32 v[160:161], v[20:21], s[2:3], v[160:161] op_sel_hi:[1,0,1]
	v_pk_fma_f32 v[158:159], v[22:23], s[2:3], v[158:159] op_sel_hi:[1,0,1]
	v_pk_fma_f32 v[156:157], v[24:25], s[2:3], v[156:157] op_sel_hi:[1,0,1]
	v_pk_fma_f32 v[154:155], v[26:27], s[2:3], v[154:155] op_sel_hi:[1,0,1]
	v_pk_fma_f32 v[152:153], v[28:29], s[2:3], v[152:153] op_sel_hi:[1,0,1]
	v_pk_fma_f32 v[150:151], v[30:31], s[2:3], v[150:151] op_sel_hi:[1,0,1]
	v_readlane_b32 s2, v241, 28
	v_readlane_b32 s3, v241, 29
	v_readlane_b32 s100, v241, 30
	v_readlane_b32 s101, v241, 31
	s_nop 1
	buffer_load_dwordx4 v[98:101], v129, s[44:47], s2 offen nt
	buffer_load_dwordx2 v[102:103], v210, s[44:47], s2 offen nt
	buffer_load_dwordx4 v[92:95], v129, s[44:47], s3 offen nt
	buffer_load_dwordx2 v[96:97], v210, s[44:47], s3 offen nt
	buffer_load_dwordx4 v[86:89], v129, s[44:47], s100 offen nt
	buffer_load_dwordx2 v[90:91], v210, s[44:47], s100 offen nt
	buffer_load_dwordx4 v[80:83], v129, s[44:47], s101 offen nt
	buffer_load_dwordx2 v[84:85], v210, s[44:47], s101 offen nt
	v_readlane_b32 s2, v131, 20
	s_waitcnt vmcnt(22)
	v_cvt_scalef32_pk32_f32_fp6 v[0:31], v[74:79], 1.0
	v_pk_fma_f32 v[74:75], v[0:1], s[2:3], v[180:181] op_sel_hi:[1,0,1]
	v_pk_fma_f32 v[76:77], v[2:3], s[2:3], v[178:179] op_sel_hi:[1,0,1]
	v_pk_fma_f32 v[78:79], v[4:5], s[2:3], v[176:177] op_sel_hi:[1,0,1]
	v_pk_fma_f32 v[174:175], v[6:7], s[2:3], v[174:175] op_sel_hi:[1,0,1]
	v_pk_fma_f32 v[172:173], v[8:9], s[2:3], v[172:173] op_sel_hi:[1,0,1]
	v_pk_fma_f32 v[170:171], v[10:11], s[2:3], v[170:171] op_sel_hi:[1,0,1]
	v_pk_fma_f32 v[168:169], v[12:13], s[2:3], v[168:169] op_sel_hi:[1,0,1]
	v_pk_fma_f32 v[166:167], v[14:15], s[2:3], v[166:167] op_sel_hi:[1,0,1]
	v_pk_fma_f32 v[164:165], v[16:17], s[2:3], v[164:165] op_sel_hi:[1,0,1]
	v_pk_fma_f32 v[162:163], v[18:19], s[2:3], v[162:163] op_sel_hi:[1,0,1]
	v_pk_fma_f32 v[160:161], v[20:21], s[2:3], v[160:161] op_sel_hi:[1,0,1]
	v_pk_fma_f32 v[158:159], v[22:23], s[2:3], v[158:159] op_sel_hi:[1,0,1]
	v_pk_fma_f32 v[156:157], v[24:25], s[2:3], v[156:157] op_sel_hi:[1,0,1]
	v_pk_fma_f32 v[154:155], v[26:27], s[2:3], v[154:155] op_sel_hi:[1,0,1]
	v_pk_fma_f32 v[152:153], v[28:29], s[2:3], v[152:153] op_sel_hi:[1,0,1]
	v_pk_fma_f32 v[150:151], v[30:31], s[2:3], v[150:151] op_sel_hi:[1,0,1]
	v_readlane_b32 s2, v131, 21
	s_waitcnt vmcnt(20)
	v_cvt_scalef32_pk32_f32_fp6 v[0:31], v[68:73], 1.0
	v_pk_fma_f32 v[68:69], v[0:1], s[2:3], v[74:75] op_sel_hi:[1,0,1]
	v_pk_fma_f32 v[70:71], v[2:3], s[2:3], v[76:77] op_sel_hi:[1,0,1]
	v_pk_fma_f32 v[72:73], v[4:5], s[2:3], v[78:79] op_sel_hi:[1,0,1]
	v_pk_fma_f32 v[74:75], v[6:7], s[2:3], v[174:175] op_sel_hi:[1,0,1]
	v_pk_fma_f32 v[76:77], v[8:9], s[2:3], v[172:173] op_sel_hi:[1,0,1]
	v_pk_fma_f32 v[78:79], v[10:11], s[2:3], v[170:171] op_sel_hi:[1,0,1]
	v_pk_fma_f32 v[168:169], v[12:13], s[2:3], v[168:169] op_sel_hi:[1,0,1]
	v_pk_fma_f32 v[166:167], v[14:15], s[2:3], v[166:167] op_sel_hi:[1,0,1]
	v_pk_fma_f32 v[164:165], v[16:17], s[2:3], v[164:165] op_sel_hi:[1,0,1]
	v_pk_fma_f32 v[162:163], v[18:19], s[2:3], v[162:163] op_sel_hi:[1,0,1]
	v_pk_fma_f32 v[160:161], v[20:21], s[2:3], v[160:161] op_sel_hi:[1,0,1]
	v_pk_fma_f32 v[158:159], v[22:23], s[2:3], v[158:159] op_sel_hi:[1,0,1]
	v_pk_fma_f32 v[156:157], v[24:25], s[2:3], v[156:157] op_sel_hi:[1,0,1]
	v_pk_fma_f32 v[154:155], v[26:27], s[2:3], v[154:155] op_sel_hi:[1,0,1]
	v_pk_fma_f32 v[152:153], v[28:29], s[2:3], v[152:153] op_sel_hi:[1,0,1]
	v_pk_fma_f32 v[150:151], v[30:31], s[2:3], v[150:151] op_sel_hi:[1,0,1]
	v_readlane_b32 s2, v131, 22
	s_waitcnt vmcnt(18)
	v_cvt_scalef32_pk32_f32_fp6 v[0:31], v[56:61], 1.0
	v_pk_fma_f32 v[56:57], v[0:1], s[2:3], v[68:69] op_sel_hi:[1,0,1]
	v_pk_fma_f32 v[58:59], v[2:3], s[2:3], v[70:71] op_sel_hi:[1,0,1]
	v_pk_fma_f32 v[60:61], v[4:5], s[2:3], v[72:73] op_sel_hi:[1,0,1]
	v_pk_fma_f32 v[68:69], v[6:7], s[2:3], v[74:75] op_sel_hi:[1,0,1]
	v_pk_fma_f32 v[70:71], v[8:9], s[2:3], v[76:77] op_sel_hi:[1,0,1]
	v_pk_fma_f32 v[72:73], v[10:11], s[2:3], v[78:79] op_sel_hi:[1,0,1]
	v_pk_fma_f32 v[74:75], v[12:13], s[2:3], v[168:169] op_sel_hi:[1,0,1]
	v_pk_fma_f32 v[76:77], v[14:15], s[2:3], v[166:167] op_sel_hi:[1,0,1]
	v_pk_fma_f32 v[78:79], v[16:17], s[2:3], v[164:165] op_sel_hi:[1,0,1]
	v_pk_fma_f32 v[162:163], v[18:19], s[2:3], v[162:163] op_sel_hi:[1,0,1]
	v_pk_fma_f32 v[160:161], v[20:21], s[2:3], v[160:161] op_sel_hi:[1,0,1]
	v_pk_fma_f32 v[158:159], v[22:23], s[2:3], v[158:159] op_sel_hi:[1,0,1]
	v_pk_fma_f32 v[156:157], v[24:25], s[2:3], v[156:157] op_sel_hi:[1,0,1]
	v_pk_fma_f32 v[154:155], v[26:27], s[2:3], v[154:155] op_sel_hi:[1,0,1]
	v_pk_fma_f32 v[152:153], v[28:29], s[2:3], v[152:153] op_sel_hi:[1,0,1]
	v_pk_fma_f32 v[150:151], v[30:31], s[2:3], v[150:151] op_sel_hi:[1,0,1]
	v_readlane_b32 s2, v131, 23
	s_waitcnt vmcnt(16)
	v_cvt_scalef32_pk32_f32_fp6 v[0:31], v[44:49], 1.0
	v_pk_fma_f32 v[164:165], v[0:1], s[2:3], v[56:57] op_sel_hi:[1,0,1]
	v_pk_fma_f32 v[166:167], v[2:3], s[2:3], v[58:59] op_sel_hi:[1,0,1]
	v_pk_fma_f32 v[168:169], v[4:5], s[2:3], v[60:61] op_sel_hi:[1,0,1]
	v_pk_fma_f32 v[170:171], v[6:7], s[2:3], v[68:69] op_sel_hi:[1,0,1]
	v_pk_fma_f32 v[172:173], v[8:9], s[2:3], v[70:71] op_sel_hi:[1,0,1]
	v_pk_fma_f32 v[174:175], v[10:11], s[2:3], v[72:73] op_sel_hi:[1,0,1]
	v_pk_fma_f32 v[176:177], v[12:13], s[2:3], v[74:75] op_sel_hi:[1,0,1]
	v_pk_fma_f32 v[178:179], v[14:15], s[2:3], v[76:77] op_sel_hi:[1,0,1]
	v_pk_fma_f32 v[180:181], v[16:17], s[2:3], v[78:79] op_sel_hi:[1,0,1]
	v_pk_fma_f32 v[162:163], v[18:19], s[2:3], v[162:163] op_sel_hi:[1,0,1]
	v_pk_fma_f32 v[160:161], v[20:21], s[2:3], v[160:161] op_sel_hi:[1,0,1]
	v_pk_fma_f32 v[158:159], v[22:23], s[2:3], v[158:159] op_sel_hi:[1,0,1]
	v_pk_fma_f32 v[156:157], v[24:25], s[2:3], v[156:157] op_sel_hi:[1,0,1]
	v_pk_fma_f32 v[154:155], v[26:27], s[2:3], v[154:155] op_sel_hi:[1,0,1]
	v_pk_fma_f32 v[152:153], v[28:29], s[2:3], v[152:153] op_sel_hi:[1,0,1]
	v_pk_fma_f32 v[150:151], v[30:31], s[2:3], v[150:151] op_sel_hi:[1,0,1]
	v_readlane_b32 s2, v241, 32
	v_readlane_b32 s3, v241, 33
	v_readlane_b32 s100, v241, 34
	v_readlane_b32 s101, v241, 35
	s_nop 1
	buffer_load_dwordx4 v[74:77], v129, s[44:47], s2 offen nt
	buffer_load_dwordx2 v[78:79], v210, s[44:47], s2 offen nt
	buffer_load_dwordx4 v[68:71], v129, s[44:47], s3 offen nt
	buffer_load_dwordx2 v[72:73], v210, s[44:47], s3 offen nt
	buffer_load_dwordx4 v[56:59], v129, s[44:47], s100 offen nt
	buffer_load_dwordx2 v[60:61], v210, s[44:47], s100 offen nt
	buffer_load_dwordx4 v[44:47], v129, s[44:47], s101 offen nt
	buffer_load_dwordx2 v[48:49], v210, s[44:47], s101 offen nt
	v_readlane_b32 s2, v131, 24
	s_waitcnt vmcnt(22)
	v_cvt_scalef32_pk32_f32_fp6 v[0:31], v[62:67], 1.0
	v_pk_fma_f32 v[62:63], v[0:1], s[2:3], v[164:165] op_sel_hi:[1,0,1]
	v_pk_fma_f32 v[64:65], v[2:3], s[2:3], v[166:167] op_sel_hi:[1,0,1]
	v_pk_fma_f32 v[66:67], v[4:5], s[2:3], v[168:169] op_sel_hi:[1,0,1]
	v_pk_fma_f32 v[164:165], v[6:7], s[2:3], v[170:171] op_sel_hi:[1,0,1]
	v_pk_fma_f32 v[166:167], v[8:9], s[2:3], v[172:173] op_sel_hi:[1,0,1]
	v_pk_fma_f32 v[168:169], v[10:11], s[2:3], v[174:175] op_sel_hi:[1,0,1]
	v_pk_fma_f32 v[170:171], v[12:13], s[2:3], v[176:177] op_sel_hi:[1,0,1]
	v_pk_fma_f32 v[172:173], v[14:15], s[2:3], v[178:179] op_sel_hi:[1,0,1]
	v_pk_fma_f32 v[174:175], v[16:17], s[2:3], v[180:181] op_sel_hi:[1,0,1]
	v_pk_fma_f32 v[162:163], v[18:19], s[2:3], v[162:163] op_sel_hi:[1,0,1]
	v_pk_fma_f32 v[160:161], v[20:21], s[2:3], v[160:161] op_sel_hi:[1,0,1]
	v_pk_fma_f32 v[158:159], v[22:23], s[2:3], v[158:159] op_sel_hi:[1,0,1]
	v_pk_fma_f32 v[156:157], v[24:25], s[2:3], v[156:157] op_sel_hi:[1,0,1]
	v_pk_fma_f32 v[154:155], v[26:27], s[2:3], v[154:155] op_sel_hi:[1,0,1]
	v_pk_fma_f32 v[152:153], v[28:29], s[2:3], v[152:153] op_sel_hi:[1,0,1]
	v_pk_fma_f32 v[150:151], v[30:31], s[2:3], v[150:151] op_sel_hi:[1,0,1]
	v_readlane_b32 s2, v131, 25
	s_waitcnt vmcnt(20)
	v_cvt_scalef32_pk32_f32_fp6 v[0:31], v[50:55], 1.0
	v_pk_fma_f32 v[50:51], v[0:1], s[2:3], v[62:63] op_sel_hi:[1,0,1]
	v_pk_fma_f32 v[52:53], v[2:3], s[2:3], v[64:65] op_sel_hi:[1,0,1]
	v_pk_fma_f32 v[54:55], v[4:5], s[2:3], v[66:67] op_sel_hi:[1,0,1]
	v_pk_fma_f32 v[62:63], v[6:7], s[2:3], v[164:165] op_sel_hi:[1,0,1]
	v_pk_fma_f32 v[64:65], v[8:9], s[2:3], v[166:167] op_sel_hi:[1,0,1]
	v_pk_fma_f32 v[66:67], v[10:11], s[2:3], v[168:169] op_sel_hi:[1,0,1]
	v_pk_fma_f32 v[164:165], v[12:13], s[2:3], v[170:171] op_sel_hi:[1,0,1]
	v_pk_fma_f32 v[166:167], v[14:15], s[2:3], v[172:173] op_sel_hi:[1,0,1]
	v_pk_fma_f32 v[168:169], v[16:17], s[2:3], v[174:175] op_sel_hi:[1,0,1]
	v_pk_fma_f32 v[162:163], v[18:19], s[2:3], v[162:163] op_sel_hi:[1,0,1]
	v_pk_fma_f32 v[160:161], v[20:21], s[2:3], v[160:161] op_sel_hi:[1,0,1]
	v_pk_fma_f32 v[158:159], v[22:23], s[2:3], v[158:159] op_sel_hi:[1,0,1]
	v_pk_fma_f32 v[156:157], v[24:25], s[2:3], v[156:157] op_sel_hi:[1,0,1]
	v_pk_fma_f32 v[154:155], v[26:27], s[2:3], v[154:155] op_sel_hi:[1,0,1]
	v_pk_fma_f32 v[152:153], v[28:29], s[2:3], v[152:153] op_sel_hi:[1,0,1]
	v_pk_fma_f32 v[150:151], v[30:31], s[2:3], v[150:151] op_sel_hi:[1,0,1]
	v_readlane_b32 s2, v131, 26
	s_waitcnt vmcnt(18)
	v_cvt_scalef32_pk32_f32_fp6 v[0:31], v[38:43], 1.0
	v_pk_fma_f32 v[38:39], v[0:1], s[2:3], v[50:51] op_sel_hi:[1,0,1]
	v_pk_fma_f32 v[40:41], v[2:3], s[2:3], v[52:53] op_sel_hi:[1,0,1]
	v_pk_fma_f32 v[42:43], v[4:5], s[2:3], v[54:55] op_sel_hi:[1,0,1]
	v_pk_fma_f32 v[50:51], v[6:7], s[2:3], v[62:63] op_sel_hi:[1,0,1]
	v_pk_fma_f32 v[52:53], v[8:9], s[2:3], v[64:65] op_sel_hi:[1,0,1]
	v_pk_fma_f32 v[54:55], v[10:11], s[2:3], v[66:67] op_sel_hi:[1,0,1]
	v_pk_fma_f32 v[62:63], v[12:13], s[2:3], v[164:165] op_sel_hi:[1,0,1]
	v_pk_fma_f32 v[64:65], v[14:15], s[2:3], v[166:167] op_sel_hi:[1,0,1]
	v_pk_fma_f32 v[66:67], v[16:17], s[2:3], v[168:169] op_sel_hi:[1,0,1]
	v_pk_fma_f32 v[162:163], v[18:19], s[2:3], v[162:163] op_sel_hi:[1,0,1]
	v_pk_fma_f32 v[160:161], v[20:21], s[2:3], v[160:161] op_sel_hi:[1,0,1]
	v_pk_fma_f32 v[158:159], v[22:23], s[2:3], v[158:159] op_sel_hi:[1,0,1]
	v_pk_fma_f32 v[156:157], v[24:25], s[2:3], v[156:157] op_sel_hi:[1,0,1]
	v_pk_fma_f32 v[154:155], v[26:27], s[2:3], v[154:155] op_sel_hi:[1,0,1]
	v_pk_fma_f32 v[152:153], v[28:29], s[2:3], v[152:153] op_sel_hi:[1,0,1]
	v_pk_fma_f32 v[150:151], v[30:31], s[2:3], v[150:151] op_sel_hi:[1,0,1]
	v_readlane_b32 s2, v131, 27
	s_waitcnt vmcnt(16)
	v_cvt_scalef32_pk32_f32_fp6 v[0:31], v[32:37], 1.0
	v_pk_fma_f32 v[164:165], v[0:1], s[2:3], v[38:39] op_sel_hi:[1,0,1]
	v_pk_fma_f32 v[166:167], v[2:3], s[2:3], v[40:41] op_sel_hi:[1,0,1]
	v_pk_fma_f32 v[168:169], v[4:5], s[2:3], v[42:43] op_sel_hi:[1,0,1]
	v_pk_fma_f32 v[170:171], v[6:7], s[2:3], v[50:51] op_sel_hi:[1,0,1]
	v_pk_fma_f32 v[172:173], v[8:9], s[2:3], v[52:53] op_sel_hi:[1,0,1]
	v_pk_fma_f32 v[174:175], v[10:11], s[2:3], v[54:55] op_sel_hi:[1,0,1]
	v_pk_fma_f32 v[176:177], v[12:13], s[2:3], v[62:63] op_sel_hi:[1,0,1]
	v_pk_fma_f32 v[178:179], v[14:15], s[2:3], v[64:65] op_sel_hi:[1,0,1]
	v_pk_fma_f32 v[180:181], v[16:17], s[2:3], v[66:67] op_sel_hi:[1,0,1]
	v_pk_fma_f32 v[162:163], v[18:19], s[2:3], v[162:163] op_sel_hi:[1,0,1]
	v_pk_fma_f32 v[160:161], v[20:21], s[2:3], v[160:161] op_sel_hi:[1,0,1]
	v_pk_fma_f32 v[158:159], v[22:23], s[2:3], v[158:159] op_sel_hi:[1,0,1]
	v_pk_fma_f32 v[156:157], v[24:25], s[2:3], v[156:157] op_sel_hi:[1,0,1]
	v_pk_fma_f32 v[154:155], v[26:27], s[2:3], v[154:155] op_sel_hi:[1,0,1]
	v_pk_fma_f32 v[152:153], v[28:29], s[2:3], v[152:153] op_sel_hi:[1,0,1]
	v_pk_fma_f32 v[150:151], v[30:31], s[2:3], v[150:151] op_sel_hi:[1,0,1]
	v_readlane_b32 s2, v241, 36
	v_readlane_b32 s3, v241, 37
	v_readlane_b32 s100, v241, 38
	v_readlane_b32 s101, v241, 39
	s_nop 1
	buffer_load_dwordx4 v[62:65], v129, s[44:47], s2 offen nt
	buffer_load_dwordx2 v[66:67], v210, s[44:47], s2 offen nt
	buffer_load_dwordx4 v[50:53], v129, s[44:47], s3 offen nt
	buffer_load_dwordx2 v[54:55], v210, s[44:47], s3 offen nt
	buffer_load_dwordx4 v[38:41], v129, s[44:47], s100 offen nt
	buffer_load_dwordx2 v[42:43], v210, s[44:47], s100 offen nt
	buffer_load_dwordx4 v[32:35], v129, s[44:47], s101 offen nt
	buffer_load_dwordx2 v[36:37], v210, s[44:47], s101 offen nt
	v_readlane_b32 s2, v131, 28
	s_waitcnt vmcnt(22)
	v_cvt_scalef32_pk32_f32_fp6 v[0:31], v[98:103], 1.0
	v_pk_fma_f32 v[98:99], v[0:1], s[2:3], v[164:165] op_sel_hi:[1,0,1]
	v_pk_fma_f32 v[100:101], v[2:3], s[2:3], v[166:167] op_sel_hi:[1,0,1]
	v_pk_fma_f32 v[102:103], v[4:5], s[2:3], v[168:169] op_sel_hi:[1,0,1]
	v_pk_fma_f32 v[164:165], v[6:7], s[2:3], v[170:171] op_sel_hi:[1,0,1]
	v_pk_fma_f32 v[166:167], v[8:9], s[2:3], v[172:173] op_sel_hi:[1,0,1]
	v_pk_fma_f32 v[168:169], v[10:11], s[2:3], v[174:175] op_sel_hi:[1,0,1]
	v_pk_fma_f32 v[170:171], v[12:13], s[2:3], v[176:177] op_sel_hi:[1,0,1]
	v_pk_fma_f32 v[172:173], v[14:15], s[2:3], v[178:179] op_sel_hi:[1,0,1]
	v_pk_fma_f32 v[174:175], v[16:17], s[2:3], v[180:181] op_sel_hi:[1,0,1]
	v_pk_fma_f32 v[162:163], v[18:19], s[2:3], v[162:163] op_sel_hi:[1,0,1]
	v_pk_fma_f32 v[160:161], v[20:21], s[2:3], v[160:161] op_sel_hi:[1,0,1]
	v_pk_fma_f32 v[158:159], v[22:23], s[2:3], v[158:159] op_sel_hi:[1,0,1]
	v_pk_fma_f32 v[156:157], v[24:25], s[2:3], v[156:157] op_sel_hi:[1,0,1]
	v_pk_fma_f32 v[154:155], v[26:27], s[2:3], v[154:155] op_sel_hi:[1,0,1]
	v_pk_fma_f32 v[152:153], v[28:29], s[2:3], v[152:153] op_sel_hi:[1,0,1]
	v_pk_fma_f32 v[150:151], v[30:31], s[2:3], v[150:151] op_sel_hi:[1,0,1]
	v_readlane_b32 s2, v131, 29
	s_waitcnt vmcnt(20)
	v_cvt_scalef32_pk32_f32_fp6 v[0:31], v[92:97], 1.0
	v_pk_fma_f32 v[92:93], v[0:1], s[2:3], v[98:99] op_sel_hi:[1,0,1]
	v_pk_fma_f32 v[94:95], v[2:3], s[2:3], v[100:101] op_sel_hi:[1,0,1]
	v_pk_fma_f32 v[96:97], v[4:5], s[2:3], v[102:103] op_sel_hi:[1,0,1]
	v_pk_fma_f32 v[98:99], v[6:7], s[2:3], v[164:165] op_sel_hi:[1,0,1]
	v_pk_fma_f32 v[100:101], v[8:9], s[2:3], v[166:167] op_sel_hi:[1,0,1]
	v_pk_fma_f32 v[102:103], v[10:11], s[2:3], v[168:169] op_sel_hi:[1,0,1]
	v_pk_fma_f32 v[164:165], v[12:13], s[2:3], v[170:171] op_sel_hi:[1,0,1]
	v_pk_fma_f32 v[166:167], v[14:15], s[2:3], v[172:173] op_sel_hi:[1,0,1]
	v_pk_fma_f32 v[168:169], v[16:17], s[2:3], v[174:175] op_sel_hi:[1,0,1]
	v_pk_fma_f32 v[162:163], v[18:19], s[2:3], v[162:163] op_sel_hi:[1,0,1]
	v_pk_fma_f32 v[160:161], v[20:21], s[2:3], v[160:161] op_sel_hi:[1,0,1]
	v_pk_fma_f32 v[158:159], v[22:23], s[2:3], v[158:159] op_sel_hi:[1,0,1]
	v_pk_fma_f32 v[156:157], v[24:25], s[2:3], v[156:157] op_sel_hi:[1,0,1]
	v_pk_fma_f32 v[154:155], v[26:27], s[2:3], v[154:155] op_sel_hi:[1,0,1]
	v_pk_fma_f32 v[152:153], v[28:29], s[2:3], v[152:153] op_sel_hi:[1,0,1]
	v_pk_fma_f32 v[150:151], v[30:31], s[2:3], v[150:151] op_sel_hi:[1,0,1]
	v_readlane_b32 s2, v131, 30
	s_waitcnt vmcnt(18)
	v_cvt_scalef32_pk32_f32_fp6 v[0:31], v[86:91], 1.0
	v_pk_fma_f32 v[86:87], v[0:1], s[2:3], v[92:93] op_sel_hi:[1,0,1]
	v_pk_fma_f32 v[88:89], v[2:3], s[2:3], v[94:95] op_sel_hi:[1,0,1]
	v_pk_fma_f32 v[90:91], v[4:5], s[2:3], v[96:97] op_sel_hi:[1,0,1]
	v_pk_fma_f32 v[92:93], v[6:7], s[2:3], v[98:99] op_sel_hi:[1,0,1]
	v_pk_fma_f32 v[94:95], v[8:9], s[2:3], v[100:101] op_sel_hi:[1,0,1]
	v_pk_fma_f32 v[96:97], v[10:11], s[2:3], v[102:103] op_sel_hi:[1,0,1]
	v_pk_fma_f32 v[98:99], v[12:13], s[2:3], v[164:165] op_sel_hi:[1,0,1]
	v_pk_fma_f32 v[100:101], v[14:15], s[2:3], v[166:167] op_sel_hi:[1,0,1]
	v_pk_fma_f32 v[102:103], v[16:17], s[2:3], v[168:169] op_sel_hi:[1,0,1]
	v_pk_fma_f32 v[162:163], v[18:19], s[2:3], v[162:163] op_sel_hi:[1,0,1]
	v_pk_fma_f32 v[160:161], v[20:21], s[2:3], v[160:161] op_sel_hi:[1,0,1]
	v_pk_fma_f32 v[158:159], v[22:23], s[2:3], v[158:159] op_sel_hi:[1,0,1]
	v_pk_fma_f32 v[156:157], v[24:25], s[2:3], v[156:157] op_sel_hi:[1,0,1]
	v_pk_fma_f32 v[154:155], v[26:27], s[2:3], v[154:155] op_sel_hi:[1,0,1]
	v_pk_fma_f32 v[152:153], v[28:29], s[2:3], v[152:153] op_sel_hi:[1,0,1]
	v_pk_fma_f32 v[150:151], v[30:31], s[2:3], v[150:151] op_sel_hi:[1,0,1]
	v_readlane_b32 s2, v131, 31
	s_waitcnt vmcnt(16)
	v_cvt_scalef32_pk32_f32_fp6 v[0:31], v[80:85], 1.0
	v_pk_fma_f32 v[180:181], v[0:1], s[2:3], v[86:87] op_sel_hi:[1,0,1]
	v_pk_fma_f32 v[178:179], v[2:3], s[2:3], v[88:89] op_sel_hi:[1,0,1]
	v_pk_fma_f32 v[176:177], v[4:5], s[2:3], v[90:91] op_sel_hi:[1,0,1]
	v_pk_fma_f32 v[174:175], v[6:7], s[2:3], v[92:93] op_sel_hi:[1,0,1]
	v_pk_fma_f32 v[172:173], v[8:9], s[2:3], v[94:95] op_sel_hi:[1,0,1]
	v_pk_fma_f32 v[170:171], v[10:11], s[2:3], v[96:97] op_sel_hi:[1,0,1]
	v_pk_fma_f32 v[168:169], v[12:13], s[2:3], v[98:99] op_sel_hi:[1,0,1]
	v_pk_fma_f32 v[166:167], v[14:15], s[2:3], v[100:101] op_sel_hi:[1,0,1]
	v_pk_fma_f32 v[164:165], v[16:17], s[2:3], v[102:103] op_sel_hi:[1,0,1]
	v_pk_fma_f32 v[162:163], v[18:19], s[2:3], v[162:163] op_sel_hi:[1,0,1]
	v_pk_fma_f32 v[160:161], v[20:21], s[2:3], v[160:161] op_sel_hi:[1,0,1]
	v_pk_fma_f32 v[158:159], v[22:23], s[2:3], v[158:159] op_sel_hi:[1,0,1]
	v_pk_fma_f32 v[156:157], v[24:25], s[2:3], v[156:157] op_sel_hi:[1,0,1]
	v_pk_fma_f32 v[154:155], v[26:27], s[2:3], v[154:155] op_sel_hi:[1,0,1]
	v_pk_fma_f32 v[152:153], v[28:29], s[2:3], v[152:153] op_sel_hi:[1,0,1]
	v_pk_fma_f32 v[150:151], v[30:31], s[2:3], v[150:151] op_sel_hi:[1,0,1]
	v_readlane_b32 s2, v241, 40
	v_readlane_b32 s3, v241, 41
	v_readlane_b32 s100, v241, 42
	v_readlane_b32 s101, v241, 43
	s_nop 1
	buffer_load_dwordx4 v[98:101], v129, s[44:47], s2 offen nt
	buffer_load_dwordx2 v[102:103], v210, s[44:47], s2 offen nt
	buffer_load_dwordx4 v[92:95], v129, s[44:47], s3 offen nt
	buffer_load_dwordx2 v[96:97], v210, s[44:47], s3 offen nt
	buffer_load_dwordx4 v[86:89], v129, s[44:47], s100 offen nt
	buffer_load_dwordx2 v[90:91], v210, s[44:47], s100 offen nt
	buffer_load_dwordx4 v[80:83], v129, s[44:47], s101 offen nt
	buffer_load_dwordx2 v[84:85], v210, s[44:47], s101 offen nt
	v_readlane_b32 s2, v131, 32
	s_waitcnt vmcnt(22)
	v_cvt_scalef32_pk32_f32_fp6 v[0:31], v[74:79], 1.0
	v_pk_fma_f32 v[74:75], v[0:1], s[2:3], v[180:181] op_sel_hi:[1,0,1]
	v_pk_fma_f32 v[76:77], v[2:3], s[2:3], v[178:179] op_sel_hi:[1,0,1]
	v_pk_fma_f32 v[78:79], v[4:5], s[2:3], v[176:177] op_sel_hi:[1,0,1]
	v_pk_fma_f32 v[174:175], v[6:7], s[2:3], v[174:175] op_sel_hi:[1,0,1]
	v_pk_fma_f32 v[172:173], v[8:9], s[2:3], v[172:173] op_sel_hi:[1,0,1]
	v_pk_fma_f32 v[170:171], v[10:11], s[2:3], v[170:171] op_sel_hi:[1,0,1]
	v_pk_fma_f32 v[168:169], v[12:13], s[2:3], v[168:169] op_sel_hi:[1,0,1]
	v_pk_fma_f32 v[166:167], v[14:15], s[2:3], v[166:167] op_sel_hi:[1,0,1]
	v_pk_fma_f32 v[164:165], v[16:17], s[2:3], v[164:165] op_sel_hi:[1,0,1]
	v_pk_fma_f32 v[162:163], v[18:19], s[2:3], v[162:163] op_sel_hi:[1,0,1]
	v_pk_fma_f32 v[160:161], v[20:21], s[2:3], v[160:161] op_sel_hi:[1,0,1]
	v_pk_fma_f32 v[158:159], v[22:23], s[2:3], v[158:159] op_sel_hi:[1,0,1]
	v_pk_fma_f32 v[156:157], v[24:25], s[2:3], v[156:157] op_sel_hi:[1,0,1]
	v_pk_fma_f32 v[154:155], v[26:27], s[2:3], v[154:155] op_sel_hi:[1,0,1]
	v_pk_fma_f32 v[152:153], v[28:29], s[2:3], v[152:153] op_sel_hi:[1,0,1]
	v_pk_fma_f32 v[150:151], v[30:31], s[2:3], v[150:151] op_sel_hi:[1,0,1]
	v_readlane_b32 s2, v131, 33
	s_waitcnt vmcnt(20)
	v_cvt_scalef32_pk32_f32_fp6 v[0:31], v[68:73], 1.0
	v_pk_fma_f32 v[68:69], v[0:1], s[2:3], v[74:75] op_sel_hi:[1,0,1]
	v_pk_fma_f32 v[70:71], v[2:3], s[2:3], v[76:77] op_sel_hi:[1,0,1]
	v_pk_fma_f32 v[72:73], v[4:5], s[2:3], v[78:79] op_sel_hi:[1,0,1]
	v_pk_fma_f32 v[74:75], v[6:7], s[2:3], v[174:175] op_sel_hi:[1,0,1]
	v_pk_fma_f32 v[76:77], v[8:9], s[2:3], v[172:173] op_sel_hi:[1,0,1]
	v_pk_fma_f32 v[78:79], v[10:11], s[2:3], v[170:171] op_sel_hi:[1,0,1]
	v_pk_fma_f32 v[168:169], v[12:13], s[2:3], v[168:169] op_sel_hi:[1,0,1]
	v_pk_fma_f32 v[166:167], v[14:15], s[2:3], v[166:167] op_sel_hi:[1,0,1]
	v_pk_fma_f32 v[164:165], v[16:17], s[2:3], v[164:165] op_sel_hi:[1,0,1]
	v_pk_fma_f32 v[162:163], v[18:19], s[2:3], v[162:163] op_sel_hi:[1,0,1]
	v_pk_fma_f32 v[160:161], v[20:21], s[2:3], v[160:161] op_sel_hi:[1,0,1]
	v_pk_fma_f32 v[158:159], v[22:23], s[2:3], v[158:159] op_sel_hi:[1,0,1]
	v_pk_fma_f32 v[156:157], v[24:25], s[2:3], v[156:157] op_sel_hi:[1,0,1]
	v_pk_fma_f32 v[154:155], v[26:27], s[2:3], v[154:155] op_sel_hi:[1,0,1]
	v_pk_fma_f32 v[152:153], v[28:29], s[2:3], v[152:153] op_sel_hi:[1,0,1]
	v_pk_fma_f32 v[150:151], v[30:31], s[2:3], v[150:151] op_sel_hi:[1,0,1]
	v_readlane_b32 s2, v131, 34
	s_waitcnt vmcnt(18)
	v_cvt_scalef32_pk32_f32_fp6 v[0:31], v[56:61], 1.0
	v_pk_fma_f32 v[56:57], v[0:1], s[2:3], v[68:69] op_sel_hi:[1,0,1]
	v_pk_fma_f32 v[58:59], v[2:3], s[2:3], v[70:71] op_sel_hi:[1,0,1]
	v_pk_fma_f32 v[60:61], v[4:5], s[2:3], v[72:73] op_sel_hi:[1,0,1]
	v_pk_fma_f32 v[68:69], v[6:7], s[2:3], v[74:75] op_sel_hi:[1,0,1]
	v_pk_fma_f32 v[70:71], v[8:9], s[2:3], v[76:77] op_sel_hi:[1,0,1]
	v_pk_fma_f32 v[72:73], v[10:11], s[2:3], v[78:79] op_sel_hi:[1,0,1]
	v_pk_fma_f32 v[74:75], v[12:13], s[2:3], v[168:169] op_sel_hi:[1,0,1]
	v_pk_fma_f32 v[76:77], v[14:15], s[2:3], v[166:167] op_sel_hi:[1,0,1]
	v_pk_fma_f32 v[78:79], v[16:17], s[2:3], v[164:165] op_sel_hi:[1,0,1]
	v_pk_fma_f32 v[162:163], v[18:19], s[2:3], v[162:163] op_sel_hi:[1,0,1]
	v_pk_fma_f32 v[160:161], v[20:21], s[2:3], v[160:161] op_sel_hi:[1,0,1]
	v_pk_fma_f32 v[158:159], v[22:23], s[2:3], v[158:159] op_sel_hi:[1,0,1]
	v_pk_fma_f32 v[156:157], v[24:25], s[2:3], v[156:157] op_sel_hi:[1,0,1]
	v_pk_fma_f32 v[154:155], v[26:27], s[2:3], v[154:155] op_sel_hi:[1,0,1]
	v_pk_fma_f32 v[152:153], v[28:29], s[2:3], v[152:153] op_sel_hi:[1,0,1]
	v_pk_fma_f32 v[150:151], v[30:31], s[2:3], v[150:151] op_sel_hi:[1,0,1]
	v_readlane_b32 s2, v131, 35
	s_waitcnt vmcnt(16)
	v_cvt_scalef32_pk32_f32_fp6 v[0:31], v[44:49], 1.0
	v_pk_fma_f32 v[164:165], v[0:1], s[2:3], v[56:57] op_sel_hi:[1,0,1]
	v_pk_fma_f32 v[166:167], v[2:3], s[2:3], v[58:59] op_sel_hi:[1,0,1]
	v_pk_fma_f32 v[168:169], v[4:5], s[2:3], v[60:61] op_sel_hi:[1,0,1]
	v_pk_fma_f32 v[170:171], v[6:7], s[2:3], v[68:69] op_sel_hi:[1,0,1]
	v_pk_fma_f32 v[172:173], v[8:9], s[2:3], v[70:71] op_sel_hi:[1,0,1]
	v_pk_fma_f32 v[174:175], v[10:11], s[2:3], v[72:73] op_sel_hi:[1,0,1]
	v_pk_fma_f32 v[176:177], v[12:13], s[2:3], v[74:75] op_sel_hi:[1,0,1]
	v_pk_fma_f32 v[178:179], v[14:15], s[2:3], v[76:77] op_sel_hi:[1,0,1]
	v_pk_fma_f32 v[180:181], v[16:17], s[2:3], v[78:79] op_sel_hi:[1,0,1]
	v_pk_fma_f32 v[162:163], v[18:19], s[2:3], v[162:163] op_sel_hi:[1,0,1]
	v_pk_fma_f32 v[160:161], v[20:21], s[2:3], v[160:161] op_sel_hi:[1,0,1]
	v_pk_fma_f32 v[158:159], v[22:23], s[2:3], v[158:159] op_sel_hi:[1,0,1]
	v_pk_fma_f32 v[156:157], v[24:25], s[2:3], v[156:157] op_sel_hi:[1,0,1]
	v_pk_fma_f32 v[154:155], v[26:27], s[2:3], v[154:155] op_sel_hi:[1,0,1]
	v_pk_fma_f32 v[152:153], v[28:29], s[2:3], v[152:153] op_sel_hi:[1,0,1]
	v_pk_fma_f32 v[150:151], v[30:31], s[2:3], v[150:151] op_sel_hi:[1,0,1]
	v_readlane_b32 s2, v241, 44
	v_readlane_b32 s3, v241, 45
	v_readlane_b32 s100, v241, 46
	v_readlane_b32 s101, v241, 47
	s_nop 1
	buffer_load_dwordx4 v[74:77], v129, s[44:47], s2 offen nt
	buffer_load_dwordx2 v[78:79], v210, s[44:47], s2 offen nt
	buffer_load_dwordx4 v[68:71], v129, s[44:47], s3 offen nt
	buffer_load_dwordx2 v[72:73], v210, s[44:47], s3 offen nt
	buffer_load_dwordx4 v[56:59], v129, s[44:47], s100 offen nt
	buffer_load_dwordx2 v[60:61], v210, s[44:47], s100 offen nt
	buffer_load_dwordx4 v[44:47], v129, s[44:47], s101 offen nt
	buffer_load_dwordx2 v[48:49], v210, s[44:47], s101 offen nt
	v_readlane_b32 s2, v131, 36
	s_waitcnt vmcnt(22)
	v_cvt_scalef32_pk32_f32_fp6 v[0:31], v[62:67], 1.0
	v_pk_fma_f32 v[62:63], v[0:1], s[2:3], v[164:165] op_sel_hi:[1,0,1]
	v_pk_fma_f32 v[64:65], v[2:3], s[2:3], v[166:167] op_sel_hi:[1,0,1]
	v_pk_fma_f32 v[66:67], v[4:5], s[2:3], v[168:169] op_sel_hi:[1,0,1]
	v_pk_fma_f32 v[164:165], v[6:7], s[2:3], v[170:171] op_sel_hi:[1,0,1]
	v_pk_fma_f32 v[166:167], v[8:9], s[2:3], v[172:173] op_sel_hi:[1,0,1]
	v_pk_fma_f32 v[168:169], v[10:11], s[2:3], v[174:175] op_sel_hi:[1,0,1]
	v_pk_fma_f32 v[170:171], v[12:13], s[2:3], v[176:177] op_sel_hi:[1,0,1]
	v_pk_fma_f32 v[172:173], v[14:15], s[2:3], v[178:179] op_sel_hi:[1,0,1]
	v_pk_fma_f32 v[174:175], v[16:17], s[2:3], v[180:181] op_sel_hi:[1,0,1]
	v_pk_fma_f32 v[162:163], v[18:19], s[2:3], v[162:163] op_sel_hi:[1,0,1]
	v_pk_fma_f32 v[160:161], v[20:21], s[2:3], v[160:161] op_sel_hi:[1,0,1]
	v_pk_fma_f32 v[158:159], v[22:23], s[2:3], v[158:159] op_sel_hi:[1,0,1]
	v_pk_fma_f32 v[156:157], v[24:25], s[2:3], v[156:157] op_sel_hi:[1,0,1]
	v_pk_fma_f32 v[154:155], v[26:27], s[2:3], v[154:155] op_sel_hi:[1,0,1]
	v_pk_fma_f32 v[152:153], v[28:29], s[2:3], v[152:153] op_sel_hi:[1,0,1]
	v_pk_fma_f32 v[150:151], v[30:31], s[2:3], v[150:151] op_sel_hi:[1,0,1]
	v_readlane_b32 s2, v131, 37
	s_waitcnt vmcnt(20)
	v_cvt_scalef32_pk32_f32_fp6 v[0:31], v[50:55], 1.0
	v_pk_fma_f32 v[50:51], v[0:1], s[2:3], v[62:63] op_sel_hi:[1,0,1]
	v_pk_fma_f32 v[52:53], v[2:3], s[2:3], v[64:65] op_sel_hi:[1,0,1]
	v_pk_fma_f32 v[54:55], v[4:5], s[2:3], v[66:67] op_sel_hi:[1,0,1]
	v_pk_fma_f32 v[62:63], v[6:7], s[2:3], v[164:165] op_sel_hi:[1,0,1]
	v_pk_fma_f32 v[64:65], v[8:9], s[2:3], v[166:167] op_sel_hi:[1,0,1]
	v_pk_fma_f32 v[66:67], v[10:11], s[2:3], v[168:169] op_sel_hi:[1,0,1]
	v_pk_fma_f32 v[164:165], v[12:13], s[2:3], v[170:171] op_sel_hi:[1,0,1]
	v_pk_fma_f32 v[166:167], v[14:15], s[2:3], v[172:173] op_sel_hi:[1,0,1]
	v_pk_fma_f32 v[168:169], v[16:17], s[2:3], v[174:175] op_sel_hi:[1,0,1]
	v_pk_fma_f32 v[162:163], v[18:19], s[2:3], v[162:163] op_sel_hi:[1,0,1]
	v_pk_fma_f32 v[160:161], v[20:21], s[2:3], v[160:161] op_sel_hi:[1,0,1]
	v_pk_fma_f32 v[158:159], v[22:23], s[2:3], v[158:159] op_sel_hi:[1,0,1]
	v_pk_fma_f32 v[156:157], v[24:25], s[2:3], v[156:157] op_sel_hi:[1,0,1]
	v_pk_fma_f32 v[154:155], v[26:27], s[2:3], v[154:155] op_sel_hi:[1,0,1]
	v_pk_fma_f32 v[152:153], v[28:29], s[2:3], v[152:153] op_sel_hi:[1,0,1]
	v_pk_fma_f32 v[150:151], v[30:31], s[2:3], v[150:151] op_sel_hi:[1,0,1]
	v_readlane_b32 s2, v131, 38
	s_waitcnt vmcnt(18)
	v_cvt_scalef32_pk32_f32_fp6 v[0:31], v[38:43], 1.0
	v_pk_fma_f32 v[38:39], v[0:1], s[2:3], v[50:51] op_sel_hi:[1,0,1]
	v_pk_fma_f32 v[40:41], v[2:3], s[2:3], v[52:53] op_sel_hi:[1,0,1]
	v_pk_fma_f32 v[42:43], v[4:5], s[2:3], v[54:55] op_sel_hi:[1,0,1]
	v_pk_fma_f32 v[50:51], v[6:7], s[2:3], v[62:63] op_sel_hi:[1,0,1]
	v_pk_fma_f32 v[52:53], v[8:9], s[2:3], v[64:65] op_sel_hi:[1,0,1]
	v_pk_fma_f32 v[54:55], v[10:11], s[2:3], v[66:67] op_sel_hi:[1,0,1]
	v_pk_fma_f32 v[62:63], v[12:13], s[2:3], v[164:165] op_sel_hi:[1,0,1]
	v_pk_fma_f32 v[64:65], v[14:15], s[2:3], v[166:167] op_sel_hi:[1,0,1]
	v_pk_fma_f32 v[66:67], v[16:17], s[2:3], v[168:169] op_sel_hi:[1,0,1]
	v_pk_fma_f32 v[162:163], v[18:19], s[2:3], v[162:163] op_sel_hi:[1,0,1]
	v_pk_fma_f32 v[160:161], v[20:21], s[2:3], v[160:161] op_sel_hi:[1,0,1]
	v_pk_fma_f32 v[158:159], v[22:23], s[2:3], v[158:159] op_sel_hi:[1,0,1]
	v_pk_fma_f32 v[156:157], v[24:25], s[2:3], v[156:157] op_sel_hi:[1,0,1]
	v_pk_fma_f32 v[154:155], v[26:27], s[2:3], v[154:155] op_sel_hi:[1,0,1]
	v_pk_fma_f32 v[152:153], v[28:29], s[2:3], v[152:153] op_sel_hi:[1,0,1]
	v_pk_fma_f32 v[150:151], v[30:31], s[2:3], v[150:151] op_sel_hi:[1,0,1]
	v_readlane_b32 s2, v131, 39
	s_waitcnt vmcnt(16)
	v_cvt_scalef32_pk32_f32_fp6 v[0:31], v[32:37], 1.0
	v_pk_fma_f32 v[164:165], v[0:1], s[2:3], v[38:39] op_sel_hi:[1,0,1]
	v_pk_fma_f32 v[166:167], v[2:3], s[2:3], v[40:41] op_sel_hi:[1,0,1]
	v_pk_fma_f32 v[168:169], v[4:5], s[2:3], v[42:43] op_sel_hi:[1,0,1]
	v_pk_fma_f32 v[170:171], v[6:7], s[2:3], v[50:51] op_sel_hi:[1,0,1]
	v_pk_fma_f32 v[172:173], v[8:9], s[2:3], v[52:53] op_sel_hi:[1,0,1]
	v_pk_fma_f32 v[174:175], v[10:11], s[2:3], v[54:55] op_sel_hi:[1,0,1]
	v_pk_fma_f32 v[176:177], v[12:13], s[2:3], v[62:63] op_sel_hi:[1,0,1]
	v_pk_fma_f32 v[178:179], v[14:15], s[2:3], v[64:65] op_sel_hi:[1,0,1]
	v_pk_fma_f32 v[180:181], v[16:17], s[2:3], v[66:67] op_sel_hi:[1,0,1]
	v_pk_fma_f32 v[162:163], v[18:19], s[2:3], v[162:163] op_sel_hi:[1,0,1]
	v_pk_fma_f32 v[160:161], v[20:21], s[2:3], v[160:161] op_sel_hi:[1,0,1]
	v_pk_fma_f32 v[158:159], v[22:23], s[2:3], v[158:159] op_sel_hi:[1,0,1]
	v_pk_fma_f32 v[156:157], v[24:25], s[2:3], v[156:157] op_sel_hi:[1,0,1]
	v_pk_fma_f32 v[154:155], v[26:27], s[2:3], v[154:155] op_sel_hi:[1,0,1]
	v_pk_fma_f32 v[152:153], v[28:29], s[2:3], v[152:153] op_sel_hi:[1,0,1]
	v_pk_fma_f32 v[150:151], v[30:31], s[2:3], v[150:151] op_sel_hi:[1,0,1]
	v_readlane_b32 s2, v241, 48
	v_readlane_b32 s3, v241, 49
	v_readlane_b32 s100, v241, 50
	v_readlane_b32 s101, v241, 51
	s_nop 1
	buffer_load_dwordx4 v[62:65], v129, s[44:47], s2 offen nt
	buffer_load_dwordx2 v[66:67], v210, s[44:47], s2 offen nt
	buffer_load_dwordx4 v[50:53], v129, s[44:47], s3 offen nt
	buffer_load_dwordx2 v[54:55], v210, s[44:47], s3 offen nt
	buffer_load_dwordx4 v[38:41], v129, s[44:47], s100 offen nt
	buffer_load_dwordx2 v[42:43], v210, s[44:47], s100 offen nt
	buffer_load_dwordx4 v[32:35], v129, s[44:47], s101 offen nt
	buffer_load_dwordx2 v[36:37], v210, s[44:47], s101 offen nt
	v_readlane_b32 s2, v131, 40
	s_waitcnt vmcnt(22)
	v_cvt_scalef32_pk32_f32_fp6 v[0:31], v[98:103], 1.0
	v_pk_fma_f32 v[98:99], v[0:1], s[2:3], v[164:165] op_sel_hi:[1,0,1]
	v_pk_fma_f32 v[100:101], v[2:3], s[2:3], v[166:167] op_sel_hi:[1,0,1]
	v_pk_fma_f32 v[102:103], v[4:5], s[2:3], v[168:169] op_sel_hi:[1,0,1]
	v_pk_fma_f32 v[164:165], v[6:7], s[2:3], v[170:171] op_sel_hi:[1,0,1]
	v_pk_fma_f32 v[166:167], v[8:9], s[2:3], v[172:173] op_sel_hi:[1,0,1]
	v_pk_fma_f32 v[168:169], v[10:11], s[2:3], v[174:175] op_sel_hi:[1,0,1]
	v_pk_fma_f32 v[170:171], v[12:13], s[2:3], v[176:177] op_sel_hi:[1,0,1]
	v_pk_fma_f32 v[172:173], v[14:15], s[2:3], v[178:179] op_sel_hi:[1,0,1]
	v_pk_fma_f32 v[174:175], v[16:17], s[2:3], v[180:181] op_sel_hi:[1,0,1]
	v_pk_fma_f32 v[162:163], v[18:19], s[2:3], v[162:163] op_sel_hi:[1,0,1]
	v_pk_fma_f32 v[160:161], v[20:21], s[2:3], v[160:161] op_sel_hi:[1,0,1]
	v_pk_fma_f32 v[158:159], v[22:23], s[2:3], v[158:159] op_sel_hi:[1,0,1]
	v_pk_fma_f32 v[156:157], v[24:25], s[2:3], v[156:157] op_sel_hi:[1,0,1]
	v_pk_fma_f32 v[154:155], v[26:27], s[2:3], v[154:155] op_sel_hi:[1,0,1]
	v_pk_fma_f32 v[152:153], v[28:29], s[2:3], v[152:153] op_sel_hi:[1,0,1]
	v_pk_fma_f32 v[150:151], v[30:31], s[2:3], v[150:151] op_sel_hi:[1,0,1]
	v_readlane_b32 s2, v131, 41
	s_waitcnt vmcnt(20)
	v_cvt_scalef32_pk32_f32_fp6 v[0:31], v[92:97], 1.0
	v_pk_fma_f32 v[92:93], v[0:1], s[2:3], v[98:99] op_sel_hi:[1,0,1]
	v_pk_fma_f32 v[94:95], v[2:3], s[2:3], v[100:101] op_sel_hi:[1,0,1]
	v_pk_fma_f32 v[96:97], v[4:5], s[2:3], v[102:103] op_sel_hi:[1,0,1]
	v_pk_fma_f32 v[98:99], v[6:7], s[2:3], v[164:165] op_sel_hi:[1,0,1]
	v_pk_fma_f32 v[100:101], v[8:9], s[2:3], v[166:167] op_sel_hi:[1,0,1]
	v_pk_fma_f32 v[102:103], v[10:11], s[2:3], v[168:169] op_sel_hi:[1,0,1]
	v_pk_fma_f32 v[164:165], v[12:13], s[2:3], v[170:171] op_sel_hi:[1,0,1]
	v_pk_fma_f32 v[166:167], v[14:15], s[2:3], v[172:173] op_sel_hi:[1,0,1]
	v_pk_fma_f32 v[168:169], v[16:17], s[2:3], v[174:175] op_sel_hi:[1,0,1]
	v_pk_fma_f32 v[162:163], v[18:19], s[2:3], v[162:163] op_sel_hi:[1,0,1]
	v_pk_fma_f32 v[160:161], v[20:21], s[2:3], v[160:161] op_sel_hi:[1,0,1]
	v_pk_fma_f32 v[158:159], v[22:23], s[2:3], v[158:159] op_sel_hi:[1,0,1]
	v_pk_fma_f32 v[156:157], v[24:25], s[2:3], v[156:157] op_sel_hi:[1,0,1]
	v_pk_fma_f32 v[154:155], v[26:27], s[2:3], v[154:155] op_sel_hi:[1,0,1]
	v_pk_fma_f32 v[152:153], v[28:29], s[2:3], v[152:153] op_sel_hi:[1,0,1]
	v_pk_fma_f32 v[150:151], v[30:31], s[2:3], v[150:151] op_sel_hi:[1,0,1]
	v_readlane_b32 s2, v131, 42
	s_waitcnt vmcnt(18)
	v_cvt_scalef32_pk32_f32_fp6 v[0:31], v[86:91], 1.0
	v_pk_fma_f32 v[86:87], v[0:1], s[2:3], v[92:93] op_sel_hi:[1,0,1]
	v_pk_fma_f32 v[88:89], v[2:3], s[2:3], v[94:95] op_sel_hi:[1,0,1]
	v_pk_fma_f32 v[90:91], v[4:5], s[2:3], v[96:97] op_sel_hi:[1,0,1]
	v_pk_fma_f32 v[92:93], v[6:7], s[2:3], v[98:99] op_sel_hi:[1,0,1]
	v_pk_fma_f32 v[94:95], v[8:9], s[2:3], v[100:101] op_sel_hi:[1,0,1]
	v_pk_fma_f32 v[96:97], v[10:11], s[2:3], v[102:103] op_sel_hi:[1,0,1]
	v_pk_fma_f32 v[98:99], v[12:13], s[2:3], v[164:165] op_sel_hi:[1,0,1]
	v_pk_fma_f32 v[100:101], v[14:15], s[2:3], v[166:167] op_sel_hi:[1,0,1]
	v_pk_fma_f32 v[102:103], v[16:17], s[2:3], v[168:169] op_sel_hi:[1,0,1]
	v_pk_fma_f32 v[162:163], v[18:19], s[2:3], v[162:163] op_sel_hi:[1,0,1]
	v_pk_fma_f32 v[160:161], v[20:21], s[2:3], v[160:161] op_sel_hi:[1,0,1]
	v_pk_fma_f32 v[158:159], v[22:23], s[2:3], v[158:159] op_sel_hi:[1,0,1]
	v_pk_fma_f32 v[156:157], v[24:25], s[2:3], v[156:157] op_sel_hi:[1,0,1]
	v_pk_fma_f32 v[154:155], v[26:27], s[2:3], v[154:155] op_sel_hi:[1,0,1]
	v_pk_fma_f32 v[152:153], v[28:29], s[2:3], v[152:153] op_sel_hi:[1,0,1]
	v_pk_fma_f32 v[150:151], v[30:31], s[2:3], v[150:151] op_sel_hi:[1,0,1]
	v_readlane_b32 s2, v131, 43
	s_waitcnt vmcnt(16)
	v_cvt_scalef32_pk32_f32_fp6 v[0:31], v[80:85], 1.0
	v_pk_fma_f32 v[180:181], v[0:1], s[2:3], v[86:87] op_sel_hi:[1,0,1]
	v_pk_fma_f32 v[178:179], v[2:3], s[2:3], v[88:89] op_sel_hi:[1,0,1]
	v_pk_fma_f32 v[176:177], v[4:5], s[2:3], v[90:91] op_sel_hi:[1,0,1]
	v_pk_fma_f32 v[174:175], v[6:7], s[2:3], v[92:93] op_sel_hi:[1,0,1]
	v_pk_fma_f32 v[172:173], v[8:9], s[2:3], v[94:95] op_sel_hi:[1,0,1]
	v_pk_fma_f32 v[170:171], v[10:11], s[2:3], v[96:97] op_sel_hi:[1,0,1]
	v_pk_fma_f32 v[168:169], v[12:13], s[2:3], v[98:99] op_sel_hi:[1,0,1]
	v_pk_fma_f32 v[166:167], v[14:15], s[2:3], v[100:101] op_sel_hi:[1,0,1]
	v_pk_fma_f32 v[164:165], v[16:17], s[2:3], v[102:103] op_sel_hi:[1,0,1]
	v_pk_fma_f32 v[162:163], v[18:19], s[2:3], v[162:163] op_sel_hi:[1,0,1]
	v_pk_fma_f32 v[160:161], v[20:21], s[2:3], v[160:161] op_sel_hi:[1,0,1]
	v_pk_fma_f32 v[158:159], v[22:23], s[2:3], v[158:159] op_sel_hi:[1,0,1]
	v_pk_fma_f32 v[156:157], v[24:25], s[2:3], v[156:157] op_sel_hi:[1,0,1]
	v_pk_fma_f32 v[154:155], v[26:27], s[2:3], v[154:155] op_sel_hi:[1,0,1]
	v_pk_fma_f32 v[152:153], v[28:29], s[2:3], v[152:153] op_sel_hi:[1,0,1]
	v_pk_fma_f32 v[150:151], v[30:31], s[2:3], v[150:151] op_sel_hi:[1,0,1]
	v_readlane_b32 s2, v241, 52
	v_readlane_b32 s3, v241, 53
	v_readlane_b32 s100, v241, 54
	v_readlane_b32 s101, v241, 55
	s_nop 1
	buffer_load_dwordx4 v[98:101], v129, s[44:47], s2 offen nt
	buffer_load_dwordx2 v[102:103], v210, s[44:47], s2 offen nt
	buffer_load_dwordx4 v[92:95], v129, s[44:47], s3 offen nt
	buffer_load_dwordx2 v[96:97], v210, s[44:47], s3 offen nt
	buffer_load_dwordx4 v[86:89], v129, s[44:47], s100 offen nt
	buffer_load_dwordx2 v[90:91], v210, s[44:47], s100 offen nt
	buffer_load_dwordx4 v[80:83], v129, s[44:47], s101 offen nt
	buffer_load_dwordx2 v[84:85], v210, s[44:47], s101 offen nt
	v_readlane_b32 s2, v131, 44
	s_waitcnt vmcnt(22)
	v_cvt_scalef32_pk32_f32_fp6 v[0:31], v[74:79], 1.0
	v_pk_fma_f32 v[74:75], v[0:1], s[2:3], v[180:181] op_sel_hi:[1,0,1]
	v_pk_fma_f32 v[76:77], v[2:3], s[2:3], v[178:179] op_sel_hi:[1,0,1]
	v_pk_fma_f32 v[78:79], v[4:5], s[2:3], v[176:177] op_sel_hi:[1,0,1]
	v_pk_fma_f32 v[174:175], v[6:7], s[2:3], v[174:175] op_sel_hi:[1,0,1]
	v_pk_fma_f32 v[172:173], v[8:9], s[2:3], v[172:173] op_sel_hi:[1,0,1]
	v_pk_fma_f32 v[170:171], v[10:11], s[2:3], v[170:171] op_sel_hi:[1,0,1]
	v_pk_fma_f32 v[168:169], v[12:13], s[2:3], v[168:169] op_sel_hi:[1,0,1]
	v_pk_fma_f32 v[166:167], v[14:15], s[2:3], v[166:167] op_sel_hi:[1,0,1]
	v_pk_fma_f32 v[164:165], v[16:17], s[2:3], v[164:165] op_sel_hi:[1,0,1]
	v_pk_fma_f32 v[162:163], v[18:19], s[2:3], v[162:163] op_sel_hi:[1,0,1]
	v_pk_fma_f32 v[160:161], v[20:21], s[2:3], v[160:161] op_sel_hi:[1,0,1]
	v_pk_fma_f32 v[158:159], v[22:23], s[2:3], v[158:159] op_sel_hi:[1,0,1]
	v_pk_fma_f32 v[156:157], v[24:25], s[2:3], v[156:157] op_sel_hi:[1,0,1]
	v_pk_fma_f32 v[154:155], v[26:27], s[2:3], v[154:155] op_sel_hi:[1,0,1]
	v_pk_fma_f32 v[152:153], v[28:29], s[2:3], v[152:153] op_sel_hi:[1,0,1]
	v_pk_fma_f32 v[150:151], v[30:31], s[2:3], v[150:151] op_sel_hi:[1,0,1]
	v_readlane_b32 s2, v131, 45
	s_waitcnt vmcnt(20)
	v_cvt_scalef32_pk32_f32_fp6 v[0:31], v[68:73], 1.0
	v_pk_fma_f32 v[68:69], v[0:1], s[2:3], v[74:75] op_sel_hi:[1,0,1]
	v_pk_fma_f32 v[70:71], v[2:3], s[2:3], v[76:77] op_sel_hi:[1,0,1]
	v_pk_fma_f32 v[72:73], v[4:5], s[2:3], v[78:79] op_sel_hi:[1,0,1]
	v_pk_fma_f32 v[74:75], v[6:7], s[2:3], v[174:175] op_sel_hi:[1,0,1]
	v_pk_fma_f32 v[76:77], v[8:9], s[2:3], v[172:173] op_sel_hi:[1,0,1]
	v_pk_fma_f32 v[78:79], v[10:11], s[2:3], v[170:171] op_sel_hi:[1,0,1]
	v_pk_fma_f32 v[168:169], v[12:13], s[2:3], v[168:169] op_sel_hi:[1,0,1]
	v_pk_fma_f32 v[166:167], v[14:15], s[2:3], v[166:167] op_sel_hi:[1,0,1]
	v_pk_fma_f32 v[164:165], v[16:17], s[2:3], v[164:165] op_sel_hi:[1,0,1]
	v_pk_fma_f32 v[162:163], v[18:19], s[2:3], v[162:163] op_sel_hi:[1,0,1]
	v_pk_fma_f32 v[160:161], v[20:21], s[2:3], v[160:161] op_sel_hi:[1,0,1]
	v_pk_fma_f32 v[158:159], v[22:23], s[2:3], v[158:159] op_sel_hi:[1,0,1]
	v_pk_fma_f32 v[156:157], v[24:25], s[2:3], v[156:157] op_sel_hi:[1,0,1]
	v_pk_fma_f32 v[154:155], v[26:27], s[2:3], v[154:155] op_sel_hi:[1,0,1]
	v_pk_fma_f32 v[152:153], v[28:29], s[2:3], v[152:153] op_sel_hi:[1,0,1]
	v_pk_fma_f32 v[150:151], v[30:31], s[2:3], v[150:151] op_sel_hi:[1,0,1]
	v_readlane_b32 s2, v131, 46
	s_waitcnt vmcnt(18)
	v_cvt_scalef32_pk32_f32_fp6 v[0:31], v[56:61], 1.0
	v_pk_fma_f32 v[56:57], v[0:1], s[2:3], v[68:69] op_sel_hi:[1,0,1]
	v_pk_fma_f32 v[58:59], v[2:3], s[2:3], v[70:71] op_sel_hi:[1,0,1]
	v_pk_fma_f32 v[60:61], v[4:5], s[2:3], v[72:73] op_sel_hi:[1,0,1]
	v_pk_fma_f32 v[68:69], v[6:7], s[2:3], v[74:75] op_sel_hi:[1,0,1]
	v_pk_fma_f32 v[70:71], v[8:9], s[2:3], v[76:77] op_sel_hi:[1,0,1]
	v_pk_fma_f32 v[72:73], v[10:11], s[2:3], v[78:79] op_sel_hi:[1,0,1]
	v_pk_fma_f32 v[74:75], v[12:13], s[2:3], v[168:169] op_sel_hi:[1,0,1]
	v_pk_fma_f32 v[76:77], v[14:15], s[2:3], v[166:167] op_sel_hi:[1,0,1]
	v_pk_fma_f32 v[78:79], v[16:17], s[2:3], v[164:165] op_sel_hi:[1,0,1]
	v_pk_fma_f32 v[162:163], v[18:19], s[2:3], v[162:163] op_sel_hi:[1,0,1]
	v_pk_fma_f32 v[160:161], v[20:21], s[2:3], v[160:161] op_sel_hi:[1,0,1]
	v_pk_fma_f32 v[158:159], v[22:23], s[2:3], v[158:159] op_sel_hi:[1,0,1]
	v_pk_fma_f32 v[156:157], v[24:25], s[2:3], v[156:157] op_sel_hi:[1,0,1]
	v_pk_fma_f32 v[154:155], v[26:27], s[2:3], v[154:155] op_sel_hi:[1,0,1]
	v_pk_fma_f32 v[152:153], v[28:29], s[2:3], v[152:153] op_sel_hi:[1,0,1]
	v_pk_fma_f32 v[150:151], v[30:31], s[2:3], v[150:151] op_sel_hi:[1,0,1]
	v_readlane_b32 s2, v131, 47
	s_waitcnt vmcnt(16)
	v_cvt_scalef32_pk32_f32_fp6 v[0:31], v[44:49], 1.0
	v_pk_fma_f32 v[164:165], v[0:1], s[2:3], v[56:57] op_sel_hi:[1,0,1]
	v_pk_fma_f32 v[166:167], v[2:3], s[2:3], v[58:59] op_sel_hi:[1,0,1]
	v_pk_fma_f32 v[168:169], v[4:5], s[2:3], v[60:61] op_sel_hi:[1,0,1]
	v_pk_fma_f32 v[170:171], v[6:7], s[2:3], v[68:69] op_sel_hi:[1,0,1]
	v_pk_fma_f32 v[172:173], v[8:9], s[2:3], v[70:71] op_sel_hi:[1,0,1]
	v_pk_fma_f32 v[174:175], v[10:11], s[2:3], v[72:73] op_sel_hi:[1,0,1]
	v_pk_fma_f32 v[176:177], v[12:13], s[2:3], v[74:75] op_sel_hi:[1,0,1]
	v_pk_fma_f32 v[178:179], v[14:15], s[2:3], v[76:77] op_sel_hi:[1,0,1]
	v_pk_fma_f32 v[180:181], v[16:17], s[2:3], v[78:79] op_sel_hi:[1,0,1]
	v_pk_fma_f32 v[162:163], v[18:19], s[2:3], v[162:163] op_sel_hi:[1,0,1]
	v_pk_fma_f32 v[160:161], v[20:21], s[2:3], v[160:161] op_sel_hi:[1,0,1]
	v_pk_fma_f32 v[158:159], v[22:23], s[2:3], v[158:159] op_sel_hi:[1,0,1]
	v_pk_fma_f32 v[156:157], v[24:25], s[2:3], v[156:157] op_sel_hi:[1,0,1]
	v_pk_fma_f32 v[154:155], v[26:27], s[2:3], v[154:155] op_sel_hi:[1,0,1]
	v_pk_fma_f32 v[152:153], v[28:29], s[2:3], v[152:153] op_sel_hi:[1,0,1]
	v_pk_fma_f32 v[150:151], v[30:31], s[2:3], v[150:151] op_sel_hi:[1,0,1]
	v_readlane_b32 s2, v241, 56
	v_readlane_b32 s3, v241, 57
	v_readlane_b32 s100, v241, 58
	v_readlane_b32 s101, v241, 59
	s_nop 1
	buffer_load_dwordx4 v[74:77], v129, s[44:47], s2 offen nt
	buffer_load_dwordx2 v[78:79], v210, s[44:47], s2 offen nt
	buffer_load_dwordx4 v[68:71], v129, s[44:47], s3 offen nt
	buffer_load_dwordx2 v[72:73], v210, s[44:47], s3 offen nt
	buffer_load_dwordx4 v[56:59], v129, s[44:47], s100 offen nt
	buffer_load_dwordx2 v[60:61], v210, s[44:47], s100 offen nt
	buffer_load_dwordx4 v[44:47], v129, s[44:47], s101 offen nt
	buffer_load_dwordx2 v[48:49], v210, s[44:47], s101 offen nt
	v_readlane_b32 s2, v131, 48
	s_waitcnt vmcnt(22)
	v_cvt_scalef32_pk32_f32_fp6 v[0:31], v[62:67], 1.0
	v_pk_fma_f32 v[62:63], v[0:1], s[2:3], v[164:165] op_sel_hi:[1,0,1]
	v_pk_fma_f32 v[64:65], v[2:3], s[2:3], v[166:167] op_sel_hi:[1,0,1]
	v_pk_fma_f32 v[66:67], v[4:5], s[2:3], v[168:169] op_sel_hi:[1,0,1]
	v_pk_fma_f32 v[164:165], v[6:7], s[2:3], v[170:171] op_sel_hi:[1,0,1]
	v_pk_fma_f32 v[166:167], v[8:9], s[2:3], v[172:173] op_sel_hi:[1,0,1]
	v_pk_fma_f32 v[168:169], v[10:11], s[2:3], v[174:175] op_sel_hi:[1,0,1]
	v_pk_fma_f32 v[170:171], v[12:13], s[2:3], v[176:177] op_sel_hi:[1,0,1]
	v_pk_fma_f32 v[172:173], v[14:15], s[2:3], v[178:179] op_sel_hi:[1,0,1]
	v_pk_fma_f32 v[174:175], v[16:17], s[2:3], v[180:181] op_sel_hi:[1,0,1]
	v_pk_fma_f32 v[162:163], v[18:19], s[2:3], v[162:163] op_sel_hi:[1,0,1]
	v_pk_fma_f32 v[160:161], v[20:21], s[2:3], v[160:161] op_sel_hi:[1,0,1]
	v_pk_fma_f32 v[158:159], v[22:23], s[2:3], v[158:159] op_sel_hi:[1,0,1]
	v_pk_fma_f32 v[156:157], v[24:25], s[2:3], v[156:157] op_sel_hi:[1,0,1]
	v_pk_fma_f32 v[154:155], v[26:27], s[2:3], v[154:155] op_sel_hi:[1,0,1]
	v_pk_fma_f32 v[152:153], v[28:29], s[2:3], v[152:153] op_sel_hi:[1,0,1]
	v_pk_fma_f32 v[150:151], v[30:31], s[2:3], v[150:151] op_sel_hi:[1,0,1]
	v_readlane_b32 s2, v131, 49
	s_waitcnt vmcnt(20)
	v_cvt_scalef32_pk32_f32_fp6 v[0:31], v[50:55], 1.0
	v_pk_fma_f32 v[50:51], v[0:1], s[2:3], v[62:63] op_sel_hi:[1,0,1]
	v_pk_fma_f32 v[52:53], v[2:3], s[2:3], v[64:65] op_sel_hi:[1,0,1]
	v_pk_fma_f32 v[54:55], v[4:5], s[2:3], v[66:67] op_sel_hi:[1,0,1]
	v_pk_fma_f32 v[62:63], v[6:7], s[2:3], v[164:165] op_sel_hi:[1,0,1]
	v_pk_fma_f32 v[64:65], v[8:9], s[2:3], v[166:167] op_sel_hi:[1,0,1]
	v_pk_fma_f32 v[66:67], v[10:11], s[2:3], v[168:169] op_sel_hi:[1,0,1]
	v_pk_fma_f32 v[164:165], v[12:13], s[2:3], v[170:171] op_sel_hi:[1,0,1]
	v_pk_fma_f32 v[166:167], v[14:15], s[2:3], v[172:173] op_sel_hi:[1,0,1]
	v_pk_fma_f32 v[168:169], v[16:17], s[2:3], v[174:175] op_sel_hi:[1,0,1]
	v_pk_fma_f32 v[162:163], v[18:19], s[2:3], v[162:163] op_sel_hi:[1,0,1]
	v_pk_fma_f32 v[160:161], v[20:21], s[2:3], v[160:161] op_sel_hi:[1,0,1]
	v_pk_fma_f32 v[158:159], v[22:23], s[2:3], v[158:159] op_sel_hi:[1,0,1]
	v_pk_fma_f32 v[156:157], v[24:25], s[2:3], v[156:157] op_sel_hi:[1,0,1]
	v_pk_fma_f32 v[154:155], v[26:27], s[2:3], v[154:155] op_sel_hi:[1,0,1]
	v_pk_fma_f32 v[152:153], v[28:29], s[2:3], v[152:153] op_sel_hi:[1,0,1]
	v_pk_fma_f32 v[150:151], v[30:31], s[2:3], v[150:151] op_sel_hi:[1,0,1]
	v_readlane_b32 s2, v131, 50
	s_waitcnt vmcnt(18)
	v_cvt_scalef32_pk32_f32_fp6 v[0:31], v[38:43], 1.0
	v_pk_fma_f32 v[38:39], v[0:1], s[2:3], v[50:51] op_sel_hi:[1,0,1]
	v_pk_fma_f32 v[40:41], v[2:3], s[2:3], v[52:53] op_sel_hi:[1,0,1]
	v_pk_fma_f32 v[42:43], v[4:5], s[2:3], v[54:55] op_sel_hi:[1,0,1]
	v_pk_fma_f32 v[50:51], v[6:7], s[2:3], v[62:63] op_sel_hi:[1,0,1]
	v_pk_fma_f32 v[52:53], v[8:9], s[2:3], v[64:65] op_sel_hi:[1,0,1]
	v_pk_fma_f32 v[54:55], v[10:11], s[2:3], v[66:67] op_sel_hi:[1,0,1]
	v_pk_fma_f32 v[62:63], v[12:13], s[2:3], v[164:165] op_sel_hi:[1,0,1]
	v_pk_fma_f32 v[64:65], v[14:15], s[2:3], v[166:167] op_sel_hi:[1,0,1]
	v_pk_fma_f32 v[66:67], v[16:17], s[2:3], v[168:169] op_sel_hi:[1,0,1]
	v_pk_fma_f32 v[162:163], v[18:19], s[2:3], v[162:163] op_sel_hi:[1,0,1]
	v_pk_fma_f32 v[160:161], v[20:21], s[2:3], v[160:161] op_sel_hi:[1,0,1]
	v_pk_fma_f32 v[158:159], v[22:23], s[2:3], v[158:159] op_sel_hi:[1,0,1]
	v_pk_fma_f32 v[156:157], v[24:25], s[2:3], v[156:157] op_sel_hi:[1,0,1]
	v_pk_fma_f32 v[154:155], v[26:27], s[2:3], v[154:155] op_sel_hi:[1,0,1]
	v_pk_fma_f32 v[152:153], v[28:29], s[2:3], v[152:153] op_sel_hi:[1,0,1]
	v_pk_fma_f32 v[150:151], v[30:31], s[2:3], v[150:151] op_sel_hi:[1,0,1]
	v_readlane_b32 s2, v131, 51
	s_waitcnt vmcnt(16)
	v_cvt_scalef32_pk32_f32_fp6 v[0:31], v[32:37], 1.0
	v_pk_fma_f32 v[164:165], v[0:1], s[2:3], v[38:39] op_sel_hi:[1,0,1]
	v_pk_fma_f32 v[166:167], v[2:3], s[2:3], v[40:41] op_sel_hi:[1,0,1]
	v_pk_fma_f32 v[168:169], v[4:5], s[2:3], v[42:43] op_sel_hi:[1,0,1]
	v_pk_fma_f32 v[170:171], v[6:7], s[2:3], v[50:51] op_sel_hi:[1,0,1]
	v_pk_fma_f32 v[172:173], v[8:9], s[2:3], v[52:53] op_sel_hi:[1,0,1]
	v_pk_fma_f32 v[174:175], v[10:11], s[2:3], v[54:55] op_sel_hi:[1,0,1]
	v_pk_fma_f32 v[176:177], v[12:13], s[2:3], v[62:63] op_sel_hi:[1,0,1]
	v_pk_fma_f32 v[178:179], v[14:15], s[2:3], v[64:65] op_sel_hi:[1,0,1]
	v_pk_fma_f32 v[180:181], v[16:17], s[2:3], v[66:67] op_sel_hi:[1,0,1]
	v_pk_fma_f32 v[162:163], v[18:19], s[2:3], v[162:163] op_sel_hi:[1,0,1]
	v_pk_fma_f32 v[160:161], v[20:21], s[2:3], v[160:161] op_sel_hi:[1,0,1]
	v_pk_fma_f32 v[158:159], v[22:23], s[2:3], v[158:159] op_sel_hi:[1,0,1]
	v_pk_fma_f32 v[156:157], v[24:25], s[2:3], v[156:157] op_sel_hi:[1,0,1]
	v_pk_fma_f32 v[154:155], v[26:27], s[2:3], v[154:155] op_sel_hi:[1,0,1]
	v_pk_fma_f32 v[152:153], v[28:29], s[2:3], v[152:153] op_sel_hi:[1,0,1]
	v_pk_fma_f32 v[150:151], v[30:31], s[2:3], v[150:151] op_sel_hi:[1,0,1]
	v_readlane_b32 s2, v241, 60
	v_readlane_b32 s3, v241, 61
	v_readlane_b32 s100, v241, 62
	v_readlane_b32 s101, v241, 63
	s_nop 1
	buffer_load_dwordx4 v[62:65], v129, s[44:47], s2 offen nt
	buffer_load_dwordx2 v[66:67], v210, s[44:47], s2 offen nt
	buffer_load_dwordx4 v[50:53], v129, s[44:47], s3 offen nt
	buffer_load_dwordx2 v[54:55], v210, s[44:47], s3 offen nt
	buffer_load_dwordx4 v[38:41], v129, s[44:47], s100 offen nt
	buffer_load_dwordx2 v[42:43], v210, s[44:47], s100 offen nt
	buffer_load_dwordx4 v[32:35], v129, s[44:47], s101 offen nt
	buffer_load_dwordx2 v[36:37], v210, s[44:47], s101 offen nt
	v_readlane_b32 s2, v131, 52
	s_waitcnt vmcnt(22)
	v_cvt_scalef32_pk32_f32_fp6 v[0:31], v[98:103], 1.0
	v_pk_fma_f32 v[98:99], v[0:1], s[2:3], v[164:165] op_sel_hi:[1,0,1]
	v_pk_fma_f32 v[100:101], v[2:3], s[2:3], v[166:167] op_sel_hi:[1,0,1]
	v_pk_fma_f32 v[102:103], v[4:5], s[2:3], v[168:169] op_sel_hi:[1,0,1]
	v_pk_fma_f32 v[164:165], v[6:7], s[2:3], v[170:171] op_sel_hi:[1,0,1]
	v_pk_fma_f32 v[166:167], v[8:9], s[2:3], v[172:173] op_sel_hi:[1,0,1]
	v_pk_fma_f32 v[168:169], v[10:11], s[2:3], v[174:175] op_sel_hi:[1,0,1]
	v_pk_fma_f32 v[170:171], v[12:13], s[2:3], v[176:177] op_sel_hi:[1,0,1]
	v_pk_fma_f32 v[172:173], v[14:15], s[2:3], v[178:179] op_sel_hi:[1,0,1]
	v_pk_fma_f32 v[174:175], v[16:17], s[2:3], v[180:181] op_sel_hi:[1,0,1]
	v_pk_fma_f32 v[162:163], v[18:19], s[2:3], v[162:163] op_sel_hi:[1,0,1]
	v_pk_fma_f32 v[160:161], v[20:21], s[2:3], v[160:161] op_sel_hi:[1,0,1]
	v_pk_fma_f32 v[158:159], v[22:23], s[2:3], v[158:159] op_sel_hi:[1,0,1]
	v_pk_fma_f32 v[156:157], v[24:25], s[2:3], v[156:157] op_sel_hi:[1,0,1]
	v_pk_fma_f32 v[154:155], v[26:27], s[2:3], v[154:155] op_sel_hi:[1,0,1]
	v_pk_fma_f32 v[152:153], v[28:29], s[2:3], v[152:153] op_sel_hi:[1,0,1]
	v_pk_fma_f32 v[150:151], v[30:31], s[2:3], v[150:151] op_sel_hi:[1,0,1]
	v_readlane_b32 s2, v131, 53
	s_waitcnt vmcnt(20)
	v_cvt_scalef32_pk32_f32_fp6 v[0:31], v[92:97], 1.0
	v_pk_fma_f32 v[92:93], v[0:1], s[2:3], v[98:99] op_sel_hi:[1,0,1]
	v_pk_fma_f32 v[94:95], v[2:3], s[2:3], v[100:101] op_sel_hi:[1,0,1]
	v_pk_fma_f32 v[96:97], v[4:5], s[2:3], v[102:103] op_sel_hi:[1,0,1]
	v_pk_fma_f32 v[98:99], v[6:7], s[2:3], v[164:165] op_sel_hi:[1,0,1]
	v_pk_fma_f32 v[100:101], v[8:9], s[2:3], v[166:167] op_sel_hi:[1,0,1]
	v_pk_fma_f32 v[102:103], v[10:11], s[2:3], v[168:169] op_sel_hi:[1,0,1]
	v_pk_fma_f32 v[164:165], v[12:13], s[2:3], v[170:171] op_sel_hi:[1,0,1]
	v_pk_fma_f32 v[166:167], v[14:15], s[2:3], v[172:173] op_sel_hi:[1,0,1]
	v_pk_fma_f32 v[168:169], v[16:17], s[2:3], v[174:175] op_sel_hi:[1,0,1]
	v_pk_fma_f32 v[162:163], v[18:19], s[2:3], v[162:163] op_sel_hi:[1,0,1]
	v_pk_fma_f32 v[160:161], v[20:21], s[2:3], v[160:161] op_sel_hi:[1,0,1]
	v_pk_fma_f32 v[158:159], v[22:23], s[2:3], v[158:159] op_sel_hi:[1,0,1]
	v_pk_fma_f32 v[156:157], v[24:25], s[2:3], v[156:157] op_sel_hi:[1,0,1]
	v_pk_fma_f32 v[154:155], v[26:27], s[2:3], v[154:155] op_sel_hi:[1,0,1]
	v_pk_fma_f32 v[152:153], v[28:29], s[2:3], v[152:153] op_sel_hi:[1,0,1]
	v_pk_fma_f32 v[150:151], v[30:31], s[2:3], v[150:151] op_sel_hi:[1,0,1]
	v_readlane_b32 s2, v131, 54
	s_waitcnt vmcnt(18)
	v_cvt_scalef32_pk32_f32_fp6 v[0:31], v[86:91], 1.0
	v_pk_fma_f32 v[86:87], v[0:1], s[2:3], v[92:93] op_sel_hi:[1,0,1]
	v_pk_fma_f32 v[88:89], v[2:3], s[2:3], v[94:95] op_sel_hi:[1,0,1]
	v_pk_fma_f32 v[90:91], v[4:5], s[2:3], v[96:97] op_sel_hi:[1,0,1]
	v_pk_fma_f32 v[92:93], v[6:7], s[2:3], v[98:99] op_sel_hi:[1,0,1]
	v_pk_fma_f32 v[94:95], v[8:9], s[2:3], v[100:101] op_sel_hi:[1,0,1]
	v_pk_fma_f32 v[96:97], v[10:11], s[2:3], v[102:103] op_sel_hi:[1,0,1]
	v_pk_fma_f32 v[98:99], v[12:13], s[2:3], v[164:165] op_sel_hi:[1,0,1]
	v_pk_fma_f32 v[100:101], v[14:15], s[2:3], v[166:167] op_sel_hi:[1,0,1]
	v_pk_fma_f32 v[102:103], v[16:17], s[2:3], v[168:169] op_sel_hi:[1,0,1]
	v_pk_fma_f32 v[162:163], v[18:19], s[2:3], v[162:163] op_sel_hi:[1,0,1]
	v_pk_fma_f32 v[160:161], v[20:21], s[2:3], v[160:161] op_sel_hi:[1,0,1]
	v_pk_fma_f32 v[158:159], v[22:23], s[2:3], v[158:159] op_sel_hi:[1,0,1]
	v_pk_fma_f32 v[156:157], v[24:25], s[2:3], v[156:157] op_sel_hi:[1,0,1]
	v_pk_fma_f32 v[154:155], v[26:27], s[2:3], v[154:155] op_sel_hi:[1,0,1]
	v_pk_fma_f32 v[152:153], v[28:29], s[2:3], v[152:153] op_sel_hi:[1,0,1]
	v_pk_fma_f32 v[150:151], v[30:31], s[2:3], v[150:151] op_sel_hi:[1,0,1]
	v_readlane_b32 s2, v131, 55
	s_waitcnt vmcnt(16)
	v_cvt_scalef32_pk32_f32_fp6 v[0:31], v[80:85], 1.0
	v_pk_fma_f32 v[180:181], v[0:1], s[2:3], v[86:87] op_sel_hi:[1,0,1]
	v_pk_fma_f32 v[178:179], v[2:3], s[2:3], v[88:89] op_sel_hi:[1,0,1]
	v_pk_fma_f32 v[176:177], v[4:5], s[2:3], v[90:91] op_sel_hi:[1,0,1]
	v_pk_fma_f32 v[174:175], v[6:7], s[2:3], v[92:93] op_sel_hi:[1,0,1]
	v_pk_fma_f32 v[172:173], v[8:9], s[2:3], v[94:95] op_sel_hi:[1,0,1]
	v_pk_fma_f32 v[170:171], v[10:11], s[2:3], v[96:97] op_sel_hi:[1,0,1]
	v_pk_fma_f32 v[168:169], v[12:13], s[2:3], v[98:99] op_sel_hi:[1,0,1]
	v_pk_fma_f32 v[166:167], v[14:15], s[2:3], v[100:101] op_sel_hi:[1,0,1]
	v_pk_fma_f32 v[164:165], v[16:17], s[2:3], v[102:103] op_sel_hi:[1,0,1]
	v_pk_fma_f32 v[162:163], v[18:19], s[2:3], v[162:163] op_sel_hi:[1,0,1]
	v_pk_fma_f32 v[160:161], v[20:21], s[2:3], v[160:161] op_sel_hi:[1,0,1]
	v_pk_fma_f32 v[158:159], v[22:23], s[2:3], v[158:159] op_sel_hi:[1,0,1]
	v_pk_fma_f32 v[156:157], v[24:25], s[2:3], v[156:157] op_sel_hi:[1,0,1]
	v_pk_fma_f32 v[154:155], v[26:27], s[2:3], v[154:155] op_sel_hi:[1,0,1]
	v_pk_fma_f32 v[152:153], v[28:29], s[2:3], v[152:153] op_sel_hi:[1,0,1]
	v_pk_fma_f32 v[150:151], v[30:31], s[2:3], v[150:151] op_sel_hi:[1,0,1]
	v_readlane_b32 s0, v131, 56
	s_waitcnt vmcnt(14)
	v_cvt_scalef32_pk32_f32_fp6 v[0:31], v[74:79], 1.0
	v_pk_fma_f32 v[74:75], v[0:1], s[0:1], v[180:181] op_sel_hi:[1,0,1]
	v_pk_fma_f32 v[76:77], v[2:3], s[0:1], v[178:179] op_sel_hi:[1,0,1]
	v_pk_fma_f32 v[78:79], v[4:5], s[0:1], v[176:177] op_sel_hi:[1,0,1]
	v_pk_fma_f32 v[80:81], v[6:7], s[0:1], v[174:175] op_sel_hi:[1,0,1]
	v_pk_fma_f32 v[82:83], v[8:9], s[0:1], v[172:173] op_sel_hi:[1,0,1]
	v_pk_fma_f32 v[84:85], v[10:11], s[0:1], v[170:171] op_sel_hi:[1,0,1]
	v_pk_fma_f32 v[86:87], v[12:13], s[0:1], v[168:169] op_sel_hi:[1,0,1]
	v_pk_fma_f32 v[88:89], v[14:15], s[0:1], v[166:167] op_sel_hi:[1,0,1]
	v_pk_fma_f32 v[90:91], v[16:17], s[0:1], v[164:165] op_sel_hi:[1,0,1]
	v_pk_fma_f32 v[92:93], v[18:19], s[0:1], v[162:163] op_sel_hi:[1,0,1]
	v_pk_fma_f32 v[94:95], v[20:21], s[0:1], v[160:161] op_sel_hi:[1,0,1]
	v_pk_fma_f32 v[96:97], v[22:23], s[0:1], v[158:159] op_sel_hi:[1,0,1]
	v_pk_fma_f32 v[98:99], v[24:25], s[0:1], v[156:157] op_sel_hi:[1,0,1]
	v_pk_fma_f32 v[100:101], v[26:27], s[0:1], v[154:155] op_sel_hi:[1,0,1]
	v_pk_fma_f32 v[102:103], v[28:29], s[0:1], v[152:153] op_sel_hi:[1,0,1]
	v_pk_fma_f32 v[150:151], v[30:31], s[0:1], v[150:151] op_sel_hi:[1,0,1]
	v_readlane_b32 s0, v131, 57
	s_waitcnt vmcnt(12)
	v_cvt_scalef32_pk32_f32_fp6 v[0:31], v[68:73], 1.0
	v_pk_fma_f32 v[68:69], v[0:1], s[0:1], v[74:75] op_sel_hi:[1,0,1]
	v_pk_fma_f32 v[70:71], v[2:3], s[0:1], v[76:77] op_sel_hi:[1,0,1]
	v_pk_fma_f32 v[72:73], v[4:5], s[0:1], v[78:79] op_sel_hi:[1,0,1]
	v_pk_fma_f32 v[74:75], v[6:7], s[0:1], v[80:81] op_sel_hi:[1,0,1]
	v_pk_fma_f32 v[76:77], v[8:9], s[0:1], v[82:83] op_sel_hi:[1,0,1]
	v_pk_fma_f32 v[78:79], v[10:11], s[0:1], v[84:85] op_sel_hi:[1,0,1]
	v_pk_fma_f32 v[80:81], v[12:13], s[0:1], v[86:87] op_sel_hi:[1,0,1]
	v_pk_fma_f32 v[82:83], v[14:15], s[0:1], v[88:89] op_sel_hi:[1,0,1]
	v_pk_fma_f32 v[84:85], v[16:17], s[0:1], v[90:91] op_sel_hi:[1,0,1]
	v_pk_fma_f32 v[86:87], v[18:19], s[0:1], v[92:93] op_sel_hi:[1,0,1]
	v_pk_fma_f32 v[88:89], v[20:21], s[0:1], v[94:95] op_sel_hi:[1,0,1]
	v_pk_fma_f32 v[90:91], v[22:23], s[0:1], v[96:97] op_sel_hi:[1,0,1]
	v_pk_fma_f32 v[92:93], v[24:25], s[0:1], v[98:99] op_sel_hi:[1,0,1]
	v_pk_fma_f32 v[94:95], v[26:27], s[0:1], v[100:101] op_sel_hi:[1,0,1]
	v_pk_fma_f32 v[96:97], v[28:29], s[0:1], v[102:103] op_sel_hi:[1,0,1]
	v_pk_fma_f32 v[98:99], v[30:31], s[0:1], v[150:151] op_sel_hi:[1,0,1]
	v_readlane_b32 s0, v131, 58
	s_waitcnt vmcnt(10)
	v_cvt_scalef32_pk32_f32_fp6 v[0:31], v[56:61], 1.0
	v_pk_fma_f32 v[56:57], v[0:1], s[0:1], v[68:69] op_sel_hi:[1,0,1]
	v_pk_fma_f32 v[58:59], v[2:3], s[0:1], v[70:71] op_sel_hi:[1,0,1]
	v_pk_fma_f32 v[60:61], v[4:5], s[0:1], v[72:73] op_sel_hi:[1,0,1]
	v_pk_fma_f32 v[68:69], v[6:7], s[0:1], v[74:75] op_sel_hi:[1,0,1]
	v_pk_fma_f32 v[70:71], v[8:9], s[0:1], v[76:77] op_sel_hi:[1,0,1]
	v_pk_fma_f32 v[72:73], v[10:11], s[0:1], v[78:79] op_sel_hi:[1,0,1]
	v_pk_fma_f32 v[74:75], v[12:13], s[0:1], v[80:81] op_sel_hi:[1,0,1]
	v_pk_fma_f32 v[76:77], v[14:15], s[0:1], v[82:83] op_sel_hi:[1,0,1]
	v_pk_fma_f32 v[78:79], v[16:17], s[0:1], v[84:85] op_sel_hi:[1,0,1]
	v_pk_fma_f32 v[80:81], v[18:19], s[0:1], v[86:87] op_sel_hi:[1,0,1]
	v_pk_fma_f32 v[82:83], v[20:21], s[0:1], v[88:89] op_sel_hi:[1,0,1]
	v_pk_fma_f32 v[84:85], v[22:23], s[0:1], v[90:91] op_sel_hi:[1,0,1]
	v_pk_fma_f32 v[86:87], v[24:25], s[0:1], v[92:93] op_sel_hi:[1,0,1]
	v_pk_fma_f32 v[88:89], v[26:27], s[0:1], v[94:95] op_sel_hi:[1,0,1]
	v_pk_fma_f32 v[90:91], v[28:29], s[0:1], v[96:97] op_sel_hi:[1,0,1]
	v_pk_fma_f32 v[92:93], v[30:31], s[0:1], v[98:99] op_sel_hi:[1,0,1]
	v_readlane_b32 s0, v131, 59
	s_waitcnt vmcnt(8)
	v_cvt_scalef32_pk32_f32_fp6 v[0:31], v[44:49], 1.0
	v_pk_fma_f32 v[46:47], v[2:3], s[0:1], v[58:59] op_sel_hi:[1,0,1]
	v_pk_fma_f32 v[44:45], v[0:1], s[0:1], v[56:57] op_sel_hi:[1,0,1]
	v_pk_fma_f32 v[48:49], v[4:5], s[0:1], v[60:61] op_sel_hi:[1,0,1]
	v_pk_fma_f32 v[56:57], v[6:7], s[0:1], v[68:69] op_sel_hi:[1,0,1]
	v_pk_fma_f32 v[58:59], v[8:9], s[0:1], v[70:71] op_sel_hi:[1,0,1]
	v_pk_fma_f32 v[60:61], v[10:11], s[0:1], v[72:73] op_sel_hi:[1,0,1]
	v_pk_fma_f32 v[68:69], v[12:13], s[0:1], v[74:75] op_sel_hi:[1,0,1]
	v_pk_fma_f32 v[70:71], v[14:15], s[0:1], v[76:77] op_sel_hi:[1,0,1]
	v_pk_fma_f32 v[72:73], v[16:17], s[0:1], v[78:79] op_sel_hi:[1,0,1]
	v_pk_fma_f32 v[74:75], v[18:19], s[0:1], v[80:81] op_sel_hi:[1,0,1]
	v_pk_fma_f32 v[76:77], v[20:21], s[0:1], v[82:83] op_sel_hi:[1,0,1]
	v_pk_fma_f32 v[78:79], v[22:23], s[0:1], v[84:85] op_sel_hi:[1,0,1]
	v_pk_fma_f32 v[80:81], v[24:25], s[0:1], v[86:87] op_sel_hi:[1,0,1]
	v_pk_fma_f32 v[82:83], v[26:27], s[0:1], v[88:89] op_sel_hi:[1,0,1]
	v_pk_fma_f32 v[84:85], v[28:29], s[0:1], v[90:91] op_sel_hi:[1,0,1]
	v_pk_fma_f32 v[86:87], v[30:31], s[0:1], v[92:93] op_sel_hi:[1,0,1]
	v_readlane_b32 s0, v131, 60
	s_waitcnt vmcnt(6)
	v_cvt_scalef32_pk32_f32_fp6 v[0:31], v[62:67], 1.0
	v_pk_fma_f32 v[44:45], v[0:1], s[0:1], v[44:45] op_sel_hi:[1,0,1]
	v_pk_fma_f32 v[46:47], v[2:3], s[0:1], v[46:47] op_sel_hi:[1,0,1]
	v_pk_fma_f32 v[48:49], v[4:5], s[0:1], v[48:49] op_sel_hi:[1,0,1]
	v_pk_fma_f32 v[56:57], v[6:7], s[0:1], v[56:57] op_sel_hi:[1,0,1]
	v_pk_fma_f32 v[58:59], v[8:9], s[0:1], v[58:59] op_sel_hi:[1,0,1]
	v_pk_fma_f32 v[60:61], v[10:11], s[0:1], v[60:61] op_sel_hi:[1,0,1]
	v_pk_fma_f32 v[62:63], v[12:13], s[0:1], v[68:69] op_sel_hi:[1,0,1]
	v_pk_fma_f32 v[64:65], v[14:15], s[0:1], v[70:71] op_sel_hi:[1,0,1]
	v_pk_fma_f32 v[66:67], v[16:17], s[0:1], v[72:73] op_sel_hi:[1,0,1]
	v_pk_fma_f32 v[68:69], v[18:19], s[0:1], v[74:75] op_sel_hi:[1,0,1]
	v_pk_fma_f32 v[70:71], v[20:21], s[0:1], v[76:77] op_sel_hi:[1,0,1]
	v_pk_fma_f32 v[72:73], v[22:23], s[0:1], v[78:79] op_sel_hi:[1,0,1]
	v_pk_fma_f32 v[74:75], v[24:25], s[0:1], v[80:81] op_sel_hi:[1,0,1]
	v_pk_fma_f32 v[76:77], v[26:27], s[0:1], v[82:83] op_sel_hi:[1,0,1]
	v_pk_fma_f32 v[78:79], v[28:29], s[0:1], v[84:85] op_sel_hi:[1,0,1]
	v_pk_fma_f32 v[80:81], v[30:31], s[0:1], v[86:87] op_sel_hi:[1,0,1]
	v_readlane_b32 s0, v131, 61
	s_waitcnt vmcnt(4)
	v_cvt_scalef32_pk32_f32_fp6 v[0:31], v[50:55], 1.0
	v_pk_fma_f32 v[44:45], v[0:1], s[0:1], v[44:45] op_sel_hi:[1,0,1]
	v_pk_fma_f32 v[46:47], v[2:3], s[0:1], v[46:47] op_sel_hi:[1,0,1]
	v_pk_fma_f32 v[48:49], v[4:5], s[0:1], v[48:49] op_sel_hi:[1,0,1]
	v_pk_fma_f32 v[50:51], v[6:7], s[0:1], v[56:57] op_sel_hi:[1,0,1]
	v_pk_fma_f32 v[52:53], v[8:9], s[0:1], v[58:59] op_sel_hi:[1,0,1]
	v_pk_fma_f32 v[54:55], v[10:11], s[0:1], v[60:61] op_sel_hi:[1,0,1]
	v_pk_fma_f32 v[56:57], v[12:13], s[0:1], v[62:63] op_sel_hi:[1,0,1]
	v_pk_fma_f32 v[58:59], v[14:15], s[0:1], v[64:65] op_sel_hi:[1,0,1]
	v_pk_fma_f32 v[60:61], v[16:17], s[0:1], v[66:67] op_sel_hi:[1,0,1]
	v_pk_fma_f32 v[62:63], v[18:19], s[0:1], v[68:69] op_sel_hi:[1,0,1]
	v_pk_fma_f32 v[64:65], v[20:21], s[0:1], v[70:71] op_sel_hi:[1,0,1]
	v_pk_fma_f32 v[66:67], v[22:23], s[0:1], v[72:73] op_sel_hi:[1,0,1]
	v_pk_fma_f32 v[68:69], v[24:25], s[0:1], v[74:75] op_sel_hi:[1,0,1]
	v_pk_fma_f32 v[70:71], v[26:27], s[0:1], v[76:77] op_sel_hi:[1,0,1]
	v_pk_fma_f32 v[72:73], v[28:29], s[0:1], v[78:79] op_sel_hi:[1,0,1]
	v_pk_fma_f32 v[74:75], v[30:31], s[0:1], v[80:81] op_sel_hi:[1,0,1]
	v_readlane_b32 s0, v131, 62
	s_waitcnt vmcnt(2)
	v_cvt_scalef32_pk32_f32_fp6 v[0:31], v[38:43], 1.0
	v_pk_fma_f32 v[38:39], v[0:1], s[0:1], v[44:45] op_sel_hi:[1,0,1]
	v_pk_fma_f32 v[40:41], v[2:3], s[0:1], v[46:47] op_sel_hi:[1,0,1]
	v_pk_fma_f32 v[42:43], v[4:5], s[0:1], v[48:49] op_sel_hi:[1,0,1]
	v_pk_fma_f32 v[44:45], v[6:7], s[0:1], v[50:51] op_sel_hi:[1,0,1]
	v_pk_fma_f32 v[46:47], v[8:9], s[0:1], v[52:53] op_sel_hi:[1,0,1]
	v_pk_fma_f32 v[48:49], v[10:11], s[0:1], v[54:55] op_sel_hi:[1,0,1]
	v_pk_fma_f32 v[50:51], v[12:13], s[0:1], v[56:57] op_sel_hi:[1,0,1]
	v_pk_fma_f32 v[52:53], v[14:15], s[0:1], v[58:59] op_sel_hi:[1,0,1]
	v_pk_fma_f32 v[54:55], v[16:17], s[0:1], v[60:61] op_sel_hi:[1,0,1]
	v_pk_fma_f32 v[56:57], v[18:19], s[0:1], v[62:63] op_sel_hi:[1,0,1]
	v_pk_fma_f32 v[58:59], v[20:21], s[0:1], v[64:65] op_sel_hi:[1,0,1]
	v_pk_fma_f32 v[62:63], v[22:23], s[0:1], v[66:67] op_sel_hi:[1,0,1]
	v_pk_fma_f32 v[64:65], v[24:25], s[0:1], v[68:69] op_sel_hi:[1,0,1]
	v_pk_fma_f32 v[66:67], v[26:27], s[0:1], v[70:71] op_sel_hi:[1,0,1]
	v_pk_fma_f32 v[68:69], v[28:29], s[0:1], v[72:73] op_sel_hi:[1,0,1]
	v_pk_fma_f32 v[70:71], v[30:31], s[0:1], v[74:75] op_sel_hi:[1,0,1]
	v_readlane_b32 s0, v131, 63
	s_waitcnt vmcnt(0)
	v_cvt_scalef32_pk32_f32_fp6 v[0:31], v[32:37], 1.0
	v_pk_fma_f32 v[34:35], v[0:1], s[0:1], v[38:39] op_sel_hi:[1,0,1]
	v_pk_fma_f32 v[32:33], v[2:3], s[0:1], v[40:41] op_sel_hi:[1,0,1]
	v_pk_fma_f32 v[38:39], v[4:5], s[0:1], v[42:43] op_sel_hi:[1,0,1]
	v_pk_fma_f32 v[36:37], v[6:7], s[0:1], v[44:45] op_sel_hi:[1,0,1]
	v_pk_fma_f32 v[42:43], v[8:9], s[0:1], v[46:47] op_sel_hi:[1,0,1]
	v_pk_fma_f32 v[40:41], v[10:11], s[0:1], v[48:49] op_sel_hi:[1,0,1]
	v_pk_fma_f32 v[48:49], v[12:13], s[0:1], v[50:51] op_sel_hi:[1,0,1]
	v_pk_fma_f32 v[46:47], v[14:15], s[0:1], v[52:53] op_sel_hi:[1,0,1]
	v_pk_fma_f32 v[50:51], v[18:19], s[0:1], v[56:57] op_sel_hi:[1,0,1]
	v_pk_fma_f32 v[54:55], v[16:17], s[0:1], v[54:55] op_sel_hi:[1,0,1]
	v_pk_fma_f32 v[60:61], v[20:21], s[0:1], v[58:59] op_sel_hi:[1,0,1]
	v_pk_fma_f32 v[56:57], v[22:23], s[0:1], v[62:63] op_sel_hi:[1,0,1]
	v_pk_fma_f32 v[44:45], v[24:25], s[0:1], v[64:65] op_sel_hi:[1,0,1]
	v_pk_fma_f32 v[64:65], v[26:27], s[0:1], v[66:67] op_sel_hi:[1,0,1]
	v_pk_fma_f32 v[18:19], v[28:29], s[0:1], v[68:69] op_sel_hi:[1,0,1]
	v_pk_fma_f32 v[24:25], v[30:31], s[0:1], v[70:71] op_sel_hi:[1,0,1]
	s_lshr_b32 s0, s58, 12
	s_ashr_i32 s59, s58, 31
	s_mul_i32 s4, s0, 0x3000
	s_lshl_b64 s[0:1], s[58:59], 12
	s_add_u32 s2, s71, s0
	v_lshlrev_b32_e32 v12, 2, v148
	s_addc_u32 s3, s74, s1
	v_ashrrev_i32_e32 v13, 31, v12
	v_lshlrev_b32_e32 v63, 3, v148
	v_lshl_add_u64 v[14:15], v[12:13], 1, s[2:3]
	v_add3_u32 v62, v201, s4, v63
	global_load_dwordx2 v[16:17], v[14:15], off
	ds_read2st64_b64 v[0:3], v62 offset1:1
	global_load_dwordx2 v[20:21], v[14:15], off offset:512
	global_load_dwordx2 v[22:23], v[14:15], off offset:1024
	ds_read2st64_b64 v[4:7], v62 offset0:2 offset1:3
	global_load_dwordx2 v[52:53], v[14:15], off offset:1536
	global_load_dwordx2 v[58:59], v[14:15], off offset:2048
	ds_read2st64_b64 v[8:11], v62 offset0:4 offset1:5
	global_load_dwordx2 v[66:67], v[14:15], off offset:2560
	global_load_dwordx2 v[68:69], v[14:15], off offset:3072
	global_load_dwordx2 v[26:27], v[14:15], off offset:3584
	ds_read2st64_b64 v[28:31], v62 offset0:6 offset1:7
	s_lshl_b64 s[2:3], s[58:59], 13
	s_add_u32 s4, s16, s2
	s_addc_u32 s5, s17, s3
	s_and_b64 vcc, exec, s[54:55]
	s_waitcnt lgkmcnt(0)
	v_lshlrev_b32_e32 v72, 16, v30
	v_and_b32_e32 v73, 0xffff0000, v30
	v_lshlrev_b32_e32 v30, 16, v31
	v_and_b32_e32 v31, 0xffff0000, v31
	v_pk_mul_f32 v[24:25], v[24:25], v[30:31]
	v_lshlrev_b32_e32 v30, 16, v28
	v_and_b32_e32 v31, 0xffff0000, v28
	v_pk_mul_f32 v[30:31], v[44:45], v[30:31]
	v_lshlrev_b32_e32 v28, 16, v29
	v_and_b32_e32 v29, 0xffff0000, v29
	v_pk_mul_f32 v[28:29], v[64:65], v[28:29]
	v_pk_mul_f32 v[18:19], v[18:19], v[72:73]
	s_waitcnt vmcnt(0)
	v_lshlrev_b32_e32 v70, 16, v26
	v_and_b32_e32 v71, 0xffff0000, v26
	v_lshlrev_b32_e32 v26, 16, v27
	v_and_b32_e32 v27, 0xffff0000, v27
	v_pk_fma_f32 v[24:25], v[26:27], s[38:39], v[24:25] op_sel_hi:[1,0,1]
	v_lshlrev_b32_e32 v26, 16, v68
	v_and_b32_e32 v27, 0xffff0000, v68
	v_pk_fma_f32 v[26:27], v[26:27], s[38:39], v[30:31] op_sel_hi:[1,0,1]
	v_lshlrev_b32_e32 v30, 16, v69
	v_and_b32_e32 v31, 0xffff0000, v69
	v_pk_fma_f32 v[44:45], v[30:31], s[38:39], v[28:29] op_sel_hi:[1,0,1]
	v_lshlrev_b32_e32 v30, 16, v10
	v_and_b32_e32 v31, 0xffff0000, v10
	v_lshlrev_b32_e32 v28, 16, v66
	v_and_b32_e32 v29, 0xffff0000, v66
	v_pk_mul_f32 v[30:31], v[60:61], v[30:31]
	v_lshlrev_b32_e32 v10, 16, v11
	v_and_b32_e32 v11, 0xffff0000, v11
	v_pk_fma_f32 v[28:29], v[28:29], s[38:39], v[30:31] op_sel_hi:[1,0,1]
	v_lshlrev_b32_e32 v30, 16, v67
	v_and_b32_e32 v31, 0xffff0000, v67
	v_pk_mul_f32 v[10:11], v[56:57], v[10:11]
	v_lshlrev_b32_e32 v56, 16, v8
	v_and_b32_e32 v57, 0xffff0000, v8
	v_pk_fma_f32 v[10:11], v[30:31], s[38:39], v[10:11] op_sel_hi:[1,0,1]
	v_lshlrev_b32_e32 v30, 16, v58
	v_and_b32_e32 v31, 0xffff0000, v58
	v_pk_mul_f32 v[54:55], v[54:55], v[56:57]
	v_lshlrev_b32_e32 v8, 16, v9
	v_and_b32_e32 v9, 0xffff0000, v9
	v_pk_fma_f32 v[30:31], v[30:31], s[38:39], v[54:55] op_sel_hi:[1,0,1]
	v_lshlrev_b32_e32 v54, 16, v59
	v_and_b32_e32 v55, 0xffff0000, v59
	v_pk_mul_f32 v[8:9], v[50:51], v[8:9]
	v_lshlrev_b32_e32 v50, 16, v52
	v_pk_fma_f32 v[8:9], v[54:55], s[38:39], v[8:9] op_sel_hi:[1,0,1]
	v_lshlrev_b32_e32 v54, 16, v6
	v_and_b32_e32 v55, 0xffff0000, v6
	v_and_b32_e32 v51, 0xffff0000, v52
	v_pk_mul_f32 v[48:49], v[48:49], v[54:55]
	v_lshlrev_b32_e32 v6, 16, v7
	v_and_b32_e32 v7, 0xffff0000, v7
	v_pk_fma_f32 v[48:49], v[50:51], s[38:39], v[48:49] op_sel_hi:[1,0,1]
	v_lshlrev_b32_e32 v50, 16, v53
	v_and_b32_e32 v51, 0xffff0000, v53
	v_pk_mul_f32 v[6:7], v[46:47], v[6:7]
	v_lshlrev_b32_e32 v46, 16, v22
	v_pk_fma_f32 v[6:7], v[50:51], s[38:39], v[6:7] op_sel_hi:[1,0,1]
	v_lshlrev_b32_e32 v50, 16, v4
	v_and_b32_e32 v51, 0xffff0000, v4
	v_lshlrev_b32_e32 v4, 16, v5
	v_and_b32_e32 v5, 0xffff0000, v5
	v_and_b32_e32 v47, 0xffff0000, v22
	v_lshlrev_b32_e32 v22, 16, v23
	v_and_b32_e32 v23, 0xffff0000, v23
	v_pk_mul_f32 v[4:5], v[40:41], v[4:5]
	v_lshlrev_b32_e32 v40, 16, v2
	v_and_b32_e32 v41, 0xffff0000, v2
	v_pk_fma_f32 v[4:5], v[22:23], s[38:39], v[4:5] op_sel_hi:[1,0,1]
	v_lshlrev_b32_e32 v22, 16, v20
	v_and_b32_e32 v23, 0xffff0000, v20
	v_pk_mul_f32 v[38:39], v[38:39], v[40:41]
	v_lshlrev_b32_e32 v40, 16, v0
	v_and_b32_e32 v41, 0xffff0000, v0
	v_pk_fma_f32 v[22:23], v[22:23], s[38:39], v[38:39] op_sel_hi:[1,0,1]
	v_lshlrev_b32_e32 v38, 16, v16
	v_and_b32_e32 v39, 0xffff0000, v16
	v_pk_mul_f32 v[34:35], v[34:35], v[40:41]
	v_lshlrev_b32_e32 v16, 16, v17
	v_pk_fma_f32 v[34:35], v[38:39], s[38:39], v[34:35] op_sel_hi:[1,0,1]
	v_and_b32_e32 v17, 0xffff0000, v17
	v_add_f32_e32 v0, 0, v34
	v_add_f32_e32 v38, v35, v0
	v_lshlrev_b32_e32 v0, 16, v1
	v_and_b32_e32 v1, 0xffff0000, v1
	v_pk_mul_f32 v[0:1], v[32:33], v[0:1]
	v_lshlrev_b32_e32 v2, 16, v3
	v_pk_fma_f32 v[0:1], v[16:17], s[38:39], v[0:1] op_sel_hi:[1,0,1]
	v_and_b32_e32 v3, 0xffff0000, v3
	v_add_f32_e32 v16, v0, v38
	v_add_f32_e32 v16, v1, v16
	v_lshlrev_b32_e32 v20, 16, v21
	v_and_b32_e32 v21, 0xffff0000, v21
	v_pk_mul_f32 v[2:3], v[36:37], v[2:3]
	v_add_f32_e32 v16, v22, v16
	v_pk_fma_f32 v[2:3], v[20:21], s[38:39], v[2:3] op_sel_hi:[1,0,1]
	v_add_f32_e32 v16, v23, v16
	v_pk_mul_f32 v[42:43], v[42:43], v[50:51]
	v_add_f32_e32 v16, v2, v16
	v_pk_fma_f32 v[52:53], v[46:47], s[38:39], v[42:43] op_sel_hi:[1,0,1]
	v_add_f32_e32 v16, v3, v16
	v_add_f32_e32 v16, v52, v16
	v_add_f32_e32 v16, v53, v16
	v_add_f32_e32 v16, v4, v16
	v_add_f32_e32 v16, v5, v16
	v_add_f32_e32 v16, v48, v16
	v_add_f32_e32 v16, v49, v16
	v_add_f32_e32 v16, v6, v16
	v_add_f32_e32 v16, v7, v16
	v_add_f32_e32 v16, v30, v16
	v_add_f32_e32 v16, v31, v16
	v_add_f32_e32 v16, v8, v16
	v_add_f32_e32 v16, v9, v16
	v_add_f32_e32 v16, v28, v16
	v_add_f32_e32 v16, v29, v16
	v_add_f32_e32 v16, v10, v16
	v_add_f32_e32 v16, v11, v16
	v_add_f32_e32 v16, v26, v16
	v_add_f32_e32 v16, v27, v16
	v_add_f32_e32 v16, v44, v16
	v_pk_fma_f32 v[18:19], v[70:71], s[38:39], v[18:19] op_sel_hi:[1,0,1]
	v_add_f32_e32 v16, v45, v16
	v_add_f32_e32 v16, v18, v16
	v_add_f32_e32 v16, v19, v16
	v_add_f32_e32 v16, v24, v16
	v_add_f32_e32 v16, v25, v16
	v_mov_b32_e32 v17, v105
	v_add_u32_e32 v50, v202, v63
	v_add_f32_dpp v16, v16, v16 quad_perm:[1,0,3,2] row_mask:0xf bank_mask:0xf bound_ctrl:1
	v_add_u32_e32 v51, v203, v63
	ds_read_b64 v[20:21], v50
	ds_read_b64 v[36:37], v51
	v_add_f32_dpp v16, v16, v16 quad_perm:[2,3,0,1] row_mask:0xf bank_mask:0xf bound_ctrl:1
	s_waitcnt lgkmcnt(1)
	v_lshlrev_b32_e32 v54, 16, v20
	v_add_f32_dpp v16, v16, v16 row_half_mirror row_mask:0xf bank_mask:0xf bound_ctrl:1
	s_waitcnt lgkmcnt(0)
	v_lshlrev_b32_e32 v56, 16, v36
	v_and_b32_e32 v57, 0xffff0000, v36
	v_add_f32_dpp v16, v16, v16 row_mirror row_mask:0xf bank_mask:0xf bound_ctrl:1
	v_lshlrev_b32_e32 v60, 16, v37
	v_and_b32_e32 v61, 0xffff0000, v37
	v_mov_b32_dpp v17, v16 row_bcast:15 row_mask:0xa bank_mask:0xf
	v_add_f32_e32 v16, v16, v17
	v_mov_b32_e32 v17, v105
	v_and_b32_e32 v55, 0xffff0000, v20
	v_lshlrev_b32_e32 v58, 16, v21
	v_mov_b32_dpp v17, v16 row_bcast:31 row_mask:0xc bank_mask:0xf
	v_add_f32_e32 v16, v16, v17
	v_and_b32_e32 v59, 0xffff0000, v21
	v_readlane_b32 s2, v16, 63
	s_nop 1
	v_mul_f32_e32 v64, s2, v187
	v_pk_add_f32 v[66:67], v[34:35], v[64:65] op_sel_hi:[1,0] neg_lo:[0,1] neg_hi:[0,1]
	v_pk_add_f32 v[70:71], v[0:1], v[64:65] op_sel_hi:[1,0] neg_lo:[0,1] neg_hi:[0,1]
	v_pk_mul_f32 v[68:69], v[66:67], v[66:67]
	v_pk_mul_f32 v[0:1], v[70:71], v[70:71]
	v_add_f32_e32 v63, v68, v69
	v_pk_add_f32 v[46:47], v[22:23], v[64:65] op_sel_hi:[1,0] neg_lo:[0,1] neg_hi:[0,1]
	v_add_f32_e32 v0, v0, v63
	v_pk_mul_f32 v[72:73], v[46:47], v[46:47]
	v_add_f32_e32 v0, v1, v0
	v_pk_add_f32 v[42:43], v[2:3], v[64:65] op_sel_hi:[1,0] neg_lo:[0,1] neg_hi:[0,1]
	v_add_f32_e32 v0, v72, v0
	v_pk_mul_f32 v[2:3], v[42:43], v[42:43]
	v_add_f32_e32 v0, v73, v0
	v_pk_add_f32 v[40:41], v[52:53], v[64:65] op_sel_hi:[1,0] neg_lo:[0,1] neg_hi:[0,1]
	v_add_f32_e32 v0, v2, v0
	v_pk_mul_f32 v[52:53], v[40:41], v[40:41]
	v_add_f32_e32 v0, v3, v0
	v_pk_add_f32 v[22:23], v[4:5], v[64:65] op_sel_hi:[1,0] neg_lo:[0,1] neg_hi:[0,1]
	v_add_f32_e32 v0, v52, v0
	v_pk_mul_f32 v[4:5], v[22:23], v[22:23]
	v_add_f32_e32 v0, v53, v0
	v_pk_add_f32 v[38:39], v[48:49], v[64:65] op_sel_hi:[1,0] neg_lo:[0,1] neg_hi:[0,1]
	v_add_f32_e32 v0, v4, v0
	v_pk_mul_f32 v[48:49], v[38:39], v[38:39]
	v_add_f32_e32 v0, v5, v0
	v_pk_add_f32 v[36:37], v[6:7], v[64:65] op_sel_hi:[1,0] neg_lo:[0,1] neg_hi:[0,1]
	v_add_f32_e32 v0, v48, v0
	v_pk_mul_f32 v[74:75], v[36:37], v[36:37]
	v_add_f32_e32 v0, v49, v0
	v_pk_add_f32 v[34:35], v[30:31], v[64:65] op_sel_hi:[1,0] neg_lo:[0,1] neg_hi:[0,1]
	v_add_f32_e32 v0, v74, v0
	v_pk_mul_f32 v[76:77], v[34:35], v[34:35]
	v_add_f32_e32 v0, v75, v0
	v_pk_add_f32 v[32:33], v[8:9], v[64:65] op_sel_hi:[1,0] neg_lo:[0,1] neg_hi:[0,1]
	v_add_f32_e32 v0, v76, v0
	v_pk_mul_f32 v[78:79], v[32:33], v[32:33]
	v_add_f32_e32 v0, v77, v0
	v_pk_add_f32 v[30:31], v[28:29], v[64:65] op_sel_hi:[1,0] neg_lo:[0,1] neg_hi:[0,1]
	v_add_f32_e32 v0, v78, v0
	v_pk_mul_f32 v[80:81], v[30:31], v[30:31]
	v_add_f32_e32 v0, v79, v0
	v_pk_add_f32 v[28:29], v[10:11], v[64:65] op_sel_hi:[1,0] neg_lo:[0,1] neg_hi:[0,1]
	v_add_f32_e32 v0, v80, v0
	v_pk_mul_f32 v[10:11], v[28:29], v[28:29]
	v_add_f32_e32 v0, v81, v0
	v_pk_add_f32 v[20:21], v[26:27], v[64:65] op_sel_hi:[1,0] neg_lo:[0,1] neg_hi:[0,1]
	v_add_f32_e32 v0, v10, v0
	v_pk_mul_f32 v[26:27], v[20:21], v[20:21]
	v_add_f32_e32 v0, v11, v0
	v_pk_add_f32 v[16:17], v[44:45], v[64:65] op_sel_hi:[1,0] neg_lo:[0,1] neg_hi:[0,1]
	v_add_f32_e32 v0, v26, v0
	v_pk_mul_f32 v[44:45], v[16:17], v[16:17]
	v_add_f32_e32 v0, v27, v0
	v_pk_add_f32 v[8:9], v[18:19], v[64:65] op_sel_hi:[1,0] neg_lo:[0,1] neg_hi:[0,1]
	v_add_f32_e32 v0, v44, v0
	v_pk_mul_f32 v[18:19], v[8:9], v[8:9]
	v_add_f32_e32 v0, v45, v0
	v_pk_add_f32 v[6:7], v[24:25], v[64:65] op_sel_hi:[1,0] neg_lo:[0,1] neg_hi:[0,1]
	v_add_f32_e32 v0, v18, v0
	v_pk_mul_f32 v[24:25], v[6:7], v[6:7]
	v_add_f32_e32 v0, v19, v0
	v_add_f32_e32 v0, v24, v0
	v_add_f32_e32 v0, v25, v0
	v_mov_b32_e32 v1, v105
	s_nop 0
	v_add_f32_dpp v0, v0, v0 quad_perm:[1,0,3,2] row_mask:0xf bank_mask:0xf bound_ctrl:1
	s_nop 1
	v_add_f32_dpp v0, v0, v0 quad_perm:[2,3,0,1] row_mask:0xf bank_mask:0xf bound_ctrl:1
	s_nop 1
	v_add_f32_dpp v0, v0, v0 row_half_mirror row_mask:0xf bank_mask:0xf bound_ctrl:1
	s_nop 1
	v_add_f32_dpp v0, v0, v0 row_mirror row_mask:0xf bank_mask:0xf bound_ctrl:1
	s_nop 1
	v_mov_b32_dpp v1, v0 row_bcast:15 row_mask:0xa bank_mask:0xf
	v_add_f32_e32 v0, v0, v1
	v_mov_b32_e32 v1, v105
	s_nop 1
	v_mov_b32_dpp v1, v0 row_bcast:31 row_mask:0xc bank_mask:0xf
	v_add_f32_e32 v0, v0, v1
	s_nop 0
	v_readlane_b32 s2, v0, 63
	s_nop 1
	v_fma_f32 v0, s2, v187, v183
	v_rsq_f32_e32 v10, v0
	s_mov_b64 s[2:3], -1
	v_pk_mul_f32 v[0:1], v[66:67], v[10:11] op_sel_hi:[1,0]
	v_pk_mul_f32 v[2:3], v[70:71], v[10:11] op_sel_hi:[1,0]
	v_pk_fma_f32 v[0:1], v[0:1], v[54:55], v[56:57]
	v_pk_fma_f32 v[2:3], v[2:3], v[58:59], v[60:61]
	s_cbranch_vccz .LBB0_1142
	ds_read2st64_b64 v[24:27], v62 offset0:8 offset1:16
	v_cvt_pk_bf16_f32 v4, v0, v1
	v_cvt_pk_bf16_f32 v5, v2, v3
	global_store_dwordx2 v[14:15], v[4:5], off
	s_mov_b64 s[2:3], 0
	s_waitcnt lgkmcnt(0)
	v_lshlrev_b32_e32 v18, 16, v26
	v_and_b32_e32 v19, 0xffff0000, v26
	v_lshlrev_b32_e32 v4, 16, v24
	v_and_b32_e32 v5, 0xffff0000, v24
	v_pk_add_f32 v[18:19], v[18:19], 1.0 op_sel_hi:[1,0]
	v_lshlrev_b32_e32 v24, 16, v27
	v_pk_fma_f32 v[4:5], v[0:1], v[18:19], v[4:5]
	v_lshlrev_b32_e32 v18, 16, v25
	v_and_b32_e32 v19, 0xffff0000, v25
	v_and_b32_e32 v25, 0xffff0000, v27
	v_pk_add_f32 v[24:25], v[24:25], 1.0 op_sel_hi:[1,0]
	v_cvt_pk_bf16_f32 v4, v4, v5
	v_pk_fma_f32 v[18:19], v[2:3], v[24:25], v[18:19]
	s_nop 0
	v_cvt_pk_bf16_f32 v5, v18, v19

.LBB0_1180:
	s_add_i32 s0, s36, 0x2000
	s_ashr_i32 s1, s0, 31
	s_lshl_b64 s[4:5], s[0:1], 9
	s_add_u32 s6, s18, s4
	v_mov_b32_e32 v80, v110
	s_addc_u32 s7, s19, s5
	s_add_u32 s4, s28, s4
	v_ashrrev_i32_e32 v81, 31, v80
	s_addc_u32 s5, s50, s5
	v_lshlrev_b64 v[0:1], 2, v[80:81]
	s_lshl_b64 s[34:35], s[0:1], 12
	v_lshl_add_u64 v[2:3], s[6:7], 0, v[0:1]
	s_add_u32 s6, s51, s34
	s_waitcnt vmcnt(1)
	v_lshlrev_b32_e32 v114, 2, v80
	s_addc_u32 s7, s70, s35
	v_ashrrev_i32_e32 v115, 31, v114
	s_waitcnt vmcnt(0)
	v_lshl_add_u64 v[112:113], v[114:115], 1, s[6:7]
	global_load_dword v116, v[2:3], off
	global_load_dword v118, v[2:3], off offset:256
	s_nop 0
	global_load_dwordx2 v[2:3], v[112:113], off offset:3584
	global_load_dwordx2 v[4:5], v[112:113], off offset:3072
	global_load_dwordx2 v[6:7], v[112:113], off offset:2560
	global_load_dwordx2 v[8:9], v[112:113], off offset:2048
	global_load_dwordx2 v[10:11], v[112:113], off offset:1536
	global_load_dwordx2 v[12:13], v[112:113], off offset:1024
	global_load_dwordx2 v[14:15], v[112:113], off offset:512
	global_load_dwordx2 v[16:17], v[112:113], off
	v_lshl_add_u64 v[0:1], s[4:5], 0, v[0:1]
	global_load_dword v83, v[0:1], off
	global_load_dword v81, v[0:1], off offset:256
	v_ashrrev_i32_e32 v70, 4, v80
	v_and_b32_e32 v78, 3, v80
	v_and_b32_e32 v71, 15, v80
	v_lshlrev_b32_e32 v152, 4, v80
	v_bfe_u32 v79, v80, 2, 2
	s_waitcnt vmcnt(9)
	v_lshlrev_b32_e32 v32, 16, v3
	v_and_b32_e32 v33, 0xffff0000, v3
	v_lshlrev_b32_e32 v34, 16, v2
	v_and_b32_e32 v35, 0xffff0000, v2
	s_waitcnt vmcnt(8)
	v_lshlrev_b32_e32 v38, 16, v4
	v_and_b32_e32 v39, 0xffff0000, v4
	s_waitcnt vmcnt(6)
	v_lshlrev_b32_e32 v50, 16, v9
	v_and_b32_e32 v51, 0xffff0000, v9
	v_lshlrev_b32_e32 v40, 16, v7
	v_and_b32_e32 v41, 0xffff0000, v7
	v_lshlrev_b32_e32 v42, 16, v6
	v_and_b32_e32 v43, 0xffff0000, v6
	s_waitcnt vmcnt(4)
	v_lshlrev_b32_e32 v58, 16, v13
	v_and_b32_e32 v59, 0xffff0000, v13
	v_lshlrev_b32_e32 v60, 16, v12
	v_and_b32_e32 v61, 0xffff0000, v12
	v_max_f32_e64 v0, |v33|, |v33|
	v_max_f32_e64 v1, |v32|, |v32|
	v_max_f32_e64 v2, |v35|, |v35|
	v_max_f32_e64 v3, |v34|, |v34|
	v_max_f32_e64 v6, |v39|, |v39|
	v_max_f32_e64 v7, |v38|, |v38|
	v_max_f32_e64 v12, |v51|, |v51|
	v_max_f32_e64 v13, |v50|, |v50|
	s_waitcnt vmcnt(3)
	v_lshlrev_b32_e32 v62, 16, v15
	v_and_b32_e32 v63, 0xffff0000, v15
	v_max_f32_e32 v0, v1, v0
	v_max_f32_e32 v1, v3, v2
	v_max_f32_e32 v3, v7, v6
	v_max_f32_e32 v6, v13, v12
	v_max_f32_e64 v12, |v63|, |v63|
	v_max_f32_e64 v13, |v62|, |v62|
	v_lshlrev_b32_e32 v64, 16, v14
	v_and_b32_e32 v65, 0xffff0000, v14
	v_max_f32_e32 v12, v13, v12
	v_max_f32_e64 v13, |v65|, |v65|
	v_max_f32_e64 v14, |v64|, |v64|
	s_waitcnt vmcnt(2)
	v_lshlrev_b32_e32 v66, 16, v17
	v_and_b32_e32 v67, 0xffff0000, v17
	v_max_f32_e32 v13, v14, v13
	v_max_f32_e64 v14, |v67|, |v67|
	v_max_f32_e64 v15, |v66|, |v66|
	v_lshlrev_b32_e32 v68, 16, v16
	v_and_b32_e32 v69, 0xffff0000, v16
	v_max_f32_e32 v14, v15, v14
	v_max_f32_e64 v15, |v69|, |v69|
	v_max_f32_e64 v16, |v68|, |v68|
	v_lshlrev_b32_e32 v36, 16, v5
	v_and_b32_e32 v37, 0xffff0000, v5
	v_max_f32_e32 v15, v16, v15
	v_lshlrev_b32_e32 v54, 16, v11
	v_and_b32_e32 v55, 0xffff0000, v11
	v_lshlrev_b32_e32 v56, 16, v10
	v_and_b32_e32 v57, 0xffff0000, v10
	v_max_f32_e64 v4, |v37|, |v37|
	v_max_f32_e64 v5, |v36|, |v36|
	v_max_f32_e64 v10, |v43|, |v43|
	v_max_f32_e64 v11, |v42|, |v42|
	v_max_f32_e64 v24, |v59|, |v59|
	v_max_f32_e64 v25, |v58|, |v58|
	v_max_f32_e64 v26, |v61|, |v61|
	v_max_f32_e64 v27, |v60|, |v60|
	v_max3_f32 v14, v15, 0, v14
	v_lshlrev_b32_e32 v52, 16, v8
	v_and_b32_e32 v53, 0xffff0000, v8
	v_max_f32_e64 v8, |v41|, |v41|
	v_max_f32_e64 v9, |v40|, |v40|
	v_max_f32_e64 v20, |v55|, |v55|
	v_max_f32_e64 v21, |v54|, |v54|
	v_max_f32_e64 v22, |v57|, |v57|
	v_max_f32_e64 v23, |v56|, |v56|
	v_max_f32_e32 v2, v5, v4
	v_max_f32_e32 v5, v11, v10
	v_max_f32_e32 v10, v25, v24
	v_max_f32_e32 v11, v27, v26
	v_max3_f32 v12, v14, v13, v12
	v_max_f32_e64 v18, |v53|, |v53|
	v_max_f32_e64 v19, |v52|, |v52|
	v_max_f32_e32 v4, v9, v8
	v_max_f32_e32 v8, v21, v20
	v_max_f32_e32 v9, v23, v22
	v_max3_f32 v10, v12, v11, v10
	v_max_f32_e32 v7, v19, v18
	v_max3_f32 v8, v10, v9, v8
	v_max3_f32 v6, v8, v7, v6
	v_max3_f32 v4, v6, v5, v4
	v_max3_f32 v2, v4, v3, v2
	v_max3_f32 v0, v2, v1, v0
	v_ashrrev_i32_e32 v117, 31, v116
	v_ashrrev_i32_e32 v119, 31, v118
	v_mov_b32_dpp v1, v0 quad_perm:[1,0,3,2] row_mask:0xf bank_mask:0xf bound_ctrl:1
	v_max_f32_e32 v1, v1, v1
	v_max_f32_e32 v0, v0, v1
	s_nop 1
	v_mov_b32_dpp v1, v0 quad_perm:[2,3,0,1] row_mask:0xf bank_mask:0xf bound_ctrl:1
	v_max_f32_e32 v1, v1, v1
	v_max_f32_e32 v0, v0, v1
	s_nop 1
	v_mov_b32_dpp v1, v0 row_half_mirror row_mask:0xf bank_mask:0xf bound_ctrl:1
	v_max_f32_e32 v1, v1, v1
	v_max_f32_e32 v0, v0, v1
	s_nop 1
	v_mov_b32_dpp v1, v0 row_mirror row_mask:0xf bank_mask:0xf bound_ctrl:1
	v_max_f32_e32 v1, v1, v1
	v_max_f32_e32 v0, v0, v1
	s_nop 0
	v_readlane_b32 s5, v0, 32
	v_readlane_b32 s6, v0, 48
	v_readlane_b32 s1, v0, 0
	v_readlane_b32 s4, v0, 16
	v_max_f32_e64 v0, s6, s6
	v_max_f32_e64 v1, s5, s5
	v_max_f32_e32 v0, v1, v0
	v_mov_b32_e32 v1, s4
	v_max3_f32 v0, s1, v1, v0
	s_mov_b32 s1, 0x40f00000
	v_div_scale_f32 v1, s[4:5], v0, v0, s1
	v_rcp_f32_e32 v2, v1
	s_nop 0
	v_fma_f32 v3, -v1, v2, 1.0
	v_fmac_f32_e32 v2, v3, v2
	v_div_scale_f32 v3, vcc, s1, v0, s1
	v_mul_f32_e32 v4, v3, v2
	v_fma_f32 v5, -v1, v4, v3
	v_fmac_f32_e32 v4, v5, v2
	v_fma_f32 v1, -v1, v4, v3
	v_div_fmas_f32 v1, v1, v2, v4
	v_div_fixup_f32 v1, v1, v0, s1
	v_cmp_lt_f32_e32 vcc, 0, v0
	s_nop 1
	v_cndmask_b32_e32 v82, 1.0, v1, vcc
	s_waitcnt vmcnt(1)
	v_pk_mul_f32 v[0:1], v[82:83], v[68:69] op_sel_hi:[0,1]
	v_pk_mul_f32 v[2:3], v[82:83], v[66:67] op_sel_hi:[0,1]
	v_cvt_pk_bf16_f32 v0, v0, v1
	v_cvt_pk_bf16_f32 v1, v2, v3
	v_pk_mul_f32 v[2:3], v[82:83], v[64:65] op_sel_hi:[0,1]
	v_pk_mul_f32 v[4:5], v[82:83], v[62:63] op_sel_hi:[0,1]
	v_cvt_pk_bf16_f32 v2, v2, v3
	v_cvt_pk_bf16_f32 v3, v4, v5
	v_pk_mul_f32 v[4:5], v[82:83], v[60:61] op_sel_hi:[0,1]
	v_pk_mul_f32 v[6:7], v[82:83], v[58:59] op_sel_hi:[0,1]
	v_cvt_pk_bf16_f32 v4, v4, v5
	v_cvt_pk_bf16_f32 v5, v6, v7
	v_pk_mul_f32 v[6:7], v[82:83], v[56:57] op_sel_hi:[0,1]
	v_pk_mul_f32 v[8:9], v[82:83], v[54:55] op_sel_hi:[0,1]
	v_cvt_pk_bf16_f32 v6, v6, v7
	v_cvt_pk_bf16_f32 v7, v8, v9
	v_pk_mul_f32 v[8:9], v[82:83], v[52:53] op_sel_hi:[0,1]
	v_pk_mul_f32 v[10:11], v[82:83], v[50:51] op_sel_hi:[0,1]
	v_cvt_pk_bf16_f32 v8, v8, v9
	v_cvt_pk_bf16_f32 v9, v10, v11
	v_pk_mul_f32 v[10:11], v[82:83], v[42:43] op_sel_hi:[0,1]
	v_pk_mul_f32 v[12:13], v[82:83], v[40:41] op_sel_hi:[0,1]
	v_cvt_pk_bf16_f32 v10, v10, v11
	v_cvt_pk_bf16_f32 v11, v12, v13
	v_pk_mul_f32 v[12:13], v[82:83], v[38:39] op_sel_hi:[0,1]
	v_pk_mul_f32 v[14:15], v[82:83], v[36:37] op_sel_hi:[0,1]
	v_cvt_pk_bf16_f32 v12, v12, v13
	v_cvt_pk_bf16_f32 v13, v14, v15
	v_pk_mul_f32 v[14:15], v[82:83], v[34:35] op_sel_hi:[0,1]
	v_pk_mul_f32 v[16:17], v[82:83], v[32:33] op_sel_hi:[0,1]
	v_cvt_pk_bf16_f32 v14, v14, v15
	v_cvt_pk_bf16_f32 v15, v16, v17
	v_cvt_scalef32_pk32_fp6_bf16 v[44:49], v[0:15], 1.0
	v_cvt_scalef32_pk32_f32_fp6 v[0:31], v[44:49], 1.0
	v_pk_fma_f32 v[0:1], v[82:83], v[68:69], v[0:1] op_sel_hi:[0,1,1] neg_lo:[0,0,1] neg_hi:[0,0,1]
	v_pk_fma_f32 v[2:3], v[82:83], v[66:67], v[2:3] op_sel_hi:[0,1,1] neg_lo:[0,0,1] neg_hi:[0,0,1]
	v_pk_mul_f32 v[0:1], v[0:1], s[48:49] op_sel_hi:[1,0]
	v_pk_mul_f32 v[2:3], v[2:3], s[48:49] op_sel_hi:[1,0]
	v_cvt_pk_bf16_f32 v0, v0, v1
	v_cvt_pk_bf16_f32 v1, v2, v3
	v_pk_fma_f32 v[2:3], v[82:83], v[64:65], v[4:5] op_sel_hi:[0,1,1] neg_lo:[0,0,1] neg_hi:[0,0,1]
	v_pk_fma_f32 v[4:5], v[82:83], v[62:63], v[6:7] op_sel_hi:[0,1,1] neg_lo:[0,0,1] neg_hi:[0,0,1]
	v_pk_mul_f32 v[2:3], v[2:3], s[48:49] op_sel_hi:[1,0]
	v_pk_mul_f32 v[4:5], v[4:5], s[48:49] op_sel_hi:[1,0]
	v_cvt_pk_bf16_f32 v2, v2, v3
	v_cvt_pk_bf16_f32 v3, v4, v5
	v_pk_fma_f32 v[4:5], v[82:83], v[60:61], v[8:9] op_sel_hi:[0,1,1] neg_lo:[0,0,1] neg_hi:[0,0,1]
	v_pk_fma_f32 v[6:7], v[82:83], v[58:59], v[10:11] op_sel_hi:[0,1,1] neg_lo:[0,0,1] neg_hi:[0,0,1]
	v_pk_mul_f32 v[4:5], v[4:5], s[48:49] op_sel_hi:[1,0]
	v_pk_mul_f32 v[6:7], v[6:7], s[48:49] op_sel_hi:[1,0]
	v_cvt_pk_bf16_f32 v4, v4, v5
	v_cvt_pk_bf16_f32 v5, v6, v7
	v_pk_fma_f32 v[6:7], v[82:83], v[56:57], v[12:13] op_sel_hi:[0,1,1] neg_lo:[0,0,1] neg_hi:[0,0,1]
	v_pk_fma_f32 v[8:9], v[82:83], v[54:55], v[14:15] op_sel_hi:[0,1,1] neg_lo:[0,0,1] neg_hi:[0,0,1]
	v_pk_mul_f32 v[6:7], v[6:7], s[48:49] op_sel_hi:[1,0]
	v_pk_mul_f32 v[8:9], v[8:9], s[48:49] op_sel_hi:[1,0]
	v_cvt_pk_bf16_f32 v6, v6, v7
	v_cvt_pk_bf16_f32 v7, v8, v9
	v_pk_fma_f32 v[8:9], v[82:83], v[52:53], v[16:17] op_sel_hi:[0,1,1] neg_lo:[0,0,1] neg_hi:[0,0,1]
	v_pk_fma_f32 v[10:11], v[82:83], v[50:51], v[18:19] op_sel_hi:[0,1,1] neg_lo:[0,0,1] neg_hi:[0,0,1]
	v_pk_mul_f32 v[8:9], v[8:9], s[48:49] op_sel_hi:[1,0]
	v_pk_mul_f32 v[10:11], v[10:11], s[48:49] op_sel_hi:[1,0]
	v_cvt_pk_bf16_f32 v8, v8, v9
	v_cvt_pk_bf16_f32 v9, v10, v11
	v_pk_fma_f32 v[10:11], v[82:83], v[42:43], v[20:21] op_sel_hi:[0,1,1] neg_lo:[0,0,1] neg_hi:[0,0,1]
	v_pk_fma_f32 v[12:13], v[82:83], v[40:41], v[22:23] op_sel_hi:[0,1,1] neg_lo:[0,0,1] neg_hi:[0,0,1]
	v_pk_mul_f32 v[10:11], v[10:11], s[48:49] op_sel_hi:[1,0]
	v_pk_mul_f32 v[12:13], v[12:13], s[48:49] op_sel_hi:[1,0]
	v_cvt_pk_bf16_f32 v10, v10, v11
	v_cvt_pk_bf16_f32 v11, v12, v13
	v_pk_fma_f32 v[12:13], v[82:83], v[38:39], v[24:25] op_sel_hi:[0,1,1] neg_lo:[0,0,1] neg_hi:[0,0,1]
	v_pk_fma_f32 v[14:15], v[82:83], v[36:37], v[26:27] op_sel_hi:[0,1,1] neg_lo:[0,0,1] neg_hi:[0,0,1]
	v_pk_mul_f32 v[12:13], v[12:13], s[48:49] op_sel_hi:[1,0]
	v_pk_mul_f32 v[14:15], v[14:15], s[48:49] op_sel_hi:[1,0]
	v_cvt_pk_bf16_f32 v12, v12, v13
	v_cvt_pk_bf16_f32 v13, v14, v15
	v_pk_fma_f32 v[14:15], v[82:83], v[34:35], v[28:29] op_sel_hi:[0,1,1] neg_lo:[0,0,1] neg_hi:[0,0,1]
	v_pk_fma_f32 v[16:17], v[82:83], v[32:33], v[30:31] op_sel_hi:[0,1,1] neg_lo:[0,0,1] neg_hi:[0,0,1]
	v_pk_mul_f32 v[14:15], v[14:15], s[48:49] op_sel_hi:[1,0]
	v_pk_mul_f32 v[16:17], v[16:17], s[48:49] op_sel_hi:[1,0]
	v_cvt_pk_bf16_f32 v14, v14, v15
	v_cvt_pk_bf16_f32 v15, v16, v17
	v_cvt_scalef32_pk32_fp6_bf16 v[16:21], v[0:15], 1.0
	v_mad_u64_u32 v[0:1], s[4:5], v80, 24, v[104:105]
	v_add_u32_e32 v1, 0xe000, v0
	v_add_u32_e32 v2, 0xe600, v0
	v_add_u32_e32 v0, 16, v0
	ds_write2_b64 v1, v[44:45], v[46:47] offset1:1
	ds_write2_b64 v2, v[16:17], v[18:19] offset1:1
	ds_write2st64_b64 v0, v[48:49], v[20:21] offset0:112 offset1:115
	v_bfe_i32 v0, v80, 2, 1
	v_lshl_or_b32 v1, v70, 2, v78
	v_and_b32_e32 v0, 0x600, v0
	v_mul_lo_u32 v1, v1, 24
	v_add3_u32 v0, v104, v0, v1
	v_add_u32_e32 v1, 0xe000, v0
	v_add_u32_e32 v2, 0xe180, v0
	ds_read2_b64 v[154:157], v1 offset0:2 offset1:50
	ds_read2_b64 v[18:21], v1 offset1:1
	ds_read2_b64 v[12:15], v2 offset1:1
	v_add_u32_e32 v2, 0xe300, v0
	v_add_u32_e32 v0, 0xe480, v0
	ds_read2_b64 v[158:161], v1 offset0:98 offset1:146
	ds_read2_b64 v[6:9], v2 offset1:1
	ds_read2_b64 v[0:3], v0 offset1:1
	v_lshlrev_b32_e32 v4, 4, v78
	v_lshl_or_b32 v102, v70, 6, v4
	v_lshlrev_b32_e32 v4, 5, v70
	v_lshl_or_b32 v5, v78, 3, v4
	v_cmp_gt_u32_e32 vcc, 8, v71
	v_add_u32_e32 v103, 0x400, v5
	v_cmp_eq_u32_e64 s[4:5], 0, v71
	v_cndmask_b32_e32 v5, 0, v252, vcc
	v_cmp_lt_u32_e32 vcc, 3, v71
	s_nop 1
	v_cndmask_b32_e32 v29, 1.0, v5, vcc
	v_add_u32_e32 v5, 0x80, v80
	v_cmp_eq_u32_e32 vcc, 2, v78
	v_cndmask_b32_e64 v22, v5, v4, s[4:5]
	s_waitcnt vmcnt(0) lgkmcnt(0)
	v_lshlrev_b64 v[4:5], 2, v[116:117]
	v_lshl_add_u64 v[10:11], s[12:13], 0, v[4:5]
	v_lshl_add_u64 v[4:5], s[14:15], 0, v[4:5]
	global_load_dword v26, v[10:11], off
	global_load_dword v27, v[4:5], off
	v_lshlrev_b64 v[10:11], 2, v[118:119]
	v_lshl_add_u64 v[16:17], s[12:13], 0, v[10:11]
	v_lshl_add_u64 v[4:5], s[14:15], 0, v[10:11]
	global_load_dword v25, v[16:17], off
	global_load_dword v24, v[4:5], off
	v_or_b32_e32 v4, s53, v79
	v_lshlrev_b32_e32 v4, 2, v4
	v_cndmask_b32_e64 v28, v118, v116, s[2:3]
	ds_bpermute_b32 v4, v4, v28
	v_cmp_eq_u32_e64 s[4:5], 1, v78
	s_waitcnt lgkmcnt(0)
	v_mul_lo_u32 v4, v4, s43
	v_add_u32_e32 v5, v4, v102
	v_add_u32_e32 v4, v4, v103
	buffer_load_dwordx4 v[30:33], v5, s[44:47], 0 offen nt
	buffer_load_dwordx4 v[36:39], v5, s[44:47], s20 offen nt
	buffer_load_dwordx4 v[42:45], v5, s[44:47], s21 offen nt
	buffer_load_dwordx4 v[48:51], v5, s[44:47], s23 offen nt
	buffer_load_dwordx2 v[34:35], v4, s[44:47], 0 offen nt
	buffer_load_dwordx2 v[46:47], v4, s[44:47], s33 offen nt
	buffer_load_dwordx2 v[40:41], v4, s[44:47], s21 offen nt
	buffer_load_dwordx2 v[52:53], v4, s[44:47], s94 offen nt
	v_or_b32_e32 v4, s57, v79
	v_lshlrev_b32_e32 v4, 2, v4
	ds_bpermute_b32 v4, v4, v28
	v_cmp_eq_u32_e64 s[6:7], 3, v78
	s_waitcnt lgkmcnt(0)
	v_mul_lo_u32 v4, v4, s43
	v_add_u32_e32 v5, v4, v102
	v_add_u32_e32 v4, v4, v103
	buffer_load_dwordx4 v[54:57], v5, s[44:47], 0 offen nt
	buffer_load_dwordx4 v[60:63], v5, s[44:47], s20 offen nt
	buffer_load_dwordx4 v[66:69], v5, s[44:47], s21 offen nt
	buffer_load_dwordx4 v[72:75], v5, s[44:47], s23 offen nt
	buffer_load_dwordx2 v[58:59], v4, s[44:47], 0 offen nt
	buffer_load_dwordx2 v[70:71], v4, s[44:47], s33 offen nt
	buffer_load_dwordx2 v[64:65], v4, s[44:47], s21 offen nt
	buffer_load_dwordx2 v[76:77], v4, s[44:47], s94 offen nt
	v_or_b32_e32 v4, s58, v79
	v_lshlrev_b32_e32 v4, 2, v4
	ds_bpermute_b32 v4, v4, v28
	s_waitcnt lgkmcnt(0)
	v_mul_lo_u32 v4, v4, s43
	v_add_u32_e32 v5, v4, v102
	v_add_u32_e32 v4, v4, v103
	buffer_load_dwordx4 v[84:87], v5, s[44:47], 0 offen nt
	buffer_load_dwordx4 v[90:93], v5, s[44:47], s20 offen nt
	buffer_load_dwordx4 v[96:99], v5, s[44:47], s21 offen nt
	buffer_load_dwordx4 v[120:123], v5, s[44:47], s23 offen nt
	buffer_load_dwordx2 v[88:89], v4, s[44:47], 0 offen nt
	buffer_load_dwordx2 v[100:101], v4, s[44:47], s33 offen nt
	buffer_load_dwordx2 v[94:95], v4, s[44:47], s21 offen nt
	buffer_load_dwordx2 v[124:125], v4, s[44:47], s94 offen nt
	v_or_b32_e32 v4, s62, v79
	v_lshlrev_b32_e32 v4, 2, v4
	ds_bpermute_b32 v4, v4, v28
	v_lshl_add_u32 v78, v22, 2, v176
	s_waitcnt lgkmcnt(0)
	v_mul_lo_u32 v4, v4, s43
	v_add_u32_e32 v5, v4, v102
	v_add_u32_e32 v4, v4, v103
	buffer_load_dwordx4 v[126:129], v5, s[44:47], 0 offen nt
	buffer_load_dwordx4 v[132:135], v5, s[44:47], s20 offen nt
	buffer_load_dwordx4 v[138:141], v5, s[44:47], s21 offen nt
	buffer_load_dwordx4 v[144:147], v5, s[44:47], s23 offen nt
	buffer_load_dwordx2 v[130:131], v4, s[44:47], 0 offen nt
	buffer_load_dwordx2 v[142:143], v4, s[44:47], s33 offen nt
	buffer_load_dwordx2 v[136:137], v4, s[44:47], s21 offen nt
	buffer_load_dwordx2 v[148:149], v4, s[44:47], s94 offen nt
	v_or_b32_e32 v4, s59, v79
	v_lshlrev_b32_e32 v117, 2, v4
	v_or_b32_e32 v4, s61, v79
	v_lshlrev_b32_e32 v119, 2, v4
	v_mov_b32_e32 v22, v154
	v_mov_b32_e32 v23, v155
	v_mov_b32_e32 v16, v156
	v_mov_b32_e32 v17, v157
	s_waitcnt vmcnt(27)
	v_mfma_f32_16x16x128_f8f6f4 v[30:33], v[30:35], v[18:23], 0 cbsz:2 blgp:2
	v_mov_b32_e32 v10, v158
	v_mov_b32_e32 v11, v159
	v_mov_b32_e32 v4, v160
	s_waitcnt vmcnt(26)
	v_mfma_f32_16x16x128_f8f6f4 v[30:33], v[42:47], v[12:17], v[30:33] cbsz:2 blgp:2
	v_mov_b32_e32 v5, v161
	s_waitcnt vmcnt(25)
	v_mfma_f32_16x16x128_f8f6f4 v[30:33], v[36:41], v[6:11], v[30:33] cbsz:2 blgp:2
	s_waitcnt vmcnt(24)
	v_mfma_f32_16x16x128_f8f6f4 v[30:33], v[48:53], v[0:5], v[30:33] cbsz:2 blgp:2
	s_nop 7
	v_cndmask_b32_e64 v30, v30, v31, s[4:5]
	v_cndmask_b32_e32 v30, v30, v32, vcc
	v_cndmask_b32_e64 v30, v30, v33, s[6:7]
	v_mul_f32_e32 v31, v29, v30
	s_nop 1
	v_mov_b32_dpp v31, v31 quad_perm:[1,0,3,2] row_mask:0xf bank_mask:0xf bound_ctrl:1
	v_fmac_f32_e32 v31, v29, v30
	s_nop 1
	v_add_f32_dpp v30, v31, v31 quad_perm:[2,3,0,1] row_mask:0xf bank_mask:0xf bound_ctrl:1
	s_nop 1
	v_add_f32_dpp v30, v30, v30 row_half_mirror row_mask:0xf bank_mask:0xf bound_ctrl:1
	ds_write_b32 v78, v30 offset:49152
	v_or_b32_e32 v30, s63, v79
	v_lshlrev_b32_e32 v30, 2, v30
	ds_bpermute_b32 v30, v30, v28
	s_waitcnt lgkmcnt(0)
	v_mul_lo_u32 v30, v30, s43
	v_add_u32_e32 v34, v30, v102
	v_add_u32_e32 v52, v30, v103
	buffer_load_dwordx4 v[30:33], v34, s[44:47], 0 offen nt
	buffer_load_dwordx4 v[36:39], v34, s[44:47], s20 offen nt
	buffer_load_dwordx4 v[42:45], v34, s[44:47], s21 offen nt
	buffer_load_dwordx4 v[48:51], v34, s[44:47], s23 offen nt
	s_nop 0
	buffer_load_dwordx2 v[34:35], v52, s[44:47], 0 offen nt
	buffer_load_dwordx2 v[46:47], v52, s[44:47], s33 offen nt
	buffer_load_dwordx2 v[40:41], v52, s[44:47], s21 offen nt
	s_nop 0
	buffer_load_dwordx2 v[52:53], v52, s[44:47], s94 offen nt
	s_waitcnt vmcnt(27)
	v_mfma_f32_16x16x128_f8f6f4 v[54:57], v[54:59], v[18:23], 0 cbsz:2 blgp:2
	s_waitcnt vmcnt(26)
	v_mfma_f32_16x16x128_f8f6f4 v[54:57], v[66:71], v[12:17], v[54:57] cbsz:2 blgp:2
	s_waitcnt vmcnt(25)
	v_mfma_f32_16x16x128_f8f6f4 v[54:57], v[60:65], v[6:11], v[54:57] cbsz:2 blgp:2
	s_waitcnt vmcnt(24)
	v_mfma_f32_16x16x128_f8f6f4 v[54:57], v[72:77], v[0:5], v[54:57] cbsz:2 blgp:2
	s_nop 7
	v_cndmask_b32_e64 v54, v54, v55, s[4:5]
	v_cndmask_b32_e32 v54, v54, v56, vcc
	v_cndmask_b32_e64 v54, v54, v57, s[6:7]
	v_mul_f32_e32 v55, v29, v54
	s_nop 1
	v_mov_b32_dpp v55, v55 quad_perm:[1,0,3,2] row_mask:0xf bank_mask:0xf bound_ctrl:1
	v_fmac_f32_e32 v55, v29, v54
	s_nop 1
	v_add_f32_dpp v54, v55, v55 quad_perm:[2,3,0,1] row_mask:0xf bank_mask:0xf bound_ctrl:1
	s_nop 1
	v_add_f32_dpp v54, v54, v54 row_half_mirror row_mask:0xf bank_mask:0xf bound_ctrl:1
	ds_write_b32 v78, v54 offset:49156
	ds_bpermute_b32 v54, v117, v28
	s_waitcnt lgkmcnt(0)
	v_mul_lo_u32 v54, v54, s43
	v_add_u32_e32 v58, v54, v102
	v_add_u32_e32 v76, v54, v103
	buffer_load_dwordx4 v[54:57], v58, s[44:47], 0 offen nt
	buffer_load_dwordx4 v[60:63], v58, s[44:47], s20 offen nt
	buffer_load_dwordx4 v[66:69], v58, s[44:47], s21 offen nt
	buffer_load_dwordx4 v[72:75], v58, s[44:47], s23 offen nt
	s_nop 0
	buffer_load_dwordx2 v[58:59], v76, s[44:47], 0 offen nt
	buffer_load_dwordx2 v[70:71], v76, s[44:47], s33 offen nt
	buffer_load_dwordx2 v[64:65], v76, s[44:47], s21 offen nt
	s_nop 0
	buffer_load_dwordx2 v[76:77], v76, s[44:47], s94 offen nt
	s_waitcnt vmcnt(27)
	v_mfma_f32_16x16x128_f8f6f4 v[84:87], v[84:89], v[18:23], 0 cbsz:2 blgp:2
	s_waitcnt vmcnt(26)
	v_mfma_f32_16x16x128_f8f6f4 v[84:87], v[96:101], v[12:17], v[84:87] cbsz:2 blgp:2
	s_waitcnt vmcnt(25)
	v_mfma_f32_16x16x128_f8f6f4 v[84:87], v[90:95], v[6:11], v[84:87] cbsz:2 blgp:2
	s_waitcnt vmcnt(24)
	v_mfma_f32_16x16x128_f8f6f4 v[84:87], v[120:125], v[0:5], v[84:87] cbsz:2 blgp:2
	s_nop 7
	v_cndmask_b32_e64 v84, v84, v85, s[4:5]
	v_cndmask_b32_e32 v84, v84, v86, vcc
	v_cndmask_b32_e64 v84, v84, v87, s[6:7]
	v_mul_f32_e32 v85, v29, v84
	s_nop 1
	v_mov_b32_dpp v85, v85 quad_perm:[1,0,3,2] row_mask:0xf bank_mask:0xf bound_ctrl:1
	v_fmac_f32_e32 v85, v29, v84
	s_nop 1
	v_add_f32_dpp v84, v85, v85 quad_perm:[2,3,0,1] row_mask:0xf bank_mask:0xf bound_ctrl:1
	s_nop 1
	v_add_f32_dpp v84, v84, v84 row_half_mirror row_mask:0xf bank_mask:0xf bound_ctrl:1
	ds_write_b32 v78, v84 offset:49160
	ds_bpermute_b32 v84, v119, v28
	s_waitcnt lgkmcnt(0)
	v_mul_lo_u32 v84, v84, s43
	v_add_u32_e32 v88, v84, v102
	v_add_u32_e32 v117, v84, v103
	buffer_load_dwordx4 v[84:87], v88, s[44:47], 0 offen nt
	buffer_load_dwordx4 v[90:93], v88, s[44:47], s20 offen nt
	buffer_load_dwordx4 v[96:99], v88, s[44:47], s21 offen nt
	buffer_load_dwordx4 v[120:123], v88, s[44:47], s23 offen nt
	s_nop 0
	buffer_load_dwordx2 v[88:89], v117, s[44:47], 0 offen nt
	buffer_load_dwordx2 v[100:101], v117, s[44:47], s33 offen nt
	buffer_load_dwordx2 v[94:95], v117, s[44:47], s21 offen nt
	buffer_load_dwordx2 v[124:125], v117, s[44:47], s94 offen nt
	s_waitcnt vmcnt(27)
	v_mfma_f32_16x16x128_f8f6f4 v[126:129], v[126:131], v[18:23], 0 cbsz:2 blgp:2
	s_waitcnt vmcnt(26)
	v_mfma_f32_16x16x128_f8f6f4 v[126:129], v[138:143], v[12:17], v[126:129] cbsz:2 blgp:2
	s_waitcnt vmcnt(25)
	v_mfma_f32_16x16x128_f8f6f4 v[126:129], v[132:137], v[6:11], v[126:129] cbsz:2 blgp:2
	s_waitcnt vmcnt(24)
	v_mfma_f32_16x16x128_f8f6f4 v[126:129], v[144:149], v[0:5], v[126:129] cbsz:2 blgp:2
	s_nop 7
	v_cndmask_b32_e64 v117, v126, v127, s[4:5]
	v_cndmask_b32_e32 v117, v117, v128, vcc
	v_cndmask_b32_e64 v117, v117, v129, s[6:7]
	v_mul_f32_e32 v119, v29, v117
	s_nop 1
	v_mov_b32_dpp v119, v119 quad_perm:[1,0,3,2] row_mask:0xf bank_mask:0xf bound_ctrl:1
	v_fmac_f32_e32 v119, v29, v117
	s_nop 1
	v_add_f32_dpp v117, v119, v119 quad_perm:[2,3,0,1] row_mask:0xf bank_mask:0xf bound_ctrl:1
	s_nop 1
	v_add_f32_dpp v117, v117, v117 row_half_mirror row_mask:0xf bank_mask:0xf bound_ctrl:1
	ds_write_b32 v78, v117 offset:49164
	v_or_b32_e32 v79, s65, v79
	v_lshlrev_b32_e32 v79, 2, v79
	ds_bpermute_b32 v79, v79, v28
	s_waitcnt lgkmcnt(0)
	v_mul_lo_u32 v79, v79, s43
	v_add_u32_e32 v102, v79, v102
	v_add_u32_e32 v79, v79, v103
	buffer_load_dwordx4 v[126:129], v102, s[44:47], 0 offen nt
	buffer_load_dwordx4 v[132:135], v102, s[44:47], s20 offen nt
	buffer_load_dwordx4 v[138:141], v102, s[44:47], s21 offen nt
	buffer_load_dwordx4 v[144:147], v102, s[44:47], s23 offen nt
	buffer_load_dwordx2 v[130:131], v79, s[44:47], 0 offen nt
	buffer_load_dwordx2 v[142:143], v79, s[44:47], s33 offen nt
	buffer_load_dwordx2 v[136:137], v79, s[44:47], s21 offen nt
	buffer_load_dwordx2 v[148:149], v79, s[44:47], s94 offen nt
	s_waitcnt vmcnt(27)
	v_mfma_f32_16x16x128_f8f6f4 v[30:33], v[30:35], v[18:23], 0 cbsz:2 blgp:2
	s_waitcnt vmcnt(26)
	v_mfma_f32_16x16x128_f8f6f4 v[30:33], v[42:47], v[12:17], v[30:33] cbsz:2 blgp:2
	s_waitcnt vmcnt(25)
	v_mfma_f32_16x16x128_f8f6f4 v[30:33], v[36:41], v[6:11], v[30:33] cbsz:2 blgp:2
	s_waitcnt vmcnt(24)
	v_mfma_f32_16x16x128_f8f6f4 v[30:33], v[48:53], v[0:5], v[30:33] cbsz:2 blgp:2
	s_nop 7
	v_cndmask_b32_e64 v30, v30, v31, s[4:5]
	v_cndmask_b32_e32 v30, v30, v32, vcc
	v_cndmask_b32_e64 v30, v30, v33, s[6:7]
	v_mul_f32_e32 v31, v29, v30
	s_nop 1
	v_mov_b32_dpp v31, v31 quad_perm:[1,0,3,2] row_mask:0xf bank_mask:0xf bound_ctrl:1
	v_fmac_f32_e32 v31, v29, v30
	s_nop 1
	v_add_f32_dpp v30, v31, v31 quad_perm:[2,3,0,1] row_mask:0xf bank_mask:0xf bound_ctrl:1
	s_nop 1
	v_add_f32_dpp v30, v30, v30 row_half_mirror row_mask:0xf bank_mask:0xf bound_ctrl:1
	ds_write_b32 v78, v30 offset:49168
	s_waitcnt vmcnt(19)
	v_mfma_f32_16x16x128_f8f6f4 v[30:33], v[54:59], v[18:23], 0 cbsz:2 blgp:2
	s_waitcnt vmcnt(18)
	v_mfma_f32_16x16x128_f8f6f4 v[30:33], v[66:71], v[12:17], v[30:33] cbsz:2 blgp:2
	s_waitcnt vmcnt(17)
	v_mfma_f32_16x16x128_f8f6f4 v[30:33], v[60:65], v[6:11], v[30:33] cbsz:2 blgp:2
	s_waitcnt vmcnt(16)
	v_mfma_f32_16x16x128_f8f6f4 v[30:33], v[72:77], v[0:5], v[30:33] cbsz:2 blgp:2
	s_nop 7
	v_cndmask_b32_e64 v30, v30, v31, s[4:5]
	v_cndmask_b32_e32 v30, v30, v32, vcc
	v_cndmask_b32_e64 v30, v30, v33, s[6:7]
	v_mul_f32_e32 v31, v29, v30
	s_nop 1
	v_mov_b32_dpp v31, v31 quad_perm:[1,0,3,2] row_mask:0xf bank_mask:0xf bound_ctrl:1
	v_fmac_f32_e32 v31, v29, v30
	s_nop 1
	v_add_f32_dpp v30, v31, v31 quad_perm:[2,3,0,1] row_mask:0xf bank_mask:0xf bound_ctrl:1
	s_nop 1
	v_add_f32_dpp v30, v30, v30 row_half_mirror row_mask:0xf bank_mask:0xf bound_ctrl:1
	ds_write_b32 v78, v30 offset:49172
	s_waitcnt vmcnt(11)
	v_mfma_f32_16x16x128_f8f6f4 v[30:33], v[84:89], v[18:23], 0 cbsz:2 blgp:2
	s_waitcnt vmcnt(10)
	v_mfma_f32_16x16x128_f8f6f4 v[30:33], v[96:101], v[12:17], v[30:33] cbsz:2 blgp:2
	s_waitcnt vmcnt(9)
	v_mfma_f32_16x16x128_f8f6f4 v[30:33], v[90:95], v[6:11], v[30:33] cbsz:2 blgp:2
	s_waitcnt vmcnt(8)
	v_mfma_f32_16x16x128_f8f6f4 v[30:33], v[120:125], v[0:5], v[30:33] cbsz:2 blgp:2
	s_nop 7
	v_cndmask_b32_e64 v30, v30, v31, s[4:5]
	v_cndmask_b32_e32 v30, v30, v32, vcc
	v_cndmask_b32_e64 v30, v30, v33, s[6:7]
	v_mul_f32_e32 v31, v29, v30
	s_nop 1
	v_mov_b32_dpp v31, v31 quad_perm:[1,0,3,2] row_mask:0xf bank_mask:0xf bound_ctrl:1
	v_fmac_f32_e32 v31, v29, v30
	s_nop 1
	v_add_f32_dpp v30, v31, v31 quad_perm:[2,3,0,1] row_mask:0xf bank_mask:0xf bound_ctrl:1
	s_nop 1
	v_add_f32_dpp v30, v30, v30 row_half_mirror row_mask:0xf bank_mask:0xf bound_ctrl:1
	ds_write_b32 v78, v30 offset:49176
	s_waitcnt vmcnt(3)
	v_mfma_f32_16x16x128_f8f6f4 v[18:21], v[126:131], v[18:23], 0 cbsz:2 blgp:2
	s_waitcnt vmcnt(2)
	v_mfma_f32_16x16x128_f8f6f4 v[12:15], v[138:143], v[12:17], v[18:21] cbsz:2 blgp:2
	s_waitcnt vmcnt(1)
	v_mfma_f32_16x16x128_f8f6f4 v[6:9], v[132:137], v[6:11], v[12:15] cbsz:2 blgp:2
	s_waitcnt vmcnt(0)
	v_mfma_f32_16x16x128_f8f6f4 v[0:3], v[144:149], v[0:5], v[6:9] cbsz:2 blgp:2
	s_nop 7
	v_cndmask_b32_e64 v0, v0, v1, s[4:5]
	v_cndmask_b32_e32 v0, v0, v2, vcc
	v_cndmask_b32_e64 v0, v0, v3, s[6:7]
	v_mul_f32_e32 v1, v29, v0
	s_nop 1
	v_mov_b32_dpp v1, v1 quad_perm:[1,0,3,2] row_mask:0xf bank_mask:0xf bound_ctrl:1
	v_fmac_f32_e32 v1, v29, v0
	s_nop 1
	v_add_f32_dpp v0, v1, v1 quad_perm:[2,3,0,1] row_mask:0xf bank_mask:0xf bound_ctrl:1
	s_nop 1
	v_add_f32_dpp v0, v0, v0 row_half_mirror row_mask:0xf bank_mask:0xf bound_ctrl:1
	ds_write_b32 v78, v0 offset:49180
	v_readlane_b32 s1, v28, s42
	s_mulk_i32 s1, 0x600
	s_add_i32 s1, s1, 0x8000000
	v_lshrrev_b32_e32 v0, 1, v152
	s_nop 1
	buffer_load_dwordx4 v[74:77], v152, s[44:47], s1 offen nt
	buffer_load_dwordx2 v[78:79], v0, s[44:47], s1 offen offset:1024 nt
	v_readlane_b32 s1, v28, s66
	s_mulk_i32 s1, 0x600
	s_add_i32 s1, s1, 0x8000000
	s_nop 2
	buffer_load_dwordx4 v[68:71], v152, s[44:47], s1 offen nt
	buffer_load_dwordx2 v[72:73], v0, s[44:47], s1 offen offset:1024 nt
	v_readlane_b32 s1, v28, s67
	s_mulk_i32 s1, 0x600
	s_add_i32 s1, s1, 0x8000000
	s_nop 2
	buffer_load_dwordx4 v[56:59], v152, s[44:47], s1 offen nt
	buffer_load_dwordx2 v[60:61], v0, s[44:47], s1 offen offset:1024 nt
	v_readlane_b32 s1, v28, s68
	s_mulk_i32 s1, 0x600
	s_add_i32 s1, s1, 0x8000000
	s_nop 2
	buffer_load_dwordx4 v[44:47], v152, s[44:47], s1 offen nt
	buffer_load_dwordx2 v[48:49], v0, s[44:47], s1 offen offset:1024 nt
	v_add_u32_e32 v117, 0x400, v0
	v_readlane_b32 s1, v28, s56
	s_mulk_i32 s1, 0x600
	s_add_i32 s1, s1, 0x8000000
	s_nop 2
	buffer_load_dwordx4 v[62:65], v152, s[44:47], s1 offen nt
	buffer_load_dwordx2 v[66:67], v0, s[44:47], s1 offen offset:1024 nt
	v_readlane_b32 s1, v28, s69
	s_mulk_i32 s1, 0x600
	s_add_i32 s1, s1, 0x8000000
	s_nop 2
	buffer_load_dwordx4 v[50:53], v152, s[44:47], s1 offen nt
	buffer_load_dwordx2 v[54:55], v0, s[44:47], s1 offen offset:1024 nt
	v_readlane_b32 s1, v28, s72
	s_mulk_i32 s1, 0x600
	s_add_i32 s1, s1, 0x8000000
	s_nop 2
	buffer_load_dwordx4 v[38:41], v152, s[44:47], s1 offen nt
	buffer_load_dwordx2 v[42:43], v0, s[44:47], s1 offen offset:1024 nt
	v_readlane_b32 s1, v28, s73
	s_mulk_i32 s1, 0x600
	s_add_i32 s1, s1, 0x8000000
	s_nop 2
	buffer_load_dwordx4 v[32:35], v152, s[44:47], s1 offen nt
	buffer_load_dwordx2 v[36:37], v0, s[44:47], s1 offen offset:1024 nt
	v_div_scale_f32 v2, s[4:5], v82, v82, 1.0
	v_rcp_f32_e32 v3, v2
	v_div_scale_f32 v4, vcc, 1.0, v82, 1.0
	v_and_b32_e32 v1, -4, v80
	v_fma_f32 v0, -v2, v3, 1.0
	v_fmac_f32_e32 v3, v0, v3
	v_mul_f32_e32 v5, v4, v3
	v_fma_f32 v0, -v2, v5, v4
	v_fmac_f32_e32 v5, v0, v3
	v_lshlrev_b32_e32 v0, 7, v80
	v_and_b32_e32 v0, 0x180, v0
	v_add3_u32 v0, v111, v0, v1
	v_add_u32_e32 v0, 0xc000, v0
	ds_read2_b32 v[0:1], v0 offset1:16
	v_fma_f32 v2, -v2, v5, v4
	v_div_fmas_f32 v2, v2, v3, v5
	v_div_fixup_f32 v2, v2, v82, 1.0
	s_mov_b32 s1, 0x3e6d3388
	s_waitcnt lgkmcnt(0)
	v_mul_f32_e32 v0, v2, v0
	v_mul_f32_e32 v0, v26, v0
	v_fma_f32 v3, |v0|, s1, 1.0
	v_rcp_f32_e32 v3, v3
	v_mul_f32_e32 v5, v0, v0
	v_mul_f32_e32 v5, 0xbf38aa3b, v5
	v_exp_f32_e32 v5, v5
	v_fmamk_f32 v4, v3, 0x3f07dc22, v184
	v_fmaak_f32 v4, v3, v4, 0x3f35f0e3
	v_fmaak_f32 v4, v3, v4, 0xbe11a98e
	v_mul_f32_e32 v1, v2, v1
	v_fmaak_f32 v4, v3, v4, 0x3e027906
	v_mul_f32_e32 v3, v3, v4
	v_mul_f32_e32 v1, v25, v1
	v_mul_f32_e32 v3, v5, v3
	v_fma_f32 v5, |v1|, s1, 1.0
	v_rcp_f32_e32 v5, v5
	v_mul_f32_e32 v4, v0, v3
	v_fma_f32 v3, -v0, v3, v0
	v_cmp_gt_f32_e32 vcc, 0, v0
	v_mul_f32_e32 v2, v83, v27
	v_mov_b32_e32 v150, 0
	v_cndmask_b32_e32 v0, v3, v4, vcc
	v_mul_f32_e32 v119, v2, v0
	v_mul_f32_e32 v2, v1, v1
	v_fmamk_f32 v0, v5, 0x3f07dc22, v184
	v_mul_f32_e32 v2, 0xbf38aa3b, v2
	v_fmaak_f32 v0, v5, v0, 0x3f35f0e3
	v_exp_f32_e32 v2, v2
	v_fmaak_f32 v0, v5, v0, 0xbe11a98e
	v_fmaak_f32 v0, v5, v0, 0x3e027906
	v_mul_f32_e32 v0, v5, v0
	v_mul_f32_e32 v0, v2, v0
	v_mul_f32_e32 v2, v1, v0
	v_fma_f32 v0, -v1, v0, v1
	v_cmp_gt_f32_e32 vcc, 0, v1
	v_mul_f32_e32 v1, v81, v24
	s_mov_b32 s1, s82
	v_cndmask_b32_e32 v0, v0, v2, vcc
	v_mul_f32_e32 v153, v1, v0
	v_mov_b32_e32 v151, v150
	v_mov_b32_e32 v148, v150
	v_mov_b32_e32 v149, v150
	v_mov_b32_e32 v146, v150
	v_mov_b32_e32 v147, v150
	v_mov_b32_e32 v144, v150
	v_mov_b32_e32 v145, v150
	v_mov_b32_e32 v142, v150
	v_mov_b32_e32 v143, v150
	v_mov_b32_e32 v140, v150
	v_mov_b32_e32 v141, v150
	v_mov_b32_e32 v138, v150
	v_mov_b32_e32 v139, v150
	v_mov_b32_e32 v136, v150
	v_mov_b32_e32 v137, v150
	v_mov_b32_e32 v134, v150
	v_mov_b32_e32 v135, v150
	v_mov_b32_e32 v132, v150
	v_mov_b32_e32 v133, v150
	v_mov_b32_e32 v130, v150
	v_mov_b32_e32 v131, v150
	v_mov_b32_e32 v128, v150
	v_mov_b32_e32 v129, v150
	v_mov_b32_e32 v126, v150
	v_mov_b32_e32 v127, v150
	v_mov_b32_e32 v124, v150
	v_mov_b32_e32 v125, v150
	v_mov_b32_e32 v122, v150
	v_mov_b32_e32 v123, v150
	v_mov_b32_e32 v120, v150
	v_mov_b32_e32 v121, v150
.LBB0_1181:
	s_add_i32 s40, s1, -3
	s_sub_i32 s41, s1, 19
	s_add_i32 s26, s1, -11
	s_cmp_lt_u32 s41, 56
	s_cselect_b64 vcc, -1, 0
	v_cndmask_b32_e32 v0, v118, v116, vcc
	s_add_i32 s24, s1, -10
	v_readlane_b32 s4, v0, s26
	s_mulk_i32 s4, 0x600
	s_add_i32 s4, s4, 0x8000000
	s_nop 2
	buffer_load_dwordx4 v[98:101], v152, s[44:47], s4 offen nt
	buffer_load_dwordx2 v[102:103], v117, s[44:47], s4 offen nt
	v_readlane_b32 s4, v0, s24
	s_mulk_i32 s4, 0x600
	s_add_i32 s4, s4, 0x8000000
	s_add_i32 s7, s1, -9
	s_nop 1
	buffer_load_dwordx4 v[92:95], v152, s[44:47], s4 offen nt
	buffer_load_dwordx2 v[96:97], v117, s[44:47], s4 offen nt
	v_readlane_b32 s4, v0, s7
	s_mulk_i32 s4, 0x600
	s_add_i32 s4, s4, 0x8000000
	s_add_i32 s6, s1, -8
	s_nop 1
	buffer_load_dwordx4 v[86:89], v152, s[44:47], s4 offen nt
	buffer_load_dwordx2 v[90:91], v117, s[44:47], s4 offen nt
	v_readlane_b32 s4, v0, s6
	s_mulk_i32 s4, 0x600
	s_add_i32 s4, s4, 0x8000000
	s_nop 2
	buffer_load_dwordx4 v[80:83], v152, s[44:47], s4 offen nt
	buffer_load_dwordx2 v[84:85], v117, s[44:47], s4 offen nt
	s_cmp_lt_u32 s41, 64
	s_cselect_b64 s[4:5], -1, 0
	v_cndmask_b32_e64 v154, v153, v119, s[4:5]
	s_waitcnt vmcnt(22)
	v_cvt_scalef32_pk32_f32_fp6 v[0:31], v[74:79], 1.0
	v_readlane_b32 s4, v154, s41
	s_nop 1
	v_pk_fma_f32 v[74:75], v[0:1], s[4:5], v[150:151] op_sel_hi:[1,0,1]
	v_pk_fma_f32 v[76:77], v[2:3], s[4:5], v[148:149] op_sel_hi:[1,0,1]
	v_pk_fma_f32 v[78:79], v[4:5], s[4:5], v[146:147] op_sel_hi:[1,0,1]
	v_pk_fma_f32 v[144:145], v[6:7], s[4:5], v[144:145] op_sel_hi:[1,0,1]
	v_pk_fma_f32 v[142:143], v[8:9], s[4:5], v[142:143] op_sel_hi:[1,0,1]
	v_pk_fma_f32 v[140:141], v[10:11], s[4:5], v[140:141] op_sel_hi:[1,0,1]
	v_pk_fma_f32 v[138:139], v[12:13], s[4:5], v[138:139] op_sel_hi:[1,0,1]
	v_pk_fma_f32 v[136:137], v[14:15], s[4:5], v[136:137] op_sel_hi:[1,0,1]
	v_pk_fma_f32 v[134:135], v[16:17], s[4:5], v[134:135] op_sel_hi:[1,0,1]
	v_pk_fma_f32 v[132:133], v[18:19], s[4:5], v[132:133] op_sel_hi:[1,0,1]
	v_pk_fma_f32 v[130:131], v[20:21], s[4:5], v[130:131] op_sel_hi:[1,0,1]
	v_pk_fma_f32 v[128:129], v[22:23], s[4:5], v[128:129] op_sel_hi:[1,0,1]
	v_pk_fma_f32 v[126:127], v[24:25], s[4:5], v[126:127] op_sel_hi:[1,0,1]
	v_pk_fma_f32 v[124:125], v[26:27], s[4:5], v[124:125] op_sel_hi:[1,0,1]
	v_pk_fma_f32 v[122:123], v[28:29], s[4:5], v[122:123] op_sel_hi:[1,0,1]
	v_pk_fma_f32 v[120:121], v[30:31], s[4:5], v[120:121] op_sel_hi:[1,0,1]
	s_sub_i32 s4, s1, 18
	v_readlane_b32 s4, v154, s4
	s_waitcnt vmcnt(20)
	v_cvt_scalef32_pk32_f32_fp6 v[0:31], v[68:73], 1.0
	v_pk_fma_f32 v[68:69], v[0:1], s[4:5], v[74:75] op_sel_hi:[1,0,1]
	v_pk_fma_f32 v[70:71], v[2:3], s[4:5], v[76:77] op_sel_hi:[1,0,1]
	v_pk_fma_f32 v[72:73], v[4:5], s[4:5], v[78:79] op_sel_hi:[1,0,1]
	v_pk_fma_f32 v[74:75], v[6:7], s[4:5], v[144:145] op_sel_hi:[1,0,1]
	v_pk_fma_f32 v[76:77], v[8:9], s[4:5], v[142:143] op_sel_hi:[1,0,1]
	v_pk_fma_f32 v[78:79], v[10:11], s[4:5], v[140:141] op_sel_hi:[1,0,1]
	v_pk_fma_f32 v[138:139], v[12:13], s[4:5], v[138:139] op_sel_hi:[1,0,1]
	v_pk_fma_f32 v[136:137], v[14:15], s[4:5], v[136:137] op_sel_hi:[1,0,1]
	v_pk_fma_f32 v[134:135], v[16:17], s[4:5], v[134:135] op_sel_hi:[1,0,1]
	v_pk_fma_f32 v[132:133], v[18:19], s[4:5], v[132:133] op_sel_hi:[1,0,1]
	v_pk_fma_f32 v[130:131], v[20:21], s[4:5], v[130:131] op_sel_hi:[1,0,1]
	v_pk_fma_f32 v[128:129], v[22:23], s[4:5], v[128:129] op_sel_hi:[1,0,1]
	v_pk_fma_f32 v[126:127], v[24:25], s[4:5], v[126:127] op_sel_hi:[1,0,1]
	v_pk_fma_f32 v[124:125], v[26:27], s[4:5], v[124:125] op_sel_hi:[1,0,1]
	v_pk_fma_f32 v[122:123], v[28:29], s[4:5], v[122:123] op_sel_hi:[1,0,1]
	v_pk_fma_f32 v[120:121], v[30:31], s[4:5], v[120:121] op_sel_hi:[1,0,1]
	s_sub_i32 s4, s1, 17
	v_readlane_b32 s4, v154, s4
	s_waitcnt vmcnt(18)
	v_cvt_scalef32_pk32_f32_fp6 v[0:31], v[56:61], 1.0
	v_pk_fma_f32 v[56:57], v[0:1], s[4:5], v[68:69] op_sel_hi:[1,0,1]
	v_pk_fma_f32 v[58:59], v[2:3], s[4:5], v[70:71] op_sel_hi:[1,0,1]
	v_pk_fma_f32 v[60:61], v[4:5], s[4:5], v[72:73] op_sel_hi:[1,0,1]
	v_pk_fma_f32 v[68:69], v[6:7], s[4:5], v[74:75] op_sel_hi:[1,0,1]
	v_pk_fma_f32 v[70:71], v[8:9], s[4:5], v[76:77] op_sel_hi:[1,0,1]
	v_pk_fma_f32 v[72:73], v[10:11], s[4:5], v[78:79] op_sel_hi:[1,0,1]
	v_pk_fma_f32 v[74:75], v[12:13], s[4:5], v[138:139] op_sel_hi:[1,0,1]
	v_pk_fma_f32 v[76:77], v[14:15], s[4:5], v[136:137] op_sel_hi:[1,0,1]
	v_pk_fma_f32 v[78:79], v[16:17], s[4:5], v[134:135] op_sel_hi:[1,0,1]
	v_pk_fma_f32 v[132:133], v[18:19], s[4:5], v[132:133] op_sel_hi:[1,0,1]
	v_pk_fma_f32 v[130:131], v[20:21], s[4:5], v[130:131] op_sel_hi:[1,0,1]
	v_pk_fma_f32 v[128:129], v[22:23], s[4:5], v[128:129] op_sel_hi:[1,0,1]
	v_pk_fma_f32 v[126:127], v[24:25], s[4:5], v[126:127] op_sel_hi:[1,0,1]
	v_pk_fma_f32 v[124:125], v[26:27], s[4:5], v[124:125] op_sel_hi:[1,0,1]
	v_pk_fma_f32 v[122:123], v[28:29], s[4:5], v[122:123] op_sel_hi:[1,0,1]
	v_pk_fma_f32 v[120:121], v[30:31], s[4:5], v[120:121] op_sel_hi:[1,0,1]
	s_add_i32 s4, s1, -16
	v_readlane_b32 s4, v154, s4
	s_waitcnt vmcnt(16)
	v_cvt_scalef32_pk32_f32_fp6 v[0:31], v[44:49], 1.0
	v_pk_fma_f32 v[134:135], v[0:1], s[4:5], v[56:57] op_sel_hi:[1,0,1]
	v_pk_fma_f32 v[136:137], v[2:3], s[4:5], v[58:59] op_sel_hi:[1,0,1]
	v_pk_fma_f32 v[138:139], v[4:5], s[4:5], v[60:61] op_sel_hi:[1,0,1]
	v_pk_fma_f32 v[140:141], v[6:7], s[4:5], v[68:69] op_sel_hi:[1,0,1]
	v_pk_fma_f32 v[142:143], v[8:9], s[4:5], v[70:71] op_sel_hi:[1,0,1]
	v_pk_fma_f32 v[144:145], v[10:11], s[4:5], v[72:73] op_sel_hi:[1,0,1]
	v_pk_fma_f32 v[146:147], v[12:13], s[4:5], v[74:75] op_sel_hi:[1,0,1]
	v_pk_fma_f32 v[148:149], v[14:15], s[4:5], v[76:77] op_sel_hi:[1,0,1]
	v_pk_fma_f32 v[150:151], v[16:17], s[4:5], v[78:79] op_sel_hi:[1,0,1]
	v_pk_fma_f32 v[132:133], v[18:19], s[4:5], v[132:133] op_sel_hi:[1,0,1]
	v_pk_fma_f32 v[130:131], v[20:21], s[4:5], v[130:131] op_sel_hi:[1,0,1]
	v_pk_fma_f32 v[128:129], v[22:23], s[4:5], v[128:129] op_sel_hi:[1,0,1]
	v_pk_fma_f32 v[126:127], v[24:25], s[4:5], v[126:127] op_sel_hi:[1,0,1]
	v_pk_fma_f32 v[124:125], v[26:27], s[4:5], v[124:125] op_sel_hi:[1,0,1]
	v_pk_fma_f32 v[122:123], v[28:29], s[4:5], v[122:123] op_sel_hi:[1,0,1]
	v_pk_fma_f32 v[120:121], v[30:31], s[4:5], v[120:121] op_sel_hi:[1,0,1]
	s_add_i32 s83, s1, -7
	s_cmp_lt_u32 s41, 52
	s_cselect_b64 s[4:5], -1, 0
	v_cndmask_b32_e64 v0, v118, v116, s[4:5]
	s_nop 0
	v_readlane_b32 s4, v0, s83
	s_mulk_i32 s4, 0x600
	s_add_i32 s4, s4, 0x8000000
	s_nop 2
	buffer_load_dwordx4 v[74:77], v152, s[44:47], s4 offen nt
	buffer_load_dwordx2 v[78:79], v117, s[44:47], s4 offen nt
	s_add_i32 s4, s1, -6
	v_readlane_b32 s4, v0, s4
	s_mulk_i32 s4, 0x600
	s_add_i32 s4, s4, 0x8000000
	s_nop 2
	buffer_load_dwordx4 v[68:71], v152, s[44:47], s4 offen nt
	buffer_load_dwordx2 v[72:73], v117, s[44:47], s4 offen nt
	s_add_i32 s4, s1, -5
	v_readlane_b32 s4, v0, s4
	s_mulk_i32 s4, 0x600
	s_add_i32 s4, s4, 0x8000000
	s_nop 2
	buffer_load_dwordx4 v[56:59], v152, s[44:47], s4 offen nt
	buffer_load_dwordx2 v[60:61], v117, s[44:47], s4 offen nt
	s_add_i32 s4, s1, -4
	v_readlane_b32 s4, v0, s4
	s_mulk_i32 s4, 0x600
	s_add_i32 s4, s4, 0x8000000
	s_nop 2
	buffer_load_dwordx4 v[44:47], v152, s[44:47], s4 offen nt
	buffer_load_dwordx2 v[48:49], v117, s[44:47], s4 offen nt
	s_add_i32 s83, s1, -15
	s_cmp_lt_u32 s41, 60
	s_cselect_b64 s[4:5], -1, 0
	v_cndmask_b32_e64 v154, v153, v119, s[4:5]
	s_waitcnt vmcnt(22)
	v_cvt_scalef32_pk32_f32_fp6 v[0:31], v[62:67], 1.0
	v_readlane_b32 s4, v154, s83
	s_nop 1
	v_pk_fma_f32 v[62:63], v[0:1], s[4:5], v[134:135] op_sel_hi:[1,0,1]
	v_pk_fma_f32 v[64:65], v[2:3], s[4:5], v[136:137] op_sel_hi:[1,0,1]
	v_pk_fma_f32 v[66:67], v[4:5], s[4:5], v[138:139] op_sel_hi:[1,0,1]
	v_pk_fma_f32 v[134:135], v[6:7], s[4:5], v[140:141] op_sel_hi:[1,0,1]
	v_pk_fma_f32 v[136:137], v[8:9], s[4:5], v[142:143] op_sel_hi:[1,0,1]
	v_pk_fma_f32 v[138:139], v[10:11], s[4:5], v[144:145] op_sel_hi:[1,0,1]
	v_pk_fma_f32 v[140:141], v[12:13], s[4:5], v[146:147] op_sel_hi:[1,0,1]
	v_pk_fma_f32 v[142:143], v[14:15], s[4:5], v[148:149] op_sel_hi:[1,0,1]
	v_pk_fma_f32 v[144:145], v[16:17], s[4:5], v[150:151] op_sel_hi:[1,0,1]
	v_pk_fma_f32 v[132:133], v[18:19], s[4:5], v[132:133] op_sel_hi:[1,0,1]
	v_pk_fma_f32 v[130:131], v[20:21], s[4:5], v[130:131] op_sel_hi:[1,0,1]
	v_pk_fma_f32 v[128:129], v[22:23], s[4:5], v[128:129] op_sel_hi:[1,0,1]
	v_pk_fma_f32 v[126:127], v[24:25], s[4:5], v[126:127] op_sel_hi:[1,0,1]
	v_pk_fma_f32 v[124:125], v[26:27], s[4:5], v[124:125] op_sel_hi:[1,0,1]
	v_pk_fma_f32 v[122:123], v[28:29], s[4:5], v[122:123] op_sel_hi:[1,0,1]
	v_pk_fma_f32 v[120:121], v[30:31], s[4:5], v[120:121] op_sel_hi:[1,0,1]
	s_add_i32 s4, s1, -14
	v_readlane_b32 s4, v154, s4
	s_waitcnt vmcnt(20)
	v_cvt_scalef32_pk32_f32_fp6 v[0:31], v[50:55], 1.0
	v_pk_fma_f32 v[50:51], v[0:1], s[4:5], v[62:63] op_sel_hi:[1,0,1]
	v_pk_fma_f32 v[52:53], v[2:3], s[4:5], v[64:65] op_sel_hi:[1,0,1]
	v_pk_fma_f32 v[54:55], v[4:5], s[4:5], v[66:67] op_sel_hi:[1,0,1]
	v_pk_fma_f32 v[62:63], v[6:7], s[4:5], v[134:135] op_sel_hi:[1,0,1]
	v_pk_fma_f32 v[64:65], v[8:9], s[4:5], v[136:137] op_sel_hi:[1,0,1]
	v_pk_fma_f32 v[66:67], v[10:11], s[4:5], v[138:139] op_sel_hi:[1,0,1]
	v_pk_fma_f32 v[134:135], v[12:13], s[4:5], v[140:141] op_sel_hi:[1,0,1]
	v_pk_fma_f32 v[136:137], v[14:15], s[4:5], v[142:143] op_sel_hi:[1,0,1]
	v_pk_fma_f32 v[138:139], v[16:17], s[4:5], v[144:145] op_sel_hi:[1,0,1]
	v_pk_fma_f32 v[132:133], v[18:19], s[4:5], v[132:133] op_sel_hi:[1,0,1]
	v_pk_fma_f32 v[130:131], v[20:21], s[4:5], v[130:131] op_sel_hi:[1,0,1]
	v_pk_fma_f32 v[128:129], v[22:23], s[4:5], v[128:129] op_sel_hi:[1,0,1]
	v_pk_fma_f32 v[126:127], v[24:25], s[4:5], v[126:127] op_sel_hi:[1,0,1]
	v_pk_fma_f32 v[124:125], v[26:27], s[4:5], v[124:125] op_sel_hi:[1,0,1]
	v_pk_fma_f32 v[122:123], v[28:29], s[4:5], v[122:123] op_sel_hi:[1,0,1]
	v_pk_fma_f32 v[120:121], v[30:31], s[4:5], v[120:121] op_sel_hi:[1,0,1]
	s_add_i32 s4, s1, -13
	v_readlane_b32 s4, v154, s4
	s_waitcnt vmcnt(18)
	v_cvt_scalef32_pk32_f32_fp6 v[0:31], v[38:43], 1.0
	v_pk_fma_f32 v[38:39], v[0:1], s[4:5], v[50:51] op_sel_hi:[1,0,1]
	v_pk_fma_f32 v[40:41], v[2:3], s[4:5], v[52:53] op_sel_hi:[1,0,1]
	v_pk_fma_f32 v[42:43], v[4:5], s[4:5], v[54:55] op_sel_hi:[1,0,1]
	v_pk_fma_f32 v[50:51], v[6:7], s[4:5], v[62:63] op_sel_hi:[1,0,1]
	v_pk_fma_f32 v[52:53], v[8:9], s[4:5], v[64:65] op_sel_hi:[1,0,1]
	v_pk_fma_f32 v[54:55], v[10:11], s[4:5], v[66:67] op_sel_hi:[1,0,1]
	v_pk_fma_f32 v[62:63], v[12:13], s[4:5], v[134:135] op_sel_hi:[1,0,1]
	v_pk_fma_f32 v[64:65], v[14:15], s[4:5], v[136:137] op_sel_hi:[1,0,1]
	v_pk_fma_f32 v[66:67], v[16:17], s[4:5], v[138:139] op_sel_hi:[1,0,1]
	v_pk_fma_f32 v[132:133], v[18:19], s[4:5], v[132:133] op_sel_hi:[1,0,1]
	v_pk_fma_f32 v[130:131], v[20:21], s[4:5], v[130:131] op_sel_hi:[1,0,1]
	v_pk_fma_f32 v[128:129], v[22:23], s[4:5], v[128:129] op_sel_hi:[1,0,1]
	v_pk_fma_f32 v[126:127], v[24:25], s[4:5], v[126:127] op_sel_hi:[1,0,1]
	v_pk_fma_f32 v[124:125], v[26:27], s[4:5], v[124:125] op_sel_hi:[1,0,1]
	v_pk_fma_f32 v[122:123], v[28:29], s[4:5], v[122:123] op_sel_hi:[1,0,1]
	v_pk_fma_f32 v[120:121], v[30:31], s[4:5], v[120:121] op_sel_hi:[1,0,1]
	s_add_i32 s4, s1, -12
	v_readlane_b32 s4, v154, s4
	s_waitcnt vmcnt(16)
	v_cvt_scalef32_pk32_f32_fp6 v[0:31], v[32:37], 1.0
	v_pk_fma_f32 v[134:135], v[0:1], s[4:5], v[38:39] op_sel_hi:[1,0,1]
	v_pk_fma_f32 v[136:137], v[2:3], s[4:5], v[40:41] op_sel_hi:[1,0,1]
	v_pk_fma_f32 v[138:139], v[4:5], s[4:5], v[42:43] op_sel_hi:[1,0,1]
	v_pk_fma_f32 v[140:141], v[6:7], s[4:5], v[50:51] op_sel_hi:[1,0,1]
	v_pk_fma_f32 v[142:143], v[8:9], s[4:5], v[52:53] op_sel_hi:[1,0,1]
	v_pk_fma_f32 v[144:145], v[10:11], s[4:5], v[54:55] op_sel_hi:[1,0,1]
	v_pk_fma_f32 v[146:147], v[12:13], s[4:5], v[62:63] op_sel_hi:[1,0,1]
	v_pk_fma_f32 v[148:149], v[14:15], s[4:5], v[64:65] op_sel_hi:[1,0,1]
	v_pk_fma_f32 v[150:151], v[16:17], s[4:5], v[66:67] op_sel_hi:[1,0,1]
	v_pk_fma_f32 v[132:133], v[18:19], s[4:5], v[132:133] op_sel_hi:[1,0,1]
	v_pk_fma_f32 v[130:131], v[20:21], s[4:5], v[130:131] op_sel_hi:[1,0,1]
	v_pk_fma_f32 v[128:129], v[22:23], s[4:5], v[128:129] op_sel_hi:[1,0,1]
	v_pk_fma_f32 v[126:127], v[24:25], s[4:5], v[126:127] op_sel_hi:[1,0,1]
	v_pk_fma_f32 v[124:125], v[26:27], s[4:5], v[124:125] op_sel_hi:[1,0,1]
	v_pk_fma_f32 v[122:123], v[28:29], s[4:5], v[122:123] op_sel_hi:[1,0,1]
	v_pk_fma_f32 v[120:121], v[30:31], s[4:5], v[120:121] op_sel_hi:[1,0,1]
	s_cmp_lt_u32 s41, 48
	s_cselect_b64 s[4:5], -1, 0
	v_cndmask_b32_e64 v0, v118, v116, s[4:5]
	s_nop 0
	v_readlane_b32 s4, v0, s40
	s_mulk_i32 s4, 0x600
	s_add_i32 s4, s4, 0x8000000
	s_nop 2
	buffer_load_dwordx4 v[62:65], v152, s[44:47], s4 offen nt
	buffer_load_dwordx2 v[66:67], v117, s[44:47], s4 offen nt
	s_add_i32 s4, s1, -2
	v_readlane_b32 s4, v0, s4
	s_mulk_i32 s4, 0x600
	s_add_i32 s4, s4, 0x8000000
	s_nop 2
	buffer_load_dwordx4 v[50:53], v152, s[44:47], s4 offen nt
	buffer_load_dwordx2 v[54:55], v117, s[44:47], s4 offen nt
	s_add_i32 s4, s1, -1
	v_readlane_b32 s4, v0, s4
	s_mulk_i32 s4, 0x600
	s_add_i32 s4, s4, 0x8000000
	s_nop 2
	buffer_load_dwordx4 v[38:41], v152, s[44:47], s4 offen nt
	buffer_load_dwordx2 v[42:43], v117, s[44:47], s4 offen nt
	v_readlane_b32 s4, v0, s1
	s_mulk_i32 s4, 0x600
	s_add_i32 s4, s4, 0x8000000
	s_nop 2
	buffer_load_dwordx4 v[32:35], v152, s[44:47], s4 offen nt
	buffer_load_dwordx2 v[36:37], v117, s[44:47], s4 offen nt
	v_cndmask_b32_e32 v154, v153, v119, vcc
	s_waitcnt vmcnt(22)
	v_cvt_scalef32_pk32_f32_fp6 v[0:31], v[98:103], 1.0
	v_readlane_b32 s4, v154, s26
	s_nop 1
	v_pk_fma_f32 v[98:99], v[0:1], s[4:5], v[134:135] op_sel_hi:[1,0,1]
	v_pk_fma_f32 v[100:101], v[2:3], s[4:5], v[136:137] op_sel_hi:[1,0,1]
	v_pk_fma_f32 v[102:103], v[4:5], s[4:5], v[138:139] op_sel_hi:[1,0,1]
	v_pk_fma_f32 v[134:135], v[6:7], s[4:5], v[140:141] op_sel_hi:[1,0,1]
	v_pk_fma_f32 v[136:137], v[8:9], s[4:5], v[142:143] op_sel_hi:[1,0,1]
	v_pk_fma_f32 v[138:139], v[10:11], s[4:5], v[144:145] op_sel_hi:[1,0,1]
	v_pk_fma_f32 v[140:141], v[12:13], s[4:5], v[146:147] op_sel_hi:[1,0,1]
	v_pk_fma_f32 v[142:143], v[14:15], s[4:5], v[148:149] op_sel_hi:[1,0,1]
	v_pk_fma_f32 v[144:145], v[16:17], s[4:5], v[150:151] op_sel_hi:[1,0,1]
	v_pk_fma_f32 v[132:133], v[18:19], s[4:5], v[132:133] op_sel_hi:[1,0,1]
	v_pk_fma_f32 v[130:131], v[20:21], s[4:5], v[130:131] op_sel_hi:[1,0,1]
	v_pk_fma_f32 v[128:129], v[22:23], s[4:5], v[128:129] op_sel_hi:[1,0,1]
	v_pk_fma_f32 v[126:127], v[24:25], s[4:5], v[126:127] op_sel_hi:[1,0,1]
	v_pk_fma_f32 v[124:125], v[26:27], s[4:5], v[124:125] op_sel_hi:[1,0,1]
	v_pk_fma_f32 v[122:123], v[28:29], s[4:5], v[122:123] op_sel_hi:[1,0,1]
	v_pk_fma_f32 v[120:121], v[30:31], s[4:5], v[120:121] op_sel_hi:[1,0,1]
	v_readlane_b32 s4, v154, s24
	s_waitcnt vmcnt(20)
	v_cvt_scalef32_pk32_f32_fp6 v[0:31], v[92:97], 1.0
	v_pk_fma_f32 v[92:93], v[0:1], s[4:5], v[98:99] op_sel_hi:[1,0,1]
	v_pk_fma_f32 v[94:95], v[2:3], s[4:5], v[100:101] op_sel_hi:[1,0,1]
	v_pk_fma_f32 v[96:97], v[4:5], s[4:5], v[102:103] op_sel_hi:[1,0,1]
	v_pk_fma_f32 v[98:99], v[6:7], s[4:5], v[134:135] op_sel_hi:[1,0,1]
	v_pk_fma_f32 v[100:101], v[8:9], s[4:5], v[136:137] op_sel_hi:[1,0,1]
	v_pk_fma_f32 v[102:103], v[10:11], s[4:5], v[138:139] op_sel_hi:[1,0,1]
	v_pk_fma_f32 v[134:135], v[12:13], s[4:5], v[140:141] op_sel_hi:[1,0,1]
	v_pk_fma_f32 v[136:137], v[14:15], s[4:5], v[142:143] op_sel_hi:[1,0,1]
	v_pk_fma_f32 v[138:139], v[16:17], s[4:5], v[144:145] op_sel_hi:[1,0,1]
	v_pk_fma_f32 v[132:133], v[18:19], s[4:5], v[132:133] op_sel_hi:[1,0,1]
	v_pk_fma_f32 v[130:131], v[20:21], s[4:5], v[130:131] op_sel_hi:[1,0,1]
	v_pk_fma_f32 v[128:129], v[22:23], s[4:5], v[128:129] op_sel_hi:[1,0,1]
	v_pk_fma_f32 v[126:127], v[24:25], s[4:5], v[126:127] op_sel_hi:[1,0,1]
	v_pk_fma_f32 v[124:125], v[26:27], s[4:5], v[124:125] op_sel_hi:[1,0,1]
	v_pk_fma_f32 v[122:123], v[28:29], s[4:5], v[122:123] op_sel_hi:[1,0,1]
	v_pk_fma_f32 v[120:121], v[30:31], s[4:5], v[120:121] op_sel_hi:[1,0,1]
	v_readlane_b32 s4, v154, s7
	s_waitcnt vmcnt(18)
	v_cvt_scalef32_pk32_f32_fp6 v[0:31], v[86:91], 1.0
	v_pk_fma_f32 v[86:87], v[0:1], s[4:5], v[92:93] op_sel_hi:[1,0,1]
	v_pk_fma_f32 v[88:89], v[2:3], s[4:5], v[94:95] op_sel_hi:[1,0,1]
	v_pk_fma_f32 v[90:91], v[4:5], s[4:5], v[96:97] op_sel_hi:[1,0,1]
	v_pk_fma_f32 v[92:93], v[6:7], s[4:5], v[98:99] op_sel_hi:[1,0,1]
	v_pk_fma_f32 v[94:95], v[8:9], s[4:5], v[100:101] op_sel_hi:[1,0,1]
	v_pk_fma_f32 v[96:97], v[10:11], s[4:5], v[102:103] op_sel_hi:[1,0,1]
	v_pk_fma_f32 v[98:99], v[12:13], s[4:5], v[134:135] op_sel_hi:[1,0,1]
	v_pk_fma_f32 v[100:101], v[14:15], s[4:5], v[136:137] op_sel_hi:[1,0,1]
	v_pk_fma_f32 v[102:103], v[16:17], s[4:5], v[138:139] op_sel_hi:[1,0,1]
	v_pk_fma_f32 v[132:133], v[18:19], s[4:5], v[132:133] op_sel_hi:[1,0,1]
	v_pk_fma_f32 v[130:131], v[20:21], s[4:5], v[130:131] op_sel_hi:[1,0,1]
	v_pk_fma_f32 v[128:129], v[22:23], s[4:5], v[128:129] op_sel_hi:[1,0,1]
	v_pk_fma_f32 v[126:127], v[24:25], s[4:5], v[126:127] op_sel_hi:[1,0,1]
	v_pk_fma_f32 v[124:125], v[26:27], s[4:5], v[124:125] op_sel_hi:[1,0,1]
	v_pk_fma_f32 v[122:123], v[28:29], s[4:5], v[122:123] op_sel_hi:[1,0,1]
	v_pk_fma_f32 v[120:121], v[30:31], s[4:5], v[120:121] op_sel_hi:[1,0,1]
	v_readlane_b32 s4, v154, s6
	s_waitcnt vmcnt(16)
	v_cvt_scalef32_pk32_f32_fp6 v[0:31], v[80:85], 1.0
	v_pk_fma_f32 v[150:151], v[0:1], s[4:5], v[86:87] op_sel_hi:[1,0,1]
	v_pk_fma_f32 v[148:149], v[2:3], s[4:5], v[88:89] op_sel_hi:[1,0,1]
	v_pk_fma_f32 v[146:147], v[4:5], s[4:5], v[90:91] op_sel_hi:[1,0,1]
	v_pk_fma_f32 v[144:145], v[6:7], s[4:5], v[92:93] op_sel_hi:[1,0,1]
	v_pk_fma_f32 v[142:143], v[8:9], s[4:5], v[94:95] op_sel_hi:[1,0,1]
	v_pk_fma_f32 v[140:141], v[10:11], s[4:5], v[96:97] op_sel_hi:[1,0,1]
	v_pk_fma_f32 v[138:139], v[12:13], s[4:5], v[98:99] op_sel_hi:[1,0,1]
	v_pk_fma_f32 v[136:137], v[14:15], s[4:5], v[100:101] op_sel_hi:[1,0,1]
	v_pk_fma_f32 v[134:135], v[16:17], s[4:5], v[102:103] op_sel_hi:[1,0,1]
	v_pk_fma_f32 v[132:133], v[18:19], s[4:5], v[132:133] op_sel_hi:[1,0,1]
	v_pk_fma_f32 v[130:131], v[20:21], s[4:5], v[130:131] op_sel_hi:[1,0,1]
	v_pk_fma_f32 v[128:129], v[22:23], s[4:5], v[128:129] op_sel_hi:[1,0,1]
	v_pk_fma_f32 v[126:127], v[24:25], s[4:5], v[126:127] op_sel_hi:[1,0,1]
	v_pk_fma_f32 v[124:125], v[26:27], s[4:5], v[124:125] op_sel_hi:[1,0,1]
	v_pk_fma_f32 v[122:123], v[28:29], s[4:5], v[122:123] op_sel_hi:[1,0,1]
	v_pk_fma_f32 v[120:121], v[30:31], s[4:5], v[120:121] op_sel_hi:[1,0,1]
	s_add_i32 s4, s1, 12
	s_add_i32 s1, s1, 9
	s_cmp_lt_u32 s1, s52
	s_mov_b32 s1, s4
	s_cbranch_scc1 .LBB0_1181
	v_cndmask_b32_e64 v118, v153, v119, s[2:3]
	s_waitcnt vmcnt(14)
	v_cvt_scalef32_pk32_f32_fp6 v[0:31], v[74:79], 1.0
	v_readlane_b32 s4, v118, s60
	s_nop 1
	v_pk_fma_f32 v[74:75], v[0:1], s[4:5], v[150:151] op_sel_hi:[1,0,1]
	v_pk_fma_f32 v[76:77], v[2:3], s[4:5], v[148:149] op_sel_hi:[1,0,1]
	v_pk_fma_f32 v[78:79], v[4:5], s[4:5], v[146:147] op_sel_hi:[1,0,1]
	v_pk_fma_f32 v[80:81], v[6:7], s[4:5], v[144:145] op_sel_hi:[1,0,1]
	v_pk_fma_f32 v[82:83], v[8:9], s[4:5], v[142:143] op_sel_hi:[1,0,1]
	v_pk_fma_f32 v[84:85], v[10:11], s[4:5], v[140:141] op_sel_hi:[1,0,1]
	v_pk_fma_f32 v[86:87], v[12:13], s[4:5], v[138:139] op_sel_hi:[1,0,1]
	v_pk_fma_f32 v[88:89], v[14:15], s[4:5], v[136:137] op_sel_hi:[1,0,1]
	v_pk_fma_f32 v[90:91], v[16:17], s[4:5], v[134:135] op_sel_hi:[1,0,1]
	v_pk_fma_f32 v[92:93], v[18:19], s[4:5], v[132:133] op_sel_hi:[1,0,1]
	v_pk_fma_f32 v[94:95], v[20:21], s[4:5], v[130:131] op_sel_hi:[1,0,1]
	v_pk_fma_f32 v[96:97], v[22:23], s[4:5], v[128:129] op_sel_hi:[1,0,1]
	v_pk_fma_f32 v[98:99], v[24:25], s[4:5], v[126:127] op_sel_hi:[1,0,1]
	v_pk_fma_f32 v[100:101], v[26:27], s[4:5], v[124:125] op_sel_hi:[1,0,1]
	v_pk_fma_f32 v[102:103], v[28:29], s[4:5], v[122:123] op_sel_hi:[1,0,1]
	v_pk_fma_f32 v[116:117], v[30:31], s[4:5], v[120:121] op_sel_hi:[1,0,1]
	v_readlane_b32 s4, v118, s75
	s_waitcnt vmcnt(12)
	v_cvt_scalef32_pk32_f32_fp6 v[0:31], v[68:73], 1.0
	v_pk_fma_f32 v[68:69], v[0:1], s[4:5], v[74:75] op_sel_hi:[1,0,1]
	v_pk_fma_f32 v[70:71], v[2:3], s[4:5], v[76:77] op_sel_hi:[1,0,1]
	v_pk_fma_f32 v[72:73], v[4:5], s[4:5], v[78:79] op_sel_hi:[1,0,1]
	v_pk_fma_f32 v[74:75], v[6:7], s[4:5], v[80:81] op_sel_hi:[1,0,1]
	v_pk_fma_f32 v[76:77], v[8:9], s[4:5], v[82:83] op_sel_hi:[1,0,1]
	v_pk_fma_f32 v[78:79], v[10:11], s[4:5], v[84:85] op_sel_hi:[1,0,1]
	v_pk_fma_f32 v[80:81], v[12:13], s[4:5], v[86:87] op_sel_hi:[1,0,1]
	v_pk_fma_f32 v[82:83], v[14:15], s[4:5], v[88:89] op_sel_hi:[1,0,1]
	v_pk_fma_f32 v[84:85], v[16:17], s[4:5], v[90:91] op_sel_hi:[1,0,1]
	v_pk_fma_f32 v[86:87], v[18:19], s[4:5], v[92:93] op_sel_hi:[1,0,1]
	v_pk_fma_f32 v[88:89], v[20:21], s[4:5], v[94:95] op_sel_hi:[1,0,1]
	v_pk_fma_f32 v[90:91], v[22:23], s[4:5], v[96:97] op_sel_hi:[1,0,1]
	v_pk_fma_f32 v[92:93], v[24:25], s[4:5], v[98:99] op_sel_hi:[1,0,1]
	v_pk_fma_f32 v[94:95], v[26:27], s[4:5], v[100:101] op_sel_hi:[1,0,1]
	v_pk_fma_f32 v[96:97], v[28:29], s[4:5], v[102:103] op_sel_hi:[1,0,1]
	v_pk_fma_f32 v[98:99], v[30:31], s[4:5], v[116:117] op_sel_hi:[1,0,1]
	v_readlane_b32 s4, v118, s76
	s_waitcnt vmcnt(10)
	v_cvt_scalef32_pk32_f32_fp6 v[0:31], v[56:61], 1.0
	v_pk_fma_f32 v[56:57], v[0:1], s[4:5], v[68:69] op_sel_hi:[1,0,1]
	v_pk_fma_f32 v[58:59], v[2:3], s[4:5], v[70:71] op_sel_hi:[1,0,1]
	v_pk_fma_f32 v[60:61], v[4:5], s[4:5], v[72:73] op_sel_hi:[1,0,1]
	v_pk_fma_f32 v[68:69], v[6:7], s[4:5], v[74:75] op_sel_hi:[1,0,1]
	v_pk_fma_f32 v[70:71], v[8:9], s[4:5], v[76:77] op_sel_hi:[1,0,1]
	v_pk_fma_f32 v[72:73], v[10:11], s[4:5], v[78:79] op_sel_hi:[1,0,1]
	v_pk_fma_f32 v[74:75], v[12:13], s[4:5], v[80:81] op_sel_hi:[1,0,1]
	v_pk_fma_f32 v[76:77], v[14:15], s[4:5], v[82:83] op_sel_hi:[1,0,1]
	v_pk_fma_f32 v[78:79], v[16:17], s[4:5], v[84:85] op_sel_hi:[1,0,1]
	v_pk_fma_f32 v[80:81], v[18:19], s[4:5], v[86:87] op_sel_hi:[1,0,1]
	v_pk_fma_f32 v[82:83], v[20:21], s[4:5], v[88:89] op_sel_hi:[1,0,1]
	v_pk_fma_f32 v[84:85], v[22:23], s[4:5], v[90:91] op_sel_hi:[1,0,1]
	v_pk_fma_f32 v[86:87], v[24:25], s[4:5], v[92:93] op_sel_hi:[1,0,1]
	v_pk_fma_f32 v[88:89], v[26:27], s[4:5], v[94:95] op_sel_hi:[1,0,1]
	v_pk_fma_f32 v[90:91], v[28:29], s[4:5], v[96:97] op_sel_hi:[1,0,1]
	v_pk_fma_f32 v[92:93], v[30:31], s[4:5], v[98:99] op_sel_hi:[1,0,1]
	v_readlane_b32 s4, v118, s77
	s_waitcnt vmcnt(8)
	v_cvt_scalef32_pk32_f32_fp6 v[0:31], v[44:49], 1.0
	v_pk_fma_f32 v[44:45], v[0:1], s[4:5], v[56:57] op_sel_hi:[1,0,1]
	v_pk_fma_f32 v[48:49], v[4:5], s[4:5], v[60:61] op_sel_hi:[1,0,1]
	v_pk_fma_f32 v[56:57], v[6:7], s[4:5], v[68:69] op_sel_hi:[1,0,1]
	v_pk_fma_f32 v[60:61], v[10:11], s[4:5], v[72:73] op_sel_hi:[1,0,1]
	v_pk_fma_f32 v[68:69], v[12:13], s[4:5], v[74:75] op_sel_hi:[1,0,1]
	v_pk_fma_f32 v[72:73], v[16:17], s[4:5], v[78:79] op_sel_hi:[1,0,1]
	v_pk_fma_f32 v[74:75], v[18:19], s[4:5], v[80:81] op_sel_hi:[1,0,1]
	v_pk_fma_f32 v[78:79], v[22:23], s[4:5], v[84:85] op_sel_hi:[1,0,1]
	v_pk_fma_f32 v[80:81], v[24:25], s[4:5], v[86:87] op_sel_hi:[1,0,1]
	v_pk_fma_f32 v[84:85], v[28:29], s[4:5], v[90:91] op_sel_hi:[1,0,1]
	v_pk_fma_f32 v[46:47], v[2:3], s[4:5], v[58:59] op_sel_hi:[1,0,1]
	v_pk_fma_f32 v[58:59], v[8:9], s[4:5], v[70:71] op_sel_hi:[1,0,1]
	v_pk_fma_f32 v[70:71], v[14:15], s[4:5], v[76:77] op_sel_hi:[1,0,1]
	v_pk_fma_f32 v[76:77], v[20:21], s[4:5], v[82:83] op_sel_hi:[1,0,1]
	v_pk_fma_f32 v[82:83], v[26:27], s[4:5], v[88:89] op_sel_hi:[1,0,1]
	v_pk_fma_f32 v[86:87], v[30:31], s[4:5], v[92:93] op_sel_hi:[1,0,1]
	v_readlane_b32 s4, v118, s64
	s_waitcnt vmcnt(6)
	v_cvt_scalef32_pk32_f32_fp6 v[0:31], v[62:67], 1.0
	v_pk_fma_f32 v[44:45], v[0:1], s[4:5], v[44:45] op_sel_hi:[1,0,1]
	v_pk_fma_f32 v[46:47], v[2:3], s[4:5], v[46:47] op_sel_hi:[1,0,1]
	v_pk_fma_f32 v[48:49], v[4:5], s[4:5], v[48:49] op_sel_hi:[1,0,1]
	v_pk_fma_f32 v[56:57], v[6:7], s[4:5], v[56:57] op_sel_hi:[1,0,1]
	v_pk_fma_f32 v[58:59], v[8:9], s[4:5], v[58:59] op_sel_hi:[1,0,1]
	v_pk_fma_f32 v[60:61], v[10:11], s[4:5], v[60:61] op_sel_hi:[1,0,1]
	v_pk_fma_f32 v[62:63], v[12:13], s[4:5], v[68:69] op_sel_hi:[1,0,1]
	v_pk_fma_f32 v[64:65], v[14:15], s[4:5], v[70:71] op_sel_hi:[1,0,1]
	v_pk_fma_f32 v[66:67], v[16:17], s[4:5], v[72:73] op_sel_hi:[1,0,1]
	v_pk_fma_f32 v[68:69], v[18:19], s[4:5], v[74:75] op_sel_hi:[1,0,1]
	v_pk_fma_f32 v[70:71], v[20:21], s[4:5], v[76:77] op_sel_hi:[1,0,1]
	v_pk_fma_f32 v[72:73], v[22:23], s[4:5], v[78:79] op_sel_hi:[1,0,1]
	v_pk_fma_f32 v[74:75], v[24:25], s[4:5], v[80:81] op_sel_hi:[1,0,1]
	v_pk_fma_f32 v[76:77], v[26:27], s[4:5], v[82:83] op_sel_hi:[1,0,1]
	v_pk_fma_f32 v[78:79], v[28:29], s[4:5], v[84:85] op_sel_hi:[1,0,1]
	v_pk_fma_f32 v[80:81], v[30:31], s[4:5], v[86:87] op_sel_hi:[1,0,1]
	v_readlane_b32 s4, v118, s78
	s_waitcnt vmcnt(4)
	v_cvt_scalef32_pk32_f32_fp6 v[0:31], v[50:55], 1.0
	v_pk_fma_f32 v[44:45], v[0:1], s[4:5], v[44:45] op_sel_hi:[1,0,1]
	v_pk_fma_f32 v[46:47], v[2:3], s[4:5], v[46:47] op_sel_hi:[1,0,1]
	v_pk_fma_f32 v[48:49], v[4:5], s[4:5], v[48:49] op_sel_hi:[1,0,1]
	v_pk_fma_f32 v[50:51], v[6:7], s[4:5], v[56:57] op_sel_hi:[1,0,1]
	v_pk_fma_f32 v[52:53], v[8:9], s[4:5], v[58:59] op_sel_hi:[1,0,1]
	v_pk_fma_f32 v[54:55], v[10:11], s[4:5], v[60:61] op_sel_hi:[1,0,1]
	v_pk_fma_f32 v[56:57], v[12:13], s[4:5], v[62:63] op_sel_hi:[1,0,1]
	v_pk_fma_f32 v[58:59], v[14:15], s[4:5], v[64:65] op_sel_hi:[1,0,1]
	v_pk_fma_f32 v[60:61], v[16:17], s[4:5], v[66:67] op_sel_hi:[1,0,1]
	v_pk_fma_f32 v[62:63], v[18:19], s[4:5], v[68:69] op_sel_hi:[1,0,1]
	v_pk_fma_f32 v[64:65], v[20:21], s[4:5], v[70:71] op_sel_hi:[1,0,1]
	v_pk_fma_f32 v[66:67], v[22:23], s[4:5], v[72:73] op_sel_hi:[1,0,1]
	v_pk_fma_f32 v[68:69], v[24:25], s[4:5], v[74:75] op_sel_hi:[1,0,1]
	v_pk_fma_f32 v[70:71], v[26:27], s[4:5], v[76:77] op_sel_hi:[1,0,1]
	v_pk_fma_f32 v[72:73], v[28:29], s[4:5], v[78:79] op_sel_hi:[1,0,1]
	v_pk_fma_f32 v[74:75], v[30:31], s[4:5], v[80:81] op_sel_hi:[1,0,1]
	v_readlane_b32 s4, v118, s79
	s_waitcnt vmcnt(2)
	v_cvt_scalef32_pk32_f32_fp6 v[0:31], v[38:43], 1.0
	v_pk_fma_f32 v[38:39], v[0:1], s[4:5], v[44:45] op_sel_hi:[1,0,1]
	v_pk_fma_f32 v[40:41], v[2:3], s[4:5], v[46:47] op_sel_hi:[1,0,1]
	v_pk_fma_f32 v[42:43], v[4:5], s[4:5], v[48:49] op_sel_hi:[1,0,1]
	v_pk_fma_f32 v[44:45], v[6:7], s[4:5], v[50:51] op_sel_hi:[1,0,1]
	v_pk_fma_f32 v[46:47], v[8:9], s[4:5], v[52:53] op_sel_hi:[1,0,1]
	v_pk_fma_f32 v[48:49], v[10:11], s[4:5], v[54:55] op_sel_hi:[1,0,1]
	v_pk_fma_f32 v[50:51], v[12:13], s[4:5], v[56:57] op_sel_hi:[1,0,1]
	v_pk_fma_f32 v[52:53], v[14:15], s[4:5], v[58:59] op_sel_hi:[1,0,1]
	v_pk_fma_f32 v[54:55], v[16:17], s[4:5], v[60:61] op_sel_hi:[1,0,1]
	v_pk_fma_f32 v[56:57], v[18:19], s[4:5], v[62:63] op_sel_hi:[1,0,1]
	v_pk_fma_f32 v[58:59], v[20:21], s[4:5], v[64:65] op_sel_hi:[1,0,1]
	v_pk_fma_f32 v[60:61], v[22:23], s[4:5], v[66:67] op_sel_hi:[1,0,1]
	v_pk_fma_f32 v[62:63], v[24:25], s[4:5], v[68:69] op_sel_hi:[1,0,1]
	v_pk_fma_f32 v[66:67], v[26:27], s[4:5], v[70:71] op_sel_hi:[1,0,1]
	v_pk_fma_f32 v[70:71], v[28:29], s[4:5], v[72:73] op_sel_hi:[1,0,1]
	v_pk_fma_f32 v[72:73], v[30:31], s[4:5], v[74:75] op_sel_hi:[1,0,1]
	v_readlane_b32 s4, v118, s80
	s_waitcnt vmcnt(0)
	v_cvt_scalef32_pk32_f32_fp6 v[0:31], v[32:37], 1.0
	v_pk_fma_f32 v[32:33], v[0:1], s[4:5], v[38:39] op_sel_hi:[1,0,1]
	v_pk_fma_f32 v[34:35], v[2:3], s[4:5], v[40:41] op_sel_hi:[1,0,1]
	v_pk_fma_f32 v[78:79], v[4:5], s[4:5], v[42:43] op_sel_hi:[1,0,1]
	v_pk_fma_f32 v[80:81], v[6:7], s[4:5], v[44:45] op_sel_hi:[1,0,1]
	v_pk_fma_f32 v[100:101], v[8:9], s[4:5], v[46:47] op_sel_hi:[1,0,1]
	v_pk_fma_f32 v[102:103], v[10:11], s[4:5], v[48:49] op_sel_hi:[1,0,1]
	v_pk_fma_f32 v[84:85], v[12:13], s[4:5], v[50:51] op_sel_hi:[1,0,1]
	v_pk_fma_f32 v[90:91], v[14:15], s[4:5], v[52:53] op_sel_hi:[1,0,1]
	v_pk_fma_f32 v[64:65], v[16:17], s[4:5], v[54:55] op_sel_hi:[1,0,1]
	v_pk_fma_f32 v[68:69], v[18:19], s[4:5], v[56:57] op_sel_hi:[1,0,1]
	v_pk_fma_f32 v[42:43], v[20:21], s[4:5], v[58:59] op_sel_hi:[1,0,1]
	v_pk_fma_f32 v[44:45], v[22:23], s[4:5], v[60:61] op_sel_hi:[1,0,1]
	v_pk_fma_f32 v[38:39], v[24:25], s[4:5], v[62:63] op_sel_hi:[1,0,1]
	v_pk_fma_f32 v[40:41], v[26:27], s[4:5], v[66:67] op_sel_hi:[1,0,1]
	v_pk_fma_f32 v[22:23], v[28:29], s[4:5], v[70:71] op_sel_hi:[1,0,1]
	v_pk_fma_f32 v[20:21], v[30:31], s[4:5], v[72:73] op_sel_hi:[1,0,1]
	s_andn2_b64 vcc, exec, s[54:55]
	s_cbranch_vccnz .LBB0_1178
	ds_write2st64_b32 v174, v32, v33 offset1:1
	ds_write2st64_b32 v174, v34, v35 offset0:2 offset1:3
	ds_write2st64_b32 v174, v78, v79 offset0:4 offset1:5
	ds_write2st64_b32 v174, v80, v81 offset0:6 offset1:7
	ds_write2st64_b32 v174, v100, v101 offset0:8 offset1:9
	ds_write2st64_b32 v174, v102, v103 offset0:10 offset1:11
	ds_write2st64_b32 v174, v84, v85 offset0:12 offset1:13
	ds_write2st64_b32 v174, v90, v91 offset0:14 offset1:15
	ds_write2st64_b32 v174, v64, v65 offset0:16 offset1:17
	ds_write2st64_b32 v174, v68, v69 offset0:18 offset1:19
	ds_write2st64_b32 v174, v42, v43 offset0:20 offset1:21
	ds_write2st64_b32 v174, v44, v45 offset0:22 offset1:23
	ds_write2st64_b32 v174, v38, v39 offset0:24 offset1:25
	ds_write2st64_b32 v174, v40, v41 offset0:26 offset1:27
	ds_write2st64_b32 v174, v22, v23 offset0:28 offset1:29
	ds_write2st64_b32 v174, v20, v21 offset0:30 offset1:31
	s_branch .LBB0_1178
